# v6 + full-line epilogue stores: the two half-line stores of a row pair merged with ds_bpermute + v_cndmask so each store instruction writes 8 complete 128-byte lines (unpaired stores use the quad form
# baseline (speedup 1.0000x reference)
.LBB0_174:
	v_mbcnt_lo_u32_b32 v231, -1, 0
	v_mbcnt_hi_u32_b32 v231, -1, v231
	v_and_b32_e32 v253, 3, v231
	v_lshrrev_b32_e32 v252, 3, v231
	v_lshl_add_u32 v252, v253, 4, v252
	v_lshlrev_b32_e32 v252, 2, v252
	v_lshrrev_b32_e32 v231, 2, v231
	v_lshl_add_u32 v231, v253, 4, v231
	v_lshlrev_b32_e32 v231, 2, v231
	v_add_u32_e32 v253, 32, v252
	s_mov_b32 s100, 0xf0f0f0f0
	s_mov_b32 s101, 0xf0f0f0f0
	s_ashr_i32 s15, s60, 3
	s_add_i32 s62, s15, s75
	s_lshl_b32 s15, s60, 8
	s_and_b32 s15, s15, 0x700
	s_cmp_eq_u32 s62, 0
	v_lshl_add_u32 v174, s28, 8, v1
	s_cselect_b64 s[26:27], -1, 0
	v_or_b32_e32 v82, s15, v209
	s_and_b64 s[26:27], s[50:51], s[26:27]
	v_or_b32_e32 v180, 16, v174
	v_or_b32_e32 v178, 32, v174
	v_or_b32_e32 v176, 48, v174
	s_mov_b64 s[64:65], -1
	s_and_b64 vcc, exec, s[26:27]
	v_lshlrev_b32_e32 v114, 1, v82
	v_ashrrev_i32_e32 v175, 31, v174
	v_ashrrev_i32_e32 v181, 31, v180
	v_ashrrev_i32_e32 v179, 31, v178
	v_ashrrev_i32_e32 v177, 31, v176
	s_cbranch_vccnz .LBB0_177
	v_lshl_add_u32 v158, s14, 10, v210
	ds_read2_b32 v[88:89], v158 offset1:16
	s_ashr_i32 s63, s62, 31
	s_lshl_b64 s[26:27], s[62:63], 25
	s_add_u32 s26, s84, s26
	s_addc_u32 s27, s85, s27
	v_lshl_add_u64 v[90:91], s[26:27], 0, v[114:115]
	v_lshlrev_b64 v[82:83], 12, v[174:175]
	s_waitcnt lgkmcnt(0)
	v_pk_mul_f32 v[84:85], v[144:145], v[88:89] op_sel_hi:[1,0]
	v_lshl_add_u64 v[82:83], v[90:91], 0, v[82:83]
	v_pk_mul_f32 v[86:87], v[146:147], v[88:89] op_sel_hi:[1,0]
	v_cvt_pk_bf16_f32 v84, v84, v85
	v_pk_mul_f32 v[92:93], v[142:143], v[88:89] op_sel_hi:[1,0]
	v_cvt_pk_bf16_f32 v85, v86, v87
	v_pk_mul_f32 v[94:95], v[140:141], v[88:89] op_sel_hi:[1,0]
	v_cvt_pk_bf16_f32 v87, v92, v93
	v_pk_mul_f32 v[92:93], v[134:135], v[88:89] op_sel_hi:[1,0]
	v_cvt_pk_bf16_f32 v86, v94, v95
	v_subrev_u32_e32 v240, s82, v82
	ds_bpermute_b32 v232, v252, v84
	ds_bpermute_b32 v236, v253, v84
	ds_bpermute_b32 v233, v252, v85
	ds_bpermute_b32 v237, v253, v85
	ds_bpermute_b32 v234, v252, v86
	ds_bpermute_b32 v238, v253, v86
	ds_bpermute_b32 v235, v252, v87
	ds_bpermute_b32 v239, v253, v87
	ds_bpermute_b32 v241, v253, v240
	ds_bpermute_b32 v240, v252, v240
	v_pk_mul_f32 v[94:95], v[132:133], v[88:89] op_sel_hi:[1,0]
	s_mov_b32 s15, 0x80000
	v_pk_mul_f32 v[84:85], v[136:137], v[88:89] op_sel_hi:[1,0]
	v_pk_mul_f32 v[86:87], v[138:139], v[88:89] op_sel_hi:[1,0]
	v_cvt_pk_bf16_f32 v84, v84, v85
	v_mov_b32_e32 v88, v89
	v_cvt_pk_bf16_f32 v85, v86, v87
	v_cvt_pk_bf16_f32 v86, v94, v95
	v_cvt_pk_bf16_f32 v87, v92, v93
	v_subrev_u32_e32 v250, s82, v82
	v_add_u32_e32 v250, 0x40, v250
	ds_bpermute_b32 v242, v252, v84
	ds_bpermute_b32 v246, v253, v84
	ds_bpermute_b32 v243, v252, v85
	ds_bpermute_b32 v247, v253, v85
	ds_bpermute_b32 v244, v252, v86
	ds_bpermute_b32 v248, v253, v86
	ds_bpermute_b32 v245, v252, v87
	ds_bpermute_b32 v249, v253, v87
	ds_bpermute_b32 v251, v253, v250
	ds_bpermute_b32 v250, v252, v250
	s_waitcnt lgkmcnt(0)
	v_cndmask_b32_e64 v232, v232, v242, s[100:101]
	v_cndmask_b32_e64 v233, v233, v243, s[100:101]
	v_cndmask_b32_e64 v234, v234, v244, s[100:101]
	v_cndmask_b32_e64 v235, v235, v245, s[100:101]
	v_cndmask_b32_e64 v236, v236, v246, s[100:101]
	v_cndmask_b32_e64 v237, v237, v247, s[100:101]
	v_cndmask_b32_e64 v238, v238, v248, s[100:101]
	v_cndmask_b32_e64 v239, v239, v249, s[100:101]
	v_cndmask_b32_e64 v240, v240, v250, s[100:101]
	v_cndmask_b32_e64 v241, v241, v251, s[100:101]
	global_store_dwordx4 v240, v[232:235], s[82:83]
	global_store_dwordx4 v241, v[236:239], s[82:83]
	v_pk_mul_f32 v[94:95], v[126:127], v[88:89] op_sel_hi:[1,0]
	v_pk_mul_f32 v[96:97], v[124:125], v[88:89] op_sel_hi:[1,0]
	v_lshlrev_b64 v[84:85], 12, v[180:181]
	v_lshl_add_u64 v[92:93], v[90:91], 0, v[84:85]
	v_pk_mul_f32 v[86:87], v[130:131], v[88:89] op_sel_hi:[1,0]
	v_pk_mul_f32 v[84:85], v[128:129], v[88:89] op_sel_hi:[1,0]
	s_mov_b64 s[16:17], 0x80000
	v_cvt_pk_bf16_f32 v84, v84, v85
	v_cvt_pk_bf16_f32 v85, v86, v87
	v_cvt_pk_bf16_f32 v86, v96, v97
	v_cvt_pk_bf16_f32 v87, v94, v95
	v_subrev_u32_e32 v240, s82, v92
	ds_bpermute_b32 v232, v252, v84
	ds_bpermute_b32 v236, v253, v84
	ds_bpermute_b32 v233, v252, v85
	ds_bpermute_b32 v237, v253, v85
	ds_bpermute_b32 v234, v252, v86
	ds_bpermute_b32 v238, v253, v86
	ds_bpermute_b32 v235, v252, v87
	ds_bpermute_b32 v239, v253, v87
	ds_bpermute_b32 v241, v253, v240
	ds_bpermute_b32 v240, v252, v240
	v_pk_mul_f32 v[94:95], v[118:119], v[88:89] op_sel_hi:[1,0]
	s_nop 0
	v_pk_mul_f32 v[86:87], v[122:123], v[88:89] op_sel_hi:[1,0]
	v_pk_mul_f32 v[84:85], v[120:121], v[88:89] op_sel_hi:[1,0]
	v_pk_mul_f32 v[88:89], v[116:117], v[88:89] op_sel_hi:[1,0]
	v_cvt_pk_bf16_f32 v84, v84, v85
	v_cvt_pk_bf16_f32 v85, v86, v87
	v_cvt_pk_bf16_f32 v87, v94, v95
	s_nop 0
	v_cvt_pk_bf16_f32 v86, v88, v89
	ds_read2_b32 v[88:89], v158 offset0:32 offset1:48
	v_subrev_u32_e32 v250, s82, v92
	v_add_u32_e32 v250, 0x40, v250
	ds_bpermute_b32 v242, v252, v84
	ds_bpermute_b32 v246, v253, v84
	ds_bpermute_b32 v243, v252, v85
	ds_bpermute_b32 v247, v253, v85
	ds_bpermute_b32 v244, v252, v86
	ds_bpermute_b32 v248, v253, v86
	ds_bpermute_b32 v245, v252, v87
	ds_bpermute_b32 v249, v253, v87
	ds_bpermute_b32 v251, v253, v250
	ds_bpermute_b32 v250, v252, v250
	s_waitcnt lgkmcnt(0)
	v_cndmask_b32_e64 v232, v232, v242, s[100:101]
	v_cndmask_b32_e64 v233, v233, v243, s[100:101]
	v_cndmask_b32_e64 v234, v234, v244, s[100:101]
	v_cndmask_b32_e64 v235, v235, v245, s[100:101]
	v_cndmask_b32_e64 v236, v236, v246, s[100:101]
	v_cndmask_b32_e64 v237, v237, v247, s[100:101]
	v_cndmask_b32_e64 v238, v238, v248, s[100:101]
	v_cndmask_b32_e64 v239, v239, v249, s[100:101]
	v_cndmask_b32_e64 v240, v240, v250, s[100:101]
	v_cndmask_b32_e64 v241, v241, v251, s[100:101]
	global_store_dwordx4 v240, v[232:235], s[82:83]
	global_store_dwordx4 v241, v[236:239], s[82:83]
	s_waitcnt lgkmcnt(0)
	v_pk_mul_f32 v[94:95], v[108:109], v[88:89] op_sel_hi:[1,0]
	v_lshlrev_b64 v[84:85], 12, v[178:179]
	v_lshl_add_u64 v[92:93], v[90:91], 0, v[84:85]
	v_pk_mul_f32 v[84:85], v[110:111], v[88:89] op_sel_hi:[1,0]
	v_pk_mul_f32 v[86:87], v[112:113], v[88:89] op_sel_hi:[1,0]
	v_cvt_pk_bf16_f32 v84, v84, v85
	v_pk_mul_f32 v[96:97], v[106:107], v[88:89] op_sel_hi:[1,0]
	v_cvt_pk_bf16_f32 v85, v86, v87
	v_cvt_pk_bf16_f32 v87, v94, v95
	v_pk_mul_f32 v[94:95], v[100:101], v[88:89] op_sel_hi:[1,0]
	v_cvt_pk_bf16_f32 v86, v96, v97
	v_subrev_u32_e32 v240, s82, v92
	ds_bpermute_b32 v232, v252, v84
	ds_bpermute_b32 v236, v253, v84
	ds_bpermute_b32 v233, v252, v85
	ds_bpermute_b32 v237, v253, v85
	ds_bpermute_b32 v234, v252, v86
	ds_bpermute_b32 v238, v253, v86
	ds_bpermute_b32 v235, v252, v87
	ds_bpermute_b32 v239, v253, v87
	ds_bpermute_b32 v241, v253, v240
	ds_bpermute_b32 v240, v252, v240
	v_pk_mul_f32 v[96:97], v[98:99], v[88:89] op_sel_hi:[1,0]
	s_nop 0
	v_pk_mul_f32 v[84:85], v[102:103], v[88:89] op_sel_hi:[1,0]
	v_pk_mul_f32 v[86:87], v[104:105], v[88:89] op_sel_hi:[1,0]
	v_cvt_pk_bf16_f32 v84, v84, v85
	v_mov_b32_e32 v88, v89
	v_cvt_pk_bf16_f32 v85, v86, v87
	v_cvt_pk_bf16_f32 v86, v96, v97
	v_cvt_pk_bf16_f32 v87, v94, v95
	v_subrev_u32_e32 v250, s82, v92
	v_add_u32_e32 v250, 0x40, v250
	ds_bpermute_b32 v242, v252, v84
	ds_bpermute_b32 v246, v253, v84
	ds_bpermute_b32 v243, v252, v85
	ds_bpermute_b32 v247, v253, v85
	ds_bpermute_b32 v244, v252, v86
	ds_bpermute_b32 v248, v253, v86
	ds_bpermute_b32 v245, v252, v87
	ds_bpermute_b32 v249, v253, v87
	ds_bpermute_b32 v251, v253, v250
	ds_bpermute_b32 v250, v252, v250
	s_waitcnt lgkmcnt(0)
	v_cndmask_b32_e64 v232, v232, v242, s[100:101]
	v_cndmask_b32_e64 v233, v233, v243, s[100:101]
	v_cndmask_b32_e64 v234, v234, v244, s[100:101]
	v_cndmask_b32_e64 v235, v235, v245, s[100:101]
	v_cndmask_b32_e64 v236, v236, v246, s[100:101]
	v_cndmask_b32_e64 v237, v237, v247, s[100:101]
	v_cndmask_b32_e64 v238, v238, v248, s[100:101]
	v_cndmask_b32_e64 v239, v239, v249, s[100:101]
	v_cndmask_b32_e64 v240, v240, v250, s[100:101]
	v_cndmask_b32_e64 v241, v241, v251, s[100:101]
	global_store_dwordx4 v240, v[232:235], s[82:83]
	global_store_dwordx4 v241, v[236:239], s[82:83]
	v_pk_mul_f32 v[94:95], v[74:75], v[88:89] op_sel_hi:[1,0]
	v_pk_mul_f32 v[92:93], v[76:77], v[88:89] op_sel_hi:[1,0]
	v_lshlrev_b64 v[84:85], 12, v[176:177]
	v_lshl_add_u64 v[90:91], v[90:91], 0, v[84:85]
	v_pk_mul_f32 v[86:87], v[80:81], v[88:89] op_sel_hi:[1,0]
	v_pk_mul_f32 v[84:85], v[78:79], v[88:89] op_sel_hi:[1,0]
	s_nop 0
	v_cvt_pk_bf16_f32 v84, v84, v85
	v_cvt_pk_bf16_f32 v85, v86, v87
	v_cvt_pk_bf16_f32 v86, v94, v95
	ds_read2_b32 v[94:95], v158 offset0:128 offset1:144
	v_cvt_pk_bf16_f32 v87, v92, v93
	v_subrev_u32_e32 v240, s82, v90
	ds_bpermute_b32 v232, v252, v84
	ds_bpermute_b32 v236, v253, v84
	ds_bpermute_b32 v233, v252, v85
	ds_bpermute_b32 v237, v253, v85
	ds_bpermute_b32 v234, v252, v86
	ds_bpermute_b32 v238, v253, v86
	ds_bpermute_b32 v235, v252, v87
	ds_bpermute_b32 v239, v253, v87
	ds_bpermute_b32 v241, v253, v240
	ds_bpermute_b32 v240, v252, v240
	v_pk_mul_f32 v[92:93], v[68:69], v[88:89] op_sel_hi:[1,0]
	s_nop 0
	v_pk_mul_f32 v[86:87], v[72:73], v[88:89] op_sel_hi:[1,0]
	v_pk_mul_f32 v[84:85], v[70:71], v[88:89] op_sel_hi:[1,0]
	v_pk_mul_f32 v[88:89], v[66:67], v[88:89] op_sel_hi:[1,0]
	v_cvt_pk_bf16_f32 v84, v84, v85
	v_cvt_pk_bf16_f32 v85, v86, v87
	v_cvt_pk_bf16_f32 v87, v92, v93
	s_waitcnt lgkmcnt(0)
	v_pk_mul_f32 v[92:93], v[58:59], v[94:95] op_sel_hi:[1,0]
	v_cvt_pk_bf16_f32 v86, v88, v89
	v_subrev_u32_e32 v250, s82, v90
	v_add_u32_e32 v250, 0x40, v250
	ds_bpermute_b32 v242, v252, v84
	ds_bpermute_b32 v246, v253, v84
	ds_bpermute_b32 v243, v252, v85
	ds_bpermute_b32 v247, v253, v85
	ds_bpermute_b32 v244, v252, v86
	ds_bpermute_b32 v248, v253, v86
	ds_bpermute_b32 v245, v252, v87
	ds_bpermute_b32 v249, v253, v87
	ds_bpermute_b32 v251, v253, v250
	ds_bpermute_b32 v250, v252, v250
	s_waitcnt lgkmcnt(0)
	v_cndmask_b32_e64 v232, v232, v242, s[100:101]
	v_cndmask_b32_e64 v233, v233, v243, s[100:101]
	v_cndmask_b32_e64 v234, v234, v244, s[100:101]
	v_cndmask_b32_e64 v235, v235, v245, s[100:101]
	v_cndmask_b32_e64 v236, v236, v246, s[100:101]
	v_cndmask_b32_e64 v237, v237, v247, s[100:101]
	v_cndmask_b32_e64 v238, v238, v248, s[100:101]
	v_cndmask_b32_e64 v239, v239, v249, s[100:101]
	v_cndmask_b32_e64 v240, v240, v250, s[100:101]
	v_cndmask_b32_e64 v241, v241, v251, s[100:101]
	global_store_dwordx4 v240, v[232:235], s[82:83]
	global_store_dwordx4 v241, v[236:239], s[82:83]
	v_pk_mul_f32 v[90:91], v[60:61], v[94:95] op_sel_hi:[1,0]
	v_lshl_add_u64 v[88:89], v[82:83], 0, s[16:17]
	v_pk_mul_f32 v[86:87], v[64:65], v[94:95] op_sel_hi:[1,0]
	v_pk_mul_f32 v[84:85], v[62:63], v[94:95] op_sel_hi:[1,0]
	s_mov_b64 s[16:17], 0x90000
	v_cvt_pk_bf16_f32 v84, v84, v85
	v_cvt_pk_bf16_f32 v85, v86, v87
	v_cvt_pk_bf16_f32 v87, v90, v91
	v_add_co_u32_e32 v90, vcc, s15, v82
	v_cvt_pk_bf16_f32 v86, v92, v93
	v_pk_mul_f32 v[92:93], v[50:51], v[94:95] op_sel_hi:[1,0]
	s_nop 0
	v_addc_co_u32_e32 v91, vcc, 0, v83, vcc
	v_subrev_u32_e32 v240, s82, v90
	ds_bpermute_b32 v232, v252, v84
	ds_bpermute_b32 v236, v253, v84
	ds_bpermute_b32 v233, v252, v85
	ds_bpermute_b32 v237, v253, v85
	ds_bpermute_b32 v234, v252, v86
	ds_bpermute_b32 v238, v253, v86
	ds_bpermute_b32 v235, v252, v87
	ds_bpermute_b32 v239, v253, v87
	ds_bpermute_b32 v241, v253, v240
	ds_bpermute_b32 v240, v252, v240
	v_pk_mul_f32 v[90:91], v[52:53], v[94:95] op_sel_hi:[1,0]
	s_mov_b32 s15, 0x90000
	v_pk_mul_f32 v[86:87], v[56:57], v[94:95] op_sel_hi:[1,0]
	v_pk_mul_f32 v[84:85], v[54:55], v[94:95] op_sel_hi:[1,0]
	s_nop 0
	v_cvt_pk_bf16_f32 v84, v84, v85
	v_cvt_pk_bf16_f32 v85, v86, v87
	v_cvt_pk_bf16_f32 v86, v92, v93
	v_cvt_pk_bf16_f32 v87, v90, v91
	v_mov_b32_e32 v90, v95
	v_subrev_u32_e32 v250, s82, v88
	v_add_u32_e32 v250, 0x40, v250
	ds_bpermute_b32 v242, v252, v84
	ds_bpermute_b32 v246, v253, v84
	ds_bpermute_b32 v243, v252, v85
	ds_bpermute_b32 v247, v253, v85
	ds_bpermute_b32 v244, v252, v86
	ds_bpermute_b32 v248, v253, v86
	ds_bpermute_b32 v245, v252, v87
	ds_bpermute_b32 v249, v253, v87
	ds_bpermute_b32 v251, v253, v250
	ds_bpermute_b32 v250, v252, v250
	s_waitcnt lgkmcnt(0)
	v_cndmask_b32_e64 v232, v232, v242, s[100:101]
	v_cndmask_b32_e64 v233, v233, v243, s[100:101]
	v_cndmask_b32_e64 v234, v234, v244, s[100:101]
	v_cndmask_b32_e64 v235, v235, v245, s[100:101]
	v_cndmask_b32_e64 v236, v236, v246, s[100:101]
	v_cndmask_b32_e64 v237, v237, v247, s[100:101]
	v_cndmask_b32_e64 v238, v238, v248, s[100:101]
	v_cndmask_b32_e64 v239, v239, v249, s[100:101]
	v_cndmask_b32_e64 v240, v240, v250, s[100:101]
	v_cndmask_b32_e64 v241, v241, v251, s[100:101]
	global_store_dwordx4 v240, v[232:235], s[82:83]
	global_store_dwordx4 v241, v[236:239], s[82:83]
	v_pk_mul_f32 v[94:95], v[42:43], v[90:91] op_sel_hi:[1,0]
	v_pk_mul_f32 v[92:93], v[44:45], v[90:91] op_sel_hi:[1,0]
	v_pk_mul_f32 v[86:87], v[48:49], v[90:91] op_sel_hi:[1,0]
	v_pk_mul_f32 v[84:85], v[46:47], v[90:91] op_sel_hi:[1,0]
	v_lshl_add_u64 v[88:89], v[82:83], 0, s[16:17]
	v_cvt_pk_bf16_f32 v84, v84, v85
	v_cvt_pk_bf16_f32 v85, v86, v87
	v_cvt_pk_bf16_f32 v86, v94, v95
	ds_read2_b32 v[94:95], v158 offset0:160 offset1:176
	v_cvt_pk_bf16_f32 v87, v92, v93
	v_add_co_u32_e32 v92, vcc, s15, v82
	s_mov_b32 s15, 0xa0000
	s_nop 0
	v_addc_co_u32_e32 v93, vcc, 0, v83, vcc
	v_subrev_u32_e32 v240, s82, v92
	ds_bpermute_b32 v232, v252, v84
	ds_bpermute_b32 v236, v253, v84
	ds_bpermute_b32 v233, v252, v85
	ds_bpermute_b32 v237, v253, v85
	ds_bpermute_b32 v234, v252, v86
	ds_bpermute_b32 v238, v253, v86
	ds_bpermute_b32 v235, v252, v87
	ds_bpermute_b32 v239, v253, v87
	ds_bpermute_b32 v241, v253, v240
	ds_bpermute_b32 v240, v252, v240
	v_pk_mul_f32 v[92:93], v[36:37], v[90:91] op_sel_hi:[1,0]
	s_mov_b64 s[16:17], 0xa0000
	v_pk_mul_f32 v[86:87], v[40:41], v[90:91] op_sel_hi:[1,0]
	v_pk_mul_f32 v[84:85], v[38:39], v[90:91] op_sel_hi:[1,0]
	v_pk_mul_f32 v[90:91], v[34:35], v[90:91] op_sel_hi:[1,0]
	v_cvt_pk_bf16_f32 v84, v84, v85
	v_cvt_pk_bf16_f32 v85, v86, v87
	v_cvt_pk_bf16_f32 v87, v92, v93
	s_waitcnt lgkmcnt(0)
	v_pk_mul_f32 v[92:93], v[26:27], v[94:95] op_sel_hi:[1,0]
	v_cvt_pk_bf16_f32 v86, v90, v91
	v_subrev_u32_e32 v250, s82, v88
	v_add_u32_e32 v250, 0x40, v250
	ds_bpermute_b32 v242, v252, v84
	ds_bpermute_b32 v246, v253, v84
	ds_bpermute_b32 v243, v252, v85
	ds_bpermute_b32 v247, v253, v85
	ds_bpermute_b32 v244, v252, v86
	ds_bpermute_b32 v248, v253, v86
	ds_bpermute_b32 v245, v252, v87
	ds_bpermute_b32 v249, v253, v87
	ds_bpermute_b32 v251, v253, v250
	ds_bpermute_b32 v250, v252, v250
	s_waitcnt lgkmcnt(0)
	v_cndmask_b32_e64 v232, v232, v242, s[100:101]
	v_cndmask_b32_e64 v233, v233, v243, s[100:101]
	v_cndmask_b32_e64 v234, v234, v244, s[100:101]
	v_cndmask_b32_e64 v235, v235, v245, s[100:101]
	v_cndmask_b32_e64 v236, v236, v246, s[100:101]
	v_cndmask_b32_e64 v237, v237, v247, s[100:101]
	v_cndmask_b32_e64 v238, v238, v248, s[100:101]
	v_cndmask_b32_e64 v239, v239, v249, s[100:101]
	v_cndmask_b32_e64 v240, v240, v250, s[100:101]
	v_cndmask_b32_e64 v241, v241, v251, s[100:101]
	global_store_dwordx4 v240, v[232:235], s[82:83]
	global_store_dwordx4 v241, v[236:239], s[82:83]
	v_pk_mul_f32 v[90:91], v[28:29], v[94:95] op_sel_hi:[1,0]
	v_lshl_add_u64 v[88:89], v[82:83], 0, s[16:17]
	v_pk_mul_f32 v[86:87], v[32:33], v[94:95] op_sel_hi:[1,0]
	v_pk_mul_f32 v[84:85], v[30:31], v[94:95] op_sel_hi:[1,0]
	s_mov_b64 s[16:17], 0xb0000
	v_cvt_pk_bf16_f32 v84, v84, v85
	v_cvt_pk_bf16_f32 v85, v86, v87
	v_cvt_pk_bf16_f32 v87, v90, v91
	v_add_co_u32_e32 v90, vcc, s15, v82
	v_cvt_pk_bf16_f32 v86, v92, v93
	s_mov_b32 s15, 0xb0000
	s_nop 0
	v_addc_co_u32_e32 v91, vcc, 0, v83, vcc
	v_subrev_u32_e32 v240, s82, v90
	ds_bpermute_b32 v232, v252, v84
	ds_bpermute_b32 v236, v253, v84
	ds_bpermute_b32 v233, v252, v85
	ds_bpermute_b32 v237, v253, v85
	ds_bpermute_b32 v234, v252, v86
	ds_bpermute_b32 v238, v253, v86
	ds_bpermute_b32 v235, v252, v87
	ds_bpermute_b32 v239, v253, v87
	ds_bpermute_b32 v241, v253, v240
	ds_bpermute_b32 v240, v252, v240
	v_pk_mul_f32 v[90:91], v[20:21], v[94:95] op_sel_hi:[1,0]
	v_pk_mul_f32 v[92:93], v[18:19], v[94:95] op_sel_hi:[1,0]
	v_pk_mul_f32 v[86:87], v[24:25], v[94:95] op_sel_hi:[1,0]
	v_pk_mul_f32 v[84:85], v[22:23], v[94:95] op_sel_hi:[1,0]
	s_nop 0
	v_cvt_pk_bf16_f32 v84, v84, v85
	v_cvt_pk_bf16_f32 v85, v86, v87
	v_cvt_pk_bf16_f32 v87, v90, v91
	v_mov_b32_e32 v90, v95
	v_cvt_pk_bf16_f32 v86, v92, v93
	v_subrev_u32_e32 v250, s82, v88
	v_add_u32_e32 v250, 0x40, v250
	ds_bpermute_b32 v242, v252, v84
	ds_bpermute_b32 v246, v253, v84
	ds_bpermute_b32 v243, v252, v85
	ds_bpermute_b32 v247, v253, v85
	ds_bpermute_b32 v244, v252, v86
	ds_bpermute_b32 v248, v253, v86
	ds_bpermute_b32 v245, v252, v87
	ds_bpermute_b32 v249, v253, v87
	ds_bpermute_b32 v251, v253, v250
	ds_bpermute_b32 v250, v252, v250
	s_waitcnt lgkmcnt(0)
	v_cndmask_b32_e64 v232, v232, v242, s[100:101]
	v_cndmask_b32_e64 v233, v233, v243, s[100:101]
	v_cndmask_b32_e64 v234, v234, v244, s[100:101]
	v_cndmask_b32_e64 v235, v235, v245, s[100:101]
	v_cndmask_b32_e64 v236, v236, v246, s[100:101]
	v_cndmask_b32_e64 v237, v237, v247, s[100:101]
	v_cndmask_b32_e64 v238, v238, v248, s[100:101]
	v_cndmask_b32_e64 v239, v239, v249, s[100:101]
	v_cndmask_b32_e64 v240, v240, v250, s[100:101]
	v_cndmask_b32_e64 v241, v241, v251, s[100:101]
	global_store_dwordx4 v240, v[232:235], s[82:83]
	global_store_dwordx4 v241, v[236:239], s[82:83]
	v_lshl_add_u64 v[88:89], v[82:83], 0, s[16:17]
	v_add_co_u32_e32 v82, vcc, s15, v82
	v_pk_mul_f32 v[84:85], v[14:15], v[90:91] op_sel_hi:[1,0]
	v_pk_mul_f32 v[86:87], v[16:17], v[90:91] op_sel_hi:[1,0]
	v_cvt_pk_bf16_f32 v84, v84, v85
	v_addc_co_u32_e32 v83, vcc, 0, v83, vcc
	v_cvt_pk_bf16_f32 v85, v86, v87
	v_pk_mul_f32 v[92:93], v[12:13], v[90:91] op_sel_hi:[1,0]
	v_pk_mul_f32 v[94:95], v[10:11], v[90:91] op_sel_hi:[1,0]
	v_cvt_pk_bf16_f32 v87, v92, v93
	s_nop 0
	v_cvt_pk_bf16_f32 v86, v94, v95
	v_subrev_u32_e32 v240, s82, v82
	ds_bpermute_b32 v232, v252, v84
	ds_bpermute_b32 v236, v253, v84
	ds_bpermute_b32 v233, v252, v85
	ds_bpermute_b32 v237, v253, v85
	ds_bpermute_b32 v234, v252, v86
	ds_bpermute_b32 v238, v253, v86
	ds_bpermute_b32 v235, v252, v87
	ds_bpermute_b32 v239, v253, v87
	ds_bpermute_b32 v241, v253, v240
	ds_bpermute_b32 v240, v252, v240
	v_pk_mul_f32 v[82:83], v[6:7], v[90:91] op_sel_hi:[1,0]
	s_nop 0
	v_pk_mul_f32 v[84:85], v[8:9], v[90:91] op_sel_hi:[1,0]
	v_pk_mul_f32 v[86:87], v[4:5], v[90:91] op_sel_hi:[1,0]
	v_pk_mul_f32 v[90:91], v[2:3], v[90:91] op_sel_hi:[1,0]
	v_cvt_pk_bf16_f32 v82, v82, v83
	v_cvt_pk_bf16_f32 v83, v84, v85
	v_cvt_pk_bf16_f32 v85, v86, v87
	s_nop 0
	v_cvt_pk_bf16_f32 v84, v90, v91
	v_subrev_u32_e32 v250, s82, v88
	v_add_u32_e32 v250, 0x40, v250
	ds_bpermute_b32 v242, v252, v82
	ds_bpermute_b32 v246, v253, v82
	ds_bpermute_b32 v243, v252, v83
	ds_bpermute_b32 v247, v253, v83
	ds_bpermute_b32 v244, v252, v84
	ds_bpermute_b32 v248, v253, v84
	ds_bpermute_b32 v245, v252, v85
	ds_bpermute_b32 v249, v253, v85
	ds_bpermute_b32 v251, v253, v250
	ds_bpermute_b32 v250, v252, v250
	s_waitcnt lgkmcnt(0)
	v_cndmask_b32_e64 v232, v232, v242, s[100:101]
	v_cndmask_b32_e64 v233, v233, v243, s[100:101]
	v_cndmask_b32_e64 v234, v234, v244, s[100:101]
	v_cndmask_b32_e64 v235, v235, v245, s[100:101]
	v_cndmask_b32_e64 v236, v236, v246, s[100:101]
	v_cndmask_b32_e64 v237, v237, v247, s[100:101]
	v_cndmask_b32_e64 v238, v238, v248, s[100:101]
	v_cndmask_b32_e64 v239, v239, v249, s[100:101]
	v_cndmask_b32_e64 v240, v240, v250, s[100:101]
	v_cndmask_b32_e64 v241, v241, v251, s[100:101]
	global_store_dwordx4 v240, v[232:235], s[82:83]
	global_store_dwordx4 v241, v[236:239], s[82:83]
	s_cbranch_execz .LBB0_178

.LBB0_178:
	s_lshl_b32 s14, s14, 10
	v_add_u32_e32 v213, s14, v211
	ds_read_b32 v82, v213
	s_waitcnt lgkmcnt(0)
	v_pk_mul_f32 v[84:85], v[146:147], v[82:83] op_sel_hi:[1,0]
	v_pk_mul_f32 v[86:87], v[144:145], v[82:83] op_sel_hi:[1,0]
	v_pk_mul_f32 v[84:85], v[84:85], v[84:85]
	v_pk_mul_f32 v[88:89], v[140:141], v[82:83] op_sel_hi:[1,0]
	v_pk_fma_f32 v[84:85], v[86:87], v[86:87], v[84:85]
	v_pk_mul_f32 v[86:87], v[142:143], v[82:83] op_sel_hi:[1,0]
	s_nop 0
	v_pk_mul_f32 v[86:87], v[86:87], v[86:87]
	s_nop 0
	v_pk_fma_f32 v[86:87], v[88:89], v[88:89], v[86:87]
	v_pk_mul_f32 v[88:89], v[136:137], v[82:83] op_sel_hi:[1,0]
	v_pk_add_f32 v[84:85], v[84:85], v[86:87]
	v_pk_mul_f32 v[86:87], v[138:139], v[82:83] op_sel_hi:[1,0]
	s_nop 0
	v_pk_mul_f32 v[86:87], v[86:87], v[86:87]
	s_nop 0
	v_pk_fma_f32 v[86:87], v[88:89], v[88:89], v[86:87]
	s_nop 0
	v_pk_add_f32 v[84:85], v[86:87], v[84:85]
	v_pk_mul_f32 v[86:87], v[134:135], v[82:83] op_sel_hi:[1,0]
	v_pk_mul_f32 v[82:83], v[132:133], v[82:83] op_sel_hi:[1,0]
	v_pk_mul_f32 v[86:87], v[86:87], v[86:87]
	s_nop 0
	v_pk_fma_f32 v[82:83], v[82:83], v[82:83], v[86:87]
	s_nop 0
	v_pk_add_f32 v[82:83], v[82:83], v[84:85]
	s_nop 0
	v_add_f32_e32 v82, v82, v83
	ds_swizzle_b32 v83, v82 offset:swizzle(SWAP,16)
	s_waitcnt lgkmcnt(0)
	v_add_f32_e32 v82, v82, v83
	v_mov_b32_e32 v83, v82
	s_nop 1
	v_permlane32_swap_b32_e32 v82, v83
	s_and_saveexec_b64 s[62:63], s[38:39]
	v_add_f32_e32 v82, v82, v83
	ds_write_b32 v183, v82
	s_or_b64 exec, exec, s[62:63]
	ds_read_b32 v82, v213 offset:64
	s_waitcnt lgkmcnt(0)
	v_pk_mul_f32 v[84:85], v[130:131], v[82:83] op_sel_hi:[1,0]
	v_pk_mul_f32 v[86:87], v[128:129], v[82:83] op_sel_hi:[1,0]
	v_pk_mul_f32 v[84:85], v[84:85], v[84:85]
	v_pk_mul_f32 v[88:89], v[124:125], v[82:83] op_sel_hi:[1,0]
	v_pk_fma_f32 v[84:85], v[86:87], v[86:87], v[84:85]
	v_pk_mul_f32 v[86:87], v[126:127], v[82:83] op_sel_hi:[1,0]
	s_nop 0
	v_pk_mul_f32 v[86:87], v[86:87], v[86:87]
	s_nop 0
	v_pk_fma_f32 v[86:87], v[88:89], v[88:89], v[86:87]
	v_pk_mul_f32 v[88:89], v[120:121], v[82:83] op_sel_hi:[1,0]
	v_pk_add_f32 v[84:85], v[84:85], v[86:87]
	v_pk_mul_f32 v[86:87], v[122:123], v[82:83] op_sel_hi:[1,0]
	s_nop 0
	v_pk_mul_f32 v[86:87], v[86:87], v[86:87]
	s_nop 0
	v_pk_fma_f32 v[86:87], v[88:89], v[88:89], v[86:87]
	s_nop 0
	v_pk_add_f32 v[84:85], v[86:87], v[84:85]
	v_pk_mul_f32 v[86:87], v[118:119], v[82:83] op_sel_hi:[1,0]
	v_pk_mul_f32 v[82:83], v[116:117], v[82:83] op_sel_hi:[1,0]
	v_pk_mul_f32 v[86:87], v[86:87], v[86:87]
	s_nop 0
	v_pk_fma_f32 v[82:83], v[82:83], v[82:83], v[86:87]
	s_nop 0
	v_pk_add_f32 v[82:83], v[82:83], v[84:85]
	s_nop 0
	v_add_f32_e32 v82, v82, v83
	ds_swizzle_b32 v83, v82 offset:swizzle(SWAP,16)
	s_waitcnt lgkmcnt(0)
	v_add_f32_e32 v82, v82, v83
	v_mov_b32_e32 v83, v82
	s_nop 1
	v_permlane32_swap_b32_e32 v82, v83
	s_and_saveexec_b64 s[62:63], s[38:39]
	v_add_f32_e32 v82, v82, v83
	ds_write_b32 v195, v82
	s_or_b64 exec, exec, s[62:63]
	ds_read_b32 v82, v213 offset:128
	s_waitcnt lgkmcnt(0)
	v_pk_mul_f32 v[84:85], v[112:113], v[82:83] op_sel_hi:[1,0]
	v_pk_mul_f32 v[86:87], v[110:111], v[82:83] op_sel_hi:[1,0]
	v_pk_mul_f32 v[84:85], v[84:85], v[84:85]
	v_pk_mul_f32 v[88:89], v[106:107], v[82:83] op_sel_hi:[1,0]
	v_pk_fma_f32 v[84:85], v[86:87], v[86:87], v[84:85]
	v_pk_mul_f32 v[86:87], v[108:109], v[82:83] op_sel_hi:[1,0]
	s_nop 0
	v_pk_mul_f32 v[86:87], v[86:87], v[86:87]
	s_nop 0
	v_pk_fma_f32 v[86:87], v[88:89], v[88:89], v[86:87]
	v_pk_mul_f32 v[88:89], v[102:103], v[82:83] op_sel_hi:[1,0]
	v_pk_add_f32 v[84:85], v[84:85], v[86:87]
	v_pk_mul_f32 v[86:87], v[104:105], v[82:83] op_sel_hi:[1,0]
	s_nop 0
	v_pk_mul_f32 v[86:87], v[86:87], v[86:87]
	s_nop 0
	v_pk_fma_f32 v[86:87], v[88:89], v[88:89], v[86:87]
	s_nop 0
	v_pk_add_f32 v[84:85], v[86:87], v[84:85]
	v_pk_mul_f32 v[86:87], v[100:101], v[82:83] op_sel_hi:[1,0]
	v_pk_mul_f32 v[82:83], v[98:99], v[82:83] op_sel_hi:[1,0]
	v_pk_mul_f32 v[86:87], v[86:87], v[86:87]
	s_nop 0
	v_pk_fma_f32 v[82:83], v[82:83], v[82:83], v[86:87]
	s_nop 0
	v_pk_add_f32 v[82:83], v[82:83], v[84:85]
	s_nop 0
	v_add_f32_e32 v82, v82, v83
	ds_swizzle_b32 v83, v82 offset:swizzle(SWAP,16)
	s_waitcnt lgkmcnt(0)
	v_add_f32_e32 v82, v82, v83
	v_mov_b32_e32 v83, v82
	s_nop 1
	v_permlane32_swap_b32_e32 v82, v83
	s_and_saveexec_b64 s[62:63], s[38:39]
	v_add_f32_e32 v82, v82, v83
	ds_write_b32 v197, v82
	s_or_b64 exec, exec, s[62:63]
	ds_read_b32 v82, v213 offset:192
	s_waitcnt lgkmcnt(0)
	v_pk_mul_f32 v[84:85], v[80:81], v[82:83] op_sel_hi:[1,0]
	v_pk_mul_f32 v[86:87], v[78:79], v[82:83] op_sel_hi:[1,0]
	v_pk_mul_f32 v[84:85], v[84:85], v[84:85]
	v_pk_mul_f32 v[88:89], v[74:75], v[82:83] op_sel_hi:[1,0]
	v_pk_fma_f32 v[84:85], v[86:87], v[86:87], v[84:85]
	v_pk_mul_f32 v[86:87], v[76:77], v[82:83] op_sel_hi:[1,0]
	s_nop 0
	v_pk_mul_f32 v[86:87], v[86:87], v[86:87]
	s_nop 0
	v_pk_fma_f32 v[86:87], v[88:89], v[88:89], v[86:87]
	v_pk_mul_f32 v[88:89], v[70:71], v[82:83] op_sel_hi:[1,0]
	v_pk_add_f32 v[84:85], v[84:85], v[86:87]
	v_pk_mul_f32 v[86:87], v[72:73], v[82:83] op_sel_hi:[1,0]
	s_nop 0
	v_pk_mul_f32 v[86:87], v[86:87], v[86:87]
	s_nop 0
	v_pk_fma_f32 v[86:87], v[88:89], v[88:89], v[86:87]
	s_nop 0
	v_pk_add_f32 v[84:85], v[86:87], v[84:85]
	v_pk_mul_f32 v[86:87], v[68:69], v[82:83] op_sel_hi:[1,0]
	v_pk_mul_f32 v[82:83], v[66:67], v[82:83] op_sel_hi:[1,0]
	v_pk_mul_f32 v[86:87], v[86:87], v[86:87]
	s_nop 0
	v_pk_fma_f32 v[82:83], v[82:83], v[82:83], v[86:87]
	s_nop 0
	v_pk_add_f32 v[82:83], v[82:83], v[84:85]
	s_nop 0
	v_add_f32_e32 v82, v82, v83
	ds_swizzle_b32 v83, v82 offset:swizzle(SWAP,16)
	s_waitcnt lgkmcnt(0)
	v_add_f32_e32 v82, v82, v83
	v_mov_b32_e32 v83, v82
	s_nop 1
	v_permlane32_swap_b32_e32 v82, v83
	s_and_saveexec_b64 s[62:63], s[38:39]
	v_add_f32_e32 v82, v82, v83
	ds_write_b32 v199, v82
	s_or_b64 exec, exec, s[62:63]
	ds_read_b32 v82, v213 offset:512
	s_waitcnt lgkmcnt(0)
	v_pk_mul_f32 v[84:85], v[64:65], v[82:83] op_sel_hi:[1,0]
	v_pk_mul_f32 v[86:87], v[62:63], v[82:83] op_sel_hi:[1,0]
	v_pk_mul_f32 v[84:85], v[84:85], v[84:85]
	v_pk_mul_f32 v[88:89], v[58:59], v[82:83] op_sel_hi:[1,0]
	v_pk_fma_f32 v[84:85], v[86:87], v[86:87], v[84:85]
	v_pk_mul_f32 v[86:87], v[60:61], v[82:83] op_sel_hi:[1,0]
	s_nop 0
	v_pk_mul_f32 v[86:87], v[86:87], v[86:87]
	s_nop 0
	v_pk_fma_f32 v[86:87], v[88:89], v[88:89], v[86:87]
	v_pk_mul_f32 v[88:89], v[54:55], v[82:83] op_sel_hi:[1,0]
	v_pk_add_f32 v[84:85], v[84:85], v[86:87]
	v_pk_mul_f32 v[86:87], v[56:57], v[82:83] op_sel_hi:[1,0]
	s_nop 0
	v_pk_mul_f32 v[86:87], v[86:87], v[86:87]
	s_nop 0
	v_pk_fma_f32 v[86:87], v[88:89], v[88:89], v[86:87]
	s_nop 0
	v_pk_add_f32 v[84:85], v[86:87], v[84:85]
	v_pk_mul_f32 v[86:87], v[52:53], v[82:83] op_sel_hi:[1,0]
	v_pk_mul_f32 v[82:83], v[50:51], v[82:83] op_sel_hi:[1,0]
	v_pk_mul_f32 v[86:87], v[86:87], v[86:87]
	s_nop 0
	v_pk_fma_f32 v[82:83], v[82:83], v[82:83], v[86:87]
	s_nop 0
	v_pk_add_f32 v[82:83], v[82:83], v[84:85]
	s_nop 0
	v_add_f32_e32 v82, v82, v83
	ds_swizzle_b32 v83, v82 offset:swizzle(SWAP,16)
	s_waitcnt lgkmcnt(0)
	v_add_f32_e32 v82, v82, v83
	v_mov_b32_e32 v83, v82
	s_nop 1
	v_permlane32_swap_b32_e32 v82, v83
	s_and_saveexec_b64 s[62:63], s[38:39]
	v_add_f32_e32 v82, v82, v83
	ds_write_b32 v201, v82
	s_or_b64 exec, exec, s[62:63]
	ds_read_b32 v82, v213 offset:576
	s_waitcnt lgkmcnt(0)
	v_pk_mul_f32 v[84:85], v[48:49], v[82:83] op_sel_hi:[1,0]
	v_pk_mul_f32 v[86:87], v[46:47], v[82:83] op_sel_hi:[1,0]
	v_pk_mul_f32 v[84:85], v[84:85], v[84:85]
	v_pk_mul_f32 v[88:89], v[42:43], v[82:83] op_sel_hi:[1,0]
	v_pk_fma_f32 v[84:85], v[86:87], v[86:87], v[84:85]
	v_pk_mul_f32 v[86:87], v[44:45], v[82:83] op_sel_hi:[1,0]
	s_nop 0
	v_pk_mul_f32 v[86:87], v[86:87], v[86:87]
	s_nop 0
	v_pk_fma_f32 v[86:87], v[88:89], v[88:89], v[86:87]
	v_pk_mul_f32 v[88:89], v[38:39], v[82:83] op_sel_hi:[1,0]
	v_pk_add_f32 v[84:85], v[84:85], v[86:87]
	v_pk_mul_f32 v[86:87], v[40:41], v[82:83] op_sel_hi:[1,0]
	s_nop 0
	v_pk_mul_f32 v[86:87], v[86:87], v[86:87]
	s_nop 0
	v_pk_fma_f32 v[86:87], v[88:89], v[88:89], v[86:87]
	s_nop 0
	v_pk_add_f32 v[84:85], v[86:87], v[84:85]
	v_pk_mul_f32 v[86:87], v[36:37], v[82:83] op_sel_hi:[1,0]
	v_pk_mul_f32 v[82:83], v[34:35], v[82:83] op_sel_hi:[1,0]
	v_pk_mul_f32 v[86:87], v[86:87], v[86:87]
	s_nop 0
	v_pk_fma_f32 v[82:83], v[82:83], v[82:83], v[86:87]
	s_nop 0
	v_pk_add_f32 v[82:83], v[82:83], v[84:85]
	s_nop 0
	v_add_f32_e32 v82, v82, v83
	ds_swizzle_b32 v83, v82 offset:swizzle(SWAP,16)
	s_waitcnt lgkmcnt(0)
	v_add_f32_e32 v82, v82, v83
	v_mov_b32_e32 v83, v82
	s_nop 1
	v_permlane32_swap_b32_e32 v82, v83
	s_and_saveexec_b64 s[62:63], s[38:39]
	v_add_f32_e32 v82, v82, v83
	ds_write_b32 v203, v82
	s_or_b64 exec, exec, s[62:63]
	ds_read_b32 v82, v213 offset:640
	s_waitcnt lgkmcnt(0)
	v_pk_mul_f32 v[84:85], v[32:33], v[82:83] op_sel_hi:[1,0]
	v_pk_mul_f32 v[86:87], v[30:31], v[82:83] op_sel_hi:[1,0]
	v_pk_mul_f32 v[84:85], v[84:85], v[84:85]
	v_pk_mul_f32 v[88:89], v[26:27], v[82:83] op_sel_hi:[1,0]
	v_pk_fma_f32 v[84:85], v[86:87], v[86:87], v[84:85]
	v_pk_mul_f32 v[86:87], v[28:29], v[82:83] op_sel_hi:[1,0]
	s_nop 0
	v_pk_mul_f32 v[86:87], v[86:87], v[86:87]
	s_nop 0
	v_pk_fma_f32 v[86:87], v[88:89], v[88:89], v[86:87]
	v_pk_mul_f32 v[88:89], v[22:23], v[82:83] op_sel_hi:[1,0]
	v_pk_add_f32 v[84:85], v[84:85], v[86:87]
	v_pk_mul_f32 v[86:87], v[24:25], v[82:83] op_sel_hi:[1,0]
	s_nop 0
	v_pk_mul_f32 v[86:87], v[86:87], v[86:87]
	s_nop 0
	v_pk_fma_f32 v[86:87], v[88:89], v[88:89], v[86:87]
	s_nop 0
	v_pk_add_f32 v[84:85], v[86:87], v[84:85]
	v_pk_mul_f32 v[86:87], v[20:21], v[82:83] op_sel_hi:[1,0]
	v_pk_mul_f32 v[82:83], v[18:19], v[82:83] op_sel_hi:[1,0]
	v_pk_mul_f32 v[86:87], v[86:87], v[86:87]
	s_nop 0
	v_pk_fma_f32 v[82:83], v[82:83], v[82:83], v[86:87]
	s_nop 0
	v_pk_add_f32 v[82:83], v[82:83], v[84:85]
	s_nop 0
	v_add_f32_e32 v82, v82, v83
	ds_swizzle_b32 v83, v82 offset:swizzle(SWAP,16)
	s_waitcnt lgkmcnt(0)
	v_add_f32_e32 v82, v82, v83
	v_mov_b32_e32 v83, v82
	s_nop 1
	v_permlane32_swap_b32_e32 v82, v83
	s_and_saveexec_b64 s[62:63], s[38:39]
	v_add_f32_e32 v82, v82, v83
	ds_write_b32 v205, v82
	s_or_b64 exec, exec, s[62:63]
	ds_read_b32 v82, v213 offset:704
	s_waitcnt lgkmcnt(0)
	v_pk_mul_f32 v[84:85], v[16:17], v[82:83] op_sel_hi:[1,0]
	v_pk_mul_f32 v[86:87], v[14:15], v[82:83] op_sel_hi:[1,0]
	v_pk_mul_f32 v[84:85], v[84:85], v[84:85]
	v_pk_mul_f32 v[88:89], v[10:11], v[82:83] op_sel_hi:[1,0]
	v_pk_fma_f32 v[84:85], v[86:87], v[86:87], v[84:85]
	v_pk_mul_f32 v[86:87], v[12:13], v[82:83] op_sel_hi:[1,0]
	s_nop 0
	v_pk_mul_f32 v[86:87], v[86:87], v[86:87]
	s_nop 0
	v_pk_fma_f32 v[86:87], v[88:89], v[88:89], v[86:87]
	v_pk_mul_f32 v[88:89], v[6:7], v[82:83] op_sel_hi:[1,0]
	v_pk_add_f32 v[84:85], v[84:85], v[86:87]
	v_pk_mul_f32 v[86:87], v[8:9], v[82:83] op_sel_hi:[1,0]
	s_nop 0
	v_pk_mul_f32 v[86:87], v[86:87], v[86:87]
	s_nop 0
	v_pk_fma_f32 v[86:87], v[88:89], v[88:89], v[86:87]
	s_nop 0
	v_pk_add_f32 v[84:85], v[86:87], v[84:85]
	v_pk_mul_f32 v[86:87], v[4:5], v[82:83] op_sel_hi:[1,0]
	v_pk_mul_f32 v[82:83], v[2:3], v[82:83] op_sel_hi:[1,0]
	v_pk_mul_f32 v[86:87], v[86:87], v[86:87]
	s_nop 0
	v_pk_fma_f32 v[82:83], v[82:83], v[82:83], v[86:87]
	s_nop 0
	v_pk_add_f32 v[82:83], v[82:83], v[84:85]
	s_nop 0
	v_add_f32_e32 v82, v82, v83
	ds_swizzle_b32 v83, v82 offset:swizzle(SWAP,16)
	s_waitcnt lgkmcnt(0)
	v_add_f32_e32 v82, v82, v83
	v_mov_b32_e32 v83, v82
	s_nop 1
	v_permlane32_swap_b32_e32 v82, v83
	s_and_saveexec_b64 s[62:63], s[38:39]
	v_add_f32_e32 v82, v82, v83
	ds_write_b32 v207, v82
	s_or_b64 exec, exec, s[62:63]
	s_waitcnt lgkmcnt(0)
	s_barrier
	global_load_dwordx4 v[94:97], v[168:169], off offset:16
	global_load_dwordx4 v[90:93], v[168:169], off
	global_load_dwordx4 v[82:85], v[168:169], off offset:144
	global_load_dwordx4 v[86:89], v[168:169], off offset:128
	ds_read_b32 v158, v183
	ds_read_b32 v159, v194
	s_lshl_b32 s14, s60, 1
	s_and_b32 s14, s14, 14
	s_lshl_b32 s15, s28, 1
	s_or_b32 s14, s88, s14
	s_waitcnt lgkmcnt(0)
	v_add_f32_e32 v158, v158, v159
	v_fmamk_f32 v158, v158, 0x3c000000, v185
	v_rsq_f32_e32 v160, v158
	ds_read2_b32 v[158:159], v213 offset1:16
	s_and_b32 s15, s15, 0x7fffff0
	s_or_b32 s14, s15, s14
	s_lshl_b32 s15, s28, 2
	s_and_b32 s15, s15, 28
	s_waitcnt lgkmcnt(0)
	v_mul_f32_e32 v158, v158, v160
	v_lshlrev_b64 v[160:161], 12, v[174:175]
	v_lshl_add_u64 v[160:161], s[46:47], 0, v[160:161]
	v_pk_mul_f32 v[144:145], v[144:145], v[158:159] op_sel_hi:[1,0]
	v_pk_mul_f32 v[146:147], v[146:147], v[158:159] op_sel_hi:[1,0]
	v_pk_mul_f32 v[218:219], v[140:141], v[158:159] op_sel_hi:[1,0]
	v_lshl_add_u64 v[160:161], v[160:161], 0, v[114:115]
	v_pk_mul_f32 v[140:141], v[142:143], v[158:159] op_sel_hi:[1,0]
	s_lshl_b32 s14, s14, 5
	s_add_i32 s15, s15, s8
	s_add_i32 s28, s15, s14
	s_ashr_i32 s29, s28, 31
	s_lshl_b64 s[14:15], s[28:29], 9
	s_waitcnt vmcnt(0)
	v_pk_mul_f32 v[142:143], v[94:95], v[218:219]
	v_pk_mul_f32 v[214:215], v[92:93], v[146:147]
	v_pk_mul_f32 v[216:217], v[90:91], v[144:145]
	v_pk_fma_f32 v[218:219], v[90:91], v[144:145], 0 op_sel_hi:[1,1,0]
	v_cvt_pk_bf16_f32 v144, v216, v217
	v_cvt_pk_bf16_f32 v145, v214, v215
	v_pk_mul_f32 v[140:141], v[96:97], v[140:141]
	v_pk_fma_f32 v[220:221], v[92:93], v[146:147], 0 op_sel_hi:[1,1,0]
	v_cvt_pk_bf16_f32 v146, v142, v143
	v_cvt_pk_bf16_f32 v147, v140, v141
	v_subrev_u32_e32 v240, s82, v160
	ds_bpermute_b32 v232, v252, v144
	ds_bpermute_b32 v236, v253, v144
	ds_bpermute_b32 v233, v252, v145
	ds_bpermute_b32 v237, v253, v145
	ds_bpermute_b32 v234, v252, v146
	ds_bpermute_b32 v238, v253, v146
	ds_bpermute_b32 v235, v252, v147
	ds_bpermute_b32 v239, v253, v147
	ds_bpermute_b32 v241, v253, v240
	ds_bpermute_b32 v240, v252, v240
	s_nop 1
	v_pk_mul_f32 v[144:145], v[136:137], v[158:159] op_sel_hi:[1,0]
	v_pk_mul_f32 v[136:137], v[138:139], v[158:159] op_sel_hi:[1,0]
	v_pk_mul_f32 v[138:139], v[86:87], v[144:145]
	v_pk_mul_f32 v[144:145], v[132:133], v[158:159] op_sel_hi:[1,0]
	v_pk_mul_f32 v[132:133], v[134:135], v[158:159] op_sel_hi:[1,0]
	v_pk_mul_f32 v[136:137], v[88:89], v[136:137]
	v_pk_mul_f32 v[132:133], v[84:85], v[132:133]
	v_pk_mul_f32 v[134:135], v[82:83], v[144:145]
	v_cvt_pk_bf16_f32 v144, v138, v139
	v_cvt_pk_bf16_f32 v145, v136, v137
	v_cvt_pk_bf16_f32 v147, v132, v133
	s_nop 0
	v_cvt_pk_bf16_f32 v146, v134, v135
	v_subrev_u32_e32 v250, s82, v160
	v_add_u32_e32 v250, 0x40, v250
	ds_bpermute_b32 v242, v252, v144
	ds_bpermute_b32 v246, v253, v144
	ds_bpermute_b32 v243, v252, v145
	ds_bpermute_b32 v247, v253, v145
	ds_bpermute_b32 v244, v252, v146
	ds_bpermute_b32 v248, v253, v146
	ds_bpermute_b32 v245, v252, v147
	ds_bpermute_b32 v249, v253, v147
	ds_bpermute_b32 v251, v253, v250
	ds_bpermute_b32 v250, v252, v250
	s_waitcnt lgkmcnt(0)
	v_cndmask_b32_e64 v232, v232, v242, s[100:101]
	v_cndmask_b32_e64 v233, v233, v243, s[100:101]
	v_cndmask_b32_e64 v234, v234, v244, s[100:101]
	v_cndmask_b32_e64 v235, v235, v245, s[100:101]
	v_cndmask_b32_e64 v236, v236, v246, s[100:101]
	v_cndmask_b32_e64 v237, v237, v247, s[100:101]
	v_cndmask_b32_e64 v238, v238, v248, s[100:101]
	v_cndmask_b32_e64 v239, v239, v249, s[100:101]
	v_cndmask_b32_e64 v240, v240, v250, s[100:101]
	v_cndmask_b32_e64 v241, v241, v251, s[100:101]
	global_store_dwordx4 v240, v[232:235], s[82:83]
	global_store_dwordx4 v241, v[236:239], s[82:83]
	ds_read_b32 v144, v195
	ds_read_b32 v145, v196
	v_lshlrev_b64 v[146:147], 12, v[180:181]
	v_lshl_add_u64 v[146:147], s[46:47], 0, v[146:147]
	v_lshl_add_u64 v[146:147], v[146:147], 0, v[114:115]
	s_waitcnt lgkmcnt(0)
	v_add_f32_e32 v144, v144, v145
	v_fmamk_f32 v144, v144, 0x3c000000, v185
	v_rsq_f32_e32 v144, v144
	s_nop 0
	v_mul_f32_e32 v144, v159, v144
	v_pk_mul_f32 v[128:129], v[128:129], v[144:145] op_sel_hi:[1,0]
	v_pk_mul_f32 v[130:131], v[130:131], v[144:145] op_sel_hi:[1,0]
	v_pk_mul_f32 v[160:161], v[90:91], v[128:129]
	v_pk_mul_f32 v[158:159], v[92:93], v[130:131]
	v_pk_mul_f32 v[180:181], v[124:125], v[144:145] op_sel_hi:[1,0]
	v_pk_mul_f32 v[124:125], v[126:127], v[144:145] op_sel_hi:[1,0]
	v_pk_fma_f32 v[214:215], v[90:91], v[128:129], v[218:219]
	v_cvt_pk_bf16_f32 v128, v160, v161
	v_cvt_pk_bf16_f32 v129, v158, v159
	v_pk_mul_f32 v[124:125], v[96:97], v[124:125]
	v_pk_mul_f32 v[126:127], v[94:95], v[180:181]
	v_pk_fma_f32 v[180:181], v[92:93], v[130:131], v[220:221]
	v_cvt_pk_bf16_f32 v130, v126, v127
	v_cvt_pk_bf16_f32 v131, v124, v125
	v_subrev_u32_e32 v240, s82, v146
	ds_bpermute_b32 v232, v252, v128
	ds_bpermute_b32 v236, v253, v128
	ds_bpermute_b32 v233, v252, v129
	ds_bpermute_b32 v237, v253, v129
	ds_bpermute_b32 v234, v252, v130
	ds_bpermute_b32 v238, v253, v130
	ds_bpermute_b32 v235, v252, v131
	ds_bpermute_b32 v239, v253, v131
	ds_bpermute_b32 v241, v253, v240
	ds_bpermute_b32 v240, v252, v240
	s_nop 1
	v_pk_mul_f32 v[128:129], v[120:121], v[144:145] op_sel_hi:[1,0]
	v_pk_mul_f32 v[120:121], v[122:123], v[144:145] op_sel_hi:[1,0]
	v_pk_mul_f32 v[122:123], v[86:87], v[128:129]
	v_pk_mul_f32 v[128:129], v[116:117], v[144:145] op_sel_hi:[1,0]
	v_pk_mul_f32 v[116:117], v[118:119], v[144:145] op_sel_hi:[1,0]
	v_pk_mul_f32 v[120:121], v[88:89], v[120:121]
	v_pk_mul_f32 v[116:117], v[84:85], v[116:117]
	v_pk_mul_f32 v[118:119], v[82:83], v[128:129]
	v_cvt_pk_bf16_f32 v128, v122, v123
	v_cvt_pk_bf16_f32 v129, v120, v121
	v_cvt_pk_bf16_f32 v131, v116, v117
	s_nop 0
	v_cvt_pk_bf16_f32 v130, v118, v119
	v_subrev_u32_e32 v250, s82, v146
	v_add_u32_e32 v250, 0x40, v250
	ds_bpermute_b32 v242, v252, v128
	ds_bpermute_b32 v246, v253, v128
	ds_bpermute_b32 v243, v252, v129
	ds_bpermute_b32 v247, v253, v129
	ds_bpermute_b32 v244, v252, v130
	ds_bpermute_b32 v248, v253, v130
	ds_bpermute_b32 v245, v252, v131
	ds_bpermute_b32 v249, v253, v131
	ds_bpermute_b32 v251, v253, v250
	ds_bpermute_b32 v250, v252, v250
	s_waitcnt lgkmcnt(0)
	v_cndmask_b32_e64 v232, v232, v242, s[100:101]
	v_cndmask_b32_e64 v233, v233, v243, s[100:101]
	v_cndmask_b32_e64 v234, v234, v244, s[100:101]
	v_cndmask_b32_e64 v235, v235, v245, s[100:101]
	v_cndmask_b32_e64 v236, v236, v246, s[100:101]
	v_cndmask_b32_e64 v237, v237, v247, s[100:101]
	v_cndmask_b32_e64 v238, v238, v248, s[100:101]
	v_cndmask_b32_e64 v239, v239, v249, s[100:101]
	v_cndmask_b32_e64 v240, v240, v250, s[100:101]
	v_cndmask_b32_e64 v241, v241, v251, s[100:101]
	global_store_dwordx4 v240, v[232:235], s[82:83]
	global_store_dwordx4 v241, v[236:239], s[82:83]
	ds_read_b32 v128, v197
	ds_read_b32 v129, v198
	s_waitcnt lgkmcnt(0)
	v_add_f32_e32 v128, v128, v129
	v_fmamk_f32 v128, v128, 0x3c000000, v185
	v_rsq_f32_e32 v130, v128
	ds_read2_b32 v[128:129], v213 offset0:32 offset1:48
	s_waitcnt lgkmcnt(0)
	v_mul_f32_e32 v128, v128, v130
	v_lshlrev_b64 v[130:131], 12, v[178:179]
	v_pk_mul_f32 v[110:111], v[110:111], v[128:129] op_sel_hi:[1,0]
	v_lshl_add_u64 v[130:131], s[46:47], 0, v[130:131]
	v_pk_mul_f32 v[112:113], v[112:113], v[128:129] op_sel_hi:[1,0]
	v_pk_mul_f32 v[144:145], v[90:91], v[110:111]
	v_lshl_add_u64 v[130:131], v[130:131], 0, v[114:115]
	v_pk_mul_f32 v[146:147], v[92:93], v[112:113]
	v_pk_mul_f32 v[158:159], v[106:107], v[128:129] op_sel_hi:[1,0]
	v_pk_mul_f32 v[106:107], v[108:109], v[128:129] op_sel_hi:[1,0]
	v_cvt_pk_bf16_f32 v144, v144, v145
	v_cvt_pk_bf16_f32 v145, v146, v147
	v_pk_mul_f32 v[108:109], v[94:95], v[158:159]
	v_pk_mul_f32 v[106:107], v[96:97], v[106:107]
	v_cvt_pk_bf16_f32 v146, v108, v109
	v_pk_fma_f32 v[110:111], v[90:91], v[110:111], v[214:215]
	v_cvt_pk_bf16_f32 v147, v106, v107
	v_subrev_u32_e32 v240, s82, v130
	ds_bpermute_b32 v232, v252, v144
	ds_bpermute_b32 v236, v253, v144
	ds_bpermute_b32 v233, v252, v145
	ds_bpermute_b32 v237, v253, v145
	ds_bpermute_b32 v234, v252, v146
	ds_bpermute_b32 v238, v253, v146
	ds_bpermute_b32 v235, v252, v147
	ds_bpermute_b32 v239, v253, v147
	ds_bpermute_b32 v241, v253, v240
	ds_bpermute_b32 v240, v252, v240
	v_pk_fma_f32 v[112:113], v[92:93], v[112:113], v[180:181]
	s_nop 0
	v_pk_mul_f32 v[144:145], v[102:103], v[128:129] op_sel_hi:[1,0]
	v_pk_mul_f32 v[102:103], v[104:105], v[128:129] op_sel_hi:[1,0]
	v_pk_mul_f32 v[104:105], v[86:87], v[144:145]
	v_pk_mul_f32 v[144:145], v[98:99], v[128:129] op_sel_hi:[1,0]
	v_pk_mul_f32 v[98:99], v[100:101], v[128:129] op_sel_hi:[1,0]
	v_pk_mul_f32 v[102:103], v[88:89], v[102:103]
	v_pk_mul_f32 v[98:99], v[84:85], v[98:99]
	v_pk_mul_f32 v[100:101], v[82:83], v[144:145]
	v_cvt_pk_bf16_f32 v144, v104, v105
	v_cvt_pk_bf16_f32 v145, v102, v103
	v_cvt_pk_bf16_f32 v147, v98, v99
	s_nop 0
	v_cvt_pk_bf16_f32 v146, v100, v101
	v_subrev_u32_e32 v250, s82, v130
	v_add_u32_e32 v250, 0x40, v250
	ds_bpermute_b32 v242, v252, v144
	ds_bpermute_b32 v246, v253, v144
	ds_bpermute_b32 v243, v252, v145
	ds_bpermute_b32 v247, v253, v145
	ds_bpermute_b32 v244, v252, v146
	ds_bpermute_b32 v248, v253, v146
	ds_bpermute_b32 v245, v252, v147
	ds_bpermute_b32 v249, v253, v147
	ds_bpermute_b32 v251, v253, v250
	ds_bpermute_b32 v250, v252, v250
	s_waitcnt lgkmcnt(0)
	v_cndmask_b32_e64 v232, v232, v242, s[100:101]
	v_cndmask_b32_e64 v233, v233, v243, s[100:101]
	v_cndmask_b32_e64 v234, v234, v244, s[100:101]
	v_cndmask_b32_e64 v235, v235, v245, s[100:101]
	v_cndmask_b32_e64 v236, v236, v246, s[100:101]
	v_cndmask_b32_e64 v237, v237, v247, s[100:101]
	v_cndmask_b32_e64 v238, v238, v248, s[100:101]
	v_cndmask_b32_e64 v239, v239, v249, s[100:101]
	v_cndmask_b32_e64 v240, v240, v250, s[100:101]
	v_cndmask_b32_e64 v241, v241, v251, s[100:101]
	global_store_dwordx4 v240, v[232:235], s[82:83]
	global_store_dwordx4 v241, v[236:239], s[82:83]
	ds_read_b32 v128, v199
	ds_read_b32 v130, v200
	s_waitcnt lgkmcnt(0)
	v_add_f32_e32 v128, v128, v130
	v_fmamk_f32 v128, v128, 0x3c000000, v185
	v_rsq_f32_e32 v128, v128
	v_lshlrev_b64 v[130:131], 12, v[176:177]
	v_lshl_add_u64 v[130:131], s[46:47], 0, v[130:131]
	v_lshl_add_u64 v[130:131], v[130:131], 0, v[114:115]
	v_mul_f32_e32 v128, v129, v128
	v_pk_mul_f32 v[144:145], v[78:79], v[128:129] op_sel_hi:[1,0]
	v_pk_mul_f32 v[80:81], v[80:81], v[128:129] op_sel_hi:[1,0]
	v_pk_mul_f32 v[74:75], v[74:75], v[128:129] op_sel_hi:[1,0]
	v_pk_mul_f32 v[76:77], v[76:77], v[128:129] op_sel_hi:[1,0]
	v_pk_mul_f32 v[146:147], v[92:93], v[80:81]
	v_pk_mul_f32 v[158:159], v[90:91], v[144:145]
	v_pk_mul_f32 v[76:77], v[96:97], v[76:77]
	v_pk_mul_f32 v[78:79], v[94:95], v[74:75]
	v_pk_fma_f32 v[160:161], v[92:93], v[80:81], v[112:113]
	v_pk_fma_f32 v[80:81], v[90:91], v[144:145], v[110:111]
	v_cvt_pk_bf16_f32 v110, v158, v159
	v_cvt_pk_bf16_f32 v111, v146, v147
	v_cvt_pk_bf16_f32 v112, v78, v79
	v_cvt_pk_bf16_f32 v113, v76, v77
	v_pk_mul_f32 v[70:71], v[70:71], v[128:129] op_sel_hi:[1,0]
	v_pk_mul_f32 v[72:73], v[72:73], v[128:129] op_sel_hi:[1,0]
	v_pk_mul_f32 v[66:67], v[66:67], v[128:129] op_sel_hi:[1,0]
	v_pk_mul_f32 v[68:69], v[68:69], v[128:129] op_sel_hi:[1,0]
	v_subrev_u32_e32 v240, s82, v130
	ds_bpermute_b32 v232, v252, v110
	ds_bpermute_b32 v236, v253, v110
	ds_bpermute_b32 v233, v252, v111
	ds_bpermute_b32 v237, v253, v111
	ds_bpermute_b32 v234, v252, v112
	ds_bpermute_b32 v238, v253, v112
	ds_bpermute_b32 v235, v252, v113
	ds_bpermute_b32 v239, v253, v113
	ds_bpermute_b32 v241, v253, v240
	ds_bpermute_b32 v240, v252, v240
	v_pk_mul_f32 v[72:73], v[88:89], v[72:73]
	v_pk_mul_f32 v[74:75], v[86:87], v[70:71]
	v_pk_mul_f32 v[68:69], v[84:85], v[68:69]
	v_pk_mul_f32 v[70:71], v[82:83], v[66:67]
	v_cvt_pk_bf16_f32 v110, v74, v75
	v_cvt_pk_bf16_f32 v111, v72, v73
	v_cvt_pk_bf16_f32 v113, v68, v69
	v_lshl_add_u64 v[66:67], v[166:167], 0, s[14:15]
	v_cvt_pk_bf16_f32 v112, v70, v71
	v_subrev_u32_e32 v250, s82, v130
	v_add_u32_e32 v250, 0x40, v250
	ds_bpermute_b32 v242, v252, v110
	ds_bpermute_b32 v246, v253, v110
	ds_bpermute_b32 v243, v252, v111
	ds_bpermute_b32 v247, v253, v111
	ds_bpermute_b32 v244, v252, v112
	ds_bpermute_b32 v248, v253, v112
	ds_bpermute_b32 v245, v252, v113
	ds_bpermute_b32 v249, v253, v113
	ds_bpermute_b32 v251, v253, v250
	ds_bpermute_b32 v250, v252, v250
	s_waitcnt lgkmcnt(0)
	v_cndmask_b32_e64 v232, v232, v242, s[100:101]
	v_cndmask_b32_e64 v233, v233, v243, s[100:101]
	v_cndmask_b32_e64 v234, v234, v244, s[100:101]
	v_cndmask_b32_e64 v235, v235, v245, s[100:101]
	v_cndmask_b32_e64 v236, v236, v246, s[100:101]
	v_cndmask_b32_e64 v237, v237, v247, s[100:101]
	v_cndmask_b32_e64 v238, v238, v248, s[100:101]
	v_cndmask_b32_e64 v239, v239, v249, s[100:101]
	v_cndmask_b32_e64 v240, v240, v250, s[100:101]
	v_cndmask_b32_e64 v241, v241, v251, s[100:101]
	global_store_dwordx4 v240, v[232:235], s[82:83]
	global_store_dwordx4 v241, v[236:239], s[82:83]
	ds_swizzle_b32 v110, v80 offset:swizzle(SWAP,1)
	ds_swizzle_b32 v111, v81 offset:swizzle(SWAP,1)
	ds_swizzle_b32 v112, v160 offset:swizzle(SWAP,1)
	ds_swizzle_b32 v113, v161 offset:swizzle(SWAP,1)
	s_waitcnt lgkmcnt(2)
	v_pk_add_f32 v[80:81], v[80:81], v[110:111]
	ds_swizzle_b32 v110, v80 offset:swizzle(SWAP,2)
	s_waitcnt lgkmcnt(1)
	v_pk_add_f32 v[112:113], v[160:161], v[112:113]
	ds_swizzle_b32 v111, v81 offset:swizzle(SWAP,2)
	ds_swizzle_b32 v128, v112 offset:swizzle(SWAP,2)
	ds_swizzle_b32 v129, v113 offset:swizzle(SWAP,2)
	s_waitcnt lgkmcnt(2)
	v_pk_add_f32 v[80:81], v[80:81], v[110:111]
	ds_swizzle_b32 v110, v80 offset:swizzle(SWAP,4)
	s_waitcnt lgkmcnt(1)
	v_pk_add_f32 v[112:113], v[112:113], v[128:129]
	ds_swizzle_b32 v111, v81 offset:swizzle(SWAP,4)
	ds_swizzle_b32 v128, v112 offset:swizzle(SWAP,4)
	ds_swizzle_b32 v129, v113 offset:swizzle(SWAP,4)
	s_waitcnt lgkmcnt(2)
	v_pk_add_f32 v[80:81], v[80:81], v[110:111]
	ds_swizzle_b32 v110, v80 offset:swizzle(SWAP,8)
	s_waitcnt lgkmcnt(1)
	v_pk_add_f32 v[112:113], v[112:113], v[128:129]
	ds_swizzle_b32 v111, v81 offset:swizzle(SWAP,8)
	ds_swizzle_b32 v128, v112 offset:swizzle(SWAP,8)
	ds_swizzle_b32 v129, v113 offset:swizzle(SWAP,8)
	s_and_saveexec_b64 s[60:61], s[40:41]
	s_cbranch_execz .LBB0_196
	s_waitcnt lgkmcnt(0)
	v_pk_add_f32 v[112:113], v[112:113], v[128:129]
	v_pk_add_f32 v[110:111], v[80:81], v[110:111]
	global_store_dwordx4 v[66:67], v[110:113], off

.LBB0_202:
	s_or_b64 exec, exec, s[60:61]
	ds_read_b32 v66, v201
	ds_read_b32 v67, v202
	ds_read2_b32 v[68:69], v213 offset0:128 offset1:144
	s_mov_b64 s[14:15], 0x80000
	s_waitcnt lgkmcnt(1)
	v_add_f32_e32 v66, v66, v67
	v_fmamk_f32 v66, v66, 0x3c000000, v185
	v_rsq_f32_e32 v66, v66
	s_waitcnt lgkmcnt(0)
	v_mul_f32_e32 v68, v68, v66
	v_lshlrev_b64 v[66:67], 12, v[174:175]
	v_lshl_add_u64 v[66:67], s[46:47], 0, v[66:67]
	v_lshl_add_u64 v[66:67], v[66:67], 0, v[114:115]
	v_pk_mul_f32 v[64:65], v[64:65], v[68:69] op_sel_hi:[1,0]
	v_lshl_add_u64 v[70:71], v[66:67], 0, s[14:15]
	v_pk_mul_f32 v[62:63], v[62:63], v[68:69] op_sel_hi:[1,0]
	v_pk_mul_f32 v[72:73], v[92:93], v[64:65]
	v_pk_mul_f32 v[76:77], v[58:59], v[68:69] op_sel_hi:[1,0]
	s_mov_b32 s14, 0x80000
	v_pk_mul_f32 v[74:75], v[90:91], v[62:63]
	v_pk_mul_f32 v[58:59], v[60:61], v[68:69] op_sel_hi:[1,0]
	v_pk_mul_f32 v[60:61], v[94:95], v[76:77]
	v_pk_fma_f32 v[76:77], v[90:91], v[62:63], 0 op_sel_hi:[1,1,0]
	v_cvt_pk_bf16_f32 v63, v72, v73
	v_add_co_u32_e32 v72, vcc, s14, v66
	v_cvt_pk_bf16_f32 v62, v74, v75
	v_pk_mul_f32 v[58:59], v[96:97], v[58:59]
	s_nop 0
	v_addc_co_u32_e32 v73, vcc, 0, v67, vcc
	v_pk_fma_f32 v[78:79], v[92:93], v[64:65], 0 op_sel_hi:[1,1,0]
	v_cvt_pk_bf16_f32 v64, v60, v61
	v_cvt_pk_bf16_f32 v65, v58, v59
	v_subrev_u32_e32 v240, s82, v72
	ds_bpermute_b32 v232, v252, v62
	ds_bpermute_b32 v236, v253, v62
	ds_bpermute_b32 v233, v252, v63
	ds_bpermute_b32 v237, v253, v63
	ds_bpermute_b32 v234, v252, v64
	ds_bpermute_b32 v238, v253, v64
	ds_bpermute_b32 v235, v252, v65
	ds_bpermute_b32 v239, v253, v65
	ds_bpermute_b32 v241, v253, v240
	ds_bpermute_b32 v240, v252, v240
	s_mov_b64 s[14:15], 0x90000
	s_nop 0
	v_pk_mul_f32 v[62:63], v[54:55], v[68:69] op_sel_hi:[1,0]
	v_pk_mul_f32 v[54:55], v[56:57], v[68:69] op_sel_hi:[1,0]
	v_pk_mul_f32 v[56:57], v[86:87], v[62:63]
	v_pk_mul_f32 v[62:63], v[50:51], v[68:69] op_sel_hi:[1,0]
	v_pk_mul_f32 v[50:51], v[52:53], v[68:69] op_sel_hi:[1,0]
	v_pk_mul_f32 v[54:55], v[88:89], v[54:55]
	v_pk_mul_f32 v[50:51], v[84:85], v[50:51]
	v_pk_mul_f32 v[52:53], v[82:83], v[62:63]
	v_cvt_pk_bf16_f32 v62, v56, v57
	v_cvt_pk_bf16_f32 v63, v54, v55
	v_cvt_pk_bf16_f32 v65, v50, v51
	s_nop 0
	v_cvt_pk_bf16_f32 v64, v52, v53
	v_subrev_u32_e32 v250, s82, v70
	v_add_u32_e32 v250, 0x40, v250
	ds_bpermute_b32 v242, v252, v62
	ds_bpermute_b32 v246, v253, v62
	ds_bpermute_b32 v243, v252, v63
	ds_bpermute_b32 v247, v253, v63
	ds_bpermute_b32 v244, v252, v64
	ds_bpermute_b32 v248, v253, v64
	ds_bpermute_b32 v245, v252, v65
	ds_bpermute_b32 v249, v253, v65
	ds_bpermute_b32 v251, v253, v250
	ds_bpermute_b32 v250, v252, v250
	s_waitcnt lgkmcnt(0)
	v_cndmask_b32_e64 v232, v232, v242, s[100:101]
	v_cndmask_b32_e64 v233, v233, v243, s[100:101]
	v_cndmask_b32_e64 v234, v234, v244, s[100:101]
	v_cndmask_b32_e64 v235, v235, v245, s[100:101]
	v_cndmask_b32_e64 v236, v236, v246, s[100:101]
	v_cndmask_b32_e64 v237, v237, v247, s[100:101]
	v_cndmask_b32_e64 v238, v238, v248, s[100:101]
	v_cndmask_b32_e64 v239, v239, v249, s[100:101]
	v_cndmask_b32_e64 v240, v240, v250, s[100:101]
	v_cndmask_b32_e64 v241, v241, v251, s[100:101]
	global_store_dwordx4 v240, v[232:235], s[82:83]
	global_store_dwordx4 v241, v[236:239], s[82:83]
	ds_read_b32 v62, v203
	ds_read_b32 v63, v204
	v_lshl_add_u64 v[64:65], v[66:67], 0, s[14:15]
	s_mov_b32 s14, 0x90000
	s_waitcnt lgkmcnt(0)
	v_add_f32_e32 v62, v62, v63
	v_fmamk_f32 v62, v62, 0x3c000000, v185
	v_rsq_f32_e32 v62, v62
	s_nop 0
	v_mul_f32_e32 v62, v69, v62
	v_pk_mul_f32 v[48:49], v[48:49], v[62:63] op_sel_hi:[1,0]
	v_pk_mul_f32 v[46:47], v[46:47], v[62:63] op_sel_hi:[1,0]
	v_pk_mul_f32 v[68:69], v[92:93], v[48:49]
	v_pk_mul_f32 v[70:71], v[90:91], v[46:47]
	v_pk_fma_f32 v[74:75], v[90:91], v[46:47], v[76:77]
	v_cvt_pk_bf16_f32 v47, v68, v69
	v_add_co_u32_e32 v68, vcc, s14, v66
	v_pk_mul_f32 v[72:73], v[42:43], v[62:63] op_sel_hi:[1,0]
	v_pk_mul_f32 v[42:43], v[44:45], v[62:63] op_sel_hi:[1,0]
	v_cvt_pk_bf16_f32 v46, v70, v71
	v_addc_co_u32_e32 v69, vcc, 0, v67, vcc
	v_pk_mul_f32 v[42:43], v[96:97], v[42:43]
	v_pk_mul_f32 v[44:45], v[94:95], v[72:73]
	v_pk_fma_f32 v[72:73], v[92:93], v[48:49], v[78:79]
	v_cvt_pk_bf16_f32 v48, v44, v45
	v_cvt_pk_bf16_f32 v49, v42, v43
	v_subrev_u32_e32 v240, s82, v68
	ds_bpermute_b32 v232, v252, v46
	ds_bpermute_b32 v236, v253, v46
	ds_bpermute_b32 v233, v252, v47
	ds_bpermute_b32 v237, v253, v47
	ds_bpermute_b32 v234, v252, v48
	ds_bpermute_b32 v238, v253, v48
	ds_bpermute_b32 v235, v252, v49
	ds_bpermute_b32 v239, v253, v49
	ds_bpermute_b32 v241, v253, v240
	ds_bpermute_b32 v240, v252, v240
	s_mov_b64 s[14:15], 0xa0000
	s_nop 0
	v_pk_mul_f32 v[46:47], v[38:39], v[62:63] op_sel_hi:[1,0]
	v_pk_mul_f32 v[38:39], v[40:41], v[62:63] op_sel_hi:[1,0]
	v_pk_mul_f32 v[40:41], v[86:87], v[46:47]
	v_pk_mul_f32 v[46:47], v[34:35], v[62:63] op_sel_hi:[1,0]
	v_pk_mul_f32 v[34:35], v[36:37], v[62:63] op_sel_hi:[1,0]
	v_pk_mul_f32 v[38:39], v[88:89], v[38:39]
	v_pk_mul_f32 v[34:35], v[84:85], v[34:35]
	v_pk_mul_f32 v[36:37], v[82:83], v[46:47]
	v_cvt_pk_bf16_f32 v46, v40, v41
	v_cvt_pk_bf16_f32 v47, v38, v39
	v_cvt_pk_bf16_f32 v49, v34, v35
	s_nop 0
	v_cvt_pk_bf16_f32 v48, v36, v37
	v_subrev_u32_e32 v250, s82, v64
	v_add_u32_e32 v250, 0x40, v250
	ds_bpermute_b32 v242, v252, v46
	ds_bpermute_b32 v246, v253, v46
	ds_bpermute_b32 v243, v252, v47
	ds_bpermute_b32 v247, v253, v47
	ds_bpermute_b32 v244, v252, v48
	ds_bpermute_b32 v248, v253, v48
	ds_bpermute_b32 v245, v252, v49
	ds_bpermute_b32 v249, v253, v49
	ds_bpermute_b32 v251, v253, v250
	ds_bpermute_b32 v250, v252, v250
	s_waitcnt lgkmcnt(0)
	v_cndmask_b32_e64 v232, v232, v242, s[100:101]
	v_cndmask_b32_e64 v233, v233, v243, s[100:101]
	v_cndmask_b32_e64 v234, v234, v244, s[100:101]
	v_cndmask_b32_e64 v235, v235, v245, s[100:101]
	v_cndmask_b32_e64 v236, v236, v246, s[100:101]
	v_cndmask_b32_e64 v237, v237, v247, s[100:101]
	v_cndmask_b32_e64 v238, v238, v248, s[100:101]
	v_cndmask_b32_e64 v239, v239, v249, s[100:101]
	v_cndmask_b32_e64 v240, v240, v250, s[100:101]
	v_cndmask_b32_e64 v241, v241, v251, s[100:101]
	global_store_dwordx4 v240, v[232:235], s[82:83]
	global_store_dwordx4 v241, v[236:239], s[82:83]
	ds_read_b32 v46, v205
	ds_read_b32 v47, v206
	s_waitcnt lgkmcnt(0)
	v_add_f32_e32 v46, v46, v47
	v_fmamk_f32 v46, v46, 0x3c000000, v185
	v_rsq_f32_e32 v48, v46
	ds_read2_b32 v[46:47], v213 offset0:160 offset1:176
	s_waitcnt lgkmcnt(0)
	v_mul_f32_e32 v46, v46, v48
	v_lshl_add_u64 v[48:49], v[66:67], 0, s[14:15]
	v_pk_mul_f32 v[30:31], v[30:31], v[46:47] op_sel_hi:[1,0]
	v_pk_mul_f32 v[68:69], v[26:27], v[46:47] op_sel_hi:[1,0]
	s_mov_b32 s14, 0xa0000
	v_pk_mul_f32 v[32:33], v[32:33], v[46:47] op_sel_hi:[1,0]
	v_pk_mul_f32 v[62:63], v[90:91], v[30:31]
	v_pk_mul_f32 v[26:27], v[28:29], v[46:47] op_sel_hi:[1,0]
	v_pk_mul_f32 v[28:29], v[94:95], v[68:69]
	v_add_co_u32_e32 v68, vcc, s14, v66
	v_pk_mul_f32 v[64:65], v[92:93], v[32:33]
	v_cvt_pk_bf16_f32 v62, v62, v63
	s_nop 0
	v_addc_co_u32_e32 v69, vcc, 0, v67, vcc
	v_cvt_pk_bf16_f32 v63, v64, v65
	v_pk_mul_f32 v[26:27], v[96:97], v[26:27]
	v_cvt_pk_bf16_f32 v64, v28, v29
	s_mov_b64 s[14:15], 0xb0000
	v_cvt_pk_bf16_f32 v65, v26, v27
	v_subrev_u32_e32 v240, s82, v68
	ds_bpermute_b32 v232, v252, v62
	ds_bpermute_b32 v236, v253, v62
	ds_bpermute_b32 v233, v252, v63
	ds_bpermute_b32 v237, v253, v63
	ds_bpermute_b32 v234, v252, v64
	ds_bpermute_b32 v238, v253, v64
	ds_bpermute_b32 v235, v252, v65
	ds_bpermute_b32 v239, v253, v65
	ds_bpermute_b32 v241, v253, v240
	ds_bpermute_b32 v240, v252, v240
	v_pk_fma_f32 v[30:31], v[90:91], v[30:31], v[74:75]
	v_pk_fma_f32 v[32:33], v[92:93], v[32:33], v[72:73]
	v_pk_mul_f32 v[62:63], v[22:23], v[46:47] op_sel_hi:[1,0]
	v_pk_mul_f32 v[22:23], v[24:25], v[46:47] op_sel_hi:[1,0]
	v_pk_mul_f32 v[24:25], v[86:87], v[62:63]
	v_pk_mul_f32 v[62:63], v[18:19], v[46:47] op_sel_hi:[1,0]
	v_pk_mul_f32 v[18:19], v[20:21], v[46:47] op_sel_hi:[1,0]
	v_pk_mul_f32 v[22:23], v[88:89], v[22:23]
	v_pk_mul_f32 v[18:19], v[84:85], v[18:19]
	v_pk_mul_f32 v[20:21], v[82:83], v[62:63]
	v_cvt_pk_bf16_f32 v62, v24, v25
	v_cvt_pk_bf16_f32 v63, v22, v23
	v_cvt_pk_bf16_f32 v65, v18, v19
	s_nop 0
	v_cvt_pk_bf16_f32 v64, v20, v21
	v_subrev_u32_e32 v250, s82, v48
	v_add_u32_e32 v250, 0x40, v250
	ds_bpermute_b32 v242, v252, v62
	ds_bpermute_b32 v246, v253, v62
	ds_bpermute_b32 v243, v252, v63
	ds_bpermute_b32 v247, v253, v63
	ds_bpermute_b32 v244, v252, v64
	ds_bpermute_b32 v248, v253, v64
	ds_bpermute_b32 v245, v252, v65
	ds_bpermute_b32 v249, v253, v65
	ds_bpermute_b32 v251, v253, v250
	ds_bpermute_b32 v250, v252, v250
	s_waitcnt lgkmcnt(0)
	v_cndmask_b32_e64 v232, v232, v242, s[100:101]
	v_cndmask_b32_e64 v233, v233, v243, s[100:101]
	v_cndmask_b32_e64 v234, v234, v244, s[100:101]
	v_cndmask_b32_e64 v235, v235, v245, s[100:101]
	v_cndmask_b32_e64 v236, v236, v246, s[100:101]
	v_cndmask_b32_e64 v237, v237, v247, s[100:101]
	v_cndmask_b32_e64 v238, v238, v248, s[100:101]
	v_cndmask_b32_e64 v239, v239, v249, s[100:101]
	v_cndmask_b32_e64 v240, v240, v250, s[100:101]
	v_cndmask_b32_e64 v241, v241, v251, s[100:101]
	global_store_dwordx4 v240, v[232:235], s[82:83]
	global_store_dwordx4 v241, v[236:239], s[82:83]
	ds_read_b32 v46, v207
	ds_read_b32 v48, v208
	s_waitcnt lgkmcnt(0)
	v_add_f32_e32 v46, v46, v48
	v_fmamk_f32 v46, v46, 0x3c000000, v185
	v_rsq_f32_e32 v46, v46
	v_lshl_add_u64 v[48:49], v[66:67], 0, s[14:15]
	s_mov_b32 s14, 0xb0000
	v_mul_f32_e32 v46, v47, v46
	v_pk_mul_f32 v[10:11], v[10:11], v[46:47] op_sel_hi:[1,0]
	v_pk_mul_f32 v[62:63], v[14:15], v[46:47] op_sel_hi:[1,0]
	v_pk_mul_f32 v[16:17], v[16:17], v[46:47] op_sel_hi:[1,0]
	v_pk_mul_f32 v[12:13], v[12:13], v[46:47] op_sel_hi:[1,0]
	v_pk_mul_f32 v[14:15], v[94:95], v[10:11]
	v_add_co_u32_e32 v10, vcc, s14, v66
	v_pk_mul_f32 v[64:65], v[92:93], v[16:17]
	v_pk_mul_f32 v[68:69], v[90:91], v[62:63]
	v_pk_mul_f32 v[12:13], v[96:97], v[12:13]
	v_pk_fma_f32 v[70:71], v[92:93], v[16:17], v[32:33]
	v_pk_fma_f32 v[16:17], v[90:91], v[62:63], v[30:31]
	v_cvt_pk_bf16_f32 v30, v68, v69
	v_cvt_pk_bf16_f32 v31, v64, v65
	v_cvt_pk_bf16_f32 v32, v14, v15
	v_cvt_pk_bf16_f32 v33, v12, v13
	v_addc_co_u32_e32 v11, vcc, 0, v67, vcc
	v_pk_mul_f32 v[6:7], v[6:7], v[46:47] op_sel_hi:[1,0]
	v_pk_mul_f32 v[8:9], v[8:9], v[46:47] op_sel_hi:[1,0]
	v_pk_mul_f32 v[2:3], v[2:3], v[46:47] op_sel_hi:[1,0]
	v_pk_mul_f32 v[4:5], v[4:5], v[46:47] op_sel_hi:[1,0]
	v_subrev_u32_e32 v240, s82, v10
	ds_bpermute_b32 v232, v252, v30
	ds_bpermute_b32 v236, v253, v30
	ds_bpermute_b32 v233, v252, v31
	ds_bpermute_b32 v237, v253, v31
	ds_bpermute_b32 v234, v252, v32
	ds_bpermute_b32 v238, v253, v32
	ds_bpermute_b32 v235, v252, v33
	ds_bpermute_b32 v239, v253, v33
	ds_bpermute_b32 v241, v253, v240
	ds_bpermute_b32 v240, v252, v240
	v_pk_mul_f32 v[8:9], v[88:89], v[8:9]
	v_pk_mul_f32 v[10:11], v[86:87], v[6:7]
	v_pk_mul_f32 v[4:5], v[84:85], v[4:5]
	v_pk_mul_f32 v[6:7], v[82:83], v[2:3]
	v_cvt_pk_bf16_f32 v30, v10, v11
	v_cvt_pk_bf16_f32 v31, v8, v9
	v_cvt_pk_bf16_f32 v33, v4, v5
	s_add_i32 s14, s28, 2
	v_cvt_pk_bf16_f32 v32, v6, v7
	v_subrev_u32_e32 v250, s82, v48
	v_add_u32_e32 v250, 0x40, v250
	ds_bpermute_b32 v242, v252, v30
	ds_bpermute_b32 v246, v253, v30
	ds_bpermute_b32 v243, v252, v31
	ds_bpermute_b32 v247, v253, v31
	ds_bpermute_b32 v244, v252, v32
	ds_bpermute_b32 v248, v253, v32
	ds_bpermute_b32 v245, v252, v33
	ds_bpermute_b32 v249, v253, v33
	ds_bpermute_b32 v251, v253, v250
	ds_bpermute_b32 v250, v252, v250
	s_waitcnt lgkmcnt(0)
	v_cndmask_b32_e64 v232, v232, v242, s[100:101]
	v_cndmask_b32_e64 v233, v233, v243, s[100:101]
	v_cndmask_b32_e64 v234, v234, v244, s[100:101]
	v_cndmask_b32_e64 v235, v235, v245, s[100:101]
	v_cndmask_b32_e64 v236, v236, v246, s[100:101]
	v_cndmask_b32_e64 v237, v237, v247, s[100:101]
	v_cndmask_b32_e64 v238, v238, v248, s[100:101]
	v_cndmask_b32_e64 v239, v239, v249, s[100:101]
	v_cndmask_b32_e64 v240, v240, v250, s[100:101]
	v_cndmask_b32_e64 v241, v241, v251, s[100:101]
	global_store_dwordx4 v240, v[232:235], s[82:83]
	global_store_dwordx4 v241, v[236:239], s[82:83]
	ds_swizzle_b32 v30, v16 offset:swizzle(SWAP,1)
	ds_swizzle_b32 v31, v17 offset:swizzle(SWAP,1)
	ds_swizzle_b32 v32, v70 offset:swizzle(SWAP,1)
	ds_swizzle_b32 v33, v71 offset:swizzle(SWAP,1)
	s_ashr_i32 s15, s14, 31
	s_lshl_b64 s[14:15], s[14:15], 9
	s_waitcnt lgkmcnt(2)
	v_pk_add_f32 v[16:17], v[16:17], v[30:31]
	ds_swizzle_b32 v30, v16 offset:swizzle(SWAP,2)
	s_waitcnt lgkmcnt(1)
	v_pk_add_f32 v[32:33], v[70:71], v[32:33]
	ds_swizzle_b32 v31, v17 offset:swizzle(SWAP,2)
	ds_swizzle_b32 v46, v32 offset:swizzle(SWAP,2)
	ds_swizzle_b32 v47, v33 offset:swizzle(SWAP,2)
	v_lshl_add_u64 v[2:3], v[166:167], 0, s[14:15]
	s_waitcnt lgkmcnt(2)
	v_pk_add_f32 v[16:17], v[16:17], v[30:31]
	ds_swizzle_b32 v30, v16 offset:swizzle(SWAP,4)
	s_waitcnt lgkmcnt(1)
	v_pk_add_f32 v[32:33], v[32:33], v[46:47]
	ds_swizzle_b32 v31, v17 offset:swizzle(SWAP,4)
	ds_swizzle_b32 v46, v32 offset:swizzle(SWAP,4)
	ds_swizzle_b32 v47, v33 offset:swizzle(SWAP,4)
	s_waitcnt lgkmcnt(2)
	v_pk_add_f32 v[16:17], v[16:17], v[30:31]
	ds_swizzle_b32 v30, v16 offset:swizzle(SWAP,8)
	s_waitcnt lgkmcnt(1)
	v_pk_add_f32 v[32:33], v[32:33], v[46:47]
	ds_swizzle_b32 v31, v17 offset:swizzle(SWAP,8)
	ds_swizzle_b32 v46, v32 offset:swizzle(SWAP,8)
	ds_swizzle_b32 v47, v33 offset:swizzle(SWAP,8)
	s_and_saveexec_b64 s[28:29], s[40:41]
	s_cbranch_execz .LBB0_204
	s_waitcnt lgkmcnt(0)
	v_pk_add_f32 v[32:33], v[32:33], v[46:47]
	v_pk_add_f32 v[30:31], v[16:17], v[30:31]
	global_store_dwordx4 v[2:3], v[30:33], off

.LBB0_349:
	v_mbcnt_lo_u32_b32 v231, -1, 0
	v_mbcnt_hi_u32_b32 v231, -1, v231
	v_and_b32_e32 v253, 3, v231
	v_lshrrev_b32_e32 v252, 3, v231
	v_lshl_add_u32 v252, v253, 4, v252
	v_lshlrev_b32_e32 v252, 2, v252
	v_lshrrev_b32_e32 v231, 2, v231
	v_lshl_add_u32 v231, v253, 4, v231
	v_lshlrev_b32_e32 v231, 2, v231
	v_add_u32_e32 v253, 32, v252
	s_mov_b32 s100, 0xf0f0f0f0
	s_mov_b32 s101, 0xf0f0f0f0
	s_lshl_b32 s14, s14, 10
	v_add_u32_e32 v176, s14, v174
	ds_read_b32 v154, v176
	s_lshl_b32 s15, s28, 8
	s_ashr_i32 s58, s28, 3
	s_and_b32 s14, s15, 0x700
	v_readlane_b32 s70, v255, 13
	v_readlane_b32 s74, v255, 15
	v_lshl_add_u32 v152, s40, 8, v1
	v_or_b32_e32 v177, s14, v173
	s_cmp_lg_u32 s58, 1
	s_mov_b64 s[40:41], -1
	v_readlane_b32 s71, v255, 14
	v_readlane_b32 s75, v255, 16
	s_cbranch_scc0 .LBB0_384
	s_cmp_lt_u32 s28, 8
	s_cselect_b64 s[56:57], -1, 0
	s_cmp_gt_u32 s28, 7
	s_waitcnt lgkmcnt(0)
	v_pk_mul_f32 v[134:135], v[130:131], v[154:155] op_sel_hi:[1,0]
	v_pk_mul_f32 v[166:167], v[128:129], v[154:155] op_sel_hi:[1,0]
	v_pk_mul_f32 v[138:139], v[126:127], v[154:155] op_sel_hi:[1,0]
	v_pk_mul_f32 v[168:169], v[124:125], v[154:155] op_sel_hi:[1,0]
	s_cbranch_scc1 .LBB0_352
	v_max_f32_e32 v114, v166, v166
	v_max_f32_e32 v132, 0xc2a00000, v114
	v_max_f32_e32 v114, v168, v168
	v_max_f32_e32 v136, 0xc2a00000, v114
	v_mul_f32_e32 v114, 0xbfb8aa3b, v132
	v_exp_f32_e32 v114, v114
	v_mul_f32_e32 v133, 0xbfb8aa3b, v136
	v_exp_f32_e32 v133, v133
	v_max_f32_e32 v137, v169, v169
	v_add_f32_e32 v114, 1.0, v114
	v_rcp_f32_e32 v158, v114
	v_add_f32_e32 v114, 1.0, v133
	v_max_f32_e32 v133, v167, v167
	v_max_f32_e32 v133, 0xc2a00000, v133
	v_max_f32_e32 v137, 0xc2a00000, v137
	v_mul_f32_e32 v153, 0xbfb8aa3b, v133
	v_exp_f32_e32 v153, v153
	v_mul_f32_e32 v155, 0xbfb8aa3b, v137
	v_exp_f32_e32 v155, v155
	v_max_f32_e32 v134, v134, v134
	v_max_f32_e32 v134, 0xc2a00000, v134
	v_max_f32_e32 v138, v138, v138
	v_rcp_f32_e32 v160, v114
	v_add_f32_e32 v114, 1.0, v153
	v_max_f32_e32 v138, 0xc2a00000, v138
	v_mul_f32_e32 v153, 0xbfb8aa3b, v134
	v_rcp_f32_e32 v159, v114
	v_add_f32_e32 v114, 1.0, v155
	v_exp_f32_e32 v153, v153
	v_mul_f32_e32 v155, 0xbfb8aa3b, v138
	v_exp_f32_e32 v155, v155
	v_max_f32_e32 v135, v135, v135
	v_max_f32_e32 v135, 0xc2a00000, v135
	v_max_f32_e32 v139, v139, v139
	v_rcp_f32_e32 v161, v114
	v_add_f32_e32 v114, 1.0, v153
	v_max_f32_e32 v139, 0xc2a00000, v139
	v_mul_f32_e32 v153, 0xbfb8aa3b, v135
	v_rcp_f32_e32 v168, v114
	v_add_f32_e32 v114, 1.0, v155
	v_exp_f32_e32 v153, v153
	v_mul_f32_e32 v155, 0xbfb8aa3b, v139
	v_exp_f32_e32 v155, v155
	v_rcp_f32_e32 v170, v114
	v_add_f32_e32 v114, 1.0, v153
	v_rcp_f32_e32 v169, v114
	v_add_f32_e32 v114, 1.0, v155
	v_rcp_f32_e32 v171, v114
	v_pk_mul_f32 v[166:167], v[132:133], v[158:159]
	v_pk_mul_f32 v[134:135], v[134:135], v[168:169]
	v_pk_mul_f32 v[168:169], v[136:137], v[160:161]
	v_pk_mul_f32 v[138:139], v[138:139], v[170:171]
.LBB0_352:
	s_ashr_i32 s59, s58, 31
	s_lshl_b64 s[14:15], s[58:59], 25
	s_add_u32 s14, s37, s14
	s_addc_u32 s15, s64, s15
	v_lshlrev_b32_e32 v114, 1, v177
	v_ashrrev_i32_e32 v153, 31, v152
	v_lshl_add_u64 v[132:133], s[14:15], 0, v[114:115]
	v_lshlrev_b64 v[136:137], 12, v[152:153]
	v_mov_b32_e32 v155, v154
	v_lshl_add_u64 v[136:137], v[132:133], 0, v[136:137]
	v_cvt_pk_bf16_f32 v166, v166, v167
	v_cvt_pk_bf16_f32 v167, v134, v135
	v_cvt_pk_bf16_f32 v168, v168, v169
	v_cvt_pk_bf16_f32 v169, v138, v139
	v_mov_b32_e32 v158, v154
	v_mov_b32_e32 v159, v154
	v_cndmask_b32_e64 v114, 0, 1, s[56:57]
	ds_bpermute_b32 v242, v231, v166
	ds_bpermute_b32 v243, v231, v167
	ds_bpermute_b32 v244, v231, v168
	ds_bpermute_b32 v245, v231, v169
	ds_bpermute_b32 v246, v231, v136
	s_waitcnt lgkmcnt(0)
	v_subrev_u32_e32 v246, s82, v246
	global_store_dwordx4 v246, v[242:245], s[82:83]
	v_pk_mul_f32 v[138:139], v[122:123], v[158:159]
	v_pk_mul_f32 v[134:135], v[120:121], v[154:155]
	v_pk_mul_f32 v[166:167], v[118:119], v[158:159]
	v_cmp_ne_u32_e64 s[40:41], 1, v114
	s_andn2_b64 vcc, exec, s[56:57]
	v_pk_mul_f32 v[168:169], v[116:117], v[154:155]
	s_cbranch_vccnz .LBB0_354
	v_max_f32_e32 v114, v134, v134
	v_max_f32_e32 v134, 0xc2a00000, v114
	v_max_f32_e32 v114, v168, v168
	v_max_f32_e32 v158, 0xc2a00000, v114
	v_mul_f32_e32 v114, 0xbfb8aa3b, v134
	v_exp_f32_e32 v114, v114
	v_mul_f32_e32 v155, 0xbfb8aa3b, v158
	v_exp_f32_e32 v155, v155
	v_max_f32_e32 v135, v135, v135
	v_add_f32_e32 v114, 1.0, v114
	v_rcp_f32_e32 v160, v114
	v_add_f32_e32 v114, 1.0, v155
	v_max_f32_e32 v135, 0xc2a00000, v135
	v_max_f32_e32 v155, v169, v169
	v_max_f32_e32 v159, 0xc2a00000, v155
	v_mul_f32_e32 v155, 0xbfb8aa3b, v135
	v_exp_f32_e32 v155, v155
	v_mul_f32_e32 v161, 0xbfb8aa3b, v159
	v_exp_f32_e32 v169, v161
	v_max_f32_e32 v138, v138, v138
	v_rcp_f32_e32 v168, v114
	v_add_f32_e32 v114, 1.0, v155
	v_max_f32_e32 v138, 0xc2a00000, v138
	v_max_f32_e32 v155, v166, v166
	v_max_f32_e32 v166, 0xc2a00000, v155
	v_mul_f32_e32 v155, 0xbfb8aa3b, v138
	v_exp_f32_e32 v155, v155
	v_rcp_f32_e32 v161, v114
	v_add_f32_e32 v114, 1.0, v169
	v_mul_f32_e32 v169, 0xbfb8aa3b, v166
	v_exp_f32_e32 v171, v169
	v_max_f32_e32 v139, v139, v139
	v_rcp_f32_e32 v169, v114
	v_add_f32_e32 v114, 1.0, v155
	v_max_f32_e32 v139, 0xc2a00000, v139
	v_max_f32_e32 v155, v167, v167
	v_max_f32_e32 v167, 0xc2a00000, v155
	v_mul_f32_e32 v155, 0xbfb8aa3b, v139
	v_rcp_f32_e32 v170, v114
	v_add_f32_e32 v114, 1.0, v171
	v_exp_f32_e32 v155, v155
	v_mul_f32_e32 v171, 0xbfb8aa3b, v167
	v_exp_f32_e32 v179, v171
	v_rcp_f32_e32 v178, v114
	v_add_f32_e32 v114, 1.0, v155
	v_rcp_f32_e32 v171, v114
	v_add_f32_e32 v114, 1.0, v179
	v_rcp_f32_e32 v179, v114
	v_pk_mul_f32 v[134:135], v[134:135], v[160:161]
	v_pk_mul_f32 v[138:139], v[138:139], v[170:171]
	v_pk_mul_f32 v[168:169], v[158:159], v[168:169]
	v_pk_mul_f32 v[166:167], v[166:167], v[178:179]
.LBB0_354:
	v_cvt_pk_bf16_f32 v178, v134, v135
	ds_read_b32 v134, v176 offset:64
	v_cvt_pk_bf16_f32 v179, v138, v139
	v_cvt_pk_bf16_f32 v180, v168, v169
	v_cvt_pk_bf16_f32 v181, v166, v167
	s_and_b64 vcc, exec, s[40:41]
	s_waitcnt lgkmcnt(0)
	v_pk_mul_f32 v[138:139], v[112:113], v[134:135] op_sel_hi:[1,0]
	v_pk_mul_f32 v[168:169], v[110:111], v[134:135] op_sel_hi:[1,0]
	v_pk_mul_f32 v[166:167], v[108:109], v[134:135] op_sel_hi:[1,0]
	v_pk_mul_f32 v[170:171], v[106:107], v[134:135] op_sel_hi:[1,0]
	ds_bpermute_b32 v242, v231, v178
	ds_bpermute_b32 v243, v231, v179
	ds_bpermute_b32 v244, v231, v180
	ds_bpermute_b32 v245, v231, v181
	ds_bpermute_b32 v246, v231, v136
	s_waitcnt lgkmcnt(0)
	v_subrev_u32_e32 v246, s82, v246
	global_store_dwordx4 v246, v[242:245], s[82:83] offset:64
	s_cbranch_vccnz .LBB0_356
	v_max_f32_e32 v114, v168, v168
	v_max_f32_e32 v136, 0xc2a00000, v114
	v_max_f32_e32 v114, v170, v170
	v_max_f32_e32 v158, 0xc2a00000, v114
	v_mul_f32_e32 v114, 0xbfb8aa3b, v136
	v_exp_f32_e32 v114, v114
	v_mul_f32_e32 v135, 0xbfb8aa3b, v158
	v_exp_f32_e32 v135, v135
	v_add_f32_e32 v114, 1.0, v114
	v_rcp_f32_e32 v160, v114
	v_add_f32_e32 v114, 1.0, v135
	v_max_f32_e32 v135, v169, v169
	v_max_f32_e32 v137, 0xc2a00000, v135
	v_max_f32_e32 v135, v171, v171
	v_max_f32_e32 v159, 0xc2a00000, v135
	v_mul_f32_e32 v135, 0xbfb8aa3b, v137
	v_exp_f32_e32 v135, v135
	v_mul_f32_e32 v155, 0xbfb8aa3b, v159
	v_rcp_f32_e32 v170, v114
	v_exp_f32_e32 v155, v155
	v_add_f32_e32 v114, 1.0, v135
	v_max_f32_e32 v135, v138, v138
	v_max_f32_e32 v138, 0xc2a00000, v135
	v_max_f32_e32 v135, v166, v166
	v_max_f32_e32 v166, 0xc2a00000, v135
	v_mul_f32_e32 v135, 0xbfb8aa3b, v138
	v_exp_f32_e32 v135, v135
	v_rcp_f32_e32 v161, v114
	v_add_f32_e32 v114, 1.0, v155
	v_mul_f32_e32 v155, 0xbfb8aa3b, v166
	v_exp_f32_e32 v155, v155
	v_rcp_f32_e32 v171, v114
	v_add_f32_e32 v114, 1.0, v135
	v_max_f32_e32 v135, v139, v139
	v_max_f32_e32 v139, 0xc2a00000, v135
	v_max_f32_e32 v135, v167, v167
	v_max_f32_e32 v167, 0xc2a00000, v135
	v_mul_f32_e32 v135, 0xbfb8aa3b, v139
	v_rcp_f32_e32 v178, v114
	v_add_f32_e32 v114, 1.0, v155
	v_exp_f32_e32 v135, v135
	v_mul_f32_e32 v155, 0xbfb8aa3b, v167
	v_exp_f32_e32 v155, v155
	v_rcp_f32_e32 v180, v114
	v_add_f32_e32 v114, 1.0, v135
	v_rcp_f32_e32 v179, v114
	v_add_f32_e32 v114, 1.0, v155
	v_rcp_f32_e32 v181, v114
	v_pk_mul_f32 v[168:169], v[136:137], v[160:161]
	v_pk_mul_f32 v[138:139], v[138:139], v[178:179]
	v_pk_mul_f32 v[170:171], v[158:159], v[170:171]
	v_pk_mul_f32 v[166:167], v[166:167], v[180:181]
.LBB0_356:
	v_or_b32_e32 v136, 16, v152
	v_ashrrev_i32_e32 v137, 31, v136
	v_lshlrev_b64 v[136:137], 12, v[136:137]
	v_mov_b32_e32 v135, v134
	v_lshl_add_u64 v[136:137], v[132:133], 0, v[136:137]
	v_cvt_pk_bf16_f32 v168, v168, v169
	v_cvt_pk_bf16_f32 v169, v138, v139
	v_cvt_pk_bf16_f32 v170, v170, v171
	v_cvt_pk_bf16_f32 v171, v166, v167
	v_mov_b32_e32 v158, v134
	v_mov_b32_e32 v159, v134
	ds_bpermute_b32 v242, v231, v168
	ds_bpermute_b32 v243, v231, v169
	ds_bpermute_b32 v244, v231, v170
	ds_bpermute_b32 v245, v231, v171
	ds_bpermute_b32 v246, v231, v136
	s_waitcnt lgkmcnt(0)
	v_subrev_u32_e32 v246, s82, v246
	global_store_dwordx4 v246, v[242:245], s[82:83]
	v_pk_mul_f32 v[138:139], v[104:105], v[158:159]
	v_pk_mul_f32 v[166:167], v[100:101], v[158:159]
	v_pk_mul_f32 v[168:169], v[102:103], v[134:135]
	s_and_b64 vcc, exec, s[40:41]
	v_pk_mul_f32 v[170:171], v[98:99], v[134:135]
	s_cbranch_vccnz .LBB0_358
	v_max_f32_e32 v114, v168, v168
	v_max_f32_e32 v134, 0xc2a00000, v114
	v_max_f32_e32 v114, v170, v170
	v_max_f32_e32 v158, 0xc2a00000, v114
	v_mul_f32_e32 v114, 0xbfb8aa3b, v134
	v_exp_f32_e32 v114, v114
	v_mul_f32_e32 v135, 0xbfb8aa3b, v158
	v_exp_f32_e32 v135, v135
	v_max_f32_e32 v155, v171, v171
	v_add_f32_e32 v114, 1.0, v114
	v_rcp_f32_e32 v160, v114
	v_add_f32_e32 v114, 1.0, v135
	v_max_f32_e32 v135, v169, v169
	v_max_f32_e32 v135, 0xc2a00000, v135
	v_max_f32_e32 v159, 0xc2a00000, v155
	v_mul_f32_e32 v155, 0xbfb8aa3b, v135
	v_exp_f32_e32 v155, v155
	v_mul_f32_e32 v161, 0xbfb8aa3b, v159
	v_exp_f32_e32 v168, v161
	v_max_f32_e32 v138, v138, v138
	v_rcp_f32_e32 v170, v114
	v_add_f32_e32 v114, 1.0, v155
	v_max_f32_e32 v138, 0xc2a00000, v138
	v_max_f32_e32 v155, v166, v166
	v_max_f32_e32 v166, 0xc2a00000, v155
	v_mul_f32_e32 v155, 0xbfb8aa3b, v138
	v_exp_f32_e32 v155, v155
	v_rcp_f32_e32 v161, v114
	v_add_f32_e32 v114, 1.0, v168
	v_mul_f32_e32 v168, 0xbfb8aa3b, v166
	v_exp_f32_e32 v168, v168
	v_max_f32_e32 v139, v139, v139
	v_rcp_f32_e32 v171, v114
	v_add_f32_e32 v114, 1.0, v155
	v_max_f32_e32 v139, 0xc2a00000, v139
	v_max_f32_e32 v155, v167, v167
	v_max_f32_e32 v167, 0xc2a00000, v155
	v_mul_f32_e32 v155, 0xbfb8aa3b, v139
	v_rcp_f32_e32 v178, v114
	v_add_f32_e32 v114, 1.0, v168
	v_exp_f32_e32 v155, v155
	v_mul_f32_e32 v168, 0xbfb8aa3b, v167
	v_exp_f32_e32 v168, v168
	v_rcp_f32_e32 v180, v114
	v_add_f32_e32 v114, 1.0, v155
	v_rcp_f32_e32 v179, v114
	v_add_f32_e32 v114, 1.0, v168
	v_rcp_f32_e32 v181, v114
	v_pk_mul_f32 v[168:169], v[134:135], v[160:161]
	v_pk_mul_f32 v[138:139], v[138:139], v[178:179]
	v_pk_mul_f32 v[170:171], v[158:159], v[170:171]
	v_pk_mul_f32 v[166:167], v[166:167], v[180:181]
.LBB0_358:
	ds_read_b32 v134, v176 offset:128
	v_cvt_pk_bf16_f32 v168, v168, v169
	v_cvt_pk_bf16_f32 v169, v138, v139
	v_cvt_pk_bf16_f32 v170, v170, v171
	v_cvt_pk_bf16_f32 v171, v166, v167
	ds_bpermute_b32 v242, v231, v168
	ds_bpermute_b32 v243, v231, v169
	ds_bpermute_b32 v244, v231, v170
	ds_bpermute_b32 v245, v231, v171
	ds_bpermute_b32 v246, v231, v136
	s_waitcnt lgkmcnt(0)
	v_subrev_u32_e32 v246, s82, v246
	global_store_dwordx4 v246, v[242:245], s[82:83] offset:64
	s_waitcnt lgkmcnt(0)
	v_pk_mul_f32 v[138:139], v[96:97], v[134:135] op_sel_hi:[1,0]
	v_pk_mul_f32 v[166:167], v[92:93], v[134:135] op_sel_hi:[1,0]
	v_pk_mul_f32 v[168:169], v[94:95], v[134:135] op_sel_hi:[1,0]
	s_and_b64 vcc, exec, s[40:41]
	v_pk_mul_f32 v[170:171], v[90:91], v[134:135] op_sel_hi:[1,0]
	s_cbranch_vccnz .LBB0_360
	v_max_f32_e32 v114, v168, v168
	v_max_f32_e32 v136, 0xc2a00000, v114
	v_max_f32_e32 v114, v170, v170
	v_max_f32_e32 v158, 0xc2a00000, v114
	v_mul_f32_e32 v114, 0xbfb8aa3b, v136
	v_exp_f32_e32 v114, v114
	v_mul_f32_e32 v135, 0xbfb8aa3b, v158
	v_exp_f32_e32 v135, v135
	v_add_f32_e32 v114, 1.0, v114
	v_rcp_f32_e32 v160, v114
	v_add_f32_e32 v114, 1.0, v135
	v_max_f32_e32 v135, v169, v169
	v_max_f32_e32 v137, 0xc2a00000, v135
	v_max_f32_e32 v135, v171, v171
	v_max_f32_e32 v159, 0xc2a00000, v135
	v_mul_f32_e32 v135, 0xbfb8aa3b, v137
	v_exp_f32_e32 v135, v135
	v_mul_f32_e32 v155, 0xbfb8aa3b, v159
	v_rcp_f32_e32 v170, v114
	v_exp_f32_e32 v155, v155
	v_add_f32_e32 v114, 1.0, v135
	v_max_f32_e32 v135, v138, v138
	v_max_f32_e32 v138, 0xc2a00000, v135
	v_max_f32_e32 v135, v166, v166
	v_max_f32_e32 v166, 0xc2a00000, v135
	v_mul_f32_e32 v135, 0xbfb8aa3b, v138
	v_exp_f32_e32 v135, v135
	v_rcp_f32_e32 v161, v114
	v_add_f32_e32 v114, 1.0, v155
	v_mul_f32_e32 v155, 0xbfb8aa3b, v166
	v_exp_f32_e32 v155, v155
	v_rcp_f32_e32 v171, v114
	v_add_f32_e32 v114, 1.0, v135
	v_max_f32_e32 v135, v139, v139
	v_max_f32_e32 v139, 0xc2a00000, v135
	v_max_f32_e32 v135, v167, v167
	v_max_f32_e32 v167, 0xc2a00000, v135
	v_mul_f32_e32 v135, 0xbfb8aa3b, v139
	v_rcp_f32_e32 v178, v114
	v_add_f32_e32 v114, 1.0, v155
	v_exp_f32_e32 v135, v135
	v_mul_f32_e32 v155, 0xbfb8aa3b, v167
	v_exp_f32_e32 v155, v155
	v_rcp_f32_e32 v180, v114
	v_add_f32_e32 v114, 1.0, v135
	v_rcp_f32_e32 v179, v114
	v_add_f32_e32 v114, 1.0, v155
	v_rcp_f32_e32 v181, v114
	v_pk_mul_f32 v[168:169], v[136:137], v[160:161]
	v_pk_mul_f32 v[138:139], v[138:139], v[178:179]
	v_pk_mul_f32 v[170:171], v[158:159], v[170:171]
	v_pk_mul_f32 v[166:167], v[166:167], v[180:181]
.LBB0_360:
	v_or_b32_e32 v136, 32, v152
	v_ashrrev_i32_e32 v137, 31, v136
	v_lshlrev_b64 v[136:137], 12, v[136:137]
	v_mov_b32_e32 v135, v134
	v_lshl_add_u64 v[136:137], v[132:133], 0, v[136:137]
	v_cvt_pk_bf16_f32 v168, v168, v169
	v_cvt_pk_bf16_f32 v169, v138, v139
	v_cvt_pk_bf16_f32 v170, v170, v171
	v_cvt_pk_bf16_f32 v171, v166, v167
	v_mov_b32_e32 v158, v134
	v_mov_b32_e32 v159, v134
	ds_bpermute_b32 v242, v231, v168
	ds_bpermute_b32 v243, v231, v169
	ds_bpermute_b32 v244, v231, v170
	ds_bpermute_b32 v245, v231, v171
	ds_bpermute_b32 v246, v231, v136
	s_waitcnt lgkmcnt(0)
	v_subrev_u32_e32 v246, s82, v246
	global_store_dwordx4 v246, v[242:245], s[82:83]
	v_pk_mul_f32 v[138:139], v[88:89], v[158:159]
	v_pk_mul_f32 v[166:167], v[84:85], v[158:159]
	v_pk_mul_f32 v[168:169], v[86:87], v[134:135]
	s_and_b64 vcc, exec, s[40:41]
	v_pk_mul_f32 v[170:171], v[82:83], v[134:135]
	s_cbranch_vccnz .LBB0_362
	v_max_f32_e32 v114, v168, v168
	v_max_f32_e32 v134, 0xc2a00000, v114
	v_max_f32_e32 v114, v170, v170
	v_max_f32_e32 v158, 0xc2a00000, v114
	v_mul_f32_e32 v114, 0xbfb8aa3b, v134
	v_exp_f32_e32 v114, v114
	v_mul_f32_e32 v135, 0xbfb8aa3b, v158
	v_exp_f32_e32 v135, v135
	v_max_f32_e32 v155, v171, v171
	v_add_f32_e32 v114, 1.0, v114
	v_rcp_f32_e32 v160, v114
	v_add_f32_e32 v114, 1.0, v135
	v_max_f32_e32 v135, v169, v169
	v_max_f32_e32 v135, 0xc2a00000, v135
	v_max_f32_e32 v159, 0xc2a00000, v155
	v_mul_f32_e32 v155, 0xbfb8aa3b, v135
	v_exp_f32_e32 v155, v155
	v_mul_f32_e32 v161, 0xbfb8aa3b, v159
	v_exp_f32_e32 v168, v161
	v_max_f32_e32 v138, v138, v138
	v_rcp_f32_e32 v170, v114
	v_add_f32_e32 v114, 1.0, v155
	v_max_f32_e32 v138, 0xc2a00000, v138
	v_max_f32_e32 v155, v166, v166
	v_max_f32_e32 v166, 0xc2a00000, v155
	v_mul_f32_e32 v155, 0xbfb8aa3b, v138
	v_exp_f32_e32 v155, v155
	v_rcp_f32_e32 v161, v114
	v_add_f32_e32 v114, 1.0, v168
	v_mul_f32_e32 v168, 0xbfb8aa3b, v166
	v_exp_f32_e32 v168, v168
	v_max_f32_e32 v139, v139, v139
	v_rcp_f32_e32 v171, v114
	v_add_f32_e32 v114, 1.0, v155
	v_max_f32_e32 v139, 0xc2a00000, v139
	v_max_f32_e32 v155, v167, v167
	v_max_f32_e32 v167, 0xc2a00000, v155
	v_mul_f32_e32 v155, 0xbfb8aa3b, v139
	v_rcp_f32_e32 v178, v114
	v_add_f32_e32 v114, 1.0, v168
	v_exp_f32_e32 v155, v155
	v_mul_f32_e32 v168, 0xbfb8aa3b, v167
	v_exp_f32_e32 v168, v168
	v_rcp_f32_e32 v180, v114
	v_add_f32_e32 v114, 1.0, v155
	v_rcp_f32_e32 v179, v114
	v_add_f32_e32 v114, 1.0, v168
	v_rcp_f32_e32 v181, v114
	v_pk_mul_f32 v[168:169], v[134:135], v[160:161]
	v_pk_mul_f32 v[138:139], v[138:139], v[178:179]
	v_pk_mul_f32 v[170:171], v[158:159], v[170:171]
	v_pk_mul_f32 v[166:167], v[166:167], v[180:181]
.LBB0_362:
	ds_read_b32 v134, v176 offset:192
	v_cvt_pk_bf16_f32 v168, v168, v169
	v_cvt_pk_bf16_f32 v169, v138, v139
	v_cvt_pk_bf16_f32 v170, v170, v171
	v_cvt_pk_bf16_f32 v171, v166, v167
	ds_bpermute_b32 v242, v231, v168
	ds_bpermute_b32 v243, v231, v169
	ds_bpermute_b32 v244, v231, v170
	ds_bpermute_b32 v245, v231, v171
	ds_bpermute_b32 v246, v231, v136
	s_waitcnt lgkmcnt(0)
	v_subrev_u32_e32 v246, s82, v246
	global_store_dwordx4 v246, v[242:245], s[82:83] offset:64
	s_waitcnt lgkmcnt(0)
	v_pk_mul_f32 v[138:139], v[80:81], v[134:135] op_sel_hi:[1,0]
	v_pk_mul_f32 v[166:167], v[76:77], v[134:135] op_sel_hi:[1,0]
	v_pk_mul_f32 v[168:169], v[78:79], v[134:135] op_sel_hi:[1,0]
	s_and_b64 vcc, exec, s[40:41]
	v_pk_mul_f32 v[170:171], v[74:75], v[134:135] op_sel_hi:[1,0]
	s_cbranch_vccnz .LBB0_364
	v_max_f32_e32 v114, v168, v168
	v_max_f32_e32 v136, 0xc2a00000, v114
	v_max_f32_e32 v114, v170, v170
	v_max_f32_e32 v158, 0xc2a00000, v114
	v_mul_f32_e32 v114, 0xbfb8aa3b, v136
	v_exp_f32_e32 v114, v114
	v_mul_f32_e32 v135, 0xbfb8aa3b, v158
	v_exp_f32_e32 v135, v135
	v_add_f32_e32 v114, 1.0, v114
	v_rcp_f32_e32 v160, v114
	v_add_f32_e32 v114, 1.0, v135
	v_max_f32_e32 v135, v169, v169
	v_max_f32_e32 v137, 0xc2a00000, v135
	v_max_f32_e32 v135, v171, v171
	v_max_f32_e32 v159, 0xc2a00000, v135
	v_mul_f32_e32 v135, 0xbfb8aa3b, v137
	v_exp_f32_e32 v135, v135
	v_mul_f32_e32 v155, 0xbfb8aa3b, v159
	v_rcp_f32_e32 v170, v114
	v_exp_f32_e32 v155, v155
	v_add_f32_e32 v114, 1.0, v135
	v_max_f32_e32 v135, v138, v138
	v_max_f32_e32 v138, 0xc2a00000, v135
	v_max_f32_e32 v135, v166, v166
	v_max_f32_e32 v166, 0xc2a00000, v135
	v_mul_f32_e32 v135, 0xbfb8aa3b, v138
	v_exp_f32_e32 v135, v135
	v_rcp_f32_e32 v161, v114
	v_add_f32_e32 v114, 1.0, v155
	v_mul_f32_e32 v155, 0xbfb8aa3b, v166
	v_exp_f32_e32 v155, v155
	v_rcp_f32_e32 v171, v114
	v_add_f32_e32 v114, 1.0, v135
	v_max_f32_e32 v135, v139, v139
	v_max_f32_e32 v139, 0xc2a00000, v135
	v_max_f32_e32 v135, v167, v167
	v_max_f32_e32 v167, 0xc2a00000, v135
	v_mul_f32_e32 v135, 0xbfb8aa3b, v139
	v_rcp_f32_e32 v178, v114
	v_add_f32_e32 v114, 1.0, v155
	v_exp_f32_e32 v135, v135
	v_mul_f32_e32 v155, 0xbfb8aa3b, v167
	v_exp_f32_e32 v155, v155
	v_rcp_f32_e32 v180, v114
	v_add_f32_e32 v114, 1.0, v135
	v_rcp_f32_e32 v179, v114
	v_add_f32_e32 v114, 1.0, v155
	v_rcp_f32_e32 v181, v114
	v_pk_mul_f32 v[168:169], v[136:137], v[160:161]
	v_pk_mul_f32 v[138:139], v[138:139], v[178:179]
	v_pk_mul_f32 v[170:171], v[158:159], v[170:171]
	v_pk_mul_f32 v[166:167], v[166:167], v[180:181]
.LBB0_364:
	v_or_b32_e32 v136, 48, v152
	v_ashrrev_i32_e32 v137, 31, v136
	v_lshlrev_b64 v[136:137], 12, v[136:137]
	v_mov_b32_e32 v135, v134
	v_lshl_add_u64 v[136:137], v[132:133], 0, v[136:137]
	v_cvt_pk_bf16_f32 v168, v168, v169
	v_cvt_pk_bf16_f32 v169, v138, v139
	v_cvt_pk_bf16_f32 v170, v170, v171
	v_cvt_pk_bf16_f32 v171, v166, v167
	v_mov_b32_e32 v158, v134
	v_mov_b32_e32 v159, v134
	ds_bpermute_b32 v242, v231, v168
	ds_bpermute_b32 v243, v231, v169
	ds_bpermute_b32 v244, v231, v170
	ds_bpermute_b32 v245, v231, v171
	ds_bpermute_b32 v246, v231, v136
	s_waitcnt lgkmcnt(0)
	v_subrev_u32_e32 v246, s82, v246
	global_store_dwordx4 v246, v[242:245], s[82:83]
	v_pk_mul_f32 v[138:139], v[72:73], v[158:159]
	v_pk_mul_f32 v[166:167], v[68:69], v[158:159]
	v_pk_mul_f32 v[168:169], v[70:71], v[134:135]
	s_and_b64 vcc, exec, s[40:41]
	v_pk_mul_f32 v[170:171], v[66:67], v[134:135]
	s_cbranch_vccnz .LBB0_366
	v_max_f32_e32 v114, v168, v168
	v_max_f32_e32 v134, 0xc2a00000, v114
	v_max_f32_e32 v114, v170, v170
	v_max_f32_e32 v158, 0xc2a00000, v114
	v_mul_f32_e32 v114, 0xbfb8aa3b, v134
	v_exp_f32_e32 v114, v114
	v_mul_f32_e32 v135, 0xbfb8aa3b, v158
	v_exp_f32_e32 v135, v135
	v_max_f32_e32 v155, v171, v171
	v_add_f32_e32 v114, 1.0, v114
	v_rcp_f32_e32 v160, v114
	v_add_f32_e32 v114, 1.0, v135
	v_max_f32_e32 v135, v169, v169
	v_max_f32_e32 v135, 0xc2a00000, v135
	v_max_f32_e32 v159, 0xc2a00000, v155
	v_mul_f32_e32 v155, 0xbfb8aa3b, v135
	v_exp_f32_e32 v155, v155
	v_mul_f32_e32 v161, 0xbfb8aa3b, v159
	v_exp_f32_e32 v168, v161
	v_max_f32_e32 v138, v138, v138
	v_rcp_f32_e32 v170, v114
	v_add_f32_e32 v114, 1.0, v155
	v_max_f32_e32 v138, 0xc2a00000, v138
	v_max_f32_e32 v155, v166, v166
	v_max_f32_e32 v166, 0xc2a00000, v155
	v_mul_f32_e32 v155, 0xbfb8aa3b, v138
	v_exp_f32_e32 v155, v155
	v_rcp_f32_e32 v161, v114
	v_add_f32_e32 v114, 1.0, v168
	v_mul_f32_e32 v168, 0xbfb8aa3b, v166
	v_exp_f32_e32 v168, v168
	v_max_f32_e32 v139, v139, v139
	v_rcp_f32_e32 v171, v114
	v_add_f32_e32 v114, 1.0, v155
	v_max_f32_e32 v139, 0xc2a00000, v139
	v_max_f32_e32 v155, v167, v167
	v_max_f32_e32 v167, 0xc2a00000, v155
	v_mul_f32_e32 v155, 0xbfb8aa3b, v139
	v_rcp_f32_e32 v178, v114
	v_add_f32_e32 v114, 1.0, v168
	v_exp_f32_e32 v155, v155
	v_mul_f32_e32 v168, 0xbfb8aa3b, v167
	v_exp_f32_e32 v168, v168
	v_rcp_f32_e32 v180, v114
	v_add_f32_e32 v114, 1.0, v155
	v_rcp_f32_e32 v179, v114
	v_add_f32_e32 v114, 1.0, v168
	v_rcp_f32_e32 v181, v114
	v_pk_mul_f32 v[168:169], v[134:135], v[160:161]
	v_pk_mul_f32 v[138:139], v[138:139], v[178:179]
	v_pk_mul_f32 v[170:171], v[158:159], v[170:171]
	v_pk_mul_f32 v[166:167], v[166:167], v[180:181]
.LBB0_366:
	ds_read_b32 v134, v176 offset:512
	v_cvt_pk_bf16_f32 v168, v168, v169
	v_cvt_pk_bf16_f32 v169, v138, v139
	v_cvt_pk_bf16_f32 v170, v170, v171
	v_cvt_pk_bf16_f32 v171, v166, v167
	ds_bpermute_b32 v242, v231, v168
	ds_bpermute_b32 v243, v231, v169
	ds_bpermute_b32 v244, v231, v170
	ds_bpermute_b32 v245, v231, v171
	ds_bpermute_b32 v246, v231, v136
	s_waitcnt lgkmcnt(0)
	v_subrev_u32_e32 v246, s82, v246
	global_store_dwordx4 v246, v[242:245], s[82:83] offset:64
	s_waitcnt lgkmcnt(0)
	v_pk_mul_f32 v[138:139], v[64:65], v[134:135] op_sel_hi:[1,0]
	v_pk_mul_f32 v[166:167], v[60:61], v[134:135] op_sel_hi:[1,0]
	v_pk_mul_f32 v[168:169], v[62:63], v[134:135] op_sel_hi:[1,0]
	s_and_b64 vcc, exec, s[40:41]
	v_pk_mul_f32 v[170:171], v[58:59], v[134:135] op_sel_hi:[1,0]
	s_cbranch_vccnz .LBB0_368
	v_max_f32_e32 v114, v168, v168
	v_max_f32_e32 v136, 0xc2a00000, v114
	v_max_f32_e32 v114, v170, v170
	v_max_f32_e32 v158, 0xc2a00000, v114
	v_mul_f32_e32 v114, 0xbfb8aa3b, v136
	v_exp_f32_e32 v114, v114
	v_mul_f32_e32 v135, 0xbfb8aa3b, v158
	v_exp_f32_e32 v135, v135
	v_add_f32_e32 v114, 1.0, v114
	v_rcp_f32_e32 v160, v114
	v_add_f32_e32 v114, 1.0, v135
	v_max_f32_e32 v135, v169, v169
	v_max_f32_e32 v137, 0xc2a00000, v135
	v_max_f32_e32 v135, v171, v171
	v_max_f32_e32 v159, 0xc2a00000, v135
	v_mul_f32_e32 v135, 0xbfb8aa3b, v137
	v_exp_f32_e32 v135, v135
	v_mul_f32_e32 v155, 0xbfb8aa3b, v159
	v_rcp_f32_e32 v170, v114
	v_exp_f32_e32 v155, v155
	v_add_f32_e32 v114, 1.0, v135
	v_max_f32_e32 v135, v138, v138
	v_max_f32_e32 v138, 0xc2a00000, v135
	v_max_f32_e32 v135, v166, v166
	v_max_f32_e32 v166, 0xc2a00000, v135
	v_mul_f32_e32 v135, 0xbfb8aa3b, v138
	v_exp_f32_e32 v135, v135
	v_rcp_f32_e32 v161, v114
	v_add_f32_e32 v114, 1.0, v155
	v_mul_f32_e32 v155, 0xbfb8aa3b, v166
	v_exp_f32_e32 v155, v155
	v_rcp_f32_e32 v171, v114
	v_add_f32_e32 v114, 1.0, v135
	v_max_f32_e32 v135, v139, v139
	v_max_f32_e32 v139, 0xc2a00000, v135
	v_max_f32_e32 v135, v167, v167
	v_max_f32_e32 v167, 0xc2a00000, v135
	v_mul_f32_e32 v135, 0xbfb8aa3b, v139
	v_rcp_f32_e32 v178, v114
	v_add_f32_e32 v114, 1.0, v155
	v_exp_f32_e32 v135, v135
	v_mul_f32_e32 v155, 0xbfb8aa3b, v167
	v_exp_f32_e32 v155, v155
	v_rcp_f32_e32 v180, v114
	v_add_f32_e32 v114, 1.0, v135
	v_rcp_f32_e32 v179, v114
	v_add_f32_e32 v114, 1.0, v155
	v_rcp_f32_e32 v181, v114
	v_pk_mul_f32 v[168:169], v[136:137], v[160:161]
	v_pk_mul_f32 v[138:139], v[138:139], v[178:179]
	v_pk_mul_f32 v[170:171], v[158:159], v[170:171]
	v_pk_mul_f32 v[166:167], v[166:167], v[180:181]
.LBB0_368:
	v_lshlrev_b64 v[136:137], 12, v[152:153]
	v_lshl_add_u64 v[136:137], v[132:133], 0, v[136:137]
	s_mov_b32 s14, 0x80000
	v_cvt_pk_bf16_f32 v168, v168, v169
	v_cvt_pk_bf16_f32 v169, v138, v139
	v_add_co_u32_e32 v138, vcc, s14, v136
	v_mov_b32_e32 v135, v134
	v_cvt_pk_bf16_f32 v170, v170, v171
	v_cvt_pk_bf16_f32 v171, v166, v167
	s_nop 0
	v_addc_co_u32_e32 v139, vcc, 0, v137, vcc
	v_mov_b32_e32 v158, v134
	v_mov_b32_e32 v159, v134
	ds_bpermute_b32 v242, v231, v168
	ds_bpermute_b32 v243, v231, v169
	ds_bpermute_b32 v244, v231, v170
	ds_bpermute_b32 v245, v231, v171
	ds_bpermute_b32 v246, v231, v138
	s_waitcnt lgkmcnt(0)
	v_subrev_u32_e32 v246, s82, v246
	global_store_dwordx4 v246, v[242:245], s[82:83]
	v_pk_mul_f32 v[138:139], v[56:57], v[158:159]
	v_pk_mul_f32 v[166:167], v[52:53], v[158:159]
	v_pk_mul_f32 v[168:169], v[54:55], v[134:135]
	s_and_b64 vcc, exec, s[40:41]
	v_pk_mul_f32 v[170:171], v[50:51], v[134:135]
	s_cbranch_vccnz .LBB0_370
	v_max_f32_e32 v114, v168, v168
	v_max_f32_e32 v134, 0xc2a00000, v114
	v_max_f32_e32 v114, v170, v170
	v_max_f32_e32 v158, 0xc2a00000, v114
	v_mul_f32_e32 v114, 0xbfb8aa3b, v134
	v_exp_f32_e32 v114, v114
	v_mul_f32_e32 v135, 0xbfb8aa3b, v158
	v_exp_f32_e32 v135, v135
	v_max_f32_e32 v155, v171, v171
	v_add_f32_e32 v114, 1.0, v114
	v_rcp_f32_e32 v160, v114
	v_add_f32_e32 v114, 1.0, v135
	v_max_f32_e32 v135, v169, v169
	v_max_f32_e32 v135, 0xc2a00000, v135
	v_max_f32_e32 v159, 0xc2a00000, v155
	v_mul_f32_e32 v155, 0xbfb8aa3b, v135
	v_exp_f32_e32 v155, v155
	v_mul_f32_e32 v161, 0xbfb8aa3b, v159
	v_exp_f32_e32 v168, v161
	v_max_f32_e32 v138, v138, v138
	v_rcp_f32_e32 v170, v114
	v_add_f32_e32 v114, 1.0, v155
	v_max_f32_e32 v138, 0xc2a00000, v138
	v_max_f32_e32 v155, v166, v166
	v_max_f32_e32 v166, 0xc2a00000, v155
	v_mul_f32_e32 v155, 0xbfb8aa3b, v138
	v_exp_f32_e32 v155, v155
	v_rcp_f32_e32 v161, v114
	v_add_f32_e32 v114, 1.0, v168
	v_mul_f32_e32 v168, 0xbfb8aa3b, v166
	v_exp_f32_e32 v168, v168
	v_max_f32_e32 v139, v139, v139
	v_rcp_f32_e32 v171, v114
	v_add_f32_e32 v114, 1.0, v155
	v_max_f32_e32 v139, 0xc2a00000, v139
	v_max_f32_e32 v155, v167, v167
	v_max_f32_e32 v167, 0xc2a00000, v155
	v_mul_f32_e32 v155, 0xbfb8aa3b, v139
	v_rcp_f32_e32 v178, v114
	v_add_f32_e32 v114, 1.0, v168
	v_exp_f32_e32 v155, v155
	v_mul_f32_e32 v168, 0xbfb8aa3b, v167
	v_exp_f32_e32 v168, v168
	v_rcp_f32_e32 v180, v114
	v_add_f32_e32 v114, 1.0, v155
	v_rcp_f32_e32 v179, v114
	v_add_f32_e32 v114, 1.0, v168
	v_rcp_f32_e32 v181, v114
	v_pk_mul_f32 v[168:169], v[134:135], v[160:161]
	v_pk_mul_f32 v[138:139], v[138:139], v[178:179]
	v_pk_mul_f32 v[170:171], v[158:159], v[170:171]
	v_pk_mul_f32 v[166:167], v[166:167], v[180:181]
.LBB0_370:
	ds_read_b32 v134, v176 offset:576
	s_mov_b64 s[14:15], 0x80000
	v_lshl_add_u64 v[158:159], v[136:137], 0, s[14:15]
	v_cvt_pk_bf16_f32 v137, v138, v139
	v_cvt_pk_bf16_f32 v138, v170, v171
	v_cvt_pk_bf16_f32 v139, v166, v167
	v_cvt_pk_bf16_f32 v136, v168, v169
	ds_bpermute_b32 v242, v231, v136
	ds_bpermute_b32 v243, v231, v137
	ds_bpermute_b32 v244, v231, v138
	ds_bpermute_b32 v245, v231, v139
	ds_bpermute_b32 v246, v231, v158
	s_waitcnt lgkmcnt(0)
	v_subrev_u32_e32 v246, s82, v246
	global_store_dwordx4 v246, v[242:245], s[82:83] offset:64
	s_waitcnt lgkmcnt(0)
	v_pk_mul_f32 v[168:169], v[46:47], v[134:135] op_sel_hi:[1,0]
	v_pk_mul_f32 v[166:167], v[44:45], v[134:135] op_sel_hi:[1,0]
	v_pk_mul_f32 v[138:139], v[48:49], v[134:135] op_sel_hi:[1,0]
	s_and_b64 vcc, exec, s[40:41]
	v_pk_mul_f32 v[170:171], v[42:43], v[134:135] op_sel_hi:[1,0]
	s_cbranch_vccnz .LBB0_372
	v_max_f32_e32 v114, v168, v168
	v_max_f32_e32 v136, 0xc2a00000, v114
	v_max_f32_e32 v114, v170, v170
	v_max_f32_e32 v158, 0xc2a00000, v114
	v_mul_f32_e32 v114, 0xbfb8aa3b, v136
	v_exp_f32_e32 v114, v114
	v_mul_f32_e32 v135, 0xbfb8aa3b, v158
	v_exp_f32_e32 v135, v135
	v_add_f32_e32 v114, 1.0, v114
	v_rcp_f32_e32 v160, v114
	v_add_f32_e32 v114, 1.0, v135
	v_max_f32_e32 v135, v169, v169
	v_max_f32_e32 v137, 0xc2a00000, v135
	v_max_f32_e32 v135, v171, v171
	v_max_f32_e32 v159, 0xc2a00000, v135
	v_mul_f32_e32 v135, 0xbfb8aa3b, v137
	v_exp_f32_e32 v135, v135
	v_mul_f32_e32 v155, 0xbfb8aa3b, v159
	v_rcp_f32_e32 v170, v114
	v_exp_f32_e32 v155, v155
	v_add_f32_e32 v114, 1.0, v135
	v_max_f32_e32 v135, v138, v138
	v_max_f32_e32 v138, 0xc2a00000, v135
	v_max_f32_e32 v135, v166, v166
	v_max_f32_e32 v166, 0xc2a00000, v135
	v_mul_f32_e32 v135, 0xbfb8aa3b, v138
	v_exp_f32_e32 v135, v135
	v_rcp_f32_e32 v161, v114
	v_add_f32_e32 v114, 1.0, v155
	v_mul_f32_e32 v155, 0xbfb8aa3b, v166
	v_exp_f32_e32 v155, v155
	v_rcp_f32_e32 v171, v114
	v_add_f32_e32 v114, 1.0, v135
	v_max_f32_e32 v135, v139, v139
	v_max_f32_e32 v139, 0xc2a00000, v135
	v_max_f32_e32 v135, v167, v167
	v_max_f32_e32 v167, 0xc2a00000, v135
	v_mul_f32_e32 v135, 0xbfb8aa3b, v139
	v_rcp_f32_e32 v178, v114
	v_add_f32_e32 v114, 1.0, v155
	v_exp_f32_e32 v135, v135
	v_mul_f32_e32 v155, 0xbfb8aa3b, v167
	v_exp_f32_e32 v155, v155
	v_rcp_f32_e32 v180, v114
	v_add_f32_e32 v114, 1.0, v135
	v_rcp_f32_e32 v179, v114
	v_add_f32_e32 v114, 1.0, v155
	v_rcp_f32_e32 v181, v114
	v_pk_mul_f32 v[168:169], v[136:137], v[160:161]
	v_pk_mul_f32 v[138:139], v[138:139], v[178:179]
	v_pk_mul_f32 v[170:171], v[158:159], v[170:171]
	v_pk_mul_f32 v[166:167], v[166:167], v[180:181]
.LBB0_372:
	v_lshlrev_b64 v[136:137], 12, v[152:153]
	v_lshl_add_u64 v[136:137], v[132:133], 0, v[136:137]
	s_mov_b32 s14, 0x90000
	v_cvt_pk_bf16_f32 v168, v168, v169
	v_cvt_pk_bf16_f32 v169, v138, v139
	v_add_co_u32_e32 v138, vcc, s14, v136
	v_mov_b32_e32 v135, v134
	v_cvt_pk_bf16_f32 v170, v170, v171
	v_cvt_pk_bf16_f32 v171, v166, v167
	s_nop 0
	v_addc_co_u32_e32 v139, vcc, 0, v137, vcc
	v_mov_b32_e32 v158, v134
	v_mov_b32_e32 v159, v134
	ds_bpermute_b32 v242, v231, v168
	ds_bpermute_b32 v243, v231, v169
	ds_bpermute_b32 v244, v231, v170
	ds_bpermute_b32 v245, v231, v171
	ds_bpermute_b32 v246, v231, v138
	s_waitcnt lgkmcnt(0)
	v_subrev_u32_e32 v246, s82, v246
	global_store_dwordx4 v246, v[242:245], s[82:83]
	v_pk_mul_f32 v[138:139], v[40:41], v[158:159]
	v_pk_mul_f32 v[166:167], v[36:37], v[158:159]
	v_pk_mul_f32 v[168:169], v[38:39], v[134:135]
	s_and_b64 vcc, exec, s[40:41]
	v_pk_mul_f32 v[170:171], v[34:35], v[134:135]
	s_cbranch_vccnz .LBB0_374
	v_max_f32_e32 v114, v168, v168
	v_max_f32_e32 v134, 0xc2a00000, v114
	v_max_f32_e32 v114, v170, v170
	v_max_f32_e32 v158, 0xc2a00000, v114
	v_mul_f32_e32 v114, 0xbfb8aa3b, v134
	v_exp_f32_e32 v114, v114
	v_mul_f32_e32 v135, 0xbfb8aa3b, v158
	v_exp_f32_e32 v135, v135
	v_max_f32_e32 v155, v171, v171
	v_add_f32_e32 v114, 1.0, v114
	v_rcp_f32_e32 v160, v114
	v_add_f32_e32 v114, 1.0, v135
	v_max_f32_e32 v135, v169, v169
	v_max_f32_e32 v135, 0xc2a00000, v135
	v_max_f32_e32 v159, 0xc2a00000, v155
	v_mul_f32_e32 v155, 0xbfb8aa3b, v135
	v_exp_f32_e32 v155, v155
	v_mul_f32_e32 v161, 0xbfb8aa3b, v159
	v_exp_f32_e32 v168, v161
	v_max_f32_e32 v138, v138, v138
	v_rcp_f32_e32 v170, v114
	v_add_f32_e32 v114, 1.0, v155
	v_max_f32_e32 v138, 0xc2a00000, v138
	v_max_f32_e32 v155, v166, v166
	v_max_f32_e32 v166, 0xc2a00000, v155
	v_mul_f32_e32 v155, 0xbfb8aa3b, v138
	v_exp_f32_e32 v155, v155
	v_rcp_f32_e32 v161, v114
	v_add_f32_e32 v114, 1.0, v168
	v_mul_f32_e32 v168, 0xbfb8aa3b, v166
	v_exp_f32_e32 v168, v168
	v_max_f32_e32 v139, v139, v139
	v_rcp_f32_e32 v171, v114
	v_add_f32_e32 v114, 1.0, v155
	v_max_f32_e32 v139, 0xc2a00000, v139
	v_max_f32_e32 v155, v167, v167
	v_max_f32_e32 v167, 0xc2a00000, v155
	v_mul_f32_e32 v155, 0xbfb8aa3b, v139
	v_rcp_f32_e32 v178, v114
	v_add_f32_e32 v114, 1.0, v168
	v_exp_f32_e32 v155, v155
	v_mul_f32_e32 v168, 0xbfb8aa3b, v167
	v_exp_f32_e32 v168, v168
	v_rcp_f32_e32 v180, v114
	v_add_f32_e32 v114, 1.0, v155
	v_rcp_f32_e32 v179, v114
	v_add_f32_e32 v114, 1.0, v168
	v_rcp_f32_e32 v181, v114
	v_pk_mul_f32 v[168:169], v[134:135], v[160:161]
	v_pk_mul_f32 v[138:139], v[138:139], v[178:179]
	v_pk_mul_f32 v[170:171], v[158:159], v[170:171]
	v_pk_mul_f32 v[166:167], v[166:167], v[180:181]
.LBB0_374:
	ds_read_b32 v134, v176 offset:640
	s_mov_b64 s[14:15], 0x90000
	v_lshl_add_u64 v[158:159], v[136:137], 0, s[14:15]
	v_cvt_pk_bf16_f32 v137, v138, v139
	v_cvt_pk_bf16_f32 v138, v170, v171
	v_cvt_pk_bf16_f32 v139, v166, v167
	v_cvt_pk_bf16_f32 v136, v168, v169
	ds_bpermute_b32 v242, v231, v136
	ds_bpermute_b32 v243, v231, v137
	ds_bpermute_b32 v244, v231, v138
	ds_bpermute_b32 v245, v231, v139
	ds_bpermute_b32 v246, v231, v158
	s_waitcnt lgkmcnt(0)
	v_subrev_u32_e32 v246, s82, v246
	global_store_dwordx4 v246, v[242:245], s[82:83] offset:64
	s_waitcnt lgkmcnt(0)
	v_pk_mul_f32 v[168:169], v[30:31], v[134:135] op_sel_hi:[1,0]
	v_pk_mul_f32 v[166:167], v[28:29], v[134:135] op_sel_hi:[1,0]
	v_pk_mul_f32 v[138:139], v[32:33], v[134:135] op_sel_hi:[1,0]
	s_and_b64 vcc, exec, s[40:41]
	v_pk_mul_f32 v[170:171], v[26:27], v[134:135] op_sel_hi:[1,0]
	s_cbranch_vccnz .LBB0_376
	v_max_f32_e32 v114, v168, v168
	v_max_f32_e32 v136, 0xc2a00000, v114
	v_max_f32_e32 v114, v170, v170
	v_max_f32_e32 v158, 0xc2a00000, v114
	v_mul_f32_e32 v114, 0xbfb8aa3b, v136
	v_exp_f32_e32 v114, v114
	v_mul_f32_e32 v135, 0xbfb8aa3b, v158
	v_exp_f32_e32 v135, v135
	v_add_f32_e32 v114, 1.0, v114
	v_rcp_f32_e32 v160, v114
	v_add_f32_e32 v114, 1.0, v135
	v_max_f32_e32 v135, v169, v169
	v_max_f32_e32 v137, 0xc2a00000, v135
	v_max_f32_e32 v135, v171, v171
	v_max_f32_e32 v159, 0xc2a00000, v135
	v_mul_f32_e32 v135, 0xbfb8aa3b, v137
	v_exp_f32_e32 v135, v135
	v_mul_f32_e32 v155, 0xbfb8aa3b, v159
	v_rcp_f32_e32 v170, v114
	v_exp_f32_e32 v155, v155
	v_add_f32_e32 v114, 1.0, v135
	v_max_f32_e32 v135, v138, v138
	v_max_f32_e32 v138, 0xc2a00000, v135
	v_max_f32_e32 v135, v166, v166
	v_max_f32_e32 v166, 0xc2a00000, v135
	v_mul_f32_e32 v135, 0xbfb8aa3b, v138
	v_exp_f32_e32 v135, v135
	v_rcp_f32_e32 v161, v114
	v_add_f32_e32 v114, 1.0, v155
	v_mul_f32_e32 v155, 0xbfb8aa3b, v166
	v_exp_f32_e32 v155, v155
	v_rcp_f32_e32 v171, v114
	v_add_f32_e32 v114, 1.0, v135
	v_max_f32_e32 v135, v139, v139
	v_max_f32_e32 v139, 0xc2a00000, v135
	v_max_f32_e32 v135, v167, v167
	v_max_f32_e32 v167, 0xc2a00000, v135
	v_mul_f32_e32 v135, 0xbfb8aa3b, v139
	v_rcp_f32_e32 v178, v114
	v_add_f32_e32 v114, 1.0, v155
	v_exp_f32_e32 v135, v135
	v_mul_f32_e32 v155, 0xbfb8aa3b, v167
	v_exp_f32_e32 v155, v155
	v_rcp_f32_e32 v180, v114
	v_add_f32_e32 v114, 1.0, v135
	v_rcp_f32_e32 v179, v114
	v_add_f32_e32 v114, 1.0, v155
	v_rcp_f32_e32 v181, v114
	v_pk_mul_f32 v[168:169], v[136:137], v[160:161]
	v_pk_mul_f32 v[138:139], v[138:139], v[178:179]
	v_pk_mul_f32 v[170:171], v[158:159], v[170:171]
	v_pk_mul_f32 v[166:167], v[166:167], v[180:181]
.LBB0_376:
	v_lshlrev_b64 v[136:137], 12, v[152:153]
	v_lshl_add_u64 v[136:137], v[132:133], 0, v[136:137]
	s_mov_b32 s14, 0xa0000
	v_cvt_pk_bf16_f32 v168, v168, v169
	v_cvt_pk_bf16_f32 v169, v138, v139
	v_add_co_u32_e32 v138, vcc, s14, v136
	v_mov_b32_e32 v135, v134
	v_cvt_pk_bf16_f32 v170, v170, v171
	v_cvt_pk_bf16_f32 v171, v166, v167
	s_nop 0
	v_addc_co_u32_e32 v139, vcc, 0, v137, vcc
	v_mov_b32_e32 v158, v134
	v_mov_b32_e32 v159, v134
	ds_bpermute_b32 v242, v231, v168
	ds_bpermute_b32 v243, v231, v169
	ds_bpermute_b32 v244, v231, v170
	ds_bpermute_b32 v245, v231, v171
	ds_bpermute_b32 v246, v231, v138
	s_waitcnt lgkmcnt(0)
	v_subrev_u32_e32 v246, s82, v246
	global_store_dwordx4 v246, v[242:245], s[82:83]
	v_pk_mul_f32 v[138:139], v[24:25], v[158:159]
	v_pk_mul_f32 v[166:167], v[20:21], v[158:159]
	v_pk_mul_f32 v[168:169], v[22:23], v[134:135]
	s_and_b64 vcc, exec, s[40:41]
	v_pk_mul_f32 v[170:171], v[18:19], v[134:135]
	s_cbranch_vccnz .LBB0_378
	v_max_f32_e32 v114, v168, v168
	v_max_f32_e32 v134, 0xc2a00000, v114
	v_max_f32_e32 v114, v170, v170
	v_max_f32_e32 v158, 0xc2a00000, v114
	v_mul_f32_e32 v114, 0xbfb8aa3b, v134
	v_exp_f32_e32 v114, v114
	v_mul_f32_e32 v135, 0xbfb8aa3b, v158
	v_exp_f32_e32 v135, v135
	v_max_f32_e32 v155, v171, v171
	v_add_f32_e32 v114, 1.0, v114
	v_rcp_f32_e32 v160, v114
	v_add_f32_e32 v114, 1.0, v135
	v_max_f32_e32 v135, v169, v169
	v_max_f32_e32 v135, 0xc2a00000, v135
	v_max_f32_e32 v159, 0xc2a00000, v155
	v_mul_f32_e32 v155, 0xbfb8aa3b, v135
	v_exp_f32_e32 v155, v155
	v_mul_f32_e32 v161, 0xbfb8aa3b, v159
	v_exp_f32_e32 v168, v161
	v_max_f32_e32 v138, v138, v138
	v_rcp_f32_e32 v170, v114
	v_add_f32_e32 v114, 1.0, v155
	v_max_f32_e32 v138, 0xc2a00000, v138
	v_max_f32_e32 v155, v166, v166
	v_max_f32_e32 v166, 0xc2a00000, v155
	v_mul_f32_e32 v155, 0xbfb8aa3b, v138
	v_exp_f32_e32 v155, v155
	v_rcp_f32_e32 v161, v114
	v_add_f32_e32 v114, 1.0, v168
	v_mul_f32_e32 v168, 0xbfb8aa3b, v166
	v_exp_f32_e32 v168, v168
	v_max_f32_e32 v139, v139, v139
	v_rcp_f32_e32 v171, v114
	v_add_f32_e32 v114, 1.0, v155
	v_max_f32_e32 v139, 0xc2a00000, v139
	v_max_f32_e32 v155, v167, v167
	v_max_f32_e32 v167, 0xc2a00000, v155
	v_mul_f32_e32 v155, 0xbfb8aa3b, v139
	v_rcp_f32_e32 v178, v114
	v_add_f32_e32 v114, 1.0, v168
	v_exp_f32_e32 v155, v155
	v_mul_f32_e32 v168, 0xbfb8aa3b, v167
	v_exp_f32_e32 v168, v168
	v_rcp_f32_e32 v180, v114
	v_add_f32_e32 v114, 1.0, v155
	v_rcp_f32_e32 v179, v114
	v_add_f32_e32 v114, 1.0, v168
	v_rcp_f32_e32 v181, v114
	v_pk_mul_f32 v[168:169], v[134:135], v[160:161]
	v_pk_mul_f32 v[138:139], v[138:139], v[178:179]
	v_pk_mul_f32 v[170:171], v[158:159], v[170:171]
	v_pk_mul_f32 v[166:167], v[166:167], v[180:181]
.LBB0_378:
	ds_read_b32 v134, v176 offset:704
	s_mov_b64 s[14:15], 0xa0000
	v_lshl_add_u64 v[158:159], v[136:137], 0, s[14:15]
	v_cvt_pk_bf16_f32 v136, v168, v169
	v_cvt_pk_bf16_f32 v137, v138, v139
	v_cvt_pk_bf16_f32 v138, v170, v171
	v_cvt_pk_bf16_f32 v139, v166, v167
	ds_bpermute_b32 v242, v231, v136
	ds_bpermute_b32 v243, v231, v137
	ds_bpermute_b32 v244, v231, v138
	ds_bpermute_b32 v245, v231, v139
	ds_bpermute_b32 v246, v231, v158
	s_waitcnt lgkmcnt(0)
	v_subrev_u32_e32 v246, s82, v246
	global_store_dwordx4 v246, v[242:245], s[82:83] offset:64
	s_waitcnt lgkmcnt(0)
	v_pk_mul_f32 v[166:167], v[14:15], v[134:135] op_sel_hi:[1,0]
	s_and_b64 vcc, exec, s[40:41]
	v_pk_mul_f32 v[136:137], v[16:17], v[134:135] op_sel_hi:[1,0]
	v_pk_mul_f32 v[138:139], v[12:13], v[134:135] op_sel_hi:[1,0]
	v_pk_mul_f32 v[168:169], v[10:11], v[134:135] op_sel_hi:[1,0]
	s_cbranch_vccnz .LBB0_380
	v_max_f32_e32 v114, v166, v166
	v_max_f32_e32 v158, 0xc2a00000, v114
	v_max_f32_e32 v114, v168, v168
	v_max_f32_e32 v160, 0xc2a00000, v114
	v_mul_f32_e32 v114, 0xbfb8aa3b, v158
	v_exp_f32_e32 v114, v114
	v_mul_f32_e32 v135, 0xbfb8aa3b, v160
	v_exp_f32_e32 v135, v135
	v_add_f32_e32 v114, 1.0, v114
	v_rcp_f32_e32 v166, v114
	v_add_f32_e32 v114, 1.0, v135
	v_max_f32_e32 v135, v167, v167
	v_max_f32_e32 v159, 0xc2a00000, v135
	v_max_f32_e32 v135, v169, v169
	v_max_f32_e32 v161, 0xc2a00000, v135
	v_mul_f32_e32 v135, 0xbfb8aa3b, v159
	v_exp_f32_e32 v135, v135
	v_mul_f32_e32 v155, 0xbfb8aa3b, v161
	v_rcp_f32_e32 v168, v114
	v_exp_f32_e32 v155, v155
	v_add_f32_e32 v114, 1.0, v135
	v_max_f32_e32 v135, v136, v136
	v_max_f32_e32 v136, 0xc2a00000, v135
	v_max_f32_e32 v135, v138, v138
	v_max_f32_e32 v138, 0xc2a00000, v135
	v_mul_f32_e32 v135, 0xbfb8aa3b, v136
	v_exp_f32_e32 v135, v135
	v_rcp_f32_e32 v167, v114
	v_add_f32_e32 v114, 1.0, v155
	v_mul_f32_e32 v155, 0xbfb8aa3b, v138
	v_exp_f32_e32 v155, v155
	v_rcp_f32_e32 v169, v114
	v_add_f32_e32 v114, 1.0, v135
	v_max_f32_e32 v135, v137, v137
	v_max_f32_e32 v137, 0xc2a00000, v135
	v_max_f32_e32 v135, v139, v139
	v_max_f32_e32 v139, 0xc2a00000, v135
	v_mul_f32_e32 v135, 0xbfb8aa3b, v137
	v_rcp_f32_e32 v170, v114
	v_add_f32_e32 v114, 1.0, v155
	v_exp_f32_e32 v135, v135
	v_mul_f32_e32 v155, 0xbfb8aa3b, v139
	v_exp_f32_e32 v155, v155
	v_rcp_f32_e32 v178, v114
	v_add_f32_e32 v114, 1.0, v135
	v_rcp_f32_e32 v171, v114
	v_add_f32_e32 v114, 1.0, v155
	v_rcp_f32_e32 v179, v114
	v_pk_mul_f32 v[166:167], v[158:159], v[166:167]
	v_pk_mul_f32 v[136:137], v[136:137], v[170:171]
	v_pk_mul_f32 v[168:169], v[160:161], v[168:169]
	v_pk_mul_f32 v[138:139], v[138:139], v[178:179]
.LBB0_380:
	v_lshlrev_b64 v[158:159], 12, v[152:153]
	v_lshl_add_u64 v[132:133], v[132:133], 0, v[158:159]
	s_mov_b32 s14, 0xb0000
	v_cvt_pk_bf16_f32 v166, v166, v167
	v_cvt_pk_bf16_f32 v167, v136, v137
	v_add_co_u32_e32 v136, vcc, s14, v132
	v_mov_b32_e32 v135, v134
	s_nop 0
	v_addc_co_u32_e32 v137, vcc, 0, v133, vcc
	v_cvt_pk_bf16_f32 v168, v168, v169
	v_cvt_pk_bf16_f32 v169, v138, v139
	ds_bpermute_b32 v242, v231, v166
	ds_bpermute_b32 v243, v231, v167
	ds_bpermute_b32 v244, v231, v168
	ds_bpermute_b32 v245, v231, v169
	ds_bpermute_b32 v246, v231, v136
	s_waitcnt lgkmcnt(0)
	v_subrev_u32_e32 v246, s82, v246
	global_store_dwordx4 v246, v[242:245], s[82:83]
	v_mov_b32_e32 v136, v134
	v_mov_b32_e32 v137, v134
	v_pk_mul_f32 v[138:139], v[8:9], v[136:137]
	v_pk_mul_f32 v[168:169], v[6:7], v[134:135]
	v_pk_mul_f32 v[166:167], v[4:5], v[136:137]
	s_and_b64 vcc, exec, s[40:41]
	v_pk_mul_f32 v[134:135], v[2:3], v[134:135]
	s_cbranch_vccnz .LBB0_382
	v_max_f32_e32 v114, v168, v168
	v_max_f32_e32 v136, 0xc2a00000, v114
	v_max_f32_e32 v114, v134, v134
	v_max_f32_e32 v134, 0xc2a00000, v114
	v_mul_f32_e32 v114, 0xbfb8aa3b, v136
	v_exp_f32_e32 v114, v114
	v_mul_f32_e32 v137, 0xbfb8aa3b, v134
	v_exp_f32_e32 v137, v137
	v_max_f32_e32 v135, v135, v135
	v_add_f32_e32 v114, 1.0, v114
	v_rcp_f32_e32 v158, v114
	v_add_f32_e32 v114, 1.0, v137
	v_max_f32_e32 v137, v169, v169
	v_max_f32_e32 v137, 0xc2a00000, v137
	v_mul_f32_e32 v153, 0xbfb8aa3b, v137
	v_exp_f32_e32 v153, v153
	v_max_f32_e32 v135, 0xc2a00000, v135
	v_mul_f32_e32 v155, 0xbfb8aa3b, v135
	v_exp_f32_e32 v155, v155
	v_max_f32_e32 v138, v138, v138
	v_rcp_f32_e32 v160, v114
	v_add_f32_e32 v114, 1.0, v153
	v_max_f32_e32 v138, 0xc2a00000, v138
	v_max_f32_e32 v153, v166, v166
	v_max_f32_e32 v166, 0xc2a00000, v153
	v_mul_f32_e32 v153, 0xbfb8aa3b, v138
	v_exp_f32_e32 v153, v153
	v_rcp_f32_e32 v159, v114
	v_add_f32_e32 v114, 1.0, v155
	v_mul_f32_e32 v155, 0xbfb8aa3b, v166
	v_exp_f32_e32 v155, v155
	v_max_f32_e32 v139, v139, v139
	v_rcp_f32_e32 v161, v114
	v_add_f32_e32 v114, 1.0, v153
	v_max_f32_e32 v139, 0xc2a00000, v139
	v_max_f32_e32 v153, v167, v167
	v_max_f32_e32 v167, 0xc2a00000, v153
	v_mul_f32_e32 v153, 0xbfb8aa3b, v139
	v_rcp_f32_e32 v170, v114
	v_add_f32_e32 v114, 1.0, v155
	v_exp_f32_e32 v153, v153
	v_mul_f32_e32 v155, 0xbfb8aa3b, v167
	v_exp_f32_e32 v155, v155
	v_rcp_f32_e32 v178, v114
	v_add_f32_e32 v114, 1.0, v153
	v_rcp_f32_e32 v171, v114
	v_add_f32_e32 v114, 1.0, v155
	v_rcp_f32_e32 v179, v114
	v_pk_mul_f32 v[168:169], v[136:137], v[158:159]
	v_pk_mul_f32 v[138:139], v[138:139], v[170:171]
	v_pk_mul_f32 v[134:135], v[134:135], v[160:161]
	v_pk_mul_f32 v[166:167], v[166:167], v[178:179]

.LBB0_383:
	s_andn2_b64 vcc, exec, s[38:39]
	s_mov_b64 s[28:29], -1
	ds_bpermute_b32 v242, v231, v132
	ds_bpermute_b32 v243, v231, v133
	ds_bpermute_b32 v244, v231, v134
	ds_bpermute_b32 v245, v231, v135
	ds_bpermute_b32 v246, v231, v136
	s_waitcnt lgkmcnt(0)
	v_subrev_u32_e32 v246, s82, v246
	global_store_dwordx4 v246, v[242:245], s[82:83] offset:64
	s_cbranch_vccnz .LBB0_338
	s_branch .LBB0_386
.LBB0_384:
	s_and_b64 vcc, exec, s[40:41]
	s_cbranch_vccz .LBB0_383
	v_lshlrev_b32_e32 v155, 2, v177
	global_load_dwordx4 v[136:139], v155, s[44:45]
	global_load_dwordx4 v[132:135], v155, s[44:45] offset:16
	s_waitcnt lgkmcnt(0)
	v_mul_f32_e32 v160, v128, v154
	v_mul_f32_e32 v161, v129, v154
	v_mul_f32_e32 v166, v130, v154
	v_mul_f32_e32 v167, v131, v154
	v_mul_f32_e32 v168, v124, v154
	v_mul_f32_e32 v169, v125, v154
	v_mul_f32_e32 v170, v126, v154
	v_mul_f32_e32 v171, v127, v154
	global_load_dwordx4 v[124:127], v155, s[44:45] offset:144
	global_load_dwordx4 v[128:131], v155, s[44:45] offset:128
	v_ashrrev_i32_e32 v153, 31, v152
	v_lshlrev_b64 v[158:159], 12, v[152:153]
	v_max_f32_e32 v153, 0xc2a00000, v160
	v_max_f32_e32 v155, 0xc2a00000, v161
	v_max_f32_e32 v160, 0xc2a00000, v166
	v_max_f32_e32 v161, 0xc2a00000, v167
	v_max_f32_e32 v166, 0xc2a00000, v168
	v_max_f32_e32 v167, 0xc2a00000, v169
	v_max_f32_e32 v168, 0xc2a00000, v170
	v_max_f32_e32 v169, 0xc2a00000, v171
	v_mul_f32_e32 v153, 0xbfb8aa3b, v153
	v_mul_f32_e32 v155, 0xbfb8aa3b, v155
	v_mul_f32_e32 v168, 0xbfb8aa3b, v168
	v_mul_f32_e32 v169, 0xbfb8aa3b, v169
	v_exp_f32_e32 v153, v153
	v_exp_f32_e32 v155, v155
	v_mul_f32_e32 v160, 0xbfb8aa3b, v160
	v_mul_f32_e32 v161, 0xbfb8aa3b, v161
	v_exp_f32_e32 v168, v168
	v_exp_f32_e32 v169, v169
	v_exp_f32_e32 v160, v160
	v_exp_f32_e32 v161, v161
	v_mul_f32_e32 v120, v120, v154
	v_max_f32_e32 v120, 0xc2a00000, v120
	v_add_f32_e32 v153, 1.0, v153
	v_add_f32_e32 v155, 1.0, v155
	v_mul_f32_e32 v121, v121, v154
	v_lshlrev_b32_e32 v114, 1, v177
	v_mul_f32_e32 v166, 0xbfb8aa3b, v166
	v_mul_f32_e32 v167, 0xbfb8aa3b, v167
	v_lshl_add_u64 v[158:159], s[42:43], 0, v[158:159]
	v_add_f32_e32 v168, 1.0, v168
	v_add_f32_e32 v169, 1.0, v169
	v_rcp_f32_e32 v153, v153
	v_rcp_f32_e32 v181, v155
	v_mul_f32_e32 v120, 0xbfb8aa3b, v120
	v_max_f32_e32 v121, 0xc2a00000, v121
	v_exp_f32_e32 v170, v166
	v_exp_f32_e32 v171, v167
	v_lshl_add_u64 v[166:167], v[158:159], 0, v[114:115]
	v_add_f32_e32 v158, 1.0, v160
	v_add_f32_e32 v159, 1.0, v161
	v_rcp_f32_e32 v168, v168
	v_rcp_f32_e32 v182, v169
	v_exp_f32_e32 v120, v120
	v_mul_f32_e32 v121, 0xbfb8aa3b, v121
	v_rcp_f32_e32 v158, v158
	v_rcp_f32_e32 v159, v159
	v_exp_f32_e32 v121, v121
	v_add_f32_e32 v120, 1.0, v120
	v_rcp_f32_e32 v120, v120
	v_mul_f32_e32 v116, v116, v154
	v_add_f32_e32 v121, 1.0, v121
	v_rcp_f32_e32 v121, v121
	v_add_f32_e32 v160, 1.0, v170
	v_add_f32_e32 v161, 1.0, v171
	v_max_f32_e32 v116, 0xc2a00000, v116
	v_mul_f32_e32 v117, v117, v154
	v_rcp_f32_e32 v160, v160
	v_rcp_f32_e32 v161, v161
	v_mul_f32_e32 v116, 0xbfb8aa3b, v116
	v_max_f32_e32 v117, 0xc2a00000, v117
	v_exp_f32_e32 v116, v116
	v_mul_f32_e32 v117, 0xbfb8aa3b, v117
	v_exp_f32_e32 v117, v117
	s_mov_b64 s[14:15], 0x80000
	v_add_f32_e32 v116, 1.0, v116
	v_rcp_f32_e32 v116, v116
	v_add_f32_e32 v117, 1.0, v117
	s_waitcnt vmcnt(0)
	v_sub_f32_e32 v180, 1.0, v136
	v_sub_f32_e32 v179, 1.0, v137
	v_sub_f32_e32 v169, 1.0, v134
	v_sub_f32_e32 v155, 1.0, v135
	v_fma_f32 v153, v180, v153, v136
	v_fma_f32 v181, v179, v181, v137
	v_sub_f32_e32 v178, 1.0, v138
	v_sub_f32_e32 v177, 1.0, v139
	v_fma_f32 v168, v169, v168, v134
	v_fma_f32 v182, v155, v182, v135
	v_log_f32_e32 v153, v153
	v_log_f32_e32 v181, v181
	v_fma_f32 v158, v178, v158, v138
	v_fma_f32 v159, v177, v159, v139
	v_log_f32_e32 v168, v168
	v_log_f32_e32 v182, v182
	v_log_f32_e32 v158, v158
	v_log_f32_e32 v159, v159
	v_cvt_pk_f16_f32 v194, v153, v181
	v_sub_f32_e32 v153, 1.0, v128
	v_cvt_pk_f16_f32 v197, v168, v182
	v_fma_f32 v120, v153, v120, v128
	v_sub_f32_e32 v168, 1.0, v129
	v_cvt_pk_f16_f32 v195, v158, v159
	v_log_f32_e32 v158, v120
	v_fma_f32 v120, v168, v121, v129
	v_log_f32_e32 v159, v120
	v_mul_f32_e32 v120, v122, v154
	v_max_f32_e32 v120, 0xc2a00000, v120
	v_mul_f32_e32 v121, v123, v154
	v_mul_f32_e32 v120, 0xbfb8aa3b, v120
	v_max_f32_e32 v121, 0xc2a00000, v121
	v_exp_f32_e32 v120, v120
	v_mul_f32_e32 v121, 0xbfb8aa3b, v121
	v_exp_f32_e32 v122, v121
	v_sub_f32_e32 v171, 1.0, v132
	v_sub_f32_e32 v170, 1.0, v133
	v_add_f32_e32 v120, 1.0, v120
	v_fma_f32 v160, v171, v160, v132
	v_fma_f32 v161, v170, v161, v133
	v_rcp_f32_e32 v120, v120
	v_add_f32_e32 v122, 1.0, v122
	v_log_f32_e32 v160, v160
	v_log_f32_e32 v161, v161
	v_rcp_f32_e32 v123, v122
	v_sub_f32_e32 v121, 1.0, v130
	v_rcp_f32_e32 v117, v117
	v_fma_f32 v120, v121, v120, v130
	v_sub_f32_e32 v122, 1.0, v131
	v_cvt_pk_f16_f32 v196, v160, v161
	v_log_f32_e32 v160, v120
	v_fma_f32 v120, v122, v123, v131
	v_sub_f32_e32 v123, 1.0, v124
	v_log_f32_e32 v161, v120
	v_fma_f32 v116, v123, v116, v124
	v_sub_f32_e32 v120, 1.0, v125
	v_log_f32_e32 v181, v116
	v_fma_f32 v116, v120, v117, v125
	v_log_f32_e32 v182, v116
	v_mul_f32_e32 v116, v118, v154
	v_max_f32_e32 v116, 0xc2a00000, v116
	v_mul_f32_e32 v117, v119, v154
	v_mul_f32_e32 v116, 0xbfb8aa3b, v116
	v_max_f32_e32 v117, 0xc2a00000, v117
	v_exp_f32_e32 v116, v116
	v_mul_f32_e32 v117, 0xbfb8aa3b, v117
	v_exp_f32_e32 v117, v117
	v_sub_f32_e32 v118, 1.0, v126
	v_add_f32_e32 v116, 1.0, v116
	v_rcp_f32_e32 v116, v116
	v_add_f32_e32 v117, 1.0, v117
	v_rcp_f32_e32 v117, v117
	v_sub_f32_e32 v119, 1.0, v127
	v_fma_f32 v116, v118, v116, v126
	v_log_f32_e32 v154, v116
	v_fma_f32 v116, v119, v117, v127
	v_log_f32_e32 v183, v116
	ds_read2_b32 v[116:117], v176 offset0:16 offset1:32
	v_subrev_u32_e32 v240, s82, v166
	ds_bpermute_b32 v232, v252, v194
	ds_bpermute_b32 v236, v253, v194
	ds_bpermute_b32 v233, v252, v195
	ds_bpermute_b32 v237, v253, v195
	ds_bpermute_b32 v234, v252, v196
	ds_bpermute_b32 v238, v253, v196
	ds_bpermute_b32 v235, v252, v197
	ds_bpermute_b32 v239, v253, v197
	ds_bpermute_b32 v241, v253, v240
	ds_bpermute_b32 v240, v252, v240
	s_waitcnt lgkmcnt(0)
	v_mul_f32_e32 v106, v106, v116
	v_max_f32_e32 v106, 0xc2a00000, v106
	v_mul_f32_e32 v106, 0xbfb8aa3b, v106
	v_exp_f32_e32 v106, v106
	v_mul_f32_e32 v110, v110, v116
	v_max_f32_e32 v110, 0xc2a00000, v110
	v_mul_f32_e32 v111, v111, v116
	v_mul_f32_e32 v110, 0xbfb8aa3b, v110
	v_max_f32_e32 v111, 0xc2a00000, v111
	v_mul_f32_e32 v107, v107, v116
	v_exp_f32_e32 v110, v110
	v_mul_f32_e32 v111, 0xbfb8aa3b, v111
	v_add_f32_e32 v106, 1.0, v106
	v_max_f32_e32 v107, 0xc2a00000, v107
	v_exp_f32_e32 v111, v111
	v_rcp_f32_e32 v106, v106
	v_mul_f32_e32 v107, 0xbfb8aa3b, v107
	v_exp_f32_e32 v107, v107
	v_cvt_pk_f16_f32 v194, v158, v159
	v_or_b32_e32 v158, 16, v152
	v_add_f32_e32 v110, 1.0, v110
	v_mul_f32_e32 v112, v112, v116
	v_mul_f32_e32 v113, v113, v116
	v_cvt_pk_f16_f32 v197, v154, v183
	v_ashrrev_i32_e32 v159, 31, v158
	v_rcp_f32_e32 v154, v110
	v_add_f32_e32 v110, 1.0, v111
	v_max_f32_e32 v112, 0xc2a00000, v112
	v_max_f32_e32 v113, 0xc2a00000, v113
	v_fma_f32 v106, v171, v106, v132
	v_cvt_pk_f16_f32 v195, v160, v161
	v_rcp_f32_e32 v160, v110
	v_lshlrev_b64 v[110:111], 12, v[158:159]
	v_mul_f32_e32 v112, 0xbfb8aa3b, v112
	v_mul_f32_e32 v113, 0xbfb8aa3b, v113
	v_log_f32_e32 v159, v106
	v_add_f32_e32 v106, 1.0, v107
	v_mul_f32_e32 v107, v108, v116
	v_exp_f32_e32 v112, v112
	v_exp_f32_e32 v113, v113
	v_max_f32_e32 v107, 0xc2a00000, v107
	v_mul_f32_e32 v108, v109, v116
	v_mul_f32_e32 v107, 0xbfb8aa3b, v107
	v_max_f32_e32 v108, 0xc2a00000, v108
	v_exp_f32_e32 v107, v107
	v_mul_f32_e32 v108, 0xbfb8aa3b, v108
	v_exp_f32_e32 v108, v108
	v_add_f32_e32 v112, 1.0, v112
	v_add_f32_e32 v113, 1.0, v113
	v_rcp_f32_e32 v112, v112
	v_rcp_f32_e32 v113, v113
	v_mul_f32_e32 v98, v98, v116
	v_rcp_f32_e32 v106, v106
	v_add_f32_e32 v107, 1.0, v107
	v_max_f32_e32 v98, 0xc2a00000, v98
	v_rcp_f32_e32 v107, v107
	v_add_f32_e32 v108, 1.0, v108
	v_mul_f32_e32 v98, 0xbfb8aa3b, v98
	v_rcp_f32_e32 v108, v108
	v_exp_f32_e32 v98, v98
	v_fma_f32 v112, v178, v112, v138
	v_fma_f32 v113, v177, v113, v139
	v_log_f32_e32 v112, v112
	v_log_f32_e32 v113, v113
	v_fma_f32 v106, v170, v106, v133
	v_log_f32_e32 v109, v106
	v_fma_f32 v106, v169, v107, v134
	v_mul_f32_e32 v102, v102, v116
	v_mul_f32_e32 v99, v99, v116
	v_fma_f32 v154, v180, v154, v136
	v_fma_f32 v158, v179, v160, v137
	v_log_f32_e32 v160, v106
	v_fma_f32 v106, v155, v108, v135
	v_max_f32_e32 v102, 0xc2a00000, v102
	v_add_f32_e32 v98, 1.0, v98
	v_max_f32_e32 v99, 0xc2a00000, v99
	v_log_f32_e32 v154, v154
	v_log_f32_e32 v158, v158
	v_log_f32_e32 v161, v106
	v_mul_f32_e32 v102, 0xbfb8aa3b, v102
	v_rcp_f32_e32 v98, v98
	v_mul_f32_e32 v99, 0xbfb8aa3b, v99
	v_cvt_pk_f16_f32 v107, v112, v113
	v_exp_f32_e32 v112, v102
	v_mul_f32_e32 v102, v103, v116
	v_exp_f32_e32 v99, v99
	v_max_f32_e32 v102, 0xc2a00000, v102
	v_lshl_add_u64 v[110:111], s[42:43], 0, v[110:111]
	v_mul_f32_e32 v102, 0xbfb8aa3b, v102
	v_cvt_pk_f16_f32 v106, v154, v158
	v_cvt_pk_f16_f32 v108, v159, v109
	v_cvt_pk_f16_f32 v109, v160, v161
	v_exp_f32_e32 v113, v102
	v_lshl_add_u64 v[102:103], v[110:111], 0, v[114:115]
	v_fma_f32 v98, v123, v98, v124
	v_subrev_u32_e32 v250, s82, v102
	ds_bpermute_b32 v242, v252, v106
	ds_bpermute_b32 v246, v253, v106
	ds_bpermute_b32 v243, v252, v107
	ds_bpermute_b32 v247, v253, v107
	ds_bpermute_b32 v244, v252, v108
	ds_bpermute_b32 v248, v253, v108
	ds_bpermute_b32 v245, v252, v109
	ds_bpermute_b32 v249, v253, v109
	ds_bpermute_b32 v251, v253, v250
	ds_bpermute_b32 v250, v252, v250
	s_waitcnt lgkmcnt(0)
	v_cndmask_b32_e64 v232, v232, v242, s[100:101]
	v_cndmask_b32_e64 v233, v233, v243, s[100:101]
	v_cndmask_b32_e64 v234, v234, v244, s[100:101]
	v_cndmask_b32_e64 v235, v235, v245, s[100:101]
	v_cndmask_b32_e64 v236, v236, v246, s[100:101]
	v_cndmask_b32_e64 v237, v237, v247, s[100:101]
	v_cndmask_b32_e64 v238, v238, v248, s[100:101]
	v_cndmask_b32_e64 v239, v239, v249, s[100:101]
	v_cndmask_b32_e64 v240, v240, v250, s[100:101]
	v_cndmask_b32_e64 v241, v241, v251, s[100:101]
	global_store_dwordx4 v240, v[232:235], s[82:83]
	global_store_dwordx4 v241, v[236:239], s[82:83]
	v_mul_f32_e32 v104, v104, v116
	v_mul_f32_e32 v105, v105, v116
	v_log_f32_e32 v108, v98
	v_add_f32_e32 v98, 1.0, v99
	v_mul_f32_e32 v99, v100, v116
	v_max_f32_e32 v99, 0xc2a00000, v99
	v_mul_f32_e32 v100, v101, v116
	v_max_f32_e32 v104, 0xc2a00000, v104
	v_max_f32_e32 v105, 0xc2a00000, v105
	v_mul_f32_e32 v99, 0xbfb8aa3b, v99
	v_max_f32_e32 v100, 0xc2a00000, v100
	v_mul_f32_e32 v104, 0xbfb8aa3b, v104
	v_mul_f32_e32 v105, 0xbfb8aa3b, v105
	v_exp_f32_e32 v99, v99
	v_mul_f32_e32 v100, 0xbfb8aa3b, v100
	v_exp_f32_e32 v104, v104
	v_exp_f32_e32 v105, v105
	v_exp_f32_e32 v100, v100
	v_rcp_f32_e32 v98, v98
	v_add_f32_e32 v99, 1.0, v99
	v_add_f32_e32 v110, 1.0, v112
	v_add_f32_e32 v111, 1.0, v113
	v_add_f32_e32 v104, 1.0, v104
	v_add_f32_e32 v105, 1.0, v105
	v_rcp_f32_e32 v99, v99
	v_add_f32_e32 v100, 1.0, v100
	v_rcp_f32_e32 v110, v110
	v_rcp_f32_e32 v111, v111
	v_rcp_f32_e32 v104, v104
	v_rcp_f32_e32 v105, v105
	v_rcp_f32_e32 v100, v100
	v_mul_f32_e32 v90, v90, v117
	v_fma_f32 v98, v120, v98, v125
	v_mul_f32_e32 v94, v94, v117
	v_max_f32_e32 v90, 0xc2a00000, v90
	v_log_f32_e32 v101, v98
	v_fma_f32 v98, v118, v99, v126
	v_max_f32_e32 v94, 0xc2a00000, v94
	v_mul_f32_e32 v90, 0xbfb8aa3b, v90
	v_fma_f32 v106, v153, v110, v128
	v_fma_f32 v107, v168, v111, v129
	v_fma_f32 v104, v121, v104, v130
	v_fma_f32 v105, v122, v105, v131
	v_log_f32_e32 v109, v98
	v_fma_f32 v98, v119, v100, v127
	v_mul_f32_e32 v94, 0xbfb8aa3b, v94
	v_exp_f32_e32 v90, v90
	v_log_f32_e32 v106, v106
	v_log_f32_e32 v107, v107
	v_log_f32_e32 v104, v104
	v_log_f32_e32 v105, v105
	v_log_f32_e32 v110, v98
	v_exp_f32_e32 v94, v94
	v_mul_f32_e32 v95, v95, v117
	v_max_f32_e32 v95, 0xc2a00000, v95
	v_mul_f32_e32 v91, v91, v117
	v_mul_f32_e32 v95, 0xbfb8aa3b, v95
	v_add_f32_e32 v90, 1.0, v90
	v_max_f32_e32 v91, 0xc2a00000, v91
	v_cvt_pk_f16_f32 v98, v106, v107
	v_cvt_pk_f16_f32 v99, v104, v105
	v_cvt_pk_f16_f32 v100, v108, v101
	v_cvt_pk_f16_f32 v101, v109, v110
	v_exp_f32_e32 v95, v95
	v_add_f32_e32 v94, 1.0, v94
	v_rcp_f32_e32 v90, v90
	v_mul_f32_e32 v91, 0xbfb8aa3b, v91
	v_subrev_u32_e32 v240, s82, v102
	v_add_u32_e32 v240, 0x40, v240
	ds_bpermute_b32 v232, v252, v98
	ds_bpermute_b32 v236, v253, v98
	ds_bpermute_b32 v233, v252, v99
	ds_bpermute_b32 v237, v253, v99
	ds_bpermute_b32 v234, v252, v100
	ds_bpermute_b32 v238, v253, v100
	ds_bpermute_b32 v235, v252, v101
	ds_bpermute_b32 v239, v253, v101
	ds_bpermute_b32 v241, v253, v240
	ds_bpermute_b32 v240, v252, v240
	v_exp_f32_e32 v91, v91
	v_fma_f32 v90, v171, v90, v132
	v_rcp_f32_e32 v100, v94
	v_or_b32_e32 v98, 32, v152
	v_ashrrev_i32_e32 v99, 31, v98
	v_add_f32_e32 v94, 1.0, v95
	v_rcp_f32_e32 v101, v94
	v_lshlrev_b64 v[94:95], 12, v[98:99]
	v_fma_f32 v98, v180, v100, v136
	v_log_f32_e32 v100, v90
	v_add_f32_e32 v90, 1.0, v91
	v_mul_f32_e32 v91, v92, v117
	v_mul_f32_e32 v96, v96, v117
	v_mul_f32_e32 v97, v97, v117
	v_max_f32_e32 v91, 0xc2a00000, v91
	v_mul_f32_e32 v92, v93, v117
	v_max_f32_e32 v96, 0xc2a00000, v96
	v_max_f32_e32 v97, 0xc2a00000, v97
	v_mul_f32_e32 v91, 0xbfb8aa3b, v91
	v_max_f32_e32 v92, 0xc2a00000, v92
	v_mul_f32_e32 v96, 0xbfb8aa3b, v96
	v_mul_f32_e32 v97, 0xbfb8aa3b, v97
	v_exp_f32_e32 v91, v91
	v_mul_f32_e32 v92, 0xbfb8aa3b, v92
	v_exp_f32_e32 v96, v96
	v_exp_f32_e32 v97, v97
	v_exp_f32_e32 v92, v92
	v_mul_f32_e32 v82, v82, v117
	v_rcp_f32_e32 v90, v90
	v_add_f32_e32 v91, 1.0, v91
	v_max_f32_e32 v82, 0xc2a00000, v82
	v_add_f32_e32 v96, 1.0, v96
	v_add_f32_e32 v97, 1.0, v97
	v_rcp_f32_e32 v91, v91
	v_add_f32_e32 v92, 1.0, v92
	v_mul_f32_e32 v82, 0xbfb8aa3b, v82
	v_rcp_f32_e32 v96, v96
	v_rcp_f32_e32 v97, v97
	v_rcp_f32_e32 v92, v92
	v_exp_f32_e32 v82, v82
	v_fma_f32 v90, v170, v90, v133
	v_log_f32_e32 v93, v90
	v_fma_f32 v90, v169, v91, v134
	v_mul_f32_e32 v83, v83, v117
	v_fma_f32 v99, v179, v101, v137
	v_fma_f32 v96, v178, v96, v138
	v_fma_f32 v97, v177, v97, v139
	v_log_f32_e32 v101, v90
	v_fma_f32 v90, v155, v92, v135
	v_add_f32_e32 v82, 1.0, v82
	v_max_f32_e32 v83, 0xc2a00000, v83
	v_log_f32_e32 v98, v98
	v_log_f32_e32 v99, v99
	v_log_f32_e32 v96, v96
	v_log_f32_e32 v97, v97
	v_log_f32_e32 v102, v90
	v_rcp_f32_e32 v82, v82
	v_mul_f32_e32 v83, 0xbfb8aa3b, v83
	v_exp_f32_e32 v83, v83
	v_lshl_add_u64 v[94:95], s[42:43], 0, v[94:95]
	v_cvt_pk_f16_f32 v90, v98, v99
	v_cvt_pk_f16_f32 v91, v96, v97
	v_cvt_pk_f16_f32 v92, v100, v93
	v_cvt_pk_f16_f32 v93, v101, v102
	v_lshl_add_u64 v[94:95], v[94:95], 0, v[114:115]
	v_fma_f32 v82, v123, v82, v124
	v_subrev_u32_e32 v250, s82, v94
	ds_bpermute_b32 v242, v252, v90
	ds_bpermute_b32 v246, v253, v90
	ds_bpermute_b32 v243, v252, v91
	ds_bpermute_b32 v247, v253, v91
	ds_bpermute_b32 v244, v252, v92
	ds_bpermute_b32 v248, v253, v92
	ds_bpermute_b32 v245, v252, v93
	ds_bpermute_b32 v249, v253, v93
	ds_bpermute_b32 v251, v253, v250
	ds_bpermute_b32 v250, v252, v250
	s_waitcnt lgkmcnt(0)
	v_cndmask_b32_e64 v232, v232, v242, s[100:101]
	v_cndmask_b32_e64 v233, v233, v243, s[100:101]
	v_cndmask_b32_e64 v234, v234, v244, s[100:101]
	v_cndmask_b32_e64 v235, v235, v245, s[100:101]
	v_cndmask_b32_e64 v236, v236, v246, s[100:101]
	v_cndmask_b32_e64 v237, v237, v247, s[100:101]
	v_cndmask_b32_e64 v238, v238, v248, s[100:101]
	v_cndmask_b32_e64 v239, v239, v249, s[100:101]
	v_cndmask_b32_e64 v240, v240, v250, s[100:101]
	v_cndmask_b32_e64 v241, v241, v251, s[100:101]
	global_store_dwordx4 v240, v[232:235], s[82:83]
	global_store_dwordx4 v241, v[236:239], s[82:83]
	v_mul_f32_e32 v86, v86, v117
	v_mul_f32_e32 v87, v87, v117
	v_log_f32_e32 v90, v82
	v_add_f32_e32 v82, 1.0, v83
	v_mul_f32_e32 v83, v84, v117
	v_max_f32_e32 v83, 0xc2a00000, v83
	v_mul_f32_e32 v84, v85, v117
	v_mul_f32_e32 v83, 0xbfb8aa3b, v83
	v_max_f32_e32 v84, 0xc2a00000, v84
	v_exp_f32_e32 v83, v83
	v_mul_f32_e32 v84, 0xbfb8aa3b, v84
	v_exp_f32_e32 v84, v84
	v_rcp_f32_e32 v82, v82
	v_add_f32_e32 v83, 1.0, v83
	v_rcp_f32_e32 v83, v83
	v_add_f32_e32 v84, 1.0, v84
	v_rcp_f32_e32 v84, v84
	v_mul_f32_e32 v88, v88, v117
	v_mul_f32_e32 v89, v89, v117
	v_max_f32_e32 v86, 0xc2a00000, v86
	v_max_f32_e32 v87, 0xc2a00000, v87
	v_max_f32_e32 v88, 0xc2a00000, v88
	v_max_f32_e32 v89, 0xc2a00000, v89
	v_fma_f32 v82, v120, v82, v125
	v_mul_f32_e32 v86, 0xbfb8aa3b, v86
	v_mul_f32_e32 v87, 0xbfb8aa3b, v87
	v_mul_f32_e32 v88, 0xbfb8aa3b, v88
	v_mul_f32_e32 v89, 0xbfb8aa3b, v89
	v_log_f32_e32 v91, v82
	v_fma_f32 v82, v118, v83, v126
	v_exp_f32_e32 v86, v86
	v_exp_f32_e32 v87, v87
	v_exp_f32_e32 v88, v88
	v_exp_f32_e32 v89, v89
	v_log_f32_e32 v92, v82
	v_fma_f32 v82, v119, v84, v127
	v_log_f32_e32 v93, v82
	ds_read2_b32 v[82:83], v176 offset0:48 offset1:128
	v_add_f32_e32 v86, 1.0, v86
	v_add_f32_e32 v87, 1.0, v87
	v_add_f32_e32 v88, 1.0, v88
	v_add_f32_e32 v89, 1.0, v89
	v_rcp_f32_e32 v86, v86
	v_rcp_f32_e32 v87, v87
	v_rcp_f32_e32 v88, v88
	v_rcp_f32_e32 v89, v89
	s_waitcnt lgkmcnt(0)
	v_mul_f32_e32 v74, v74, v82
	v_mul_f32_e32 v78, v78, v82
	v_max_f32_e32 v74, 0xc2a00000, v74
	v_max_f32_e32 v78, 0xc2a00000, v78
	v_mul_f32_e32 v74, 0xbfb8aa3b, v74
	v_fma_f32 v86, v153, v86, v128
	v_fma_f32 v87, v168, v87, v129
	v_fma_f32 v88, v121, v88, v130
	v_fma_f32 v89, v122, v89, v131
	v_mul_f32_e32 v78, 0xbfb8aa3b, v78
	v_exp_f32_e32 v74, v74
	v_log_f32_e32 v86, v86
	v_log_f32_e32 v87, v87
	v_log_f32_e32 v88, v88
	v_log_f32_e32 v89, v89
	v_exp_f32_e32 v78, v78
	v_mul_f32_e32 v79, v79, v82
	v_max_f32_e32 v79, 0xc2a00000, v79
	v_mul_f32_e32 v75, v75, v82
	v_mul_f32_e32 v79, 0xbfb8aa3b, v79
	v_add_f32_e32 v74, 1.0, v74
	v_max_f32_e32 v75, 0xc2a00000, v75
	v_cvt_pk_f16_f32 v84, v86, v87
	v_cvt_pk_f16_f32 v85, v88, v89
	v_cvt_pk_f16_f32 v86, v90, v91
	v_cvt_pk_f16_f32 v87, v92, v93
	v_exp_f32_e32 v79, v79
	v_add_f32_e32 v78, 1.0, v78
	v_rcp_f32_e32 v74, v74
	v_mul_f32_e32 v75, 0xbfb8aa3b, v75
	v_subrev_u32_e32 v240, s82, v94
	v_add_u32_e32 v240, 0x40, v240
	ds_bpermute_b32 v232, v252, v84
	ds_bpermute_b32 v236, v253, v84
	ds_bpermute_b32 v233, v252, v85
	ds_bpermute_b32 v237, v253, v85
	ds_bpermute_b32 v234, v252, v86
	ds_bpermute_b32 v238, v253, v86
	ds_bpermute_b32 v235, v252, v87
	ds_bpermute_b32 v239, v253, v87
	ds_bpermute_b32 v241, v253, v240
	ds_bpermute_b32 v240, v252, v240
	v_exp_f32_e32 v75, v75
	v_mul_f32_e32 v80, v80, v82
	v_rcp_f32_e32 v86, v78
	v_or_b32_e32 v84, 48, v152
	v_mul_f32_e32 v81, v81, v82
	v_ashrrev_i32_e32 v85, 31, v84
	v_add_f32_e32 v78, 1.0, v79
	v_max_f32_e32 v80, 0xc2a00000, v80
	v_max_f32_e32 v81, 0xc2a00000, v81
	v_fma_f32 v74, v171, v74, v132
	v_rcp_f32_e32 v87, v78
	v_lshlrev_b64 v[78:79], 12, v[84:85]
	v_fma_f32 v84, v180, v86, v136
	v_mul_f32_e32 v80, 0xbfb8aa3b, v80
	v_mul_f32_e32 v81, 0xbfb8aa3b, v81
	v_log_f32_e32 v86, v74
	v_add_f32_e32 v74, 1.0, v75
	v_mul_f32_e32 v75, v76, v82
	v_exp_f32_e32 v80, v80
	v_exp_f32_e32 v81, v81
	v_max_f32_e32 v75, 0xc2a00000, v75
	v_mul_f32_e32 v76, v77, v82
	v_mul_f32_e32 v75, 0xbfb8aa3b, v75
	v_max_f32_e32 v76, 0xc2a00000, v76
	v_exp_f32_e32 v75, v75
	v_mul_f32_e32 v76, 0xbfb8aa3b, v76
	v_exp_f32_e32 v76, v76
	v_add_f32_e32 v80, 1.0, v80
	v_add_f32_e32 v81, 1.0, v81
	v_rcp_f32_e32 v80, v80
	v_rcp_f32_e32 v81, v81
	v_mul_f32_e32 v66, v66, v82
	v_rcp_f32_e32 v74, v74
	v_add_f32_e32 v75, 1.0, v75
	v_max_f32_e32 v66, 0xc2a00000, v66
	v_rcp_f32_e32 v75, v75
	v_add_f32_e32 v76, 1.0, v76
	v_mul_f32_e32 v66, 0xbfb8aa3b, v66
	v_rcp_f32_e32 v76, v76
	v_exp_f32_e32 v66, v66
	v_fma_f32 v80, v178, v80, v138
	v_fma_f32 v81, v177, v81, v139
	v_log_f32_e32 v80, v80
	v_log_f32_e32 v81, v81
	v_fma_f32 v74, v170, v74, v133
	v_log_f32_e32 v77, v74
	v_fma_f32 v74, v169, v75, v134
	v_mul_f32_e32 v70, v70, v82
	v_mul_f32_e32 v67, v67, v82
	v_fma_f32 v85, v179, v87, v137
	v_log_f32_e32 v87, v74
	v_fma_f32 v74, v155, v76, v135
	v_max_f32_e32 v70, 0xc2a00000, v70
	v_add_f32_e32 v66, 1.0, v66
	v_max_f32_e32 v67, 0xc2a00000, v67
	v_log_f32_e32 v84, v84
	v_log_f32_e32 v85, v85
	v_log_f32_e32 v88, v74
	v_mul_f32_e32 v70, 0xbfb8aa3b, v70
	v_rcp_f32_e32 v66, v66
	v_mul_f32_e32 v67, 0xbfb8aa3b, v67
	v_cvt_pk_f16_f32 v75, v80, v81
	v_exp_f32_e32 v80, v70
	v_mul_f32_e32 v70, v71, v82
	v_exp_f32_e32 v67, v67
	v_max_f32_e32 v70, 0xc2a00000, v70
	v_lshl_add_u64 v[78:79], s[42:43], 0, v[78:79]
	v_mul_f32_e32 v70, 0xbfb8aa3b, v70
	v_cvt_pk_f16_f32 v74, v84, v85
	v_cvt_pk_f16_f32 v76, v86, v77
	v_cvt_pk_f16_f32 v77, v87, v88
	v_exp_f32_e32 v81, v70
	v_lshl_add_u64 v[70:71], v[78:79], 0, v[114:115]
	v_fma_f32 v66, v123, v66, v124
	v_subrev_u32_e32 v250, s82, v70
	ds_bpermute_b32 v242, v252, v74
	ds_bpermute_b32 v246, v253, v74
	ds_bpermute_b32 v243, v252, v75
	ds_bpermute_b32 v247, v253, v75
	ds_bpermute_b32 v244, v252, v76
	ds_bpermute_b32 v248, v253, v76
	ds_bpermute_b32 v245, v252, v77
	ds_bpermute_b32 v249, v253, v77
	ds_bpermute_b32 v251, v253, v250
	ds_bpermute_b32 v250, v252, v250
	s_waitcnt lgkmcnt(0)
	v_cndmask_b32_e64 v232, v232, v242, s[100:101]
	v_cndmask_b32_e64 v233, v233, v243, s[100:101]
	v_cndmask_b32_e64 v234, v234, v244, s[100:101]
	v_cndmask_b32_e64 v235, v235, v245, s[100:101]
	v_cndmask_b32_e64 v236, v236, v246, s[100:101]
	v_cndmask_b32_e64 v237, v237, v247, s[100:101]
	v_cndmask_b32_e64 v238, v238, v248, s[100:101]
	v_cndmask_b32_e64 v239, v239, v249, s[100:101]
	v_cndmask_b32_e64 v240, v240, v250, s[100:101]
	v_cndmask_b32_e64 v241, v241, v251, s[100:101]
	global_store_dwordx4 v240, v[232:235], s[82:83]
	global_store_dwordx4 v241, v[236:239], s[82:83]
	v_mul_f32_e32 v72, v72, v82
	v_mul_f32_e32 v73, v73, v82
	v_log_f32_e32 v76, v66
	v_add_f32_e32 v66, 1.0, v67
	v_mul_f32_e32 v67, v68, v82
	v_max_f32_e32 v67, 0xc2a00000, v67
	v_mul_f32_e32 v68, v69, v82
	v_max_f32_e32 v72, 0xc2a00000, v72
	v_max_f32_e32 v73, 0xc2a00000, v73
	v_mul_f32_e32 v67, 0xbfb8aa3b, v67
	v_max_f32_e32 v68, 0xc2a00000, v68
	v_mul_f32_e32 v72, 0xbfb8aa3b, v72
	v_mul_f32_e32 v73, 0xbfb8aa3b, v73
	v_exp_f32_e32 v67, v67
	v_mul_f32_e32 v68, 0xbfb8aa3b, v68
	v_exp_f32_e32 v72, v72
	v_exp_f32_e32 v73, v73
	v_exp_f32_e32 v68, v68
	v_mul_f32_e32 v58, v58, v83
	v_rcp_f32_e32 v66, v66
	v_add_f32_e32 v67, 1.0, v67
	v_max_f32_e32 v58, 0xc2a00000, v58
	v_add_f32_e32 v78, 1.0, v80
	v_add_f32_e32 v79, 1.0, v81
	v_add_f32_e32 v72, 1.0, v72
	v_add_f32_e32 v73, 1.0, v73
	v_rcp_f32_e32 v67, v67
	v_add_f32_e32 v68, 1.0, v68
	v_mul_f32_e32 v58, 0xbfb8aa3b, v58
	v_rcp_f32_e32 v78, v78
	v_rcp_f32_e32 v79, v79
	v_rcp_f32_e32 v72, v72
	v_rcp_f32_e32 v73, v73
	v_rcp_f32_e32 v68, v68
	v_exp_f32_e32 v58, v58
	v_fma_f32 v66, v120, v66, v125
	v_log_f32_e32 v69, v66
	v_fma_f32 v66, v118, v67, v126
	v_mul_f32_e32 v59, v59, v83
	v_fma_f32 v74, v153, v78, v128
	v_fma_f32 v75, v168, v79, v129
	v_fma_f32 v72, v121, v72, v130
	v_fma_f32 v73, v122, v73, v131
	v_log_f32_e32 v77, v66
	v_fma_f32 v66, v119, v68, v127
	v_add_f32_e32 v58, 1.0, v58
	v_max_f32_e32 v59, 0xc2a00000, v59
	v_log_f32_e32 v74, v74
	v_log_f32_e32 v75, v75
	v_log_f32_e32 v72, v72
	v_log_f32_e32 v73, v73
	v_log_f32_e32 v78, v66
	v_rcp_f32_e32 v58, v58
	v_mul_f32_e32 v59, 0xbfb8aa3b, v59
	v_exp_f32_e32 v59, v59
	v_mul_f32_e32 v64, v64, v83
	v_mul_f32_e32 v65, v65, v83
	v_max_f32_e32 v64, 0xc2a00000, v64
	v_max_f32_e32 v65, 0xc2a00000, v65
	v_cvt_pk_f16_f32 v66, v74, v75
	v_cvt_pk_f16_f32 v67, v72, v73
	v_cvt_pk_f16_f32 v68, v76, v69
	v_mul_f32_e32 v62, v62, v83
	v_mul_f32_e32 v63, v63, v83
	v_cvt_pk_f16_f32 v69, v77, v78
	v_mul_f32_e32 v64, 0xbfb8aa3b, v64
	v_mul_f32_e32 v65, 0xbfb8aa3b, v65
	v_fma_f32 v58, v171, v58, v132
	v_max_f32_e32 v62, 0xc2a00000, v62
	v_max_f32_e32 v63, 0xc2a00000, v63
	v_subrev_u32_e32 v240, s82, v70
	v_add_u32_e32 v240, 0x40, v240
	ds_bpermute_b32 v232, v252, v66
	ds_bpermute_b32 v236, v253, v66
	ds_bpermute_b32 v233, v252, v67
	ds_bpermute_b32 v237, v253, v67
	ds_bpermute_b32 v234, v252, v68
	ds_bpermute_b32 v238, v253, v68
	ds_bpermute_b32 v235, v252, v69
	ds_bpermute_b32 v239, v253, v69
	ds_bpermute_b32 v241, v253, v240
	ds_bpermute_b32 v240, v252, v240
	v_exp_f32_e32 v64, v64
	v_exp_f32_e32 v65, v65
	v_log_f32_e32 v66, v58
	v_add_f32_e32 v58, 1.0, v59
	v_mul_f32_e32 v59, v60, v83
	v_mul_f32_e32 v62, 0xbfb8aa3b, v62
	v_mul_f32_e32 v63, 0xbfb8aa3b, v63
	v_max_f32_e32 v59, 0xc2a00000, v59
	v_mul_f32_e32 v60, v61, v83
	v_exp_f32_e32 v62, v62
	v_exp_f32_e32 v63, v63
	v_mul_f32_e32 v59, 0xbfb8aa3b, v59
	v_max_f32_e32 v60, 0xc2a00000, v60
	v_exp_f32_e32 v59, v59
	v_mul_f32_e32 v60, 0xbfb8aa3b, v60
	v_add_f32_e32 v64, 1.0, v64
	v_add_f32_e32 v65, 1.0, v65
	v_exp_f32_e32 v60, v60
	v_rcp_f32_e32 v64, v64
	v_rcp_f32_e32 v65, v65
	v_add_f32_e32 v62, 1.0, v62
	v_add_f32_e32 v63, 1.0, v63
	v_mul_f32_e32 v50, v50, v83
	v_rcp_f32_e32 v62, v62
	v_rcp_f32_e32 v63, v63
	v_rcp_f32_e32 v58, v58
	v_add_f32_e32 v59, 1.0, v59
	v_max_f32_e32 v50, 0xc2a00000, v50
	v_rcp_f32_e32 v59, v59
	v_add_f32_e32 v60, 1.0, v60
	v_mul_f32_e32 v50, 0xbfb8aa3b, v50
	v_fma_f32 v64, v178, v64, v138
	v_fma_f32 v65, v177, v65, v139
	v_rcp_f32_e32 v60, v60
	v_exp_f32_e32 v50, v50
	v_log_f32_e32 v64, v64
	v_log_f32_e32 v65, v65
	v_fma_f32 v62, v180, v62, v136
	v_fma_f32 v63, v179, v63, v137
	v_fma_f32 v58, v170, v58, v133
	v_mul_f32_e32 v54, v54, v83
	v_log_f32_e32 v62, v62
	v_log_f32_e32 v63, v63
	v_log_f32_e32 v61, v58
	v_fma_f32 v58, v169, v59, v134
	v_max_f32_e32 v54, 0xc2a00000, v54
	v_mul_f32_e32 v51, v51, v83
	v_log_f32_e32 v67, v58
	v_fma_f32 v58, v155, v60, v135
	v_mul_f32_e32 v54, 0xbfb8aa3b, v54
	v_add_f32_e32 v50, 1.0, v50
	v_max_f32_e32 v51, 0xc2a00000, v51
	v_log_f32_e32 v68, v58
	v_cvt_pk_f16_f32 v59, v64, v65
	v_exp_f32_e32 v64, v54
	v_mul_f32_e32 v54, v55, v83
	v_rcp_f32_e32 v50, v50
	v_mul_f32_e32 v51, 0xbfb8aa3b, v51
	v_max_f32_e32 v54, 0xc2a00000, v54
	v_exp_f32_e32 v51, v51
	v_cvt_pk_f16_f32 v58, v62, v63
	v_lshl_add_u64 v[62:63], v[166:167], 0, s[14:15]
	v_mul_f32_e32 v54, 0xbfb8aa3b, v54
	s_mov_b32 s14, 0x80000
	v_exp_f32_e32 v65, v54
	v_add_co_u32_e32 v54, vcc, s14, v166
	v_cvt_pk_f16_f32 v60, v66, v61
	v_cvt_pk_f16_f32 v61, v67, v68
	v_addc_co_u32_e32 v55, vcc, 0, v167, vcc
	v_fma_f32 v50, v123, v50, v124
	v_subrev_u32_e32 v250, s82, v54
	ds_bpermute_b32 v242, v252, v58
	ds_bpermute_b32 v246, v253, v58
	ds_bpermute_b32 v243, v252, v59
	ds_bpermute_b32 v247, v253, v59
	ds_bpermute_b32 v244, v252, v60
	ds_bpermute_b32 v248, v253, v60
	ds_bpermute_b32 v245, v252, v61
	ds_bpermute_b32 v249, v253, v61
	ds_bpermute_b32 v251, v253, v250
	ds_bpermute_b32 v250, v252, v250
	s_waitcnt lgkmcnt(0)
	v_cndmask_b32_e64 v232, v232, v242, s[100:101]
	v_cndmask_b32_e64 v233, v233, v243, s[100:101]
	v_cndmask_b32_e64 v234, v234, v244, s[100:101]
	v_cndmask_b32_e64 v235, v235, v245, s[100:101]
	v_cndmask_b32_e64 v236, v236, v246, s[100:101]
	v_cndmask_b32_e64 v237, v237, v247, s[100:101]
	v_cndmask_b32_e64 v238, v238, v248, s[100:101]
	v_cndmask_b32_e64 v239, v239, v249, s[100:101]
	v_cndmask_b32_e64 v240, v240, v250, s[100:101]
	v_cndmask_b32_e64 v241, v241, v251, s[100:101]
	global_store_dwordx4 v240, v[232:235], s[82:83]
	global_store_dwordx4 v241, v[236:239], s[82:83]
	v_mul_f32_e32 v56, v56, v83
	v_mul_f32_e32 v57, v57, v83
	v_log_f32_e32 v58, v50
	v_add_f32_e32 v50, 1.0, v51
	v_mul_f32_e32 v51, v52, v83
	v_max_f32_e32 v51, 0xc2a00000, v51
	v_mul_f32_e32 v51, 0xbfb8aa3b, v51
	v_exp_f32_e32 v51, v51
	v_rcp_f32_e32 v50, v50
	v_mul_f32_e32 v52, v53, v83
	v_max_f32_e32 v56, 0xc2a00000, v56
	v_add_f32_e32 v51, 1.0, v51
	v_rcp_f32_e32 v51, v51
	v_fma_f32 v50, v120, v50, v125
	v_log_f32_e32 v59, v50
	v_max_f32_e32 v57, 0xc2a00000, v57
	v_fma_f32 v50, v118, v51, v126
	v_log_f32_e32 v60, v50
	ds_read2_b32 v[50:51], v176 offset0:144 offset1:160
	v_max_f32_e32 v52, 0xc2a00000, v52
	v_mul_f32_e32 v56, 0xbfb8aa3b, v56
	v_mul_f32_e32 v57, 0xbfb8aa3b, v57
	v_mul_f32_e32 v52, 0xbfb8aa3b, v52
	v_exp_f32_e32 v56, v56
	v_exp_f32_e32 v57, v57
	v_exp_f32_e32 v52, v52
	s_waitcnt lgkmcnt(0)
	v_mul_f32_e32 v42, v42, v50
	v_max_f32_e32 v42, 0xc2a00000, v42
	v_add_f32_e32 v64, 1.0, v64
	v_add_f32_e32 v65, 1.0, v65
	v_add_f32_e32 v56, 1.0, v56
	v_add_f32_e32 v57, 1.0, v57
	v_add_f32_e32 v52, 1.0, v52
	v_mul_f32_e32 v42, 0xbfb8aa3b, v42
	v_rcp_f32_e32 v64, v64
	v_rcp_f32_e32 v65, v65
	v_rcp_f32_e32 v56, v56
	v_rcp_f32_e32 v57, v57
	v_rcp_f32_e32 v52, v52
	v_exp_f32_e32 v42, v42
	v_mul_f32_e32 v43, v43, v50
	v_fma_f32 v54, v153, v64, v128
	v_fma_f32 v55, v168, v65, v129
	v_fma_f32 v56, v121, v56, v130
	v_fma_f32 v57, v122, v57, v131
	v_fma_f32 v52, v119, v52, v127
	v_add_f32_e32 v42, 1.0, v42
	v_max_f32_e32 v43, 0xc2a00000, v43
	v_log_f32_e32 v54, v54
	v_log_f32_e32 v55, v55
	v_log_f32_e32 v56, v56
	v_log_f32_e32 v57, v57
	v_log_f32_e32 v61, v52
	v_rcp_f32_e32 v42, v42
	v_mul_f32_e32 v43, 0xbfb8aa3b, v43
	v_exp_f32_e32 v43, v43
	v_mul_f32_e32 v48, v48, v50
	v_mul_f32_e32 v49, v49, v50
	v_max_f32_e32 v48, 0xc2a00000, v48
	v_max_f32_e32 v49, 0xc2a00000, v49
	v_cvt_pk_f16_f32 v52, v54, v55
	v_cvt_pk_f16_f32 v53, v56, v57
	v_cvt_pk_f16_f32 v54, v58, v59
	v_mul_f32_e32 v46, v46, v50
	v_mul_f32_e32 v47, v47, v50
	v_cvt_pk_f16_f32 v55, v60, v61
	v_mul_f32_e32 v48, 0xbfb8aa3b, v48
	v_mul_f32_e32 v49, 0xbfb8aa3b, v49
	v_fma_f32 v42, v171, v42, v132
	v_max_f32_e32 v46, 0xc2a00000, v46
	v_max_f32_e32 v47, 0xc2a00000, v47
	v_subrev_u32_e32 v240, s82, v62
	v_add_u32_e32 v240, 0x40, v240
	ds_bpermute_b32 v232, v252, v52
	ds_bpermute_b32 v236, v253, v52
	ds_bpermute_b32 v233, v252, v53
	ds_bpermute_b32 v237, v253, v53
	ds_bpermute_b32 v234, v252, v54
	ds_bpermute_b32 v238, v253, v54
	ds_bpermute_b32 v235, v252, v55
	ds_bpermute_b32 v239, v253, v55
	ds_bpermute_b32 v241, v253, v240
	ds_bpermute_b32 v240, v252, v240
	v_exp_f32_e32 v48, v48
	v_exp_f32_e32 v49, v49
	v_log_f32_e32 v52, v42
	v_add_f32_e32 v42, 1.0, v43
	v_mul_f32_e32 v43, v44, v50
	v_mul_f32_e32 v46, 0xbfb8aa3b, v46
	v_mul_f32_e32 v47, 0xbfb8aa3b, v47
	v_max_f32_e32 v43, 0xc2a00000, v43
	v_mul_f32_e32 v44, v45, v50
	v_exp_f32_e32 v46, v46
	v_exp_f32_e32 v47, v47
	v_mul_f32_e32 v43, 0xbfb8aa3b, v43
	v_max_f32_e32 v44, 0xc2a00000, v44
	v_exp_f32_e32 v43, v43
	v_mul_f32_e32 v44, 0xbfb8aa3b, v44
	v_add_f32_e32 v48, 1.0, v48
	v_add_f32_e32 v49, 1.0, v49
	v_exp_f32_e32 v44, v44
	v_rcp_f32_e32 v48, v48
	v_rcp_f32_e32 v49, v49
	v_add_f32_e32 v46, 1.0, v46
	v_add_f32_e32 v47, 1.0, v47
	v_mul_f32_e32 v34, v34, v50
	v_rcp_f32_e32 v46, v46
	v_rcp_f32_e32 v47, v47
	v_rcp_f32_e32 v42, v42
	v_add_f32_e32 v43, 1.0, v43
	v_max_f32_e32 v34, 0xc2a00000, v34
	v_rcp_f32_e32 v43, v43
	v_add_f32_e32 v44, 1.0, v44
	v_mul_f32_e32 v34, 0xbfb8aa3b, v34
	v_fma_f32 v48, v178, v48, v138
	v_fma_f32 v49, v177, v49, v139
	v_rcp_f32_e32 v44, v44
	v_exp_f32_e32 v34, v34
	v_log_f32_e32 v48, v48
	v_log_f32_e32 v49, v49
	v_fma_f32 v46, v180, v46, v136
	v_fma_f32 v47, v179, v47, v137
	v_fma_f32 v42, v170, v42, v133
	v_mul_f32_e32 v38, v38, v50
	v_log_f32_e32 v46, v46
	v_log_f32_e32 v47, v47
	v_log_f32_e32 v45, v42
	v_fma_f32 v42, v169, v43, v134
	v_max_f32_e32 v38, 0xc2a00000, v38
	v_mul_f32_e32 v35, v35, v50
	v_log_f32_e32 v53, v42
	v_fma_f32 v42, v155, v44, v135
	v_mul_f32_e32 v38, 0xbfb8aa3b, v38
	v_add_f32_e32 v34, 1.0, v34
	v_max_f32_e32 v35, 0xc2a00000, v35
	v_log_f32_e32 v54, v42
	v_cvt_pk_f16_f32 v43, v48, v49
	v_exp_f32_e32 v48, v38
	v_mul_f32_e32 v38, v39, v50
	v_rcp_f32_e32 v34, v34
	v_mul_f32_e32 v35, 0xbfb8aa3b, v35
	s_mov_b64 s[14:15], 0x90000
	v_max_f32_e32 v38, 0xc2a00000, v38
	v_exp_f32_e32 v35, v35
	v_cvt_pk_f16_f32 v42, v46, v47
	v_lshl_add_u64 v[46:47], v[166:167], 0, s[14:15]
	v_mul_f32_e32 v38, 0xbfb8aa3b, v38
	s_mov_b32 s14, 0x90000
	v_exp_f32_e32 v49, v38
	v_add_co_u32_e32 v38, vcc, s14, v166
	v_cvt_pk_f16_f32 v44, v52, v45
	v_cvt_pk_f16_f32 v45, v53, v54
	v_addc_co_u32_e32 v39, vcc, 0, v167, vcc
	v_fma_f32 v34, v123, v34, v124
	v_subrev_u32_e32 v250, s82, v38
	ds_bpermute_b32 v242, v252, v42
	ds_bpermute_b32 v246, v253, v42
	ds_bpermute_b32 v243, v252, v43
	ds_bpermute_b32 v247, v253, v43
	ds_bpermute_b32 v244, v252, v44
	ds_bpermute_b32 v248, v253, v44
	ds_bpermute_b32 v245, v252, v45
	ds_bpermute_b32 v249, v253, v45
	ds_bpermute_b32 v251, v253, v250
	ds_bpermute_b32 v250, v252, v250
	s_waitcnt lgkmcnt(0)
	v_cndmask_b32_e64 v232, v232, v242, s[100:101]
	v_cndmask_b32_e64 v233, v233, v243, s[100:101]
	v_cndmask_b32_e64 v234, v234, v244, s[100:101]
	v_cndmask_b32_e64 v235, v235, v245, s[100:101]
	v_cndmask_b32_e64 v236, v236, v246, s[100:101]
	v_cndmask_b32_e64 v237, v237, v247, s[100:101]
	v_cndmask_b32_e64 v238, v238, v248, s[100:101]
	v_cndmask_b32_e64 v239, v239, v249, s[100:101]
	v_cndmask_b32_e64 v240, v240, v250, s[100:101]
	v_cndmask_b32_e64 v241, v241, v251, s[100:101]
	global_store_dwordx4 v240, v[232:235], s[82:83]
	global_store_dwordx4 v241, v[236:239], s[82:83]
	v_mul_f32_e32 v40, v40, v50
	v_mul_f32_e32 v41, v41, v50
	v_log_f32_e32 v42, v34
	v_add_f32_e32 v34, 1.0, v35
	v_mul_f32_e32 v35, v36, v50
	v_max_f32_e32 v35, 0xc2a00000, v35
	v_mul_f32_e32 v36, v37, v50
	v_max_f32_e32 v40, 0xc2a00000, v40
	v_max_f32_e32 v41, 0xc2a00000, v41
	v_mul_f32_e32 v35, 0xbfb8aa3b, v35
	v_max_f32_e32 v36, 0xc2a00000, v36
	v_mul_f32_e32 v40, 0xbfb8aa3b, v40
	v_mul_f32_e32 v41, 0xbfb8aa3b, v41
	v_exp_f32_e32 v35, v35
	v_mul_f32_e32 v36, 0xbfb8aa3b, v36
	v_exp_f32_e32 v40, v40
	v_exp_f32_e32 v41, v41
	v_exp_f32_e32 v36, v36
	v_mul_f32_e32 v26, v26, v51
	v_rcp_f32_e32 v34, v34
	v_add_f32_e32 v35, 1.0, v35
	v_max_f32_e32 v26, 0xc2a00000, v26
	v_add_f32_e32 v48, 1.0, v48
	v_add_f32_e32 v49, 1.0, v49
	v_add_f32_e32 v40, 1.0, v40
	v_add_f32_e32 v41, 1.0, v41
	v_rcp_f32_e32 v35, v35
	v_add_f32_e32 v36, 1.0, v36
	v_mul_f32_e32 v26, 0xbfb8aa3b, v26
	v_rcp_f32_e32 v48, v48
	v_rcp_f32_e32 v49, v49
	v_rcp_f32_e32 v40, v40
	v_rcp_f32_e32 v41, v41
	v_rcp_f32_e32 v36, v36
	v_exp_f32_e32 v26, v26
	v_fma_f32 v34, v120, v34, v125
	v_log_f32_e32 v37, v34
	v_fma_f32 v34, v118, v35, v126
	v_mul_f32_e32 v27, v27, v51
	v_fma_f32 v38, v153, v48, v128
	v_fma_f32 v39, v168, v49, v129
	v_fma_f32 v40, v121, v40, v130
	v_fma_f32 v41, v122, v41, v131
	v_log_f32_e32 v43, v34
	v_fma_f32 v34, v119, v36, v127
	v_add_f32_e32 v26, 1.0, v26
	v_max_f32_e32 v27, 0xc2a00000, v27
	v_log_f32_e32 v38, v38
	v_log_f32_e32 v39, v39
	v_log_f32_e32 v40, v40
	v_log_f32_e32 v41, v41
	v_log_f32_e32 v44, v34
	v_rcp_f32_e32 v26, v26
	v_mul_f32_e32 v27, 0xbfb8aa3b, v27
	v_exp_f32_e32 v27, v27
	v_mul_f32_e32 v32, v32, v51
	v_mul_f32_e32 v33, v33, v51
	v_max_f32_e32 v32, 0xc2a00000, v32
	v_max_f32_e32 v33, 0xc2a00000, v33
	v_cvt_pk_f16_f32 v34, v38, v39
	v_cvt_pk_f16_f32 v35, v40, v41
	v_cvt_pk_f16_f32 v36, v42, v37
	v_mul_f32_e32 v30, v30, v51
	v_mul_f32_e32 v31, v31, v51
	v_cvt_pk_f16_f32 v37, v43, v44
	v_mul_f32_e32 v32, 0xbfb8aa3b, v32
	v_mul_f32_e32 v33, 0xbfb8aa3b, v33
	v_fma_f32 v26, v171, v26, v132
	v_max_f32_e32 v30, 0xc2a00000, v30
	v_max_f32_e32 v31, 0xc2a00000, v31
	v_subrev_u32_e32 v240, s82, v46
	v_add_u32_e32 v240, 0x40, v240
	ds_bpermute_b32 v232, v252, v34
	ds_bpermute_b32 v236, v253, v34
	ds_bpermute_b32 v233, v252, v35
	ds_bpermute_b32 v237, v253, v35
	ds_bpermute_b32 v234, v252, v36
	ds_bpermute_b32 v238, v253, v36
	ds_bpermute_b32 v235, v252, v37
	ds_bpermute_b32 v239, v253, v37
	ds_bpermute_b32 v241, v253, v240
	ds_bpermute_b32 v240, v252, v240
	v_exp_f32_e32 v32, v32
	v_exp_f32_e32 v33, v33
	v_log_f32_e32 v34, v26
	v_add_f32_e32 v26, 1.0, v27
	v_mul_f32_e32 v27, v28, v51
	v_mul_f32_e32 v30, 0xbfb8aa3b, v30
	v_mul_f32_e32 v31, 0xbfb8aa3b, v31
	v_max_f32_e32 v27, 0xc2a00000, v27
	v_mul_f32_e32 v28, v29, v51
	v_exp_f32_e32 v30, v30
	v_exp_f32_e32 v31, v31
	v_mul_f32_e32 v27, 0xbfb8aa3b, v27
	v_max_f32_e32 v28, 0xc2a00000, v28
	v_exp_f32_e32 v27, v27
	v_mul_f32_e32 v28, 0xbfb8aa3b, v28
	v_add_f32_e32 v32, 1.0, v32
	v_add_f32_e32 v33, 1.0, v33
	v_exp_f32_e32 v28, v28
	v_rcp_f32_e32 v32, v32
	v_rcp_f32_e32 v33, v33
	v_add_f32_e32 v30, 1.0, v30
	v_add_f32_e32 v31, 1.0, v31
	v_mul_f32_e32 v18, v18, v51
	v_rcp_f32_e32 v30, v30
	v_rcp_f32_e32 v31, v31
	v_rcp_f32_e32 v26, v26
	v_add_f32_e32 v27, 1.0, v27
	v_max_f32_e32 v18, 0xc2a00000, v18
	v_rcp_f32_e32 v27, v27
	v_add_f32_e32 v28, 1.0, v28
	v_mul_f32_e32 v18, 0xbfb8aa3b, v18
	v_fma_f32 v32, v178, v32, v138
	v_fma_f32 v33, v177, v33, v139
	v_rcp_f32_e32 v28, v28
	v_exp_f32_e32 v18, v18
	v_log_f32_e32 v32, v32
	v_log_f32_e32 v33, v33
	v_fma_f32 v30, v180, v30, v136
	v_fma_f32 v31, v179, v31, v137
	v_fma_f32 v26, v170, v26, v133
	v_mul_f32_e32 v22, v22, v51
	v_log_f32_e32 v30, v30
	v_log_f32_e32 v31, v31
	v_log_f32_e32 v29, v26
	v_fma_f32 v26, v169, v27, v134
	v_max_f32_e32 v22, 0xc2a00000, v22
	v_mul_f32_e32 v19, v19, v51
	v_log_f32_e32 v35, v26
	v_fma_f32 v26, v155, v28, v135
	v_mul_f32_e32 v22, 0xbfb8aa3b, v22
	v_add_f32_e32 v18, 1.0, v18
	v_max_f32_e32 v19, 0xc2a00000, v19
	v_log_f32_e32 v36, v26
	v_cvt_pk_f16_f32 v27, v32, v33
	v_exp_f32_e32 v32, v22
	v_mul_f32_e32 v22, v23, v51
	v_rcp_f32_e32 v18, v18
	v_mul_f32_e32 v19, 0xbfb8aa3b, v19
	s_mov_b64 s[14:15], 0xa0000
	v_max_f32_e32 v22, 0xc2a00000, v22
	v_exp_f32_e32 v19, v19
	v_cvt_pk_f16_f32 v26, v30, v31
	v_lshl_add_u64 v[30:31], v[166:167], 0, s[14:15]
	v_mul_f32_e32 v22, 0xbfb8aa3b, v22
	s_mov_b32 s14, 0xa0000
	v_exp_f32_e32 v33, v22
	v_add_co_u32_e32 v22, vcc, s14, v166
	v_cvt_pk_f16_f32 v28, v34, v29
	v_cvt_pk_f16_f32 v29, v35, v36
	v_addc_co_u32_e32 v23, vcc, 0, v167, vcc
	v_fma_f32 v18, v123, v18, v124
	v_subrev_u32_e32 v250, s82, v22
	ds_bpermute_b32 v242, v252, v26
	ds_bpermute_b32 v246, v253, v26
	ds_bpermute_b32 v243, v252, v27
	ds_bpermute_b32 v247, v253, v27
	ds_bpermute_b32 v244, v252, v28
	ds_bpermute_b32 v248, v253, v28
	ds_bpermute_b32 v245, v252, v29
	ds_bpermute_b32 v249, v253, v29
	ds_bpermute_b32 v251, v253, v250
	ds_bpermute_b32 v250, v252, v250
	s_waitcnt lgkmcnt(0)
	v_cndmask_b32_e64 v232, v232, v242, s[100:101]
	v_cndmask_b32_e64 v233, v233, v243, s[100:101]
	v_cndmask_b32_e64 v234, v234, v244, s[100:101]
	v_cndmask_b32_e64 v235, v235, v245, s[100:101]
	v_cndmask_b32_e64 v236, v236, v246, s[100:101]
	v_cndmask_b32_e64 v237, v237, v247, s[100:101]
	v_cndmask_b32_e64 v238, v238, v248, s[100:101]
	v_cndmask_b32_e64 v239, v239, v249, s[100:101]
	v_cndmask_b32_e64 v240, v240, v250, s[100:101]
	v_cndmask_b32_e64 v241, v241, v251, s[100:101]
	global_store_dwordx4 v240, v[232:235], s[82:83]
	global_store_dwordx4 v241, v[236:239], s[82:83]
	v_mul_f32_e32 v24, v24, v51
	v_mul_f32_e32 v25, v25, v51
	v_log_f32_e32 v26, v18
	v_add_f32_e32 v18, 1.0, v19
	v_mul_f32_e32 v19, v20, v51
	v_max_f32_e32 v19, 0xc2a00000, v19
	v_mul_f32_e32 v20, v21, v51
	ds_read_b32 v28, v176 offset:704
	v_max_f32_e32 v24, 0xc2a00000, v24
	v_max_f32_e32 v25, 0xc2a00000, v25
	v_mul_f32_e32 v19, 0xbfb8aa3b, v19
	v_max_f32_e32 v20, 0xc2a00000, v20
	v_mul_f32_e32 v24, 0xbfb8aa3b, v24
	v_mul_f32_e32 v25, 0xbfb8aa3b, v25
	v_exp_f32_e32 v19, v19
	v_mul_f32_e32 v20, 0xbfb8aa3b, v20
	v_exp_f32_e32 v24, v24
	v_exp_f32_e32 v25, v25
	v_exp_f32_e32 v20, v20
	s_waitcnt lgkmcnt(0)
	v_mul_f32_e32 v10, v10, v28
	v_rcp_f32_e32 v18, v18
	v_add_f32_e32 v19, 1.0, v19
	v_max_f32_e32 v10, 0xc2a00000, v10
	v_add_f32_e32 v32, 1.0, v32
	v_add_f32_e32 v33, 1.0, v33
	v_add_f32_e32 v24, 1.0, v24
	v_add_f32_e32 v25, 1.0, v25
	v_rcp_f32_e32 v19, v19
	v_add_f32_e32 v20, 1.0, v20
	v_mul_f32_e32 v10, 0xbfb8aa3b, v10
	v_rcp_f32_e32 v32, v32
	v_rcp_f32_e32 v33, v33
	v_rcp_f32_e32 v24, v24
	v_rcp_f32_e32 v25, v25
	v_rcp_f32_e32 v20, v20
	v_exp_f32_e32 v10, v10
	v_fma_f32 v18, v120, v18, v125
	v_log_f32_e32 v21, v18
	v_fma_f32 v18, v118, v19, v126
	v_mul_f32_e32 v11, v11, v28
	v_fma_f32 v22, v153, v32, v128
	v_fma_f32 v23, v168, v33, v129
	v_fma_f32 v24, v121, v24, v130
	v_fma_f32 v25, v122, v25, v131
	v_log_f32_e32 v27, v18
	v_fma_f32 v18, v119, v20, v127
	v_add_f32_e32 v10, 1.0, v10
	v_max_f32_e32 v11, 0xc2a00000, v11
	v_log_f32_e32 v22, v22
	v_log_f32_e32 v23, v23
	v_log_f32_e32 v24, v24
	v_log_f32_e32 v25, v25
	v_log_f32_e32 v29, v18
	v_rcp_f32_e32 v10, v10
	v_mul_f32_e32 v11, 0xbfb8aa3b, v11
	v_mul_f32_e32 v14, v14, v28
	v_mul_f32_e32 v15, v15, v28
	v_exp_f32_e32 v11, v11
	v_max_f32_e32 v14, 0xc2a00000, v14
	v_max_f32_e32 v15, 0xc2a00000, v15
	v_mul_f32_e32 v14, 0xbfb8aa3b, v14
	v_mul_f32_e32 v15, 0xbfb8aa3b, v15
	v_cvt_pk_f16_f32 v18, v22, v23
	v_cvt_pk_f16_f32 v19, v24, v25
	v_cvt_pk_f16_f32 v20, v26, v21
	v_exp_f32_e32 v14, v14
	v_exp_f32_e32 v15, v15
	v_cvt_pk_f16_f32 v21, v27, v29
	v_fma_f32 v10, v171, v10, v132
	v_subrev_u32_e32 v240, s82, v30
	v_add_u32_e32 v240, 0x40, v240
	ds_bpermute_b32 v232, v252, v18
	ds_bpermute_b32 v236, v253, v18
	ds_bpermute_b32 v233, v252, v19
	ds_bpermute_b32 v237, v253, v19
	ds_bpermute_b32 v234, v252, v20
	ds_bpermute_b32 v238, v253, v20
	ds_bpermute_b32 v235, v252, v21
	ds_bpermute_b32 v239, v253, v21
	ds_bpermute_b32 v241, v253, v240
	ds_bpermute_b32 v240, v252, v240
	v_add_f32_e32 v14, 1.0, v14
	v_add_f32_e32 v15, 1.0, v15
	v_log_f32_e32 v18, v10
	v_add_f32_e32 v10, 1.0, v11
	v_mul_f32_e32 v11, v12, v28
	v_max_f32_e32 v11, 0xc2a00000, v11
	v_mul_f32_e32 v11, 0xbfb8aa3b, v11
	v_exp_f32_e32 v11, v11
	v_rcp_f32_e32 v14, v14
	v_rcp_f32_e32 v15, v15
	v_mul_f32_e32 v16, v16, v28
	v_mul_f32_e32 v17, v17, v28
	v_rcp_f32_e32 v10, v10
	v_mul_f32_e32 v12, v13, v28
	v_add_f32_e32 v11, 1.0, v11
	v_fma_f32 v14, v180, v14, v136
	v_fma_f32 v15, v179, v15, v137
	v_max_f32_e32 v16, 0xc2a00000, v16
	v_max_f32_e32 v17, 0xc2a00000, v17
	v_max_f32_e32 v12, 0xc2a00000, v12
	v_rcp_f32_e32 v11, v11
	v_log_f32_e32 v14, v14
	v_mul_f32_e32 v16, 0xbfb8aa3b, v16
	v_mul_f32_e32 v17, 0xbfb8aa3b, v17
	v_log_f32_e32 v15, v15
	v_mul_f32_e32 v12, 0xbfb8aa3b, v12
	v_exp_f32_e32 v16, v16
	v_exp_f32_e32 v17, v17
	v_exp_f32_e32 v12, v12
	v_mul_f32_e32 v6, v6, v28
	v_fma_f32 v10, v170, v10, v133
	v_max_f32_e32 v6, 0xc2a00000, v6
	v_log_f32_e32 v13, v10
	v_fma_f32 v10, v169, v11, v134
	v_mul_f32_e32 v6, 0xbfb8aa3b, v6
	v_log_f32_e32 v19, v10
	v_cvt_pk_f16_f32 v10, v14, v15
	v_exp_f32_e32 v14, v6
	v_mul_f32_e32 v6, v7, v28
	v_mul_f32_e32 v8, v8, v28
	v_mul_f32_e32 v9, v9, v28
	v_mul_f32_e32 v2, v2, v28
	v_mul_f32_e32 v3, v3, v28
	v_mul_f32_e32 v4, v4, v28
	v_mul_f32_e32 v5, v5, v28
	v_add_f32_e32 v16, 1.0, v16
	v_add_f32_e32 v17, 1.0, v17
	v_add_f32_e32 v12, 1.0, v12
	v_max_f32_e32 v6, 0xc2a00000, v6
	v_max_f32_e32 v8, 0xc2a00000, v8
	v_max_f32_e32 v9, 0xc2a00000, v9
	v_max_f32_e32 v2, 0xc2a00000, v2
	v_max_f32_e32 v3, 0xc2a00000, v3
	v_max_f32_e32 v4, 0xc2a00000, v4
	v_max_f32_e32 v5, 0xc2a00000, v5
	v_rcp_f32_e32 v16, v16
	v_rcp_f32_e32 v17, v17
	v_rcp_f32_e32 v12, v12
	v_mul_f32_e32 v6, 0xbfb8aa3b, v6
	v_mul_f32_e32 v8, 0xbfb8aa3b, v8
	v_mul_f32_e32 v9, 0xbfb8aa3b, v9
	v_mul_f32_e32 v2, 0xbfb8aa3b, v2
	v_mul_f32_e32 v3, 0xbfb8aa3b, v3
	v_mul_f32_e32 v4, 0xbfb8aa3b, v4
	v_mul_f32_e32 v5, 0xbfb8aa3b, v5
	v_exp_f32_e32 v15, v6
	v_exp_f32_e32 v8, v8
	v_exp_f32_e32 v9, v9
	v_exp_f32_e32 v2, v2
	v_exp_f32_e32 v3, v3
	v_exp_f32_e32 v4, v4
	v_exp_f32_e32 v5, v5
	v_fma_f32 v16, v178, v16, v138
	v_fmac_f32_e32 v139, v177, v17
	v_fmac_f32_e32 v135, v155, v12
	v_log_f32_e32 v16, v16
	v_log_f32_e32 v17, v139
	v_log_f32_e32 v20, v135
	v_add_f32_e32 v14, 1.0, v14
	v_add_f32_e32 v15, 1.0, v15
	v_add_f32_e32 v8, 1.0, v8
	v_add_f32_e32 v9, 1.0, v9
	v_add_f32_e32 v2, 1.0, v2
	v_add_f32_e32 v3, 1.0, v3
	v_add_f32_e32 v4, 1.0, v4
	v_add_f32_e32 v5, 1.0, v5
	s_mov_b64 s[14:15], 0xb0000
	v_rcp_f32_e32 v14, v14
	v_rcp_f32_e32 v15, v15
	v_rcp_f32_e32 v8, v8
	v_rcp_f32_e32 v9, v9
	v_rcp_f32_e32 v2, v2
	v_rcp_f32_e32 v3, v3
	v_rcp_f32_e32 v4, v4
	v_rcp_f32_e32 v5, v5
	v_lshl_add_u64 v[136:137], v[166:167], 0, s[14:15]
	s_mov_b32 s14, 0xb0000
	v_add_co_u32_e32 v6, vcc, s14, v166
	v_cvt_pk_f16_f32 v11, v16, v17
	v_cvt_pk_f16_f32 v12, v18, v13
	v_cvt_pk_f16_f32 v13, v19, v20
	v_addc_co_u32_e32 v7, vcc, 0, v167, vcc
	v_subrev_u32_e32 v250, s82, v6
	ds_bpermute_b32 v242, v252, v10
	ds_bpermute_b32 v246, v253, v10
	ds_bpermute_b32 v243, v252, v11
	ds_bpermute_b32 v247, v253, v11
	ds_bpermute_b32 v244, v252, v12
	ds_bpermute_b32 v248, v253, v12
	ds_bpermute_b32 v245, v252, v13
	ds_bpermute_b32 v249, v253, v13
	ds_bpermute_b32 v251, v253, v250
	ds_bpermute_b32 v250, v252, v250
	s_waitcnt lgkmcnt(0)
	v_cndmask_b32_e64 v232, v232, v242, s[100:101]
	v_cndmask_b32_e64 v233, v233, v243, s[100:101]
	v_cndmask_b32_e64 v234, v234, v244, s[100:101]
	v_cndmask_b32_e64 v235, v235, v245, s[100:101]
	v_cndmask_b32_e64 v236, v236, v246, s[100:101]
	v_cndmask_b32_e64 v237, v237, v247, s[100:101]
	v_cndmask_b32_e64 v238, v238, v248, s[100:101]
	v_cndmask_b32_e64 v239, v239, v249, s[100:101]
	v_cndmask_b32_e64 v240, v240, v250, s[100:101]
	v_cndmask_b32_e64 v241, v241, v251, s[100:101]
	global_store_dwordx4 v240, v[232:235], s[82:83]
	global_store_dwordx4 v241, v[236:239], s[82:83]
	v_fma_f32 v6, v153, v14, v128
	v_fma_f32 v7, v168, v15, v129
	v_fma_f32 v8, v121, v8, v130
	v_fmac_f32_e32 v131, v122, v9
	v_fma_f32 v2, v123, v2, v124
	v_fma_f32 v3, v120, v3, v125
	v_fma_f32 v4, v118, v4, v126
	v_fmac_f32_e32 v127, v119, v5
	v_log_f32_e32 v6, v6
	v_log_f32_e32 v7, v7
	v_log_f32_e32 v8, v8
	v_log_f32_e32 v9, v131
	v_log_f32_e32 v2, v2
	v_log_f32_e32 v3, v3
	v_log_f32_e32 v4, v4
	v_log_f32_e32 v5, v127
	v_cvt_pk_f16_f32 v196, v181, v182
	v_cvt_pk_f16_f32 v132, v6, v7
	v_cvt_pk_f16_f32 v133, v8, v9
	v_cvt_pk_f16_f32 v134, v2, v3
	v_cvt_pk_f16_f32 v135, v4, v5
	v_subrev_u32_e32 v240, s82, v166
	v_add_u32_e32 v240, 0x40, v240
	ds_bpermute_b32 v232, v252, v194
	ds_bpermute_b32 v236, v253, v194
	ds_bpermute_b32 v233, v252, v195
	ds_bpermute_b32 v237, v253, v195
	ds_bpermute_b32 v234, v252, v196
	ds_bpermute_b32 v238, v253, v196
	ds_bpermute_b32 v235, v252, v197
	ds_bpermute_b32 v239, v253, v197
	ds_bpermute_b32 v241, v253, v240
	ds_bpermute_b32 v240, v252, v240
	s_andn2_b64 vcc, exec, s[38:39]
	s_mov_b64 s[28:29], -1
	v_subrev_u32_e32 v250, s82, v136
	v_add_u32_e32 v250, 0x40, v250
	ds_bpermute_b32 v242, v252, v132
	ds_bpermute_b32 v246, v253, v132
	ds_bpermute_b32 v243, v252, v133
	ds_bpermute_b32 v247, v253, v133
	ds_bpermute_b32 v244, v252, v134
	ds_bpermute_b32 v248, v253, v134
	ds_bpermute_b32 v245, v252, v135
	ds_bpermute_b32 v249, v253, v135
	ds_bpermute_b32 v251, v253, v250
	ds_bpermute_b32 v250, v252, v250
	s_waitcnt lgkmcnt(0)
	v_cndmask_b32_e64 v232, v232, v242, s[100:101]
	v_cndmask_b32_e64 v233, v233, v243, s[100:101]
	v_cndmask_b32_e64 v234, v234, v244, s[100:101]
	v_cndmask_b32_e64 v235, v235, v245, s[100:101]
	v_cndmask_b32_e64 v236, v236, v246, s[100:101]
	v_cndmask_b32_e64 v237, v237, v247, s[100:101]
	v_cndmask_b32_e64 v238, v238, v248, s[100:101]
	v_cndmask_b32_e64 v239, v239, v249, s[100:101]
	v_cndmask_b32_e64 v240, v240, v250, s[100:101]
	v_cndmask_b32_e64 v241, v241, v251, s[100:101]
	global_store_dwordx4 v240, v[232:235], s[82:83]
	global_store_dwordx4 v241, v[236:239], s[82:83]
	s_cbranch_vccnz .LBB0_338

.LBB0_506:
	v_mbcnt_lo_u32_b32 v231, -1, 0
	v_mbcnt_hi_u32_b32 v231, -1, v231
	v_and_b32_e32 v253, 3, v231
	v_lshrrev_b32_e32 v252, 3, v231
	v_lshl_add_u32 v252, v253, 4, v252
	v_lshlrev_b32_e32 v252, 2, v252
	v_lshrrev_b32_e32 v231, 2, v231
	v_lshl_add_u32 v231, v253, 4, v231
	v_lshlrev_b32_e32 v231, 2, v231
	v_add_u32_e32 v253, 32, v252
	s_mov_b32 s100, 0xf0f0f0f0
	s_mov_b32 s101, 0xf0f0f0f0
	s_lshl_b32 s14, s14, 10
	v_add_u32_e32 v176, s14, v174
	ds_read_b32 v154, v176
	s_lshl_b32 s15, s28, 8
	s_ashr_i32 s56, s28, 3
	s_and_b32 s14, s15, 0x700
	v_lshl_add_u32 v152, s40, 8, v1
	v_or_b32_e32 v177, s14, v173
	s_cmp_lg_u32 s56, 1
	s_mov_b64 s[40:41], -1
	s_cbranch_scc0 .LBB0_541
	s_cmp_lt_u32 s28, 8
	s_cselect_b64 s[54:55], -1, 0
	s_cmp_gt_u32 s28, 7
	s_waitcnt lgkmcnt(0)
	v_pk_mul_f32 v[134:135], v[130:131], v[154:155] op_sel_hi:[1,0]
	v_pk_mul_f32 v[166:167], v[128:129], v[154:155] op_sel_hi:[1,0]
	v_pk_mul_f32 v[138:139], v[126:127], v[154:155] op_sel_hi:[1,0]
	v_pk_mul_f32 v[168:169], v[124:125], v[154:155] op_sel_hi:[1,0]
	s_cbranch_scc1 .LBB0_509
	v_max_f32_e32 v114, v166, v166
	v_max_f32_e32 v132, 0xc2a00000, v114
	v_max_f32_e32 v114, v168, v168
	v_max_f32_e32 v136, 0xc2a00000, v114
	v_mul_f32_e32 v114, 0xbfb8aa3b, v132
	v_exp_f32_e32 v114, v114
	v_mul_f32_e32 v133, 0xbfb8aa3b, v136
	v_exp_f32_e32 v133, v133
	v_max_f32_e32 v137, v169, v169
	v_add_f32_e32 v114, 1.0, v114
	v_rcp_f32_e32 v158, v114
	v_add_f32_e32 v114, 1.0, v133
	v_max_f32_e32 v133, v167, v167
	v_max_f32_e32 v133, 0xc2a00000, v133
	v_max_f32_e32 v137, 0xc2a00000, v137
	v_mul_f32_e32 v153, 0xbfb8aa3b, v133
	v_exp_f32_e32 v153, v153
	v_mul_f32_e32 v155, 0xbfb8aa3b, v137
	v_exp_f32_e32 v155, v155
	v_max_f32_e32 v134, v134, v134
	v_max_f32_e32 v134, 0xc2a00000, v134
	v_max_f32_e32 v138, v138, v138
	v_rcp_f32_e32 v160, v114
	v_add_f32_e32 v114, 1.0, v153
	v_max_f32_e32 v138, 0xc2a00000, v138
	v_mul_f32_e32 v153, 0xbfb8aa3b, v134
	v_rcp_f32_e32 v159, v114
	v_add_f32_e32 v114, 1.0, v155
	v_exp_f32_e32 v153, v153
	v_mul_f32_e32 v155, 0xbfb8aa3b, v138
	v_exp_f32_e32 v155, v155
	v_max_f32_e32 v135, v135, v135
	v_max_f32_e32 v135, 0xc2a00000, v135
	v_max_f32_e32 v139, v139, v139
	v_rcp_f32_e32 v161, v114
	v_add_f32_e32 v114, 1.0, v153
	v_max_f32_e32 v139, 0xc2a00000, v139
	v_mul_f32_e32 v153, 0xbfb8aa3b, v135
	v_rcp_f32_e32 v168, v114
	v_add_f32_e32 v114, 1.0, v155
	v_exp_f32_e32 v153, v153
	v_mul_f32_e32 v155, 0xbfb8aa3b, v139
	v_exp_f32_e32 v155, v155
	v_rcp_f32_e32 v170, v114
	v_add_f32_e32 v114, 1.0, v153
	v_rcp_f32_e32 v169, v114
	v_add_f32_e32 v114, 1.0, v155
	v_rcp_f32_e32 v171, v114
	v_pk_mul_f32 v[166:167], v[132:133], v[158:159]
	v_pk_mul_f32 v[134:135], v[134:135], v[168:169]
	v_pk_mul_f32 v[168:169], v[136:137], v[160:161]
	v_pk_mul_f32 v[138:139], v[138:139], v[170:171]
.LBB0_509:
	s_ashr_i32 s57, s56, 31
	s_lshl_b64 s[14:15], s[56:57], 25
	s_add_u32 s14, s24, s14
	s_addc_u32 s15, s37, s15
	v_lshlrev_b32_e32 v114, 1, v177
	v_ashrrev_i32_e32 v153, 31, v152
	v_lshl_add_u64 v[132:133], s[14:15], 0, v[114:115]
	v_lshlrev_b64 v[136:137], 12, v[152:153]
	v_mov_b32_e32 v155, v154
	v_lshl_add_u64 v[136:137], v[132:133], 0, v[136:137]
	v_cvt_pk_bf16_f32 v166, v166, v167
	v_cvt_pk_bf16_f32 v167, v134, v135
	v_cvt_pk_bf16_f32 v168, v168, v169
	v_cvt_pk_bf16_f32 v169, v138, v139
	v_mov_b32_e32 v158, v154
	v_mov_b32_e32 v159, v154
	v_cndmask_b32_e64 v114, 0, 1, s[54:55]
	ds_bpermute_b32 v242, v231, v166
	ds_bpermute_b32 v243, v231, v167
	ds_bpermute_b32 v244, v231, v168
	ds_bpermute_b32 v245, v231, v169
	ds_bpermute_b32 v246, v231, v136
	s_waitcnt lgkmcnt(0)
	v_subrev_u32_e32 v246, s82, v246
	global_store_dwordx4 v246, v[242:245], s[82:83]
	v_pk_mul_f32 v[138:139], v[122:123], v[158:159]
	v_pk_mul_f32 v[134:135], v[120:121], v[154:155]
	v_pk_mul_f32 v[166:167], v[118:119], v[158:159]
	v_cmp_ne_u32_e64 s[40:41], 1, v114
	s_andn2_b64 vcc, exec, s[54:55]
	v_pk_mul_f32 v[168:169], v[116:117], v[154:155]
	s_cbranch_vccnz .LBB0_511
	v_max_f32_e32 v114, v134, v134
	v_max_f32_e32 v134, 0xc2a00000, v114
	v_max_f32_e32 v114, v168, v168
	v_max_f32_e32 v158, 0xc2a00000, v114
	v_mul_f32_e32 v114, 0xbfb8aa3b, v134
	v_exp_f32_e32 v114, v114
	v_mul_f32_e32 v155, 0xbfb8aa3b, v158
	v_exp_f32_e32 v155, v155
	v_max_f32_e32 v135, v135, v135
	v_add_f32_e32 v114, 1.0, v114
	v_rcp_f32_e32 v160, v114
	v_add_f32_e32 v114, 1.0, v155
	v_max_f32_e32 v135, 0xc2a00000, v135
	v_max_f32_e32 v155, v169, v169
	v_max_f32_e32 v159, 0xc2a00000, v155
	v_mul_f32_e32 v155, 0xbfb8aa3b, v135
	v_exp_f32_e32 v155, v155
	v_mul_f32_e32 v161, 0xbfb8aa3b, v159
	v_exp_f32_e32 v169, v161
	v_max_f32_e32 v138, v138, v138
	v_rcp_f32_e32 v168, v114
	v_add_f32_e32 v114, 1.0, v155
	v_max_f32_e32 v138, 0xc2a00000, v138
	v_max_f32_e32 v155, v166, v166
	v_max_f32_e32 v166, 0xc2a00000, v155
	v_mul_f32_e32 v155, 0xbfb8aa3b, v138
	v_exp_f32_e32 v155, v155
	v_rcp_f32_e32 v161, v114
	v_add_f32_e32 v114, 1.0, v169
	v_mul_f32_e32 v169, 0xbfb8aa3b, v166
	v_exp_f32_e32 v171, v169
	v_max_f32_e32 v139, v139, v139
	v_rcp_f32_e32 v169, v114
	v_add_f32_e32 v114, 1.0, v155
	v_max_f32_e32 v139, 0xc2a00000, v139
	v_max_f32_e32 v155, v167, v167
	v_max_f32_e32 v167, 0xc2a00000, v155
	v_mul_f32_e32 v155, 0xbfb8aa3b, v139
	v_rcp_f32_e32 v170, v114
	v_add_f32_e32 v114, 1.0, v171
	v_exp_f32_e32 v155, v155
	v_mul_f32_e32 v171, 0xbfb8aa3b, v167
	v_exp_f32_e32 v179, v171
	v_rcp_f32_e32 v178, v114
	v_add_f32_e32 v114, 1.0, v155
	v_rcp_f32_e32 v171, v114
	v_add_f32_e32 v114, 1.0, v179
	v_rcp_f32_e32 v179, v114
	v_pk_mul_f32 v[134:135], v[134:135], v[160:161]
	v_pk_mul_f32 v[138:139], v[138:139], v[170:171]
	v_pk_mul_f32 v[168:169], v[158:159], v[168:169]
	v_pk_mul_f32 v[166:167], v[166:167], v[178:179]

.LBB0_541:
	s_and_b64 vcc, exec, s[40:41]
	s_cbranch_vccz .LBB0_540
	v_lshlrev_b32_e32 v155, 2, v177
	global_load_dwordx4 v[136:139], v155, s[42:43]
	global_load_dwordx4 v[132:135], v155, s[42:43] offset:16
	s_waitcnt lgkmcnt(0)
	v_mul_f32_e32 v160, v128, v154
	v_mul_f32_e32 v161, v129, v154
	v_mul_f32_e32 v166, v130, v154
	v_mul_f32_e32 v167, v131, v154
	v_mul_f32_e32 v168, v124, v154
	v_mul_f32_e32 v169, v125, v154
	v_mul_f32_e32 v170, v126, v154
	v_mul_f32_e32 v171, v127, v154
	global_load_dwordx4 v[124:127], v155, s[42:43] offset:144
	global_load_dwordx4 v[128:131], v155, s[42:43] offset:128
	v_ashrrev_i32_e32 v153, 31, v152
	v_lshlrev_b64 v[158:159], 12, v[152:153]
	v_max_f32_e32 v153, 0xc2a00000, v160
	v_max_f32_e32 v155, 0xc2a00000, v161
	v_max_f32_e32 v160, 0xc2a00000, v166
	v_max_f32_e32 v161, 0xc2a00000, v167
	v_max_f32_e32 v166, 0xc2a00000, v168
	v_max_f32_e32 v167, 0xc2a00000, v169
	v_max_f32_e32 v168, 0xc2a00000, v170
	v_max_f32_e32 v169, 0xc2a00000, v171
	v_mul_f32_e32 v153, 0xbfb8aa3b, v153
	v_mul_f32_e32 v155, 0xbfb8aa3b, v155
	v_mul_f32_e32 v168, 0xbfb8aa3b, v168
	v_mul_f32_e32 v169, 0xbfb8aa3b, v169
	v_exp_f32_e32 v153, v153
	v_exp_f32_e32 v155, v155
	v_mul_f32_e32 v160, 0xbfb8aa3b, v160
	v_mul_f32_e32 v161, 0xbfb8aa3b, v161
	v_exp_f32_e32 v168, v168
	v_exp_f32_e32 v169, v169
	v_exp_f32_e32 v160, v160
	v_exp_f32_e32 v161, v161
	v_mul_f32_e32 v120, v120, v154
	v_max_f32_e32 v120, 0xc2a00000, v120
	v_add_f32_e32 v153, 1.0, v153
	v_add_f32_e32 v155, 1.0, v155
	v_mul_f32_e32 v121, v121, v154
	v_lshlrev_b32_e32 v114, 1, v177
	v_mul_f32_e32 v166, 0xbfb8aa3b, v166
	v_mul_f32_e32 v167, 0xbfb8aa3b, v167
	v_lshl_add_u64 v[158:159], s[26:27], 0, v[158:159]
	v_add_f32_e32 v168, 1.0, v168
	v_add_f32_e32 v169, 1.0, v169
	v_rcp_f32_e32 v153, v153
	v_rcp_f32_e32 v181, v155
	v_mul_f32_e32 v120, 0xbfb8aa3b, v120
	v_max_f32_e32 v121, 0xc2a00000, v121
	v_exp_f32_e32 v170, v166
	v_exp_f32_e32 v171, v167
	v_lshl_add_u64 v[166:167], v[158:159], 0, v[114:115]
	v_add_f32_e32 v158, 1.0, v160
	v_add_f32_e32 v159, 1.0, v161
	v_rcp_f32_e32 v168, v168
	v_rcp_f32_e32 v182, v169
	v_exp_f32_e32 v120, v120
	v_mul_f32_e32 v121, 0xbfb8aa3b, v121
	v_rcp_f32_e32 v158, v158
	v_rcp_f32_e32 v159, v159
	v_exp_f32_e32 v121, v121
	v_add_f32_e32 v120, 1.0, v120
	v_rcp_f32_e32 v120, v120
	v_mul_f32_e32 v116, v116, v154
	v_add_f32_e32 v121, 1.0, v121
	v_rcp_f32_e32 v121, v121
	v_add_f32_e32 v160, 1.0, v170
	v_add_f32_e32 v161, 1.0, v171
	v_max_f32_e32 v116, 0xc2a00000, v116
	v_mul_f32_e32 v117, v117, v154
	v_rcp_f32_e32 v160, v160
	v_rcp_f32_e32 v161, v161
	v_mul_f32_e32 v116, 0xbfb8aa3b, v116
	v_max_f32_e32 v117, 0xc2a00000, v117
	v_exp_f32_e32 v116, v116
	v_mul_f32_e32 v117, 0xbfb8aa3b, v117
	v_exp_f32_e32 v117, v117
	s_mov_b64 s[14:15], 0x80000
	v_add_f32_e32 v116, 1.0, v116
	v_rcp_f32_e32 v116, v116
	v_add_f32_e32 v117, 1.0, v117
	s_waitcnt vmcnt(0)
	v_sub_f32_e32 v180, 1.0, v136
	v_sub_f32_e32 v179, 1.0, v137
	v_sub_f32_e32 v169, 1.0, v134
	v_sub_f32_e32 v155, 1.0, v135
	v_fma_f32 v153, v180, v153, v136
	v_fma_f32 v181, v179, v181, v137
	v_sub_f32_e32 v178, 1.0, v138
	v_sub_f32_e32 v177, 1.0, v139
	v_fma_f32 v168, v169, v168, v134
	v_fma_f32 v182, v155, v182, v135
	v_log_f32_e32 v153, v153
	v_log_f32_e32 v181, v181
	v_fma_f32 v158, v178, v158, v138
	v_fma_f32 v159, v177, v159, v139
	v_log_f32_e32 v168, v168
	v_log_f32_e32 v182, v182
	v_log_f32_e32 v158, v158
	v_log_f32_e32 v159, v159
	v_cvt_pk_f16_f32 v194, v153, v181
	v_sub_f32_e32 v153, 1.0, v128
	v_cvt_pk_f16_f32 v197, v168, v182
	v_fma_f32 v120, v153, v120, v128
	v_sub_f32_e32 v168, 1.0, v129
	v_cvt_pk_f16_f32 v195, v158, v159
	v_log_f32_e32 v158, v120
	v_fma_f32 v120, v168, v121, v129
	v_log_f32_e32 v159, v120
	v_mul_f32_e32 v120, v122, v154
	v_max_f32_e32 v120, 0xc2a00000, v120
	v_mul_f32_e32 v121, v123, v154
	v_mul_f32_e32 v120, 0xbfb8aa3b, v120
	v_max_f32_e32 v121, 0xc2a00000, v121
	v_exp_f32_e32 v120, v120
	v_mul_f32_e32 v121, 0xbfb8aa3b, v121
	v_exp_f32_e32 v122, v121
	v_sub_f32_e32 v171, 1.0, v132
	v_sub_f32_e32 v170, 1.0, v133
	v_add_f32_e32 v120, 1.0, v120
	v_fma_f32 v160, v171, v160, v132
	v_fma_f32 v161, v170, v161, v133
	v_rcp_f32_e32 v120, v120
	v_add_f32_e32 v122, 1.0, v122
	v_log_f32_e32 v160, v160
	v_log_f32_e32 v161, v161
	v_rcp_f32_e32 v123, v122
	v_sub_f32_e32 v121, 1.0, v130
	v_rcp_f32_e32 v117, v117
	v_fma_f32 v120, v121, v120, v130
	v_sub_f32_e32 v122, 1.0, v131
	v_cvt_pk_f16_f32 v196, v160, v161
	v_log_f32_e32 v160, v120
	v_fma_f32 v120, v122, v123, v131
	v_sub_f32_e32 v123, 1.0, v124
	v_log_f32_e32 v161, v120
	v_fma_f32 v116, v123, v116, v124
	v_sub_f32_e32 v120, 1.0, v125
	v_log_f32_e32 v181, v116
	v_fma_f32 v116, v120, v117, v125
	v_log_f32_e32 v182, v116
	v_mul_f32_e32 v116, v118, v154
	v_max_f32_e32 v116, 0xc2a00000, v116
	v_mul_f32_e32 v117, v119, v154
	v_mul_f32_e32 v116, 0xbfb8aa3b, v116
	v_max_f32_e32 v117, 0xc2a00000, v117
	v_exp_f32_e32 v116, v116
	v_mul_f32_e32 v117, 0xbfb8aa3b, v117
	v_exp_f32_e32 v117, v117
	v_sub_f32_e32 v118, 1.0, v126
	v_add_f32_e32 v116, 1.0, v116
	v_rcp_f32_e32 v116, v116
	v_add_f32_e32 v117, 1.0, v117
	v_rcp_f32_e32 v117, v117
	v_sub_f32_e32 v119, 1.0, v127
	v_fma_f32 v116, v118, v116, v126
	v_log_f32_e32 v154, v116
	v_fma_f32 v116, v119, v117, v127
	v_log_f32_e32 v183, v116
	ds_read2_b32 v[116:117], v176 offset0:16 offset1:32
	v_subrev_u32_e32 v240, s82, v166
	ds_bpermute_b32 v232, v252, v194
	ds_bpermute_b32 v236, v253, v194
	ds_bpermute_b32 v233, v252, v195
	ds_bpermute_b32 v237, v253, v195
	ds_bpermute_b32 v234, v252, v196
	ds_bpermute_b32 v238, v253, v196
	ds_bpermute_b32 v235, v252, v197
	ds_bpermute_b32 v239, v253, v197
	ds_bpermute_b32 v241, v253, v240
	ds_bpermute_b32 v240, v252, v240
	s_waitcnt lgkmcnt(0)
	v_mul_f32_e32 v106, v106, v116
	v_max_f32_e32 v106, 0xc2a00000, v106
	v_mul_f32_e32 v106, 0xbfb8aa3b, v106
	v_exp_f32_e32 v106, v106
	v_mul_f32_e32 v110, v110, v116
	v_max_f32_e32 v110, 0xc2a00000, v110
	v_mul_f32_e32 v111, v111, v116
	v_mul_f32_e32 v110, 0xbfb8aa3b, v110
	v_max_f32_e32 v111, 0xc2a00000, v111
	v_mul_f32_e32 v107, v107, v116
	v_exp_f32_e32 v110, v110
	v_mul_f32_e32 v111, 0xbfb8aa3b, v111
	v_add_f32_e32 v106, 1.0, v106
	v_max_f32_e32 v107, 0xc2a00000, v107
	v_exp_f32_e32 v111, v111
	v_rcp_f32_e32 v106, v106
	v_mul_f32_e32 v107, 0xbfb8aa3b, v107
	v_exp_f32_e32 v107, v107
	v_cvt_pk_f16_f32 v194, v158, v159
	v_or_b32_e32 v158, 16, v152
	v_add_f32_e32 v110, 1.0, v110
	v_mul_f32_e32 v112, v112, v116
	v_mul_f32_e32 v113, v113, v116
	v_cvt_pk_f16_f32 v197, v154, v183
	v_ashrrev_i32_e32 v159, 31, v158
	v_rcp_f32_e32 v154, v110
	v_add_f32_e32 v110, 1.0, v111
	v_max_f32_e32 v112, 0xc2a00000, v112
	v_max_f32_e32 v113, 0xc2a00000, v113
	v_fma_f32 v106, v171, v106, v132
	v_cvt_pk_f16_f32 v195, v160, v161
	v_rcp_f32_e32 v160, v110
	v_lshlrev_b64 v[110:111], 12, v[158:159]
	v_mul_f32_e32 v112, 0xbfb8aa3b, v112
	v_mul_f32_e32 v113, 0xbfb8aa3b, v113
	v_log_f32_e32 v159, v106
	v_add_f32_e32 v106, 1.0, v107
	v_mul_f32_e32 v107, v108, v116
	v_exp_f32_e32 v112, v112
	v_exp_f32_e32 v113, v113
	v_max_f32_e32 v107, 0xc2a00000, v107
	v_mul_f32_e32 v108, v109, v116
	v_mul_f32_e32 v107, 0xbfb8aa3b, v107
	v_max_f32_e32 v108, 0xc2a00000, v108
	v_exp_f32_e32 v107, v107
	v_mul_f32_e32 v108, 0xbfb8aa3b, v108
	v_exp_f32_e32 v108, v108
	v_add_f32_e32 v112, 1.0, v112
	v_add_f32_e32 v113, 1.0, v113
	v_rcp_f32_e32 v112, v112
	v_rcp_f32_e32 v113, v113
	v_mul_f32_e32 v98, v98, v116
	v_rcp_f32_e32 v106, v106
	v_add_f32_e32 v107, 1.0, v107
	v_max_f32_e32 v98, 0xc2a00000, v98
	v_rcp_f32_e32 v107, v107
	v_add_f32_e32 v108, 1.0, v108
	v_mul_f32_e32 v98, 0xbfb8aa3b, v98
	v_rcp_f32_e32 v108, v108
	v_exp_f32_e32 v98, v98
	v_fma_f32 v112, v178, v112, v138
	v_fma_f32 v113, v177, v113, v139
	v_log_f32_e32 v112, v112
	v_log_f32_e32 v113, v113
	v_fma_f32 v106, v170, v106, v133
	v_log_f32_e32 v109, v106
	v_fma_f32 v106, v169, v107, v134
	v_mul_f32_e32 v102, v102, v116
	v_mul_f32_e32 v99, v99, v116
	v_fma_f32 v154, v180, v154, v136
	v_fma_f32 v158, v179, v160, v137
	v_log_f32_e32 v160, v106
	v_fma_f32 v106, v155, v108, v135
	v_max_f32_e32 v102, 0xc2a00000, v102
	v_add_f32_e32 v98, 1.0, v98
	v_max_f32_e32 v99, 0xc2a00000, v99
	v_log_f32_e32 v154, v154
	v_log_f32_e32 v158, v158
	v_log_f32_e32 v161, v106
	v_mul_f32_e32 v102, 0xbfb8aa3b, v102
	v_rcp_f32_e32 v98, v98
	v_mul_f32_e32 v99, 0xbfb8aa3b, v99
	v_cvt_pk_f16_f32 v107, v112, v113
	v_exp_f32_e32 v112, v102
	v_mul_f32_e32 v102, v103, v116
	v_exp_f32_e32 v99, v99
	v_max_f32_e32 v102, 0xc2a00000, v102
	v_lshl_add_u64 v[110:111], s[26:27], 0, v[110:111]
	v_mul_f32_e32 v102, 0xbfb8aa3b, v102
	v_cvt_pk_f16_f32 v106, v154, v158
	v_cvt_pk_f16_f32 v108, v159, v109
	v_cvt_pk_f16_f32 v109, v160, v161
	v_exp_f32_e32 v113, v102
	v_lshl_add_u64 v[102:103], v[110:111], 0, v[114:115]
	v_fma_f32 v98, v123, v98, v124
	v_subrev_u32_e32 v250, s82, v102
	ds_bpermute_b32 v242, v252, v106
	ds_bpermute_b32 v246, v253, v106
	ds_bpermute_b32 v243, v252, v107
	ds_bpermute_b32 v247, v253, v107
	ds_bpermute_b32 v244, v252, v108
	ds_bpermute_b32 v248, v253, v108
	ds_bpermute_b32 v245, v252, v109
	ds_bpermute_b32 v249, v253, v109
	ds_bpermute_b32 v251, v253, v250
	ds_bpermute_b32 v250, v252, v250
	s_waitcnt lgkmcnt(0)
	v_cndmask_b32_e64 v232, v232, v242, s[100:101]
	v_cndmask_b32_e64 v233, v233, v243, s[100:101]
	v_cndmask_b32_e64 v234, v234, v244, s[100:101]
	v_cndmask_b32_e64 v235, v235, v245, s[100:101]
	v_cndmask_b32_e64 v236, v236, v246, s[100:101]
	v_cndmask_b32_e64 v237, v237, v247, s[100:101]
	v_cndmask_b32_e64 v238, v238, v248, s[100:101]
	v_cndmask_b32_e64 v239, v239, v249, s[100:101]
	v_cndmask_b32_e64 v240, v240, v250, s[100:101]
	v_cndmask_b32_e64 v241, v241, v251, s[100:101]
	global_store_dwordx4 v240, v[232:235], s[82:83]
	global_store_dwordx4 v241, v[236:239], s[82:83]
	v_mul_f32_e32 v104, v104, v116
	v_mul_f32_e32 v105, v105, v116
	v_log_f32_e32 v108, v98
	v_add_f32_e32 v98, 1.0, v99
	v_mul_f32_e32 v99, v100, v116
	v_max_f32_e32 v99, 0xc2a00000, v99
	v_mul_f32_e32 v100, v101, v116
	v_max_f32_e32 v104, 0xc2a00000, v104
	v_max_f32_e32 v105, 0xc2a00000, v105
	v_mul_f32_e32 v99, 0xbfb8aa3b, v99
	v_max_f32_e32 v100, 0xc2a00000, v100
	v_mul_f32_e32 v104, 0xbfb8aa3b, v104
	v_mul_f32_e32 v105, 0xbfb8aa3b, v105
	v_exp_f32_e32 v99, v99
	v_mul_f32_e32 v100, 0xbfb8aa3b, v100
	v_exp_f32_e32 v104, v104
	v_exp_f32_e32 v105, v105
	v_exp_f32_e32 v100, v100
	v_rcp_f32_e32 v98, v98
	v_add_f32_e32 v99, 1.0, v99
	v_add_f32_e32 v110, 1.0, v112
	v_add_f32_e32 v111, 1.0, v113
	v_add_f32_e32 v104, 1.0, v104
	v_add_f32_e32 v105, 1.0, v105
	v_rcp_f32_e32 v99, v99
	v_add_f32_e32 v100, 1.0, v100
	v_rcp_f32_e32 v110, v110
	v_rcp_f32_e32 v111, v111
	v_rcp_f32_e32 v104, v104
	v_rcp_f32_e32 v105, v105
	v_rcp_f32_e32 v100, v100
	v_mul_f32_e32 v90, v90, v117
	v_fma_f32 v98, v120, v98, v125
	v_mul_f32_e32 v94, v94, v117
	v_max_f32_e32 v90, 0xc2a00000, v90
	v_log_f32_e32 v101, v98
	v_fma_f32 v98, v118, v99, v126
	v_max_f32_e32 v94, 0xc2a00000, v94
	v_mul_f32_e32 v90, 0xbfb8aa3b, v90
	v_fma_f32 v106, v153, v110, v128
	v_fma_f32 v107, v168, v111, v129
	v_fma_f32 v104, v121, v104, v130
	v_fma_f32 v105, v122, v105, v131
	v_log_f32_e32 v109, v98
	v_fma_f32 v98, v119, v100, v127
	v_mul_f32_e32 v94, 0xbfb8aa3b, v94
	v_exp_f32_e32 v90, v90
	v_log_f32_e32 v106, v106
	v_log_f32_e32 v107, v107
	v_log_f32_e32 v104, v104
	v_log_f32_e32 v105, v105
	v_log_f32_e32 v110, v98
	v_exp_f32_e32 v94, v94
	v_mul_f32_e32 v95, v95, v117
	v_max_f32_e32 v95, 0xc2a00000, v95
	v_mul_f32_e32 v91, v91, v117
	v_mul_f32_e32 v95, 0xbfb8aa3b, v95
	v_add_f32_e32 v90, 1.0, v90
	v_max_f32_e32 v91, 0xc2a00000, v91
	v_cvt_pk_f16_f32 v98, v106, v107
	v_cvt_pk_f16_f32 v99, v104, v105
	v_cvt_pk_f16_f32 v100, v108, v101
	v_cvt_pk_f16_f32 v101, v109, v110
	v_exp_f32_e32 v95, v95
	v_add_f32_e32 v94, 1.0, v94
	v_rcp_f32_e32 v90, v90
	v_mul_f32_e32 v91, 0xbfb8aa3b, v91
	v_subrev_u32_e32 v240, s82, v102
	v_add_u32_e32 v240, 0x40, v240
	ds_bpermute_b32 v232, v252, v98
	ds_bpermute_b32 v236, v253, v98
	ds_bpermute_b32 v233, v252, v99
	ds_bpermute_b32 v237, v253, v99
	ds_bpermute_b32 v234, v252, v100
	ds_bpermute_b32 v238, v253, v100
	ds_bpermute_b32 v235, v252, v101
	ds_bpermute_b32 v239, v253, v101
	ds_bpermute_b32 v241, v253, v240
	ds_bpermute_b32 v240, v252, v240
	v_exp_f32_e32 v91, v91
	v_fma_f32 v90, v171, v90, v132
	v_rcp_f32_e32 v100, v94
	v_or_b32_e32 v98, 32, v152
	v_ashrrev_i32_e32 v99, 31, v98
	v_add_f32_e32 v94, 1.0, v95
	v_rcp_f32_e32 v101, v94
	v_lshlrev_b64 v[94:95], 12, v[98:99]
	v_fma_f32 v98, v180, v100, v136
	v_log_f32_e32 v100, v90
	v_add_f32_e32 v90, 1.0, v91
	v_mul_f32_e32 v91, v92, v117
	v_mul_f32_e32 v96, v96, v117
	v_mul_f32_e32 v97, v97, v117
	v_max_f32_e32 v91, 0xc2a00000, v91
	v_mul_f32_e32 v92, v93, v117
	v_max_f32_e32 v96, 0xc2a00000, v96
	v_max_f32_e32 v97, 0xc2a00000, v97
	v_mul_f32_e32 v91, 0xbfb8aa3b, v91
	v_max_f32_e32 v92, 0xc2a00000, v92
	v_mul_f32_e32 v96, 0xbfb8aa3b, v96
	v_mul_f32_e32 v97, 0xbfb8aa3b, v97
	v_exp_f32_e32 v91, v91
	v_mul_f32_e32 v92, 0xbfb8aa3b, v92
	v_exp_f32_e32 v96, v96
	v_exp_f32_e32 v97, v97
	v_exp_f32_e32 v92, v92
	v_mul_f32_e32 v82, v82, v117
	v_rcp_f32_e32 v90, v90
	v_add_f32_e32 v91, 1.0, v91
	v_max_f32_e32 v82, 0xc2a00000, v82
	v_add_f32_e32 v96, 1.0, v96
	v_add_f32_e32 v97, 1.0, v97
	v_rcp_f32_e32 v91, v91
	v_add_f32_e32 v92, 1.0, v92
	v_mul_f32_e32 v82, 0xbfb8aa3b, v82
	v_rcp_f32_e32 v96, v96
	v_rcp_f32_e32 v97, v97
	v_rcp_f32_e32 v92, v92
	v_exp_f32_e32 v82, v82
	v_fma_f32 v90, v170, v90, v133
	v_log_f32_e32 v93, v90
	v_fma_f32 v90, v169, v91, v134
	v_mul_f32_e32 v83, v83, v117
	v_fma_f32 v99, v179, v101, v137
	v_fma_f32 v96, v178, v96, v138
	v_fma_f32 v97, v177, v97, v139
	v_log_f32_e32 v101, v90
	v_fma_f32 v90, v155, v92, v135
	v_add_f32_e32 v82, 1.0, v82
	v_max_f32_e32 v83, 0xc2a00000, v83
	v_log_f32_e32 v98, v98
	v_log_f32_e32 v99, v99
	v_log_f32_e32 v96, v96
	v_log_f32_e32 v97, v97
	v_log_f32_e32 v102, v90
	v_rcp_f32_e32 v82, v82
	v_mul_f32_e32 v83, 0xbfb8aa3b, v83
	v_exp_f32_e32 v83, v83
	v_lshl_add_u64 v[94:95], s[26:27], 0, v[94:95]
	v_cvt_pk_f16_f32 v90, v98, v99
	v_cvt_pk_f16_f32 v91, v96, v97
	v_cvt_pk_f16_f32 v92, v100, v93
	v_cvt_pk_f16_f32 v93, v101, v102
	v_lshl_add_u64 v[94:95], v[94:95], 0, v[114:115]
	v_fma_f32 v82, v123, v82, v124
	v_subrev_u32_e32 v250, s82, v94
	ds_bpermute_b32 v242, v252, v90
	ds_bpermute_b32 v246, v253, v90
	ds_bpermute_b32 v243, v252, v91
	ds_bpermute_b32 v247, v253, v91
	ds_bpermute_b32 v244, v252, v92
	ds_bpermute_b32 v248, v253, v92
	ds_bpermute_b32 v245, v252, v93
	ds_bpermute_b32 v249, v253, v93
	ds_bpermute_b32 v251, v253, v250
	ds_bpermute_b32 v250, v252, v250
	s_waitcnt lgkmcnt(0)
	v_cndmask_b32_e64 v232, v232, v242, s[100:101]
	v_cndmask_b32_e64 v233, v233, v243, s[100:101]
	v_cndmask_b32_e64 v234, v234, v244, s[100:101]
	v_cndmask_b32_e64 v235, v235, v245, s[100:101]
	v_cndmask_b32_e64 v236, v236, v246, s[100:101]
	v_cndmask_b32_e64 v237, v237, v247, s[100:101]
	v_cndmask_b32_e64 v238, v238, v248, s[100:101]
	v_cndmask_b32_e64 v239, v239, v249, s[100:101]
	v_cndmask_b32_e64 v240, v240, v250, s[100:101]
	v_cndmask_b32_e64 v241, v241, v251, s[100:101]
	global_store_dwordx4 v240, v[232:235], s[82:83]
	global_store_dwordx4 v241, v[236:239], s[82:83]
	v_mul_f32_e32 v86, v86, v117
	v_mul_f32_e32 v87, v87, v117
	v_log_f32_e32 v90, v82
	v_add_f32_e32 v82, 1.0, v83
	v_mul_f32_e32 v83, v84, v117
	v_max_f32_e32 v83, 0xc2a00000, v83
	v_mul_f32_e32 v84, v85, v117
	v_mul_f32_e32 v83, 0xbfb8aa3b, v83
	v_max_f32_e32 v84, 0xc2a00000, v84
	v_exp_f32_e32 v83, v83
	v_mul_f32_e32 v84, 0xbfb8aa3b, v84
	v_exp_f32_e32 v84, v84
	v_rcp_f32_e32 v82, v82
	v_add_f32_e32 v83, 1.0, v83
	v_rcp_f32_e32 v83, v83
	v_add_f32_e32 v84, 1.0, v84
	v_rcp_f32_e32 v84, v84
	v_mul_f32_e32 v88, v88, v117
	v_mul_f32_e32 v89, v89, v117
	v_max_f32_e32 v86, 0xc2a00000, v86
	v_max_f32_e32 v87, 0xc2a00000, v87
	v_max_f32_e32 v88, 0xc2a00000, v88
	v_max_f32_e32 v89, 0xc2a00000, v89
	v_fma_f32 v82, v120, v82, v125
	v_mul_f32_e32 v86, 0xbfb8aa3b, v86
	v_mul_f32_e32 v87, 0xbfb8aa3b, v87
	v_mul_f32_e32 v88, 0xbfb8aa3b, v88
	v_mul_f32_e32 v89, 0xbfb8aa3b, v89
	v_log_f32_e32 v91, v82
	v_fma_f32 v82, v118, v83, v126
	v_exp_f32_e32 v86, v86
	v_exp_f32_e32 v87, v87
	v_exp_f32_e32 v88, v88
	v_exp_f32_e32 v89, v89
	v_log_f32_e32 v92, v82
	v_fma_f32 v82, v119, v84, v127
	v_log_f32_e32 v93, v82
	ds_read2_b32 v[82:83], v176 offset0:48 offset1:128
	v_add_f32_e32 v86, 1.0, v86
	v_add_f32_e32 v87, 1.0, v87
	v_add_f32_e32 v88, 1.0, v88
	v_add_f32_e32 v89, 1.0, v89
	v_rcp_f32_e32 v86, v86
	v_rcp_f32_e32 v87, v87
	v_rcp_f32_e32 v88, v88
	v_rcp_f32_e32 v89, v89
	s_waitcnt lgkmcnt(0)
	v_mul_f32_e32 v74, v74, v82
	v_mul_f32_e32 v78, v78, v82
	v_max_f32_e32 v74, 0xc2a00000, v74
	v_max_f32_e32 v78, 0xc2a00000, v78
	v_mul_f32_e32 v74, 0xbfb8aa3b, v74
	v_fma_f32 v86, v153, v86, v128
	v_fma_f32 v87, v168, v87, v129
	v_fma_f32 v88, v121, v88, v130
	v_fma_f32 v89, v122, v89, v131
	v_mul_f32_e32 v78, 0xbfb8aa3b, v78
	v_exp_f32_e32 v74, v74
	v_log_f32_e32 v86, v86
	v_log_f32_e32 v87, v87
	v_log_f32_e32 v88, v88
	v_log_f32_e32 v89, v89
	v_exp_f32_e32 v78, v78
	v_mul_f32_e32 v79, v79, v82
	v_max_f32_e32 v79, 0xc2a00000, v79
	v_mul_f32_e32 v75, v75, v82
	v_mul_f32_e32 v79, 0xbfb8aa3b, v79
	v_add_f32_e32 v74, 1.0, v74
	v_max_f32_e32 v75, 0xc2a00000, v75
	v_cvt_pk_f16_f32 v84, v86, v87
	v_cvt_pk_f16_f32 v85, v88, v89
	v_cvt_pk_f16_f32 v86, v90, v91
	v_cvt_pk_f16_f32 v87, v92, v93
	v_exp_f32_e32 v79, v79
	v_add_f32_e32 v78, 1.0, v78
	v_rcp_f32_e32 v74, v74
	v_mul_f32_e32 v75, 0xbfb8aa3b, v75
	v_subrev_u32_e32 v240, s82, v94
	v_add_u32_e32 v240, 0x40, v240
	ds_bpermute_b32 v232, v252, v84
	ds_bpermute_b32 v236, v253, v84
	ds_bpermute_b32 v233, v252, v85
	ds_bpermute_b32 v237, v253, v85
	ds_bpermute_b32 v234, v252, v86
	ds_bpermute_b32 v238, v253, v86
	ds_bpermute_b32 v235, v252, v87
	ds_bpermute_b32 v239, v253, v87
	ds_bpermute_b32 v241, v253, v240
	ds_bpermute_b32 v240, v252, v240
	v_exp_f32_e32 v75, v75
	v_mul_f32_e32 v80, v80, v82
	v_rcp_f32_e32 v86, v78
	v_or_b32_e32 v84, 48, v152
	v_mul_f32_e32 v81, v81, v82
	v_ashrrev_i32_e32 v85, 31, v84
	v_add_f32_e32 v78, 1.0, v79
	v_max_f32_e32 v80, 0xc2a00000, v80
	v_max_f32_e32 v81, 0xc2a00000, v81
	v_fma_f32 v74, v171, v74, v132
	v_rcp_f32_e32 v87, v78
	v_lshlrev_b64 v[78:79], 12, v[84:85]
	v_fma_f32 v84, v180, v86, v136
	v_mul_f32_e32 v80, 0xbfb8aa3b, v80
	v_mul_f32_e32 v81, 0xbfb8aa3b, v81
	v_log_f32_e32 v86, v74
	v_add_f32_e32 v74, 1.0, v75
	v_mul_f32_e32 v75, v76, v82
	v_exp_f32_e32 v80, v80
	v_exp_f32_e32 v81, v81
	v_max_f32_e32 v75, 0xc2a00000, v75
	v_mul_f32_e32 v76, v77, v82
	v_mul_f32_e32 v75, 0xbfb8aa3b, v75
	v_max_f32_e32 v76, 0xc2a00000, v76
	v_exp_f32_e32 v75, v75
	v_mul_f32_e32 v76, 0xbfb8aa3b, v76
	v_exp_f32_e32 v76, v76
	v_add_f32_e32 v80, 1.0, v80
	v_add_f32_e32 v81, 1.0, v81
	v_rcp_f32_e32 v80, v80
	v_rcp_f32_e32 v81, v81
	v_mul_f32_e32 v66, v66, v82
	v_rcp_f32_e32 v74, v74
	v_add_f32_e32 v75, 1.0, v75
	v_max_f32_e32 v66, 0xc2a00000, v66
	v_rcp_f32_e32 v75, v75
	v_add_f32_e32 v76, 1.0, v76
	v_mul_f32_e32 v66, 0xbfb8aa3b, v66
	v_rcp_f32_e32 v76, v76
	v_exp_f32_e32 v66, v66
	v_fma_f32 v80, v178, v80, v138
	v_fma_f32 v81, v177, v81, v139
	v_log_f32_e32 v80, v80
	v_log_f32_e32 v81, v81
	v_fma_f32 v74, v170, v74, v133
	v_log_f32_e32 v77, v74
	v_fma_f32 v74, v169, v75, v134
	v_mul_f32_e32 v70, v70, v82
	v_mul_f32_e32 v67, v67, v82
	v_fma_f32 v85, v179, v87, v137
	v_log_f32_e32 v87, v74
	v_fma_f32 v74, v155, v76, v135
	v_max_f32_e32 v70, 0xc2a00000, v70
	v_add_f32_e32 v66, 1.0, v66
	v_max_f32_e32 v67, 0xc2a00000, v67
	v_log_f32_e32 v84, v84
	v_log_f32_e32 v85, v85
	v_log_f32_e32 v88, v74
	v_mul_f32_e32 v70, 0xbfb8aa3b, v70
	v_rcp_f32_e32 v66, v66
	v_mul_f32_e32 v67, 0xbfb8aa3b, v67
	v_cvt_pk_f16_f32 v75, v80, v81
	v_exp_f32_e32 v80, v70
	v_mul_f32_e32 v70, v71, v82
	v_exp_f32_e32 v67, v67
	v_max_f32_e32 v70, 0xc2a00000, v70
	v_lshl_add_u64 v[78:79], s[26:27], 0, v[78:79]
	v_mul_f32_e32 v70, 0xbfb8aa3b, v70
	v_cvt_pk_f16_f32 v74, v84, v85
	v_cvt_pk_f16_f32 v76, v86, v77
	v_cvt_pk_f16_f32 v77, v87, v88
	v_exp_f32_e32 v81, v70
	v_lshl_add_u64 v[70:71], v[78:79], 0, v[114:115]
	v_fma_f32 v66, v123, v66, v124
	v_subrev_u32_e32 v250, s82, v70
	ds_bpermute_b32 v242, v252, v74
	ds_bpermute_b32 v246, v253, v74
	ds_bpermute_b32 v243, v252, v75
	ds_bpermute_b32 v247, v253, v75
	ds_bpermute_b32 v244, v252, v76
	ds_bpermute_b32 v248, v253, v76
	ds_bpermute_b32 v245, v252, v77
	ds_bpermute_b32 v249, v253, v77
	ds_bpermute_b32 v251, v253, v250
	ds_bpermute_b32 v250, v252, v250
	s_waitcnt lgkmcnt(0)
	v_cndmask_b32_e64 v232, v232, v242, s[100:101]
	v_cndmask_b32_e64 v233, v233, v243, s[100:101]
	v_cndmask_b32_e64 v234, v234, v244, s[100:101]
	v_cndmask_b32_e64 v235, v235, v245, s[100:101]
	v_cndmask_b32_e64 v236, v236, v246, s[100:101]
	v_cndmask_b32_e64 v237, v237, v247, s[100:101]
	v_cndmask_b32_e64 v238, v238, v248, s[100:101]
	v_cndmask_b32_e64 v239, v239, v249, s[100:101]
	v_cndmask_b32_e64 v240, v240, v250, s[100:101]
	v_cndmask_b32_e64 v241, v241, v251, s[100:101]
	global_store_dwordx4 v240, v[232:235], s[82:83]
	global_store_dwordx4 v241, v[236:239], s[82:83]
	v_mul_f32_e32 v72, v72, v82
	v_mul_f32_e32 v73, v73, v82
	v_log_f32_e32 v76, v66
	v_add_f32_e32 v66, 1.0, v67
	v_mul_f32_e32 v67, v68, v82
	v_max_f32_e32 v67, 0xc2a00000, v67
	v_mul_f32_e32 v68, v69, v82
	v_max_f32_e32 v72, 0xc2a00000, v72
	v_max_f32_e32 v73, 0xc2a00000, v73
	v_mul_f32_e32 v67, 0xbfb8aa3b, v67
	v_max_f32_e32 v68, 0xc2a00000, v68
	v_mul_f32_e32 v72, 0xbfb8aa3b, v72
	v_mul_f32_e32 v73, 0xbfb8aa3b, v73
	v_exp_f32_e32 v67, v67
	v_mul_f32_e32 v68, 0xbfb8aa3b, v68
	v_exp_f32_e32 v72, v72
	v_exp_f32_e32 v73, v73
	v_exp_f32_e32 v68, v68
	v_mul_f32_e32 v58, v58, v83
	v_rcp_f32_e32 v66, v66
	v_add_f32_e32 v67, 1.0, v67
	v_max_f32_e32 v58, 0xc2a00000, v58
	v_add_f32_e32 v78, 1.0, v80
	v_add_f32_e32 v79, 1.0, v81
	v_add_f32_e32 v72, 1.0, v72
	v_add_f32_e32 v73, 1.0, v73
	v_rcp_f32_e32 v67, v67
	v_add_f32_e32 v68, 1.0, v68
	v_mul_f32_e32 v58, 0xbfb8aa3b, v58
	v_rcp_f32_e32 v78, v78
	v_rcp_f32_e32 v79, v79
	v_rcp_f32_e32 v72, v72
	v_rcp_f32_e32 v73, v73
	v_rcp_f32_e32 v68, v68
	v_exp_f32_e32 v58, v58
	v_fma_f32 v66, v120, v66, v125
	v_log_f32_e32 v69, v66
	v_fma_f32 v66, v118, v67, v126
	v_mul_f32_e32 v59, v59, v83
	v_fma_f32 v74, v153, v78, v128
	v_fma_f32 v75, v168, v79, v129
	v_fma_f32 v72, v121, v72, v130
	v_fma_f32 v73, v122, v73, v131
	v_log_f32_e32 v77, v66
	v_fma_f32 v66, v119, v68, v127
	v_add_f32_e32 v58, 1.0, v58
	v_max_f32_e32 v59, 0xc2a00000, v59
	v_log_f32_e32 v74, v74
	v_log_f32_e32 v75, v75
	v_log_f32_e32 v72, v72
	v_log_f32_e32 v73, v73
	v_log_f32_e32 v78, v66
	v_rcp_f32_e32 v58, v58
	v_mul_f32_e32 v59, 0xbfb8aa3b, v59
	v_exp_f32_e32 v59, v59
	v_mul_f32_e32 v64, v64, v83
	v_mul_f32_e32 v65, v65, v83
	v_max_f32_e32 v64, 0xc2a00000, v64
	v_max_f32_e32 v65, 0xc2a00000, v65
	v_cvt_pk_f16_f32 v66, v74, v75
	v_cvt_pk_f16_f32 v67, v72, v73
	v_cvt_pk_f16_f32 v68, v76, v69
	v_mul_f32_e32 v62, v62, v83
	v_mul_f32_e32 v63, v63, v83
	v_cvt_pk_f16_f32 v69, v77, v78
	v_mul_f32_e32 v64, 0xbfb8aa3b, v64
	v_mul_f32_e32 v65, 0xbfb8aa3b, v65
	v_fma_f32 v58, v171, v58, v132
	v_max_f32_e32 v62, 0xc2a00000, v62
	v_max_f32_e32 v63, 0xc2a00000, v63
	v_subrev_u32_e32 v240, s82, v70
	v_add_u32_e32 v240, 0x40, v240
	ds_bpermute_b32 v232, v252, v66
	ds_bpermute_b32 v236, v253, v66
	ds_bpermute_b32 v233, v252, v67
	ds_bpermute_b32 v237, v253, v67
	ds_bpermute_b32 v234, v252, v68
	ds_bpermute_b32 v238, v253, v68
	ds_bpermute_b32 v235, v252, v69
	ds_bpermute_b32 v239, v253, v69
	ds_bpermute_b32 v241, v253, v240
	ds_bpermute_b32 v240, v252, v240
	v_exp_f32_e32 v64, v64
	v_exp_f32_e32 v65, v65
	v_log_f32_e32 v66, v58
	v_add_f32_e32 v58, 1.0, v59
	v_mul_f32_e32 v59, v60, v83
	v_mul_f32_e32 v62, 0xbfb8aa3b, v62
	v_mul_f32_e32 v63, 0xbfb8aa3b, v63
	v_max_f32_e32 v59, 0xc2a00000, v59
	v_mul_f32_e32 v60, v61, v83
	v_exp_f32_e32 v62, v62
	v_exp_f32_e32 v63, v63
	v_mul_f32_e32 v59, 0xbfb8aa3b, v59
	v_max_f32_e32 v60, 0xc2a00000, v60
	v_exp_f32_e32 v59, v59
	v_mul_f32_e32 v60, 0xbfb8aa3b, v60
	v_add_f32_e32 v64, 1.0, v64
	v_add_f32_e32 v65, 1.0, v65
	v_exp_f32_e32 v60, v60
	v_rcp_f32_e32 v64, v64
	v_rcp_f32_e32 v65, v65
	v_add_f32_e32 v62, 1.0, v62
	v_add_f32_e32 v63, 1.0, v63
	v_mul_f32_e32 v50, v50, v83
	v_rcp_f32_e32 v62, v62
	v_rcp_f32_e32 v63, v63
	v_rcp_f32_e32 v58, v58
	v_add_f32_e32 v59, 1.0, v59
	v_max_f32_e32 v50, 0xc2a00000, v50
	v_rcp_f32_e32 v59, v59
	v_add_f32_e32 v60, 1.0, v60
	v_mul_f32_e32 v50, 0xbfb8aa3b, v50
	v_fma_f32 v64, v178, v64, v138
	v_fma_f32 v65, v177, v65, v139
	v_rcp_f32_e32 v60, v60
	v_exp_f32_e32 v50, v50
	v_log_f32_e32 v64, v64
	v_log_f32_e32 v65, v65
	v_fma_f32 v62, v180, v62, v136
	v_fma_f32 v63, v179, v63, v137
	v_fma_f32 v58, v170, v58, v133
	v_mul_f32_e32 v54, v54, v83
	v_log_f32_e32 v62, v62
	v_log_f32_e32 v63, v63
	v_log_f32_e32 v61, v58
	v_fma_f32 v58, v169, v59, v134
	v_max_f32_e32 v54, 0xc2a00000, v54
	v_mul_f32_e32 v51, v51, v83
	v_log_f32_e32 v67, v58
	v_fma_f32 v58, v155, v60, v135
	v_mul_f32_e32 v54, 0xbfb8aa3b, v54
	v_add_f32_e32 v50, 1.0, v50
	v_max_f32_e32 v51, 0xc2a00000, v51
	v_log_f32_e32 v68, v58
	v_cvt_pk_f16_f32 v59, v64, v65
	v_exp_f32_e32 v64, v54
	v_mul_f32_e32 v54, v55, v83
	v_rcp_f32_e32 v50, v50
	v_mul_f32_e32 v51, 0xbfb8aa3b, v51
	v_max_f32_e32 v54, 0xc2a00000, v54
	v_exp_f32_e32 v51, v51
	v_cvt_pk_f16_f32 v58, v62, v63
	v_lshl_add_u64 v[62:63], v[166:167], 0, s[14:15]
	v_mul_f32_e32 v54, 0xbfb8aa3b, v54
	s_mov_b32 s14, 0x80000
	v_exp_f32_e32 v65, v54
	v_add_co_u32_e32 v54, vcc, s14, v166
	v_cvt_pk_f16_f32 v60, v66, v61
	v_cvt_pk_f16_f32 v61, v67, v68
	v_addc_co_u32_e32 v55, vcc, 0, v167, vcc
	v_fma_f32 v50, v123, v50, v124
	v_subrev_u32_e32 v250, s82, v54
	ds_bpermute_b32 v242, v252, v58
	ds_bpermute_b32 v246, v253, v58
	ds_bpermute_b32 v243, v252, v59
	ds_bpermute_b32 v247, v253, v59
	ds_bpermute_b32 v244, v252, v60
	ds_bpermute_b32 v248, v253, v60
	ds_bpermute_b32 v245, v252, v61
	ds_bpermute_b32 v249, v253, v61
	ds_bpermute_b32 v251, v253, v250
	ds_bpermute_b32 v250, v252, v250
	s_waitcnt lgkmcnt(0)
	v_cndmask_b32_e64 v232, v232, v242, s[100:101]
	v_cndmask_b32_e64 v233, v233, v243, s[100:101]
	v_cndmask_b32_e64 v234, v234, v244, s[100:101]
	v_cndmask_b32_e64 v235, v235, v245, s[100:101]
	v_cndmask_b32_e64 v236, v236, v246, s[100:101]
	v_cndmask_b32_e64 v237, v237, v247, s[100:101]
	v_cndmask_b32_e64 v238, v238, v248, s[100:101]
	v_cndmask_b32_e64 v239, v239, v249, s[100:101]
	v_cndmask_b32_e64 v240, v240, v250, s[100:101]
	v_cndmask_b32_e64 v241, v241, v251, s[100:101]
	global_store_dwordx4 v240, v[232:235], s[82:83]
	global_store_dwordx4 v241, v[236:239], s[82:83]
	v_mul_f32_e32 v56, v56, v83
	v_mul_f32_e32 v57, v57, v83
	v_log_f32_e32 v58, v50
	v_add_f32_e32 v50, 1.0, v51
	v_mul_f32_e32 v51, v52, v83
	v_max_f32_e32 v51, 0xc2a00000, v51
	v_mul_f32_e32 v51, 0xbfb8aa3b, v51
	v_exp_f32_e32 v51, v51
	v_rcp_f32_e32 v50, v50
	v_mul_f32_e32 v52, v53, v83
	v_max_f32_e32 v56, 0xc2a00000, v56
	v_add_f32_e32 v51, 1.0, v51
	v_rcp_f32_e32 v51, v51
	v_fma_f32 v50, v120, v50, v125
	v_log_f32_e32 v59, v50
	v_max_f32_e32 v57, 0xc2a00000, v57
	v_fma_f32 v50, v118, v51, v126
	v_log_f32_e32 v60, v50
	ds_read2_b32 v[50:51], v176 offset0:144 offset1:160
	v_max_f32_e32 v52, 0xc2a00000, v52
	v_mul_f32_e32 v56, 0xbfb8aa3b, v56
	v_mul_f32_e32 v57, 0xbfb8aa3b, v57
	v_mul_f32_e32 v52, 0xbfb8aa3b, v52
	v_exp_f32_e32 v56, v56
	v_exp_f32_e32 v57, v57
	v_exp_f32_e32 v52, v52
	s_waitcnt lgkmcnt(0)
	v_mul_f32_e32 v42, v42, v50
	v_max_f32_e32 v42, 0xc2a00000, v42
	v_add_f32_e32 v64, 1.0, v64
	v_add_f32_e32 v65, 1.0, v65
	v_add_f32_e32 v56, 1.0, v56
	v_add_f32_e32 v57, 1.0, v57
	v_add_f32_e32 v52, 1.0, v52
	v_mul_f32_e32 v42, 0xbfb8aa3b, v42
	v_rcp_f32_e32 v64, v64
	v_rcp_f32_e32 v65, v65
	v_rcp_f32_e32 v56, v56
	v_rcp_f32_e32 v57, v57
	v_rcp_f32_e32 v52, v52
	v_exp_f32_e32 v42, v42
	v_mul_f32_e32 v43, v43, v50
	v_fma_f32 v54, v153, v64, v128
	v_fma_f32 v55, v168, v65, v129
	v_fma_f32 v56, v121, v56, v130
	v_fma_f32 v57, v122, v57, v131
	v_fma_f32 v52, v119, v52, v127
	v_add_f32_e32 v42, 1.0, v42
	v_max_f32_e32 v43, 0xc2a00000, v43
	v_log_f32_e32 v54, v54
	v_log_f32_e32 v55, v55
	v_log_f32_e32 v56, v56
	v_log_f32_e32 v57, v57
	v_log_f32_e32 v61, v52
	v_rcp_f32_e32 v42, v42
	v_mul_f32_e32 v43, 0xbfb8aa3b, v43
	v_exp_f32_e32 v43, v43
	v_mul_f32_e32 v48, v48, v50
	v_mul_f32_e32 v49, v49, v50
	v_max_f32_e32 v48, 0xc2a00000, v48
	v_max_f32_e32 v49, 0xc2a00000, v49
	v_cvt_pk_f16_f32 v52, v54, v55
	v_cvt_pk_f16_f32 v53, v56, v57
	v_cvt_pk_f16_f32 v54, v58, v59
	v_mul_f32_e32 v46, v46, v50
	v_mul_f32_e32 v47, v47, v50
	v_cvt_pk_f16_f32 v55, v60, v61
	v_mul_f32_e32 v48, 0xbfb8aa3b, v48
	v_mul_f32_e32 v49, 0xbfb8aa3b, v49
	v_fma_f32 v42, v171, v42, v132
	v_max_f32_e32 v46, 0xc2a00000, v46
	v_max_f32_e32 v47, 0xc2a00000, v47
	v_subrev_u32_e32 v240, s82, v62
	v_add_u32_e32 v240, 0x40, v240
	ds_bpermute_b32 v232, v252, v52
	ds_bpermute_b32 v236, v253, v52
	ds_bpermute_b32 v233, v252, v53
	ds_bpermute_b32 v237, v253, v53
	ds_bpermute_b32 v234, v252, v54
	ds_bpermute_b32 v238, v253, v54
	ds_bpermute_b32 v235, v252, v55
	ds_bpermute_b32 v239, v253, v55
	ds_bpermute_b32 v241, v253, v240
	ds_bpermute_b32 v240, v252, v240
	v_exp_f32_e32 v48, v48
	v_exp_f32_e32 v49, v49
	v_log_f32_e32 v52, v42
	v_add_f32_e32 v42, 1.0, v43
	v_mul_f32_e32 v43, v44, v50
	v_mul_f32_e32 v46, 0xbfb8aa3b, v46
	v_mul_f32_e32 v47, 0xbfb8aa3b, v47
	v_max_f32_e32 v43, 0xc2a00000, v43
	v_mul_f32_e32 v44, v45, v50
	v_exp_f32_e32 v46, v46
	v_exp_f32_e32 v47, v47
	v_mul_f32_e32 v43, 0xbfb8aa3b, v43
	v_max_f32_e32 v44, 0xc2a00000, v44
	v_exp_f32_e32 v43, v43
	v_mul_f32_e32 v44, 0xbfb8aa3b, v44
	v_add_f32_e32 v48, 1.0, v48
	v_add_f32_e32 v49, 1.0, v49
	v_exp_f32_e32 v44, v44
	v_rcp_f32_e32 v48, v48
	v_rcp_f32_e32 v49, v49
	v_add_f32_e32 v46, 1.0, v46
	v_add_f32_e32 v47, 1.0, v47
	v_mul_f32_e32 v34, v34, v50
	v_rcp_f32_e32 v46, v46
	v_rcp_f32_e32 v47, v47
	v_rcp_f32_e32 v42, v42
	v_add_f32_e32 v43, 1.0, v43
	v_max_f32_e32 v34, 0xc2a00000, v34
	v_rcp_f32_e32 v43, v43
	v_add_f32_e32 v44, 1.0, v44
	v_mul_f32_e32 v34, 0xbfb8aa3b, v34
	v_fma_f32 v48, v178, v48, v138
	v_fma_f32 v49, v177, v49, v139
	v_rcp_f32_e32 v44, v44
	v_exp_f32_e32 v34, v34
	v_log_f32_e32 v48, v48
	v_log_f32_e32 v49, v49
	v_fma_f32 v46, v180, v46, v136
	v_fma_f32 v47, v179, v47, v137
	v_fma_f32 v42, v170, v42, v133
	v_mul_f32_e32 v38, v38, v50
	v_log_f32_e32 v46, v46
	v_log_f32_e32 v47, v47
	v_log_f32_e32 v45, v42
	v_fma_f32 v42, v169, v43, v134
	v_max_f32_e32 v38, 0xc2a00000, v38
	v_mul_f32_e32 v35, v35, v50
	v_log_f32_e32 v53, v42
	v_fma_f32 v42, v155, v44, v135
	v_mul_f32_e32 v38, 0xbfb8aa3b, v38
	v_add_f32_e32 v34, 1.0, v34
	v_max_f32_e32 v35, 0xc2a00000, v35
	v_log_f32_e32 v54, v42
	v_cvt_pk_f16_f32 v43, v48, v49
	v_exp_f32_e32 v48, v38
	v_mul_f32_e32 v38, v39, v50
	v_rcp_f32_e32 v34, v34
	v_mul_f32_e32 v35, 0xbfb8aa3b, v35
	s_mov_b64 s[14:15], 0x90000
	v_max_f32_e32 v38, 0xc2a00000, v38
	v_exp_f32_e32 v35, v35
	v_cvt_pk_f16_f32 v42, v46, v47
	v_lshl_add_u64 v[46:47], v[166:167], 0, s[14:15]
	v_mul_f32_e32 v38, 0xbfb8aa3b, v38
	s_mov_b32 s14, 0x90000
	v_exp_f32_e32 v49, v38
	v_add_co_u32_e32 v38, vcc, s14, v166
	v_cvt_pk_f16_f32 v44, v52, v45
	v_cvt_pk_f16_f32 v45, v53, v54
	v_addc_co_u32_e32 v39, vcc, 0, v167, vcc
	v_fma_f32 v34, v123, v34, v124
	v_subrev_u32_e32 v250, s82, v38
	ds_bpermute_b32 v242, v252, v42
	ds_bpermute_b32 v246, v253, v42
	ds_bpermute_b32 v243, v252, v43
	ds_bpermute_b32 v247, v253, v43
	ds_bpermute_b32 v244, v252, v44
	ds_bpermute_b32 v248, v253, v44
	ds_bpermute_b32 v245, v252, v45
	ds_bpermute_b32 v249, v253, v45
	ds_bpermute_b32 v251, v253, v250
	ds_bpermute_b32 v250, v252, v250
	s_waitcnt lgkmcnt(0)
	v_cndmask_b32_e64 v232, v232, v242, s[100:101]
	v_cndmask_b32_e64 v233, v233, v243, s[100:101]
	v_cndmask_b32_e64 v234, v234, v244, s[100:101]
	v_cndmask_b32_e64 v235, v235, v245, s[100:101]
	v_cndmask_b32_e64 v236, v236, v246, s[100:101]
	v_cndmask_b32_e64 v237, v237, v247, s[100:101]
	v_cndmask_b32_e64 v238, v238, v248, s[100:101]
	v_cndmask_b32_e64 v239, v239, v249, s[100:101]
	v_cndmask_b32_e64 v240, v240, v250, s[100:101]
	v_cndmask_b32_e64 v241, v241, v251, s[100:101]
	global_store_dwordx4 v240, v[232:235], s[82:83]
	global_store_dwordx4 v241, v[236:239], s[82:83]
	v_mul_f32_e32 v40, v40, v50
	v_mul_f32_e32 v41, v41, v50
	v_log_f32_e32 v42, v34
	v_add_f32_e32 v34, 1.0, v35
	v_mul_f32_e32 v35, v36, v50
	v_max_f32_e32 v35, 0xc2a00000, v35
	v_mul_f32_e32 v36, v37, v50
	v_max_f32_e32 v40, 0xc2a00000, v40
	v_max_f32_e32 v41, 0xc2a00000, v41
	v_mul_f32_e32 v35, 0xbfb8aa3b, v35
	v_max_f32_e32 v36, 0xc2a00000, v36
	v_mul_f32_e32 v40, 0xbfb8aa3b, v40
	v_mul_f32_e32 v41, 0xbfb8aa3b, v41
	v_exp_f32_e32 v35, v35
	v_mul_f32_e32 v36, 0xbfb8aa3b, v36
	v_exp_f32_e32 v40, v40
	v_exp_f32_e32 v41, v41
	v_exp_f32_e32 v36, v36
	v_mul_f32_e32 v26, v26, v51
	v_rcp_f32_e32 v34, v34
	v_add_f32_e32 v35, 1.0, v35
	v_max_f32_e32 v26, 0xc2a00000, v26
	v_add_f32_e32 v48, 1.0, v48
	v_add_f32_e32 v49, 1.0, v49
	v_add_f32_e32 v40, 1.0, v40
	v_add_f32_e32 v41, 1.0, v41
	v_rcp_f32_e32 v35, v35
	v_add_f32_e32 v36, 1.0, v36
	v_mul_f32_e32 v26, 0xbfb8aa3b, v26
	v_rcp_f32_e32 v48, v48
	v_rcp_f32_e32 v49, v49
	v_rcp_f32_e32 v40, v40
	v_rcp_f32_e32 v41, v41
	v_rcp_f32_e32 v36, v36
	v_exp_f32_e32 v26, v26
	v_fma_f32 v34, v120, v34, v125
	v_log_f32_e32 v37, v34
	v_fma_f32 v34, v118, v35, v126
	v_mul_f32_e32 v27, v27, v51
	v_fma_f32 v38, v153, v48, v128
	v_fma_f32 v39, v168, v49, v129
	v_fma_f32 v40, v121, v40, v130
	v_fma_f32 v41, v122, v41, v131
	v_log_f32_e32 v43, v34
	v_fma_f32 v34, v119, v36, v127
	v_add_f32_e32 v26, 1.0, v26
	v_max_f32_e32 v27, 0xc2a00000, v27
	v_log_f32_e32 v38, v38
	v_log_f32_e32 v39, v39
	v_log_f32_e32 v40, v40
	v_log_f32_e32 v41, v41
	v_log_f32_e32 v44, v34
	v_rcp_f32_e32 v26, v26
	v_mul_f32_e32 v27, 0xbfb8aa3b, v27
	v_exp_f32_e32 v27, v27
	v_mul_f32_e32 v32, v32, v51
	v_mul_f32_e32 v33, v33, v51
	v_max_f32_e32 v32, 0xc2a00000, v32
	v_max_f32_e32 v33, 0xc2a00000, v33
	v_cvt_pk_f16_f32 v34, v38, v39
	v_cvt_pk_f16_f32 v35, v40, v41
	v_cvt_pk_f16_f32 v36, v42, v37
	v_mul_f32_e32 v30, v30, v51
	v_mul_f32_e32 v31, v31, v51
	v_cvt_pk_f16_f32 v37, v43, v44
	v_mul_f32_e32 v32, 0xbfb8aa3b, v32
	v_mul_f32_e32 v33, 0xbfb8aa3b, v33
	v_fma_f32 v26, v171, v26, v132
	v_max_f32_e32 v30, 0xc2a00000, v30
	v_max_f32_e32 v31, 0xc2a00000, v31
	v_subrev_u32_e32 v240, s82, v46
	v_add_u32_e32 v240, 0x40, v240
	ds_bpermute_b32 v232, v252, v34
	ds_bpermute_b32 v236, v253, v34
	ds_bpermute_b32 v233, v252, v35
	ds_bpermute_b32 v237, v253, v35
	ds_bpermute_b32 v234, v252, v36
	ds_bpermute_b32 v238, v253, v36
	ds_bpermute_b32 v235, v252, v37
	ds_bpermute_b32 v239, v253, v37
	ds_bpermute_b32 v241, v253, v240
	ds_bpermute_b32 v240, v252, v240
	v_exp_f32_e32 v32, v32
	v_exp_f32_e32 v33, v33
	v_log_f32_e32 v34, v26
	v_add_f32_e32 v26, 1.0, v27
	v_mul_f32_e32 v27, v28, v51
	v_mul_f32_e32 v30, 0xbfb8aa3b, v30
	v_mul_f32_e32 v31, 0xbfb8aa3b, v31
	v_max_f32_e32 v27, 0xc2a00000, v27
	v_mul_f32_e32 v28, v29, v51
	v_exp_f32_e32 v30, v30
	v_exp_f32_e32 v31, v31
	v_mul_f32_e32 v27, 0xbfb8aa3b, v27
	v_max_f32_e32 v28, 0xc2a00000, v28
	v_exp_f32_e32 v27, v27
	v_mul_f32_e32 v28, 0xbfb8aa3b, v28
	v_add_f32_e32 v32, 1.0, v32
	v_add_f32_e32 v33, 1.0, v33
	v_exp_f32_e32 v28, v28
	v_rcp_f32_e32 v32, v32
	v_rcp_f32_e32 v33, v33
	v_add_f32_e32 v30, 1.0, v30
	v_add_f32_e32 v31, 1.0, v31
	v_mul_f32_e32 v18, v18, v51
	v_rcp_f32_e32 v30, v30
	v_rcp_f32_e32 v31, v31
	v_rcp_f32_e32 v26, v26
	v_add_f32_e32 v27, 1.0, v27
	v_max_f32_e32 v18, 0xc2a00000, v18
	v_rcp_f32_e32 v27, v27
	v_add_f32_e32 v28, 1.0, v28
	v_mul_f32_e32 v18, 0xbfb8aa3b, v18
	v_fma_f32 v32, v178, v32, v138
	v_fma_f32 v33, v177, v33, v139
	v_rcp_f32_e32 v28, v28
	v_exp_f32_e32 v18, v18
	v_log_f32_e32 v32, v32
	v_log_f32_e32 v33, v33
	v_fma_f32 v30, v180, v30, v136
	v_fma_f32 v31, v179, v31, v137
	v_fma_f32 v26, v170, v26, v133
	v_mul_f32_e32 v22, v22, v51
	v_log_f32_e32 v30, v30
	v_log_f32_e32 v31, v31
	v_log_f32_e32 v29, v26
	v_fma_f32 v26, v169, v27, v134
	v_max_f32_e32 v22, 0xc2a00000, v22
	v_mul_f32_e32 v19, v19, v51
	v_log_f32_e32 v35, v26
	v_fma_f32 v26, v155, v28, v135
	v_mul_f32_e32 v22, 0xbfb8aa3b, v22
	v_add_f32_e32 v18, 1.0, v18
	v_max_f32_e32 v19, 0xc2a00000, v19
	v_log_f32_e32 v36, v26
	v_cvt_pk_f16_f32 v27, v32, v33
	v_exp_f32_e32 v32, v22
	v_mul_f32_e32 v22, v23, v51
	v_rcp_f32_e32 v18, v18
	v_mul_f32_e32 v19, 0xbfb8aa3b, v19
	s_mov_b64 s[14:15], 0xa0000
	v_max_f32_e32 v22, 0xc2a00000, v22
	v_exp_f32_e32 v19, v19
	v_cvt_pk_f16_f32 v26, v30, v31
	v_lshl_add_u64 v[30:31], v[166:167], 0, s[14:15]
	v_mul_f32_e32 v22, 0xbfb8aa3b, v22
	s_mov_b32 s14, 0xa0000
	v_exp_f32_e32 v33, v22
	v_add_co_u32_e32 v22, vcc, s14, v166
	v_cvt_pk_f16_f32 v28, v34, v29
	v_cvt_pk_f16_f32 v29, v35, v36
	v_addc_co_u32_e32 v23, vcc, 0, v167, vcc
	v_fma_f32 v18, v123, v18, v124
	v_subrev_u32_e32 v250, s82, v22
	ds_bpermute_b32 v242, v252, v26
	ds_bpermute_b32 v246, v253, v26
	ds_bpermute_b32 v243, v252, v27
	ds_bpermute_b32 v247, v253, v27
	ds_bpermute_b32 v244, v252, v28
	ds_bpermute_b32 v248, v253, v28
	ds_bpermute_b32 v245, v252, v29
	ds_bpermute_b32 v249, v253, v29
	ds_bpermute_b32 v251, v253, v250
	ds_bpermute_b32 v250, v252, v250
	s_waitcnt lgkmcnt(0)
	v_cndmask_b32_e64 v232, v232, v242, s[100:101]
	v_cndmask_b32_e64 v233, v233, v243, s[100:101]
	v_cndmask_b32_e64 v234, v234, v244, s[100:101]
	v_cndmask_b32_e64 v235, v235, v245, s[100:101]
	v_cndmask_b32_e64 v236, v236, v246, s[100:101]
	v_cndmask_b32_e64 v237, v237, v247, s[100:101]
	v_cndmask_b32_e64 v238, v238, v248, s[100:101]
	v_cndmask_b32_e64 v239, v239, v249, s[100:101]
	v_cndmask_b32_e64 v240, v240, v250, s[100:101]
	v_cndmask_b32_e64 v241, v241, v251, s[100:101]
	global_store_dwordx4 v240, v[232:235], s[82:83]
	global_store_dwordx4 v241, v[236:239], s[82:83]
	v_mul_f32_e32 v24, v24, v51
	v_mul_f32_e32 v25, v25, v51
	v_log_f32_e32 v26, v18
	v_add_f32_e32 v18, 1.0, v19
	v_mul_f32_e32 v19, v20, v51
	v_max_f32_e32 v19, 0xc2a00000, v19
	v_mul_f32_e32 v20, v21, v51
	ds_read_b32 v28, v176 offset:704
	v_max_f32_e32 v24, 0xc2a00000, v24
	v_max_f32_e32 v25, 0xc2a00000, v25
	v_mul_f32_e32 v19, 0xbfb8aa3b, v19
	v_max_f32_e32 v20, 0xc2a00000, v20
	v_mul_f32_e32 v24, 0xbfb8aa3b, v24
	v_mul_f32_e32 v25, 0xbfb8aa3b, v25
	v_exp_f32_e32 v19, v19
	v_mul_f32_e32 v20, 0xbfb8aa3b, v20
	v_exp_f32_e32 v24, v24
	v_exp_f32_e32 v25, v25
	v_exp_f32_e32 v20, v20
	s_waitcnt lgkmcnt(0)
	v_mul_f32_e32 v10, v10, v28
	v_rcp_f32_e32 v18, v18
	v_add_f32_e32 v19, 1.0, v19
	v_max_f32_e32 v10, 0xc2a00000, v10
	v_add_f32_e32 v32, 1.0, v32
	v_add_f32_e32 v33, 1.0, v33
	v_add_f32_e32 v24, 1.0, v24
	v_add_f32_e32 v25, 1.0, v25
	v_rcp_f32_e32 v19, v19
	v_add_f32_e32 v20, 1.0, v20
	v_mul_f32_e32 v10, 0xbfb8aa3b, v10
	v_rcp_f32_e32 v32, v32
	v_rcp_f32_e32 v33, v33
	v_rcp_f32_e32 v24, v24
	v_rcp_f32_e32 v25, v25
	v_rcp_f32_e32 v20, v20
	v_exp_f32_e32 v10, v10
	v_fma_f32 v18, v120, v18, v125
	v_log_f32_e32 v21, v18
	v_fma_f32 v18, v118, v19, v126
	v_mul_f32_e32 v11, v11, v28
	v_fma_f32 v22, v153, v32, v128
	v_fma_f32 v23, v168, v33, v129
	v_fma_f32 v24, v121, v24, v130
	v_fma_f32 v25, v122, v25, v131
	v_log_f32_e32 v27, v18
	v_fma_f32 v18, v119, v20, v127
	v_add_f32_e32 v10, 1.0, v10
	v_max_f32_e32 v11, 0xc2a00000, v11
	v_log_f32_e32 v22, v22
	v_log_f32_e32 v23, v23
	v_log_f32_e32 v24, v24
	v_log_f32_e32 v25, v25
	v_log_f32_e32 v29, v18
	v_rcp_f32_e32 v10, v10
	v_mul_f32_e32 v11, 0xbfb8aa3b, v11
	v_mul_f32_e32 v14, v14, v28
	v_mul_f32_e32 v15, v15, v28
	v_exp_f32_e32 v11, v11
	v_max_f32_e32 v14, 0xc2a00000, v14
	v_max_f32_e32 v15, 0xc2a00000, v15
	v_mul_f32_e32 v14, 0xbfb8aa3b, v14
	v_mul_f32_e32 v15, 0xbfb8aa3b, v15
	v_cvt_pk_f16_f32 v18, v22, v23
	v_cvt_pk_f16_f32 v19, v24, v25
	v_cvt_pk_f16_f32 v20, v26, v21
	v_exp_f32_e32 v14, v14
	v_exp_f32_e32 v15, v15
	v_cvt_pk_f16_f32 v21, v27, v29
	v_fma_f32 v10, v171, v10, v132
	v_subrev_u32_e32 v240, s82, v30
	v_add_u32_e32 v240, 0x40, v240
	ds_bpermute_b32 v232, v252, v18
	ds_bpermute_b32 v236, v253, v18
	ds_bpermute_b32 v233, v252, v19
	ds_bpermute_b32 v237, v253, v19
	ds_bpermute_b32 v234, v252, v20
	ds_bpermute_b32 v238, v253, v20
	ds_bpermute_b32 v235, v252, v21
	ds_bpermute_b32 v239, v253, v21
	ds_bpermute_b32 v241, v253, v240
	ds_bpermute_b32 v240, v252, v240
	v_add_f32_e32 v14, 1.0, v14
	v_add_f32_e32 v15, 1.0, v15
	v_log_f32_e32 v18, v10
	v_add_f32_e32 v10, 1.0, v11
	v_mul_f32_e32 v11, v12, v28
	v_max_f32_e32 v11, 0xc2a00000, v11
	v_mul_f32_e32 v11, 0xbfb8aa3b, v11
	v_exp_f32_e32 v11, v11
	v_rcp_f32_e32 v14, v14
	v_rcp_f32_e32 v15, v15
	v_mul_f32_e32 v16, v16, v28
	v_mul_f32_e32 v17, v17, v28
	v_rcp_f32_e32 v10, v10
	v_mul_f32_e32 v12, v13, v28
	v_add_f32_e32 v11, 1.0, v11
	v_fma_f32 v14, v180, v14, v136
	v_fma_f32 v15, v179, v15, v137
	v_max_f32_e32 v16, 0xc2a00000, v16
	v_max_f32_e32 v17, 0xc2a00000, v17
	v_max_f32_e32 v12, 0xc2a00000, v12
	v_rcp_f32_e32 v11, v11
	v_log_f32_e32 v14, v14
	v_mul_f32_e32 v16, 0xbfb8aa3b, v16
	v_mul_f32_e32 v17, 0xbfb8aa3b, v17
	v_log_f32_e32 v15, v15
	v_mul_f32_e32 v12, 0xbfb8aa3b, v12
	v_exp_f32_e32 v16, v16
	v_exp_f32_e32 v17, v17
	v_exp_f32_e32 v12, v12
	v_mul_f32_e32 v6, v6, v28
	v_fma_f32 v10, v170, v10, v133
	v_max_f32_e32 v6, 0xc2a00000, v6
	v_log_f32_e32 v13, v10
	v_fma_f32 v10, v169, v11, v134
	v_mul_f32_e32 v6, 0xbfb8aa3b, v6
	v_log_f32_e32 v19, v10
	v_cvt_pk_f16_f32 v10, v14, v15
	v_exp_f32_e32 v14, v6
	v_mul_f32_e32 v6, v7, v28
	v_mul_f32_e32 v8, v8, v28
	v_mul_f32_e32 v9, v9, v28
	v_mul_f32_e32 v2, v2, v28
	v_mul_f32_e32 v3, v3, v28
	v_mul_f32_e32 v4, v4, v28
	v_mul_f32_e32 v5, v5, v28
	v_add_f32_e32 v16, 1.0, v16
	v_add_f32_e32 v17, 1.0, v17
	v_add_f32_e32 v12, 1.0, v12
	v_max_f32_e32 v6, 0xc2a00000, v6
	v_max_f32_e32 v8, 0xc2a00000, v8
	v_max_f32_e32 v9, 0xc2a00000, v9
	v_max_f32_e32 v2, 0xc2a00000, v2
	v_max_f32_e32 v3, 0xc2a00000, v3
	v_max_f32_e32 v4, 0xc2a00000, v4
	v_max_f32_e32 v5, 0xc2a00000, v5
	v_rcp_f32_e32 v16, v16
	v_rcp_f32_e32 v17, v17
	v_rcp_f32_e32 v12, v12
	v_mul_f32_e32 v6, 0xbfb8aa3b, v6
	v_mul_f32_e32 v8, 0xbfb8aa3b, v8
	v_mul_f32_e32 v9, 0xbfb8aa3b, v9
	v_mul_f32_e32 v2, 0xbfb8aa3b, v2
	v_mul_f32_e32 v3, 0xbfb8aa3b, v3
	v_mul_f32_e32 v4, 0xbfb8aa3b, v4
	v_mul_f32_e32 v5, 0xbfb8aa3b, v5
	v_exp_f32_e32 v15, v6
	v_exp_f32_e32 v8, v8
	v_exp_f32_e32 v9, v9
	v_exp_f32_e32 v2, v2
	v_exp_f32_e32 v3, v3
	v_exp_f32_e32 v4, v4
	v_exp_f32_e32 v5, v5
	v_fma_f32 v16, v178, v16, v138
	v_fmac_f32_e32 v139, v177, v17
	v_fmac_f32_e32 v135, v155, v12
	v_log_f32_e32 v16, v16
	v_log_f32_e32 v17, v139
	v_log_f32_e32 v20, v135
	v_add_f32_e32 v14, 1.0, v14
	v_add_f32_e32 v15, 1.0, v15
	v_add_f32_e32 v8, 1.0, v8
	v_add_f32_e32 v9, 1.0, v9
	v_add_f32_e32 v2, 1.0, v2
	v_add_f32_e32 v3, 1.0, v3
	v_add_f32_e32 v4, 1.0, v4
	v_add_f32_e32 v5, 1.0, v5
	s_mov_b64 s[14:15], 0xb0000
	v_rcp_f32_e32 v14, v14
	v_rcp_f32_e32 v15, v15
	v_rcp_f32_e32 v8, v8
	v_rcp_f32_e32 v9, v9
	v_rcp_f32_e32 v2, v2
	v_rcp_f32_e32 v3, v3
	v_rcp_f32_e32 v4, v4
	v_rcp_f32_e32 v5, v5
	v_lshl_add_u64 v[136:137], v[166:167], 0, s[14:15]
	s_mov_b32 s14, 0xb0000
	v_add_co_u32_e32 v6, vcc, s14, v166
	v_cvt_pk_f16_f32 v11, v16, v17
	v_cvt_pk_f16_f32 v12, v18, v13
	v_cvt_pk_f16_f32 v13, v19, v20
	v_addc_co_u32_e32 v7, vcc, 0, v167, vcc
	v_subrev_u32_e32 v250, s82, v6
	ds_bpermute_b32 v242, v252, v10
	ds_bpermute_b32 v246, v253, v10
	ds_bpermute_b32 v243, v252, v11
	ds_bpermute_b32 v247, v253, v11
	ds_bpermute_b32 v244, v252, v12
	ds_bpermute_b32 v248, v253, v12
	ds_bpermute_b32 v245, v252, v13
	ds_bpermute_b32 v249, v253, v13
	ds_bpermute_b32 v251, v253, v250
	ds_bpermute_b32 v250, v252, v250
	s_waitcnt lgkmcnt(0)
	v_cndmask_b32_e64 v232, v232, v242, s[100:101]
	v_cndmask_b32_e64 v233, v233, v243, s[100:101]
	v_cndmask_b32_e64 v234, v234, v244, s[100:101]
	v_cndmask_b32_e64 v235, v235, v245, s[100:101]
	v_cndmask_b32_e64 v236, v236, v246, s[100:101]
	v_cndmask_b32_e64 v237, v237, v247, s[100:101]
	v_cndmask_b32_e64 v238, v238, v248, s[100:101]
	v_cndmask_b32_e64 v239, v239, v249, s[100:101]
	v_cndmask_b32_e64 v240, v240, v250, s[100:101]
	v_cndmask_b32_e64 v241, v241, v251, s[100:101]
	global_store_dwordx4 v240, v[232:235], s[82:83]
	global_store_dwordx4 v241, v[236:239], s[82:83]
	v_fma_f32 v6, v153, v14, v128
	v_fma_f32 v7, v168, v15, v129
	v_fma_f32 v8, v121, v8, v130
	v_fmac_f32_e32 v131, v122, v9
	v_fma_f32 v2, v123, v2, v124
	v_fma_f32 v3, v120, v3, v125
	v_fma_f32 v4, v118, v4, v126
	v_fmac_f32_e32 v127, v119, v5
	v_log_f32_e32 v6, v6
	v_log_f32_e32 v7, v7
	v_log_f32_e32 v8, v8
	v_log_f32_e32 v9, v131
	v_log_f32_e32 v2, v2
	v_log_f32_e32 v3, v3
	v_log_f32_e32 v4, v4
	v_log_f32_e32 v5, v127
	v_cvt_pk_f16_f32 v196, v181, v182
	v_cvt_pk_f16_f32 v132, v6, v7
	v_cvt_pk_f16_f32 v133, v8, v9
	v_cvt_pk_f16_f32 v134, v2, v3
	v_cvt_pk_f16_f32 v135, v4, v5
	v_subrev_u32_e32 v240, s82, v166
	v_add_u32_e32 v240, 0x40, v240
	ds_bpermute_b32 v232, v252, v194
	ds_bpermute_b32 v236, v253, v194
	ds_bpermute_b32 v233, v252, v195
	ds_bpermute_b32 v237, v253, v195
	ds_bpermute_b32 v234, v252, v196
	ds_bpermute_b32 v238, v253, v196
	ds_bpermute_b32 v235, v252, v197
	ds_bpermute_b32 v239, v253, v197
	ds_bpermute_b32 v241, v253, v240
	ds_bpermute_b32 v240, v252, v240
	s_andn2_b64 vcc, exec, s[38:39]
	s_mov_b64 s[28:29], -1
	v_subrev_u32_e32 v250, s82, v136
	v_add_u32_e32 v250, 0x40, v250
	ds_bpermute_b32 v242, v252, v132
	ds_bpermute_b32 v246, v253, v132
	ds_bpermute_b32 v243, v252, v133
	ds_bpermute_b32 v247, v253, v133
	ds_bpermute_b32 v244, v252, v134
	ds_bpermute_b32 v248, v253, v134
	ds_bpermute_b32 v245, v252, v135
	ds_bpermute_b32 v249, v253, v135
	ds_bpermute_b32 v251, v253, v250
	ds_bpermute_b32 v250, v252, v250
	s_waitcnt lgkmcnt(0)
	v_cndmask_b32_e64 v232, v232, v242, s[100:101]
	v_cndmask_b32_e64 v233, v233, v243, s[100:101]
	v_cndmask_b32_e64 v234, v234, v244, s[100:101]
	v_cndmask_b32_e64 v235, v235, v245, s[100:101]
	v_cndmask_b32_e64 v236, v236, v246, s[100:101]
	v_cndmask_b32_e64 v237, v237, v247, s[100:101]
	v_cndmask_b32_e64 v238, v238, v248, s[100:101]
	v_cndmask_b32_e64 v239, v239, v249, s[100:101]
	v_cndmask_b32_e64 v240, v240, v250, s[100:101]
	v_cndmask_b32_e64 v241, v241, v251, s[100:101]
	global_store_dwordx4 v240, v[232:235], s[82:83]
	global_store_dwordx4 v241, v[236:239], s[82:83]
	s_cbranch_vccnz .LBB0_495

.LBB0_1082:
	v_mbcnt_lo_u32_b32 v231, -1, 0
	v_mbcnt_hi_u32_b32 v231, -1, v231
	v_and_b32_e32 v253, 3, v231
	v_lshrrev_b32_e32 v252, 3, v231
	v_lshl_add_u32 v252, v253, 4, v252
	v_lshlrev_b32_e32 v252, 2, v252
	v_lshrrev_b32_e32 v231, 2, v231
	v_lshl_add_u32 v231, v253, 4, v231
	v_lshlrev_b32_e32 v231, 2, v231
	v_add_u32_e32 v253, 32, v252
	s_mov_b32 s100, 0xf0f0f0f0
	s_mov_b32 s101, 0xf0f0f0f0
	v_pk_mul_f32 v[148:149], v[118:119], v[118:119]
	v_pk_mul_f32 v[150:151], v[126:127], v[126:127]
	v_pk_fma_f32 v[148:149], v[116:117], v[116:117], v[148:149]
	v_pk_fma_f32 v[150:151], v[124:125], v[124:125], v[150:151]
	v_lshl_add_u32 v144, s46, 8, v1
	v_pk_add_f32 v[152:153], v[148:149], v[150:151]
	v_cvt_pk_bf16_f32 v149, v118, v119
	v_cvt_pk_bf16_f32 v150, v124, v125
	v_pk_mul_f32 v[118:119], v[122:123], v[122:123]
	v_pk_mul_f32 v[124:125], v[130:131], v[130:131]
	v_pk_fma_f32 v[118:119], v[120:121], v[120:121], v[118:119]
	v_pk_fma_f32 v[124:125], v[128:129], v[128:129], v[124:125]
	s_lshl_b32 s16, s46, 5
	v_pk_add_f32 v[118:119], v[118:119], v[124:125]
	s_lshl_b32 s46, s48, 2
	v_pk_add_f32 v[124:125], v[152:153], v[118:119]
	s_or_b32 s17, s46, s12
	v_add_f32_e32 v124, v124, v125
	ds_swizzle_b32 v125, v124 offset:swizzle(SWAP,16)
	s_add_i32 s16, s17, s16
	s_ashr_i32 s17, s16, 31
	s_lshl_b64 s[16:17], s[16:17], 15
	v_cvt_pk_bf16_f32 v148, v116, v117
	v_lshl_add_u64 v[116:117], v[138:139], 0, s[16:17]
	v_cvt_pk_bf16_f32 v118, v120, v121
	v_cvt_pk_bf16_f32 v119, v122, v123
	v_cvt_pk_bf16_f32 v120, v128, v129
	v_cvt_pk_bf16_f32 v121, v130, v131
	v_subrev_u32_e32 v240, s82, v116
	v_add_u32_e32 v240, 0x40, v240
	ds_bpermute_b32 v232, v252, v118
	ds_bpermute_b32 v236, v253, v118
	ds_bpermute_b32 v233, v252, v119
	ds_bpermute_b32 v237, v253, v119
	ds_bpermute_b32 v234, v252, v120
	ds_bpermute_b32 v238, v253, v120
	ds_bpermute_b32 v235, v252, v121
	ds_bpermute_b32 v239, v253, v121
	ds_bpermute_b32 v241, v253, v240
	ds_bpermute_b32 v240, v252, v240
	s_ashr_i32 s47, s46, 31
	v_cvt_pk_bf16_f32 v151, v126, v127
	v_subrev_u32_e32 v250, s82, v116
	ds_bpermute_b32 v242, v252, v148
	ds_bpermute_b32 v246, v253, v148
	ds_bpermute_b32 v243, v252, v149
	ds_bpermute_b32 v247, v253, v149
	ds_bpermute_b32 v244, v252, v150
	ds_bpermute_b32 v248, v253, v150
	ds_bpermute_b32 v245, v252, v151
	ds_bpermute_b32 v249, v253, v151
	ds_bpermute_b32 v251, v253, v250
	ds_bpermute_b32 v250, v252, v250
	s_waitcnt lgkmcnt(0)
	v_cndmask_b32_e64 v232, v232, v242, s[100:101]
	v_cndmask_b32_e64 v233, v233, v243, s[100:101]
	v_cndmask_b32_e64 v234, v234, v244, s[100:101]
	v_cndmask_b32_e64 v235, v235, v245, s[100:101]
	v_cndmask_b32_e64 v236, v236, v246, s[100:101]
	v_cndmask_b32_e64 v237, v237, v247, s[100:101]
	v_cndmask_b32_e64 v238, v238, v248, s[100:101]
	v_cndmask_b32_e64 v239, v239, v249, s[100:101]
	v_cndmask_b32_e64 v240, v240, v250, s[100:101]
	v_cndmask_b32_e64 v241, v241, v251, s[100:101]
	global_store_dwordx4 v240, v[232:235], s[82:83]
	global_store_dwordx4 v241, v[236:239], s[82:83]
	s_waitcnt lgkmcnt(0)
	v_add_f32_e32 v118, v124, v125
	v_mov_b32_e32 v119, v118
	s_nop 1
	v_permlane32_swap_b32_e32 v118, v119
	s_and_saveexec_b64 s[48:49], s[38:39]
	s_cbranch_execz .LBB0_1084
	v_ashrrev_i32_e32 v145, 31, v144
	v_add_f32_e32 v120, v118, v119
	v_lshlrev_b64 v[118:119], 7, v[144:145]
	v_lshl_add_u64 v[118:119], s[8:9], 0, v[118:119]
	v_lshl_add_u64 v[118:119], s[46:47], 2, v[118:119]
	s_lshl_b32 s24, s12, 2
	v_lshl_add_u64 v[118:119], v[118:119], 0, s[24:25]
	global_store_dword v[118:119], v120, off
.LBB0_1084:
	s_or_b64 exec, exec, s[48:49]
	v_pk_mul_f32 v[118:119], v[100:101], v[100:101]
	v_pk_mul_f32 v[120:121], v[104:105], v[104:105]
	v_pk_fma_f32 v[118:119], v[98:99], v[98:99], v[118:119]
	v_cvt_pk_bf16_f32 v98, v98, v99
	v_cvt_pk_bf16_f32 v99, v100, v101
	v_cvt_pk_bf16_f32 v100, v102, v103
	v_cvt_pk_bf16_f32 v101, v104, v105
	v_subrev_u32_e32 v240, s82, v116
	v_add_u32_e32 v240, 0x800, v240
	ds_bpermute_b32 v232, v252, v98
	ds_bpermute_b32 v236, v253, v98
	ds_bpermute_b32 v233, v252, v99
	ds_bpermute_b32 v237, v253, v99
	ds_bpermute_b32 v234, v252, v100
	ds_bpermute_b32 v238, v253, v100
	ds_bpermute_b32 v235, v252, v101
	ds_bpermute_b32 v239, v253, v101
	ds_bpermute_b32 v241, v253, v240
	ds_bpermute_b32 v240, v252, v240
	v_pk_fma_f32 v[120:121], v[102:103], v[102:103], v[120:121]
	s_nop 0
	v_pk_mul_f32 v[98:99], v[108:109], v[108:109]
	v_pk_mul_f32 v[100:101], v[112:113], v[112:113]
	v_pk_fma_f32 v[98:99], v[106:107], v[106:107], v[98:99]
	v_pk_fma_f32 v[100:101], v[110:111], v[110:111], v[100:101]
	v_pk_add_f32 v[118:119], v[118:119], v[120:121]
	v_pk_add_f32 v[98:99], v[98:99], v[100:101]
	s_nop 0
	v_pk_add_f32 v[100:101], v[118:119], v[98:99]
	v_cvt_pk_bf16_f32 v98, v106, v107
	v_cvt_pk_bf16_f32 v99, v108, v109
	s_nop 0
	v_add_f32_e32 v102, v100, v101
	ds_swizzle_b32 v103, v102 offset:swizzle(SWAP,16)
	v_cvt_pk_bf16_f32 v100, v110, v111
	v_cvt_pk_bf16_f32 v101, v112, v113
	v_subrev_u32_e32 v250, s82, v116
	v_add_u32_e32 v250, 0x840, v250
	ds_bpermute_b32 v242, v252, v98
	ds_bpermute_b32 v246, v253, v98
	ds_bpermute_b32 v243, v252, v99
	ds_bpermute_b32 v247, v253, v99
	ds_bpermute_b32 v244, v252, v100
	ds_bpermute_b32 v248, v253, v100
	ds_bpermute_b32 v245, v252, v101
	ds_bpermute_b32 v249, v253, v101
	ds_bpermute_b32 v251, v253, v250
	ds_bpermute_b32 v250, v252, v250
	s_waitcnt lgkmcnt(0)
	v_cndmask_b32_e64 v232, v232, v242, s[100:101]
	v_cndmask_b32_e64 v233, v233, v243, s[100:101]
	v_cndmask_b32_e64 v234, v234, v244, s[100:101]
	v_cndmask_b32_e64 v235, v235, v245, s[100:101]
	v_cndmask_b32_e64 v236, v236, v246, s[100:101]
	v_cndmask_b32_e64 v237, v237, v247, s[100:101]
	v_cndmask_b32_e64 v238, v238, v248, s[100:101]
	v_cndmask_b32_e64 v239, v239, v249, s[100:101]
	v_cndmask_b32_e64 v240, v240, v250, s[100:101]
	v_cndmask_b32_e64 v241, v241, v251, s[100:101]
	global_store_dwordx4 v240, v[232:235], s[82:83]
	global_store_dwordx4 v241, v[236:239], s[82:83]
	s_waitcnt lgkmcnt(0)
	s_nop 0
	v_add_f32_e32 v98, v102, v103
	v_mov_b32_e32 v99, v98
	s_nop 1
	v_permlane32_swap_b32_e32 v98, v99
	s_and_saveexec_b64 s[48:49], s[38:39]
	s_cbranch_execz .LBB0_1086
	v_or_b32_e32 v100, 16, v144
	v_ashrrev_i32_e32 v101, 31, v100
	v_add_f32_e32 v102, v98, v99
	v_lshlrev_b64 v[98:99], 7, v[100:101]
	v_lshl_add_u64 v[98:99], s[8:9], 0, v[98:99]
	v_lshl_add_u64 v[98:99], s[46:47], 2, v[98:99]
	s_lshl_b32 s24, s12, 2
	v_lshl_add_u64 v[98:99], v[98:99], 0, s[24:25]
	global_store_dword v[98:99], v102, off
.LBB0_1086:
	s_or_b64 exec, exec, s[48:49]
	v_pk_mul_f32 v[98:99], v[84:85], v[84:85]
	v_pk_mul_f32 v[100:101], v[92:93], v[92:93]
	v_pk_fma_f32 v[98:99], v[82:83], v[82:83], v[98:99]
	v_pk_fma_f32 v[100:101], v[90:91], v[90:91], v[100:101]
	s_nop 0
	v_pk_add_f32 v[102:103], v[98:99], v[100:101]
	v_cvt_pk_bf16_f32 v99, v84, v85
	v_cvt_pk_bf16_f32 v100, v90, v91
	v_pk_mul_f32 v[84:85], v[88:89], v[88:89]
	v_pk_mul_f32 v[90:91], v[96:97], v[96:97]
	v_pk_fma_f32 v[84:85], v[86:87], v[86:87], v[84:85]
	v_pk_fma_f32 v[90:91], v[94:95], v[94:95], v[90:91]
	v_cvt_pk_bf16_f32 v98, v82, v83
	v_add_co_u32_e32 v82, vcc, s73, v116
	v_pk_add_f32 v[84:85], v[84:85], v[90:91]
	s_nop 0
	v_addc_co_u32_e32 v83, vcc, 0, v117, vcc
	v_pk_add_f32 v[90:91], v[102:103], v[84:85]
	v_cvt_pk_bf16_f32 v84, v86, v87
	v_cvt_pk_bf16_f32 v85, v88, v89
	v_cvt_pk_bf16_f32 v86, v94, v95
	v_cvt_pk_bf16_f32 v87, v96, v97
	v_subrev_u32_e32 v240, s82, v82
	v_add_u32_e32 v240, 0x40, v240
	ds_bpermute_b32 v232, v252, v84
	ds_bpermute_b32 v236, v253, v84
	ds_bpermute_b32 v233, v252, v85
	ds_bpermute_b32 v237, v253, v85
	ds_bpermute_b32 v234, v252, v86
	ds_bpermute_b32 v238, v253, v86
	ds_bpermute_b32 v235, v252, v87
	ds_bpermute_b32 v239, v253, v87
	ds_bpermute_b32 v241, v253, v240
	ds_bpermute_b32 v240, v252, v240
	v_add_f32_e32 v90, v90, v91
	ds_swizzle_b32 v91, v90 offset:swizzle(SWAP,16)
	v_cvt_pk_bf16_f32 v101, v92, v93
	v_subrev_u32_e32 v250, s82, v82
	ds_bpermute_b32 v242, v252, v98
	ds_bpermute_b32 v246, v253, v98
	ds_bpermute_b32 v243, v252, v99
	ds_bpermute_b32 v247, v253, v99
	ds_bpermute_b32 v244, v252, v100
	ds_bpermute_b32 v248, v253, v100
	ds_bpermute_b32 v245, v252, v101
	ds_bpermute_b32 v249, v253, v101
	ds_bpermute_b32 v251, v253, v250
	ds_bpermute_b32 v250, v252, v250
	s_waitcnt lgkmcnt(0)
	v_cndmask_b32_e64 v232, v232, v242, s[100:101]
	v_cndmask_b32_e64 v233, v233, v243, s[100:101]
	v_cndmask_b32_e64 v234, v234, v244, s[100:101]
	v_cndmask_b32_e64 v235, v235, v245, s[100:101]
	v_cndmask_b32_e64 v236, v236, v246, s[100:101]
	v_cndmask_b32_e64 v237, v237, v247, s[100:101]
	v_cndmask_b32_e64 v238, v238, v248, s[100:101]
	v_cndmask_b32_e64 v239, v239, v249, s[100:101]
	v_cndmask_b32_e64 v240, v240, v250, s[100:101]
	v_cndmask_b32_e64 v241, v241, v251, s[100:101]
	global_store_dwordx4 v240, v[232:235], s[82:83]
	global_store_dwordx4 v241, v[236:239], s[82:83]
	s_waitcnt lgkmcnt(0)
	v_add_f32_e32 v84, v90, v91
	v_mov_b32_e32 v85, v84
	s_nop 1
	v_permlane32_swap_b32_e32 v84, v85
	s_and_saveexec_b64 s[48:49], s[38:39]
	s_cbranch_execz .LBB0_1088
	v_or_b32_e32 v86, 32, v144
	v_ashrrev_i32_e32 v87, 31, v86
	v_add_f32_e32 v88, v84, v85
	v_lshlrev_b64 v[84:85], 7, v[86:87]
	v_lshl_add_u64 v[84:85], s[8:9], 0, v[84:85]
	v_lshl_add_u64 v[84:85], s[46:47], 2, v[84:85]
	s_lshl_b32 s24, s12, 2
	v_lshl_add_u64 v[84:85], v[84:85], 0, s[24:25]
	global_store_dword v[84:85], v88, off
.LBB0_1088:
	s_or_b64 exec, exec, s[48:49]
	v_pk_mul_f32 v[84:85], v[60:61], v[60:61]
	v_pk_mul_f32 v[86:87], v[72:73], v[72:73]
	v_pk_fma_f32 v[84:85], v[58:59], v[58:59], v[84:85]
	v_cvt_pk_bf16_f32 v58, v58, v59
	v_cvt_pk_bf16_f32 v59, v60, v61
	v_cvt_pk_bf16_f32 v60, v70, v71
	v_cvt_pk_bf16_f32 v61, v72, v73
	v_subrev_u32_e32 v240, s82, v82
	v_add_u32_e32 v240, 0x800, v240
	ds_bpermute_b32 v232, v252, v58
	ds_bpermute_b32 v236, v253, v58
	ds_bpermute_b32 v233, v252, v59
	ds_bpermute_b32 v237, v253, v59
	ds_bpermute_b32 v234, v252, v60
	ds_bpermute_b32 v238, v253, v60
	ds_bpermute_b32 v235, v252, v61
	ds_bpermute_b32 v239, v253, v61
	ds_bpermute_b32 v241, v253, v240
	ds_bpermute_b32 v240, v252, v240
	v_pk_fma_f32 v[86:87], v[70:71], v[70:71], v[86:87]
	s_nop 0
	v_pk_mul_f32 v[58:59], v[76:77], v[76:77]
	v_pk_mul_f32 v[60:61], v[80:81], v[80:81]
	v_pk_fma_f32 v[58:59], v[74:75], v[74:75], v[58:59]
	v_pk_fma_f32 v[60:61], v[78:79], v[78:79], v[60:61]
	v_pk_add_f32 v[84:85], v[84:85], v[86:87]
	v_pk_add_f32 v[58:59], v[58:59], v[60:61]
	s_nop 0
	v_pk_add_f32 v[60:61], v[84:85], v[58:59]
	v_cvt_pk_bf16_f32 v58, v74, v75
	v_cvt_pk_bf16_f32 v59, v76, v77
	s_nop 0
	v_add_f32_e32 v70, v60, v61
	ds_swizzle_b32 v71, v70 offset:swizzle(SWAP,16)
	v_cvt_pk_bf16_f32 v60, v78, v79
	v_cvt_pk_bf16_f32 v61, v80, v81
	v_subrev_u32_e32 v250, s82, v82
	v_add_u32_e32 v250, 0x840, v250
	ds_bpermute_b32 v242, v252, v58
	ds_bpermute_b32 v246, v253, v58
	ds_bpermute_b32 v243, v252, v59
	ds_bpermute_b32 v247, v253, v59
	ds_bpermute_b32 v244, v252, v60
	ds_bpermute_b32 v248, v253, v60
	ds_bpermute_b32 v245, v252, v61
	ds_bpermute_b32 v249, v253, v61
	ds_bpermute_b32 v251, v253, v250
	ds_bpermute_b32 v250, v252, v250
	s_waitcnt lgkmcnt(0)
	v_cndmask_b32_e64 v232, v232, v242, s[100:101]
	v_cndmask_b32_e64 v233, v233, v243, s[100:101]
	v_cndmask_b32_e64 v234, v234, v244, s[100:101]
	v_cndmask_b32_e64 v235, v235, v245, s[100:101]
	v_cndmask_b32_e64 v236, v236, v246, s[100:101]
	v_cndmask_b32_e64 v237, v237, v247, s[100:101]
	v_cndmask_b32_e64 v238, v238, v248, s[100:101]
	v_cndmask_b32_e64 v239, v239, v249, s[100:101]
	v_cndmask_b32_e64 v240, v240, v250, s[100:101]
	v_cndmask_b32_e64 v241, v241, v251, s[100:101]
	global_store_dwordx4 v240, v[232:235], s[82:83]
	global_store_dwordx4 v241, v[236:239], s[82:83]
	s_waitcnt lgkmcnt(0)
	s_nop 0
	v_add_f32_e32 v58, v70, v71
	v_mov_b32_e32 v59, v58
	s_nop 1
	v_permlane32_swap_b32_e32 v58, v59
	s_and_saveexec_b64 s[48:49], s[38:39]
	s_cbranch_execz .LBB0_1090
	v_or_b32_e32 v60, 48, v144
	v_ashrrev_i32_e32 v61, 31, v60
	v_add_f32_e32 v70, v58, v59
	v_lshlrev_b64 v[58:59], 7, v[60:61]
	v_lshl_add_u64 v[58:59], s[8:9], 0, v[58:59]
	v_lshl_add_u64 v[58:59], s[46:47], 2, v[58:59]
	s_lshl_b32 s24, s12, 2
	v_lshl_add_u64 v[58:59], v[58:59], 0, s[24:25]
	global_store_dword v[58:59], v70, off
.LBB0_1090:
	s_or_b64 exec, exec, s[48:49]
	v_pk_mul_f32 v[58:59], v[52:53], v[52:53]
	v_pk_mul_f32 v[60:61], v[64:65], v[64:65]
	v_pk_fma_f32 v[58:59], v[50:51], v[50:51], v[58:59]
	v_pk_fma_f32 v[60:61], v[62:63], v[62:63], v[60:61]
	s_nop 0
	v_pk_add_f32 v[70:71], v[58:59], v[60:61]
	v_cvt_pk_bf16_f32 v58, v50, v51
	v_add_co_u32_e32 v50, vcc, s72, v116
	v_cvt_pk_bf16_f32 v59, v52, v53
	v_cvt_pk_bf16_f32 v60, v62, v63
	v_cvt_pk_bf16_f32 v61, v64, v65
	v_pk_mul_f32 v[52:53], v[56:57], v[56:57]
	s_nop 0
	v_addc_co_u32_e32 v51, vcc, 0, v117, vcc
	v_subrev_u32_e32 v240, s82, v50
	ds_bpermute_b32 v232, v252, v58
	ds_bpermute_b32 v236, v253, v58
	ds_bpermute_b32 v233, v252, v59
	ds_bpermute_b32 v237, v253, v59
	ds_bpermute_b32 v234, v252, v60
	ds_bpermute_b32 v238, v253, v60
	ds_bpermute_b32 v235, v252, v61
	ds_bpermute_b32 v239, v253, v61
	ds_bpermute_b32 v241, v253, v240
	ds_bpermute_b32 v240, v252, v240
	v_pk_fma_f32 v[52:53], v[54:55], v[54:55], v[52:53]
	s_nop 0
	v_pk_mul_f32 v[58:59], v[68:69], v[68:69]
	s_nop 0
	v_pk_fma_f32 v[58:59], v[66:67], v[66:67], v[58:59]
	s_nop 0
	v_pk_add_f32 v[52:53], v[52:53], v[58:59]
	s_nop 0
	v_pk_add_f32 v[58:59], v[70:71], v[52:53]
	v_cvt_pk_bf16_f32 v52, v54, v55
	v_cvt_pk_bf16_f32 v53, v56, v57
	v_cvt_pk_bf16_f32 v54, v66, v67
	v_cvt_pk_bf16_f32 v55, v68, v69
	v_subrev_u32_e32 v250, s82, v50
	v_add_u32_e32 v250, 0x40, v250
	ds_bpermute_b32 v242, v252, v52
	ds_bpermute_b32 v246, v253, v52
	ds_bpermute_b32 v243, v252, v53
	ds_bpermute_b32 v247, v253, v53
	ds_bpermute_b32 v244, v252, v54
	ds_bpermute_b32 v248, v253, v54
	ds_bpermute_b32 v245, v252, v55
	ds_bpermute_b32 v249, v253, v55
	ds_bpermute_b32 v251, v253, v250
	ds_bpermute_b32 v250, v252, v250
	s_waitcnt lgkmcnt(0)
	v_cndmask_b32_e64 v232, v232, v242, s[100:101]
	v_cndmask_b32_e64 v233, v233, v243, s[100:101]
	v_cndmask_b32_e64 v234, v234, v244, s[100:101]
	v_cndmask_b32_e64 v235, v235, v245, s[100:101]
	v_cndmask_b32_e64 v236, v236, v246, s[100:101]
	v_cndmask_b32_e64 v237, v237, v247, s[100:101]
	v_cndmask_b32_e64 v238, v238, v248, s[100:101]
	v_cndmask_b32_e64 v239, v239, v249, s[100:101]
	v_cndmask_b32_e64 v240, v240, v250, s[100:101]
	v_cndmask_b32_e64 v241, v241, v251, s[100:101]
	global_store_dwordx4 v240, v[232:235], s[82:83]
	global_store_dwordx4 v241, v[236:239], s[82:83]
	v_add_f32_e32 v58, v58, v59
	ds_swizzle_b32 v59, v58 offset:swizzle(SWAP,16)
	s_waitcnt lgkmcnt(0)
	v_add_f32_e32 v52, v58, v59
	v_mov_b32_e32 v53, v52
	s_nop 1
	v_permlane32_swap_b32_e32 v52, v53
	s_and_saveexec_b64 s[48:49], s[38:39]
	s_cbranch_execz .LBB0_1092
	v_ashrrev_i32_e32 v145, 31, v144
	v_add_f32_e32 v54, v52, v53
	v_lshlrev_b64 v[52:53], 7, v[144:145]
	v_lshl_add_u64 v[52:53], s[8:9], 0, v[52:53]
	v_lshl_add_u64 v[52:53], s[46:47], 2, v[52:53]
	s_lshl_b32 s24, s12, 2
	v_lshl_add_u64 v[52:53], v[52:53], 0, s[24:25]
	v_add_co_u32_e32 v52, vcc, 0x4000, v52
	s_nop 1
	v_addc_co_u32_e32 v53, vcc, 0, v53, vcc
	global_store_dword v[52:53], v54, off
.LBB0_1092:
	s_or_b64 exec, exec, s[48:49]
	v_pk_mul_f32 v[52:53], v[36:37], v[36:37]
	v_pk_mul_f32 v[54:55], v[40:41], v[40:41]
	v_pk_fma_f32 v[52:53], v[34:35], v[34:35], v[52:53]
	v_cvt_pk_bf16_f32 v34, v34, v35
	v_cvt_pk_bf16_f32 v35, v36, v37
	v_cvt_pk_bf16_f32 v36, v38, v39
	v_cvt_pk_bf16_f32 v37, v40, v41
	v_subrev_u32_e32 v240, s82, v50
	v_add_u32_e32 v240, 0x800, v240
	ds_bpermute_b32 v232, v252, v34
	ds_bpermute_b32 v236, v253, v34
	ds_bpermute_b32 v233, v252, v35
	ds_bpermute_b32 v237, v253, v35
	ds_bpermute_b32 v234, v252, v36
	ds_bpermute_b32 v238, v253, v36
	ds_bpermute_b32 v235, v252, v37
	ds_bpermute_b32 v239, v253, v37
	ds_bpermute_b32 v241, v253, v240
	ds_bpermute_b32 v240, v252, v240
	v_pk_fma_f32 v[54:55], v[38:39], v[38:39], v[54:55]
	s_nop 0
	v_pk_mul_f32 v[34:35], v[44:45], v[44:45]
	v_pk_mul_f32 v[36:37], v[48:49], v[48:49]
	v_pk_fma_f32 v[34:35], v[42:43], v[42:43], v[34:35]
	v_pk_fma_f32 v[36:37], v[46:47], v[46:47], v[36:37]
	v_pk_add_f32 v[52:53], v[52:53], v[54:55]
	v_pk_add_f32 v[34:35], v[34:35], v[36:37]
	s_nop 0
	v_pk_add_f32 v[36:37], v[52:53], v[34:35]
	v_cvt_pk_bf16_f32 v34, v42, v43
	v_cvt_pk_bf16_f32 v35, v44, v45
	s_nop 0
	v_add_f32_e32 v38, v36, v37
	ds_swizzle_b32 v39, v38 offset:swizzle(SWAP,16)
	v_cvt_pk_bf16_f32 v36, v46, v47
	v_cvt_pk_bf16_f32 v37, v48, v49
	v_subrev_u32_e32 v250, s82, v50
	v_add_u32_e32 v250, 0x840, v250
	ds_bpermute_b32 v242, v252, v34
	ds_bpermute_b32 v246, v253, v34
	ds_bpermute_b32 v243, v252, v35
	ds_bpermute_b32 v247, v253, v35
	ds_bpermute_b32 v244, v252, v36
	ds_bpermute_b32 v248, v253, v36
	ds_bpermute_b32 v245, v252, v37
	ds_bpermute_b32 v249, v253, v37
	ds_bpermute_b32 v251, v253, v250
	ds_bpermute_b32 v250, v252, v250
	s_waitcnt lgkmcnt(0)
	v_cndmask_b32_e64 v232, v232, v242, s[100:101]
	v_cndmask_b32_e64 v233, v233, v243, s[100:101]
	v_cndmask_b32_e64 v234, v234, v244, s[100:101]
	v_cndmask_b32_e64 v235, v235, v245, s[100:101]
	v_cndmask_b32_e64 v236, v236, v246, s[100:101]
	v_cndmask_b32_e64 v237, v237, v247, s[100:101]
	v_cndmask_b32_e64 v238, v238, v248, s[100:101]
	v_cndmask_b32_e64 v239, v239, v249, s[100:101]
	v_cndmask_b32_e64 v240, v240, v250, s[100:101]
	v_cndmask_b32_e64 v241, v241, v251, s[100:101]
	global_store_dwordx4 v240, v[232:235], s[82:83]
	global_store_dwordx4 v241, v[236:239], s[82:83]
	s_waitcnt lgkmcnt(0)
	s_nop 0
	v_add_f32_e32 v34, v38, v39
	v_mov_b32_e32 v35, v34
	s_nop 1
	v_permlane32_swap_b32_e32 v34, v35
	s_and_saveexec_b64 s[48:49], s[38:39]
	s_cbranch_execz .LBB0_1094
	v_ashrrev_i32_e32 v145, 31, v144
	v_add_f32_e32 v36, v34, v35
	v_lshlrev_b64 v[34:35], 7, v[144:145]
	v_lshl_add_u64 v[34:35], s[8:9], 0, v[34:35]
	v_lshl_add_u64 v[34:35], s[46:47], 2, v[34:35]
	s_lshl_b32 s24, s12, 2
	v_lshl_add_u64 v[34:35], v[34:35], 0, s[24:25]
	v_add_co_u32_e32 v34, vcc, 0x4000, v34
	s_nop 1
	v_addc_co_u32_e32 v35, vcc, 0, v35, vcc
	global_store_dword v[34:35], v36, off offset:2048
.LBB0_1094:
	s_or_b64 exec, exec, s[48:49]
	v_pk_mul_f32 v[34:35], v[20:21], v[20:21]
	v_pk_mul_f32 v[36:37], v[28:29], v[28:29]
	v_pk_fma_f32 v[34:35], v[18:19], v[18:19], v[34:35]
	v_pk_fma_f32 v[36:37], v[26:27], v[26:27], v[36:37]
	s_nop 0
	v_pk_add_f32 v[38:39], v[34:35], v[36:37]
	v_cvt_pk_bf16_f32 v35, v20, v21
	v_cvt_pk_bf16_f32 v36, v26, v27
	v_pk_mul_f32 v[20:21], v[24:25], v[24:25]
	v_pk_mul_f32 v[26:27], v[32:33], v[32:33]
	v_pk_fma_f32 v[20:21], v[22:23], v[22:23], v[20:21]
	v_pk_fma_f32 v[26:27], v[30:31], v[30:31], v[26:27]
	v_cvt_pk_bf16_f32 v34, v18, v19
	v_add_co_u32_e32 v18, vcc, s31, v116
	v_pk_add_f32 v[20:21], v[20:21], v[26:27]
	s_nop 0
	v_addc_co_u32_e32 v19, vcc, 0, v117, vcc
	v_pk_add_f32 v[26:27], v[38:39], v[20:21]
	v_cvt_pk_bf16_f32 v20, v22, v23
	v_cvt_pk_bf16_f32 v21, v24, v25
	v_cvt_pk_bf16_f32 v22, v30, v31
	v_cvt_pk_bf16_f32 v23, v32, v33
	v_subrev_u32_e32 v240, s82, v18
	v_add_u32_e32 v240, 0x40, v240
	ds_bpermute_b32 v232, v252, v20
	ds_bpermute_b32 v236, v253, v20
	ds_bpermute_b32 v233, v252, v21
	ds_bpermute_b32 v237, v253, v21
	ds_bpermute_b32 v234, v252, v22
	ds_bpermute_b32 v238, v253, v22
	ds_bpermute_b32 v235, v252, v23
	ds_bpermute_b32 v239, v253, v23
	ds_bpermute_b32 v241, v253, v240
	ds_bpermute_b32 v240, v252, v240
	v_add_f32_e32 v26, v26, v27
	ds_swizzle_b32 v27, v26 offset:swizzle(SWAP,16)
	v_cvt_pk_bf16_f32 v37, v28, v29
	v_subrev_u32_e32 v250, s82, v18
	ds_bpermute_b32 v242, v252, v34
	ds_bpermute_b32 v246, v253, v34
	ds_bpermute_b32 v243, v252, v35
	ds_bpermute_b32 v247, v253, v35
	ds_bpermute_b32 v244, v252, v36
	ds_bpermute_b32 v248, v253, v36
	ds_bpermute_b32 v245, v252, v37
	ds_bpermute_b32 v249, v253, v37
	ds_bpermute_b32 v251, v253, v250
	ds_bpermute_b32 v250, v252, v250
	s_waitcnt lgkmcnt(0)
	v_cndmask_b32_e64 v232, v232, v242, s[100:101]
	v_cndmask_b32_e64 v233, v233, v243, s[100:101]
	v_cndmask_b32_e64 v234, v234, v244, s[100:101]
	v_cndmask_b32_e64 v235, v235, v245, s[100:101]
	v_cndmask_b32_e64 v236, v236, v246, s[100:101]
	v_cndmask_b32_e64 v237, v237, v247, s[100:101]
	v_cndmask_b32_e64 v238, v238, v248, s[100:101]
	v_cndmask_b32_e64 v239, v239, v249, s[100:101]
	v_cndmask_b32_e64 v240, v240, v250, s[100:101]
	v_cndmask_b32_e64 v241, v241, v251, s[100:101]
	global_store_dwordx4 v240, v[232:235], s[82:83]
	global_store_dwordx4 v241, v[236:239], s[82:83]
	s_waitcnt lgkmcnt(0)
	v_add_f32_e32 v20, v26, v27
	v_mov_b32_e32 v21, v20
	s_nop 1
	v_permlane32_swap_b32_e32 v20, v21
	s_and_saveexec_b64 s[48:49], s[38:39]
	s_cbranch_execz .LBB0_1096
	v_ashrrev_i32_e32 v145, 31, v144
	v_add_f32_e32 v22, v20, v21
	v_lshlrev_b64 v[20:21], 7, v[144:145]
	v_lshl_add_u64 v[20:21], s[8:9], 0, v[20:21]
	v_lshl_add_u64 v[20:21], s[46:47], 2, v[20:21]
	s_lshl_b32 s24, s12, 2
	v_lshl_add_u64 v[20:21], v[20:21], 0, s[24:25]
	v_add_co_u32_e32 v20, vcc, 0x5000, v20
	s_nop 1
	v_addc_co_u32_e32 v21, vcc, 0, v21, vcc
	global_store_dword v[20:21], v22, off
.LBB0_1096:
	s_or_b64 exec, exec, s[48:49]
	v_pk_mul_f32 v[20:21], v[4:5], v[4:5]
	v_pk_mul_f32 v[22:23], v[8:9], v[8:9]
	v_pk_fma_f32 v[20:21], v[2:3], v[2:3], v[20:21]
	v_cvt_pk_bf16_f32 v2, v2, v3
	v_cvt_pk_bf16_f32 v3, v4, v5
	v_cvt_pk_bf16_f32 v4, v6, v7
	v_cvt_pk_bf16_f32 v5, v8, v9
	v_subrev_u32_e32 v240, s82, v18
	v_add_u32_e32 v240, 0x800, v240
	ds_bpermute_b32 v232, v252, v2
	ds_bpermute_b32 v236, v253, v2
	ds_bpermute_b32 v233, v252, v3
	ds_bpermute_b32 v237, v253, v3
	ds_bpermute_b32 v234, v252, v4
	ds_bpermute_b32 v238, v253, v4
	ds_bpermute_b32 v235, v252, v5
	ds_bpermute_b32 v239, v253, v5
	ds_bpermute_b32 v241, v253, v240
	ds_bpermute_b32 v240, v252, v240
	v_pk_fma_f32 v[22:23], v[6:7], v[6:7], v[22:23]
	s_nop 0
	v_pk_mul_f32 v[2:3], v[12:13], v[12:13]
	v_pk_mul_f32 v[4:5], v[16:17], v[16:17]
	v_pk_fma_f32 v[2:3], v[10:11], v[10:11], v[2:3]
	v_pk_fma_f32 v[4:5], v[14:15], v[14:15], v[4:5]
	v_pk_add_f32 v[20:21], v[20:21], v[22:23]
	v_pk_add_f32 v[2:3], v[2:3], v[4:5]
	s_nop 0
	v_pk_add_f32 v[4:5], v[20:21], v[2:3]
	v_cvt_pk_bf16_f32 v2, v10, v11
	v_cvt_pk_bf16_f32 v3, v12, v13
	s_nop 0
	v_add_f32_e32 v6, v4, v5
	ds_swizzle_b32 v7, v6 offset:swizzle(SWAP,16)
	v_cvt_pk_bf16_f32 v4, v14, v15
	v_cvt_pk_bf16_f32 v5, v16, v17
	v_subrev_u32_e32 v250, s82, v18
	v_add_u32_e32 v250, 0x840, v250
	ds_bpermute_b32 v242, v252, v2
	ds_bpermute_b32 v246, v253, v2
	ds_bpermute_b32 v243, v252, v3
	ds_bpermute_b32 v247, v253, v3
	ds_bpermute_b32 v244, v252, v4
	ds_bpermute_b32 v248, v253, v4
	ds_bpermute_b32 v245, v252, v5
	ds_bpermute_b32 v249, v253, v5
	ds_bpermute_b32 v251, v253, v250
	ds_bpermute_b32 v250, v252, v250
	s_waitcnt lgkmcnt(0)
	v_cndmask_b32_e64 v232, v232, v242, s[100:101]
	v_cndmask_b32_e64 v233, v233, v243, s[100:101]
	v_cndmask_b32_e64 v234, v234, v244, s[100:101]
	v_cndmask_b32_e64 v235, v235, v245, s[100:101]
	v_cndmask_b32_e64 v236, v236, v246, s[100:101]
	v_cndmask_b32_e64 v237, v237, v247, s[100:101]
	v_cndmask_b32_e64 v238, v238, v248, s[100:101]
	v_cndmask_b32_e64 v239, v239, v249, s[100:101]
	v_cndmask_b32_e64 v240, v240, v250, s[100:101]
	v_cndmask_b32_e64 v241, v241, v251, s[100:101]
	global_store_dwordx4 v240, v[232:235], s[82:83]
	global_store_dwordx4 v241, v[236:239], s[82:83]
	s_waitcnt lgkmcnt(0)
	s_nop 0
	v_add_f32_e32 v2, v6, v7
	v_mov_b32_e32 v3, v2
	s_nop 1
	v_permlane32_swap_b32_e32 v2, v3
	s_and_saveexec_b64 s[48:49], s[38:39]
	s_cbranch_execz .LBB0_1098
	v_ashrrev_i32_e32 v145, 31, v144
	v_add_f32_e32 v4, v2, v3
	v_lshlrev_b64 v[2:3], 7, v[144:145]
	v_lshl_add_u64 v[2:3], s[8:9], 0, v[2:3]
	v_lshl_add_u64 v[2:3], s[46:47], 2, v[2:3]
	s_lshl_b32 s24, s12, 2
	v_lshl_add_u64 v[2:3], v[2:3], 0, s[24:25]
	v_add_co_u32_e32 v2, vcc, 0x5000, v2
	s_nop 1
	v_addc_co_u32_e32 v3, vcc, 0, v3, vcc
	global_store_dword v[2:3], v4, off offset:2048

.LBB0_1233:
	v_mbcnt_lo_u32_b32 v231, -1, 0
	v_mbcnt_hi_u32_b32 v231, -1, v231
	v_and_b32_e32 v253, 3, v231
	v_lshrrev_b32_e32 v252, 3, v231
	v_lshl_add_u32 v252, v253, 4, v252
	v_lshlrev_b32_e32 v252, 2, v252
	v_lshrrev_b32_e32 v231, 2, v231
	v_lshl_add_u32 v231, v253, 4, v231
	v_lshlrev_b32_e32 v231, 2, v231
	v_add_u32_e32 v253, 32, v252
	s_mov_b32 s100, 0xf0f0f0f0
	s_mov_b32 s101, 0xf0f0f0f0
	v_lshl_add_u32 v148, s59, 10, v146
	ds_read2_b32 v[150:151], v148 offset1:16
	s_lshl_b32 s17, s58, 2
	v_med3_f32 v124, v124, 0, v193
	v_med3_f32 v125, v125, 0, v193
	s_lshl_b32 s16, s44, 7
	s_or_b32 s17, s17, s45
	s_waitcnt lgkmcnt(0)
	v_mul_f32_e32 v150, v150, v150
	v_pk_mul_f32 v[124:125], v[124:125], v[124:125]
	s_add_i32 s16, s17, s16
	v_pk_mul_f32 v[152:153], v[124:125], v[150:151] op_sel_hi:[1,0]
	v_med3_f32 v124, v130, 0, v193
	v_med3_f32 v125, v131, 0, v193
	s_ashr_i32 s17, s16, 31
	v_med3_f32 v128, v128, 0, v193
	v_med3_f32 v129, v129, 0, v193
	v_med3_f32 v126, v126, 0, v193
	v_med3_f32 v127, v127, 0, v193
	v_pk_mul_f32 v[124:125], v[124:125], v[124:125]
	s_lshl_b64 s[16:17], s[16:17], 15
	v_pk_mul_f32 v[128:129], v[128:129], v[128:129]
	v_pk_mul_f32 v[130:131], v[124:125], v[150:151] op_sel_hi:[1,0]
	v_pk_mul_f32 v[124:125], v[126:127], v[126:127]
	v_med3_f32 v116, v116, 0, v193
	v_med3_f32 v117, v117, 0, v193
	v_lshl_add_u64 v[144:145], v[138:139], 0, s[16:17]
	v_pk_mul_f32 v[128:129], v[128:129], v[150:151] op_sel_hi:[1,0]
	v_pk_mul_f32 v[154:155], v[124:125], v[150:151] op_sel_hi:[1,0]
	v_cvt_pk_bf16_f32 v124, v128, v129
	v_cvt_pk_bf16_f32 v125, v130, v131
	v_pk_mul_f32 v[116:117], v[116:117], v[116:117]
	v_cvt_pk_bf16_f32 v126, v152, v153
	v_cvt_pk_bf16_f32 v127, v154, v155
	v_subrev_u32_e32 v240, s82, v144
	ds_bpermute_b32 v232, v252, v124
	ds_bpermute_b32 v236, v253, v124
	ds_bpermute_b32 v233, v252, v125
	ds_bpermute_b32 v237, v253, v125
	ds_bpermute_b32 v234, v252, v126
	ds_bpermute_b32 v238, v253, v126
	ds_bpermute_b32 v235, v252, v127
	ds_bpermute_b32 v239, v253, v127
	ds_bpermute_b32 v241, v253, v240
	ds_bpermute_b32 v240, v252, v240
	v_med3_f32 v120, v120, 0, v193
	v_med3_f32 v121, v121, 0, v193
	v_pk_mul_f32 v[124:125], v[116:117], v[150:151] op_sel_hi:[1,0]
	v_med3_f32 v116, v122, 0, v193
	v_med3_f32 v117, v123, 0, v193
	v_med3_f32 v118, v118, 0, v193
	v_med3_f32 v119, v119, 0, v193
	v_pk_mul_f32 v[116:117], v[116:117], v[116:117]
	v_pk_mul_f32 v[120:121], v[120:121], v[120:121]
	v_pk_mul_f32 v[122:123], v[116:117], v[150:151] op_sel_hi:[1,0]
	v_pk_mul_f32 v[116:117], v[118:119], v[118:119]
	v_pk_mul_f32 v[120:121], v[120:121], v[150:151] op_sel_hi:[1,0]
	v_pk_mul_f32 v[126:127], v[116:117], v[150:151] op_sel_hi:[1,0]
	v_cvt_pk_bf16_f32 v116, v120, v121
	v_med3_f32 v106, v106, 0, v193
	v_med3_f32 v107, v107, 0, v193
	v_cvt_pk_bf16_f32 v117, v122, v123
	v_cvt_pk_bf16_f32 v118, v124, v125
	v_cvt_pk_bf16_f32 v119, v126, v127
	v_subrev_u32_e32 v250, s82, v144
	v_add_u32_e32 v250, 0x40, v250
	ds_bpermute_b32 v242, v252, v116
	ds_bpermute_b32 v246, v253, v116
	ds_bpermute_b32 v243, v252, v117
	ds_bpermute_b32 v247, v253, v117
	ds_bpermute_b32 v244, v252, v118
	ds_bpermute_b32 v248, v253, v118
	ds_bpermute_b32 v245, v252, v119
	ds_bpermute_b32 v249, v253, v119
	ds_bpermute_b32 v251, v253, v250
	ds_bpermute_b32 v250, v252, v250
	s_waitcnt lgkmcnt(0)
	v_cndmask_b32_e64 v232, v232, v242, s[100:101]
	v_cndmask_b32_e64 v233, v233, v243, s[100:101]
	v_cndmask_b32_e64 v234, v234, v244, s[100:101]
	v_cndmask_b32_e64 v235, v235, v245, s[100:101]
	v_cndmask_b32_e64 v236, v236, v246, s[100:101]
	v_cndmask_b32_e64 v237, v237, v247, s[100:101]
	v_cndmask_b32_e64 v238, v238, v248, s[100:101]
	v_cndmask_b32_e64 v239, v239, v249, s[100:101]
	v_cndmask_b32_e64 v240, v240, v250, s[100:101]
	v_cndmask_b32_e64 v241, v241, v251, s[100:101]
	global_store_dwordx4 v240, v[232:235], s[82:83]
	global_store_dwordx4 v241, v[236:239], s[82:83]
	v_pk_mul_f32 v[106:107], v[106:107], v[106:107]
	v_med3_f32 v110, v110, 0, v193
	v_mul_f32_e32 v116, v151, v151
	v_pk_mul_f32 v[118:119], v[106:107], v[116:117] op_sel_hi:[1,0]
	v_med3_f32 v106, v112, 0, v193
	v_med3_f32 v107, v113, 0, v193
	v_med3_f32 v111, v111, 0, v193
	v_med3_f32 v108, v108, 0, v193
	v_med3_f32 v109, v109, 0, v193
	v_pk_mul_f32 v[106:107], v[106:107], v[106:107]
	v_pk_mul_f32 v[110:111], v[110:111], v[110:111]
	v_pk_mul_f32 v[112:113], v[106:107], v[116:117] op_sel_hi:[1,0]
	v_pk_mul_f32 v[106:107], v[108:109], v[108:109]
	v_med3_f32 v98, v98, 0, v193
	v_med3_f32 v99, v99, 0, v193
	v_pk_mul_f32 v[110:111], v[110:111], v[116:117] op_sel_hi:[1,0]
	v_pk_mul_f32 v[120:121], v[106:107], v[116:117] op_sel_hi:[1,0]
	v_cvt_pk_bf16_f32 v106, v110, v111
	v_cvt_pk_bf16_f32 v107, v112, v113
	v_pk_mul_f32 v[98:99], v[98:99], v[98:99]
	v_cvt_pk_bf16_f32 v108, v118, v119
	v_cvt_pk_bf16_f32 v109, v120, v121
	v_subrev_u32_e32 v240, s82, v144
	v_add_u32_e32 v240, 0x800, v240
	ds_bpermute_b32 v232, v252, v106
	ds_bpermute_b32 v236, v253, v106
	ds_bpermute_b32 v233, v252, v107
	ds_bpermute_b32 v237, v253, v107
	ds_bpermute_b32 v234, v252, v108
	ds_bpermute_b32 v238, v253, v108
	ds_bpermute_b32 v235, v252, v109
	ds_bpermute_b32 v239, v253, v109
	ds_bpermute_b32 v241, v253, v240
	ds_bpermute_b32 v240, v252, v240
	v_med3_f32 v102, v102, 0, v193
	v_med3_f32 v103, v103, 0, v193
	v_pk_mul_f32 v[106:107], v[98:99], v[116:117] op_sel_hi:[1,0]
	v_med3_f32 v98, v104, 0, v193
	v_med3_f32 v99, v105, 0, v193
	v_pk_mul_f32 v[102:103], v[102:103], v[102:103]
	v_med3_f32 v100, v100, 0, v193
	v_med3_f32 v101, v101, 0, v193
	v_pk_mul_f32 v[98:99], v[98:99], v[98:99]
	v_pk_mul_f32 v[102:103], v[102:103], v[116:117] op_sel_hi:[1,0]
	v_pk_mul_f32 v[104:105], v[98:99], v[116:117] op_sel_hi:[1,0]
	v_pk_mul_f32 v[98:99], v[100:101], v[100:101]
	v_med3_f32 v90, v90, 0, v193
	v_pk_mul_f32 v[108:109], v[98:99], v[116:117] op_sel_hi:[1,0]
	v_cvt_pk_bf16_f32 v98, v102, v103
	ds_read2_b32 v[102:103], v148 offset0:32 offset1:48
	v_med3_f32 v91, v91, 0, v193
	v_cvt_pk_bf16_f32 v99, v104, v105
	v_cvt_pk_bf16_f32 v100, v106, v107
	v_cvt_pk_bf16_f32 v101, v108, v109
	v_subrev_u32_e32 v250, s82, v144
	v_add_u32_e32 v250, 0x840, v250
	ds_bpermute_b32 v242, v252, v98
	ds_bpermute_b32 v246, v253, v98
	ds_bpermute_b32 v243, v252, v99
	ds_bpermute_b32 v247, v253, v99
	ds_bpermute_b32 v244, v252, v100
	ds_bpermute_b32 v248, v253, v100
	ds_bpermute_b32 v245, v252, v101
	ds_bpermute_b32 v249, v253, v101
	ds_bpermute_b32 v251, v253, v250
	ds_bpermute_b32 v250, v252, v250
	s_waitcnt lgkmcnt(0)
	v_cndmask_b32_e64 v232, v232, v242, s[100:101]
	v_cndmask_b32_e64 v233, v233, v243, s[100:101]
	v_cndmask_b32_e64 v234, v234, v244, s[100:101]
	v_cndmask_b32_e64 v235, v235, v245, s[100:101]
	v_cndmask_b32_e64 v236, v236, v246, s[100:101]
	v_cndmask_b32_e64 v237, v237, v247, s[100:101]
	v_cndmask_b32_e64 v238, v238, v248, s[100:101]
	v_cndmask_b32_e64 v239, v239, v249, s[100:101]
	v_cndmask_b32_e64 v240, v240, v250, s[100:101]
	v_cndmask_b32_e64 v241, v241, v251, s[100:101]
	global_store_dwordx4 v240, v[232:235], s[82:83]
	global_store_dwordx4 v241, v[236:239], s[82:83]
	v_pk_mul_f32 v[90:91], v[90:91], v[90:91]
	v_med3_f32 v94, v94, 0, v193
	s_waitcnt lgkmcnt(0)
	v_mul_f32_e32 v98, v102, v102
	v_med3_f32 v95, v95, 0, v193
	v_pk_mul_f32 v[100:101], v[90:91], v[98:99] op_sel_hi:[1,0]
	v_med3_f32 v90, v96, 0, v193
	v_med3_f32 v91, v97, 0, v193
	v_pk_mul_f32 v[94:95], v[94:95], v[94:95]
	v_med3_f32 v92, v92, 0, v193
	v_med3_f32 v93, v93, 0, v193
	v_pk_mul_f32 v[90:91], v[90:91], v[90:91]
	v_pk_mul_f32 v[94:95], v[94:95], v[98:99] op_sel_hi:[1,0]
	v_pk_mul_f32 v[96:97], v[90:91], v[98:99] op_sel_hi:[1,0]
	v_pk_mul_f32 v[90:91], v[92:93], v[92:93]
	v_med3_f32 v82, v82, 0, v193
	v_pk_mul_f32 v[104:105], v[90:91], v[98:99] op_sel_hi:[1,0]
	v_cvt_pk_bf16_f32 v90, v94, v95
	v_add_co_u32_e32 v94, vcc, s73, v144
	v_med3_f32 v83, v83, 0, v193
	v_cvt_pk_bf16_f32 v91, v96, v97
	s_nop 0
	v_addc_co_u32_e32 v95, vcc, 0, v145, vcc
	v_pk_mul_f32 v[82:83], v[82:83], v[82:83]
	v_cvt_pk_bf16_f32 v92, v100, v101
	v_cvt_pk_bf16_f32 v93, v104, v105
	v_subrev_u32_e32 v240, s82, v94
	ds_bpermute_b32 v232, v252, v90
	ds_bpermute_b32 v236, v253, v90
	ds_bpermute_b32 v233, v252, v91
	ds_bpermute_b32 v237, v253, v91
	ds_bpermute_b32 v234, v252, v92
	ds_bpermute_b32 v238, v253, v92
	ds_bpermute_b32 v235, v252, v93
	ds_bpermute_b32 v239, v253, v93
	ds_bpermute_b32 v241, v253, v240
	ds_bpermute_b32 v240, v252, v240
	v_med3_f32 v86, v86, 0, v193
	v_med3_f32 v87, v87, 0, v193
	v_pk_mul_f32 v[90:91], v[82:83], v[98:99] op_sel_hi:[1,0]
	v_med3_f32 v82, v88, 0, v193
	v_med3_f32 v83, v89, 0, v193
	v_med3_f32 v84, v84, 0, v193
	v_med3_f32 v85, v85, 0, v193
	v_pk_mul_f32 v[82:83], v[82:83], v[82:83]
	v_pk_mul_f32 v[86:87], v[86:87], v[86:87]
	v_pk_mul_f32 v[88:89], v[82:83], v[98:99] op_sel_hi:[1,0]
	v_pk_mul_f32 v[82:83], v[84:85], v[84:85]
	v_pk_mul_f32 v[86:87], v[86:87], v[98:99] op_sel_hi:[1,0]
	v_pk_mul_f32 v[92:93], v[82:83], v[98:99] op_sel_hi:[1,0]
	v_cvt_pk_bf16_f32 v82, v86, v87
	v_med3_f32 v74, v74, 0, v193
	v_med3_f32 v75, v75, 0, v193
	v_cvt_pk_bf16_f32 v83, v88, v89
	v_cvt_pk_bf16_f32 v84, v90, v91
	v_cvt_pk_bf16_f32 v85, v92, v93
	v_subrev_u32_e32 v250, s82, v94
	v_add_u32_e32 v250, 0x40, v250
	ds_bpermute_b32 v242, v252, v82
	ds_bpermute_b32 v246, v253, v82
	ds_bpermute_b32 v243, v252, v83
	ds_bpermute_b32 v247, v253, v83
	ds_bpermute_b32 v244, v252, v84
	ds_bpermute_b32 v248, v253, v84
	ds_bpermute_b32 v245, v252, v85
	ds_bpermute_b32 v249, v253, v85
	ds_bpermute_b32 v251, v253, v250
	ds_bpermute_b32 v250, v252, v250
	s_waitcnt lgkmcnt(0)
	v_cndmask_b32_e64 v232, v232, v242, s[100:101]
	v_cndmask_b32_e64 v233, v233, v243, s[100:101]
	v_cndmask_b32_e64 v234, v234, v244, s[100:101]
	v_cndmask_b32_e64 v235, v235, v245, s[100:101]
	v_cndmask_b32_e64 v236, v236, v246, s[100:101]
	v_cndmask_b32_e64 v237, v237, v247, s[100:101]
	v_cndmask_b32_e64 v238, v238, v248, s[100:101]
	v_cndmask_b32_e64 v239, v239, v249, s[100:101]
	v_cndmask_b32_e64 v240, v240, v250, s[100:101]
	v_cndmask_b32_e64 v241, v241, v251, s[100:101]
	global_store_dwordx4 v240, v[232:235], s[82:83]
	global_store_dwordx4 v241, v[236:239], s[82:83]
	v_pk_mul_f32 v[74:75], v[74:75], v[74:75]
	v_med3_f32 v78, v78, 0, v193
	v_mul_f32_e32 v82, v103, v103
	v_pk_mul_f32 v[84:85], v[74:75], v[82:83] op_sel_hi:[1,0]
	v_med3_f32 v74, v80, 0, v193
	v_med3_f32 v75, v81, 0, v193
	v_med3_f32 v79, v79, 0, v193
	v_med3_f32 v76, v76, 0, v193
	v_med3_f32 v77, v77, 0, v193
	v_pk_mul_f32 v[74:75], v[74:75], v[74:75]
	v_pk_mul_f32 v[78:79], v[78:79], v[78:79]
	v_pk_mul_f32 v[80:81], v[74:75], v[82:83] op_sel_hi:[1,0]
	v_pk_mul_f32 v[74:75], v[76:77], v[76:77]
	v_med3_f32 v66, v66, 0, v193
	v_med3_f32 v67, v67, 0, v193
	v_pk_mul_f32 v[78:79], v[78:79], v[82:83] op_sel_hi:[1,0]
	v_pk_mul_f32 v[86:87], v[74:75], v[82:83] op_sel_hi:[1,0]
	v_cvt_pk_bf16_f32 v74, v78, v79
	v_cvt_pk_bf16_f32 v75, v80, v81
	v_pk_mul_f32 v[66:67], v[66:67], v[66:67]
	v_cvt_pk_bf16_f32 v76, v84, v85
	v_cvt_pk_bf16_f32 v77, v86, v87
	v_subrev_u32_e32 v240, s82, v94
	v_add_u32_e32 v240, 0x800, v240
	ds_bpermute_b32 v232, v252, v74
	ds_bpermute_b32 v236, v253, v74
	ds_bpermute_b32 v233, v252, v75
	ds_bpermute_b32 v237, v253, v75
	ds_bpermute_b32 v234, v252, v76
	ds_bpermute_b32 v238, v253, v76
	ds_bpermute_b32 v235, v252, v77
	ds_bpermute_b32 v239, v253, v77
	ds_bpermute_b32 v241, v253, v240
	ds_bpermute_b32 v240, v252, v240
	v_med3_f32 v70, v70, 0, v193
	v_med3_f32 v71, v71, 0, v193
	v_pk_mul_f32 v[74:75], v[66:67], v[82:83] op_sel_hi:[1,0]
	v_med3_f32 v66, v72, 0, v193
	v_med3_f32 v67, v73, 0, v193
	v_pk_mul_f32 v[70:71], v[70:71], v[70:71]
	v_med3_f32 v68, v68, 0, v193
	v_med3_f32 v69, v69, 0, v193
	v_pk_mul_f32 v[66:67], v[66:67], v[66:67]
	v_pk_mul_f32 v[70:71], v[70:71], v[82:83] op_sel_hi:[1,0]
	v_pk_mul_f32 v[72:73], v[66:67], v[82:83] op_sel_hi:[1,0]
	v_pk_mul_f32 v[66:67], v[68:69], v[68:69]
	v_med3_f32 v64, v64, 0, v193
	v_pk_mul_f32 v[76:77], v[66:67], v[82:83] op_sel_hi:[1,0]
	v_cvt_pk_bf16_f32 v66, v70, v71
	ds_read2_b32 v[70:71], v148 offset0:128 offset1:144
	v_med3_f32 v65, v65, 0, v193
	v_cvt_pk_bf16_f32 v67, v72, v73
	v_cvt_pk_bf16_f32 v68, v74, v75
	v_cvt_pk_bf16_f32 v69, v76, v77
	v_subrev_u32_e32 v250, s82, v94
	v_add_u32_e32 v250, 0x840, v250
	ds_bpermute_b32 v242, v252, v66
	ds_bpermute_b32 v246, v253, v66
	ds_bpermute_b32 v243, v252, v67
	ds_bpermute_b32 v247, v253, v67
	ds_bpermute_b32 v244, v252, v68
	ds_bpermute_b32 v248, v253, v68
	ds_bpermute_b32 v245, v252, v69
	ds_bpermute_b32 v249, v253, v69
	ds_bpermute_b32 v251, v253, v250
	ds_bpermute_b32 v250, v252, v250
	s_waitcnt lgkmcnt(0)
	v_cndmask_b32_e64 v232, v232, v242, s[100:101]
	v_cndmask_b32_e64 v233, v233, v243, s[100:101]
	v_cndmask_b32_e64 v234, v234, v244, s[100:101]
	v_cndmask_b32_e64 v235, v235, v245, s[100:101]
	v_cndmask_b32_e64 v236, v236, v246, s[100:101]
	v_cndmask_b32_e64 v237, v237, v247, s[100:101]
	v_cndmask_b32_e64 v238, v238, v248, s[100:101]
	v_cndmask_b32_e64 v239, v239, v249, s[100:101]
	v_cndmask_b32_e64 v240, v240, v250, s[100:101]
	v_cndmask_b32_e64 v241, v241, v251, s[100:101]
	global_store_dwordx4 v240, v[232:235], s[82:83]
	global_store_dwordx4 v241, v[236:239], s[82:83]
	v_med3_f32 v60, v60, 0, v193
	v_med3_f32 v61, v61, 0, v193
	s_waitcnt lgkmcnt(0)
	v_mul_f32_e32 v66, v70, v70
	v_pk_mul_f32 v[64:65], v[64:65], v[64:65]
	v_med3_f32 v62, v62, 0, v193
	v_med3_f32 v63, v63, 0, v193
	v_med3_f32 v58, v58, 0, v193
	v_med3_f32 v59, v59, 0, v193
	v_pk_mul_f32 v[64:65], v[64:65], v[66:67] op_sel_hi:[1,0]
	v_pk_mul_f32 v[60:61], v[60:61], v[60:61]
	v_pk_mul_f32 v[62:63], v[62:63], v[62:63]
	v_pk_mul_f32 v[58:59], v[58:59], v[58:59]
	v_pk_mul_f32 v[68:69], v[60:61], v[66:67] op_sel_hi:[1,0]
	v_cvt_pk_bf16_f32 v61, v64, v65
	v_add_co_u32_e32 v64, vcc, s72, v144
	v_pk_mul_f32 v[62:63], v[62:63], v[66:67] op_sel_hi:[1,0]
	v_pk_mul_f32 v[58:59], v[58:59], v[66:67] op_sel_hi:[1,0]
	v_addc_co_u32_e32 v65, vcc, 0, v145, vcc
	v_cvt_pk_bf16_f32 v60, v62, v63
	v_cvt_pk_bf16_f32 v62, v58, v59
	v_add_co_u32_e32 v58, vcc, s31, v144
	v_med3_f32 v50, v50, 0, v193
	v_med3_f32 v51, v51, 0, v193
	v_addc_co_u32_e32 v59, vcc, 0, v145, vcc
	v_pk_mul_f32 v[50:51], v[50:51], v[50:51]
	v_cvt_pk_bf16_f32 v63, v68, v69
	v_subrev_u32_e32 v240, s82, v58
	v_add_u32_e32 v240, 0xfffff000, v240
	ds_bpermute_b32 v232, v252, v60
	ds_bpermute_b32 v236, v253, v60
	ds_bpermute_b32 v233, v252, v61
	ds_bpermute_b32 v237, v253, v61
	ds_bpermute_b32 v234, v252, v62
	ds_bpermute_b32 v238, v253, v62
	ds_bpermute_b32 v235, v252, v63
	ds_bpermute_b32 v239, v253, v63
	ds_bpermute_b32 v241, v253, v240
	ds_bpermute_b32 v240, v252, v240
	v_med3_f32 v54, v54, 0, v193
	v_med3_f32 v55, v55, 0, v193
	v_pk_mul_f32 v[60:61], v[50:51], v[66:67] op_sel_hi:[1,0]
	v_med3_f32 v50, v56, 0, v193
	v_med3_f32 v51, v57, 0, v193
	v_med3_f32 v52, v52, 0, v193
	v_med3_f32 v53, v53, 0, v193
	v_pk_mul_f32 v[50:51], v[50:51], v[50:51]
	v_pk_mul_f32 v[54:55], v[54:55], v[54:55]
	v_pk_mul_f32 v[56:57], v[50:51], v[66:67] op_sel_hi:[1,0]
	v_pk_mul_f32 v[50:51], v[52:53], v[52:53]
	v_pk_mul_f32 v[54:55], v[54:55], v[66:67] op_sel_hi:[1,0]
	v_pk_mul_f32 v[62:63], v[50:51], v[66:67] op_sel_hi:[1,0]
	v_cvt_pk_bf16_f32 v50, v54, v55
	v_med3_f32 v42, v42, 0, v193
	v_med3_f32 v43, v43, 0, v193
	v_cvt_pk_bf16_f32 v51, v56, v57
	v_cvt_pk_bf16_f32 v52, v60, v61
	v_cvt_pk_bf16_f32 v53, v62, v63
	v_subrev_u32_e32 v250, s82, v64
	v_add_u32_e32 v250, 0x40, v250
	ds_bpermute_b32 v242, v252, v50
	ds_bpermute_b32 v246, v253, v50
	ds_bpermute_b32 v243, v252, v51
	ds_bpermute_b32 v247, v253, v51
	ds_bpermute_b32 v244, v252, v52
	ds_bpermute_b32 v248, v253, v52
	ds_bpermute_b32 v245, v252, v53
	ds_bpermute_b32 v249, v253, v53
	ds_bpermute_b32 v251, v253, v250
	ds_bpermute_b32 v250, v252, v250
	s_waitcnt lgkmcnt(0)
	v_cndmask_b32_e64 v232, v232, v242, s[100:101]
	v_cndmask_b32_e64 v233, v233, v243, s[100:101]
	v_cndmask_b32_e64 v234, v234, v244, s[100:101]
	v_cndmask_b32_e64 v235, v235, v245, s[100:101]
	v_cndmask_b32_e64 v236, v236, v246, s[100:101]
	v_cndmask_b32_e64 v237, v237, v247, s[100:101]
	v_cndmask_b32_e64 v238, v238, v248, s[100:101]
	v_cndmask_b32_e64 v239, v239, v249, s[100:101]
	v_cndmask_b32_e64 v240, v240, v250, s[100:101]
	v_cndmask_b32_e64 v241, v241, v251, s[100:101]
	global_store_dwordx4 v240, v[232:235], s[82:83]
	global_store_dwordx4 v241, v[236:239], s[82:83]
	v_pk_mul_f32 v[42:43], v[42:43], v[42:43]
	v_med3_f32 v46, v46, 0, v193
	v_mul_f32_e32 v50, v71, v71
	v_pk_mul_f32 v[52:53], v[42:43], v[50:51] op_sel_hi:[1,0]
	v_med3_f32 v42, v48, 0, v193
	v_med3_f32 v43, v49, 0, v193
	v_med3_f32 v47, v47, 0, v193
	v_med3_f32 v44, v44, 0, v193
	v_med3_f32 v45, v45, 0, v193
	v_pk_mul_f32 v[42:43], v[42:43], v[42:43]
	v_pk_mul_f32 v[46:47], v[46:47], v[46:47]
	v_pk_mul_f32 v[48:49], v[42:43], v[50:51] op_sel_hi:[1,0]
	v_pk_mul_f32 v[42:43], v[44:45], v[44:45]
	v_med3_f32 v34, v34, 0, v193
	v_med3_f32 v35, v35, 0, v193
	v_pk_mul_f32 v[46:47], v[46:47], v[50:51] op_sel_hi:[1,0]
	v_pk_mul_f32 v[54:55], v[42:43], v[50:51] op_sel_hi:[1,0]
	v_cvt_pk_bf16_f32 v42, v46, v47
	v_cvt_pk_bf16_f32 v43, v48, v49
	v_pk_mul_f32 v[34:35], v[34:35], v[34:35]
	v_cvt_pk_bf16_f32 v44, v52, v53
	v_cvt_pk_bf16_f32 v45, v54, v55
	v_subrev_u32_e32 v240, s82, v64
	v_add_u32_e32 v240, 0x800, v240
	ds_bpermute_b32 v232, v252, v42
	ds_bpermute_b32 v236, v253, v42
	ds_bpermute_b32 v233, v252, v43
	ds_bpermute_b32 v237, v253, v43
	ds_bpermute_b32 v234, v252, v44
	ds_bpermute_b32 v238, v253, v44
	ds_bpermute_b32 v235, v252, v45
	ds_bpermute_b32 v239, v253, v45
	ds_bpermute_b32 v241, v253, v240
	ds_bpermute_b32 v240, v252, v240
	v_med3_f32 v38, v38, 0, v193
	v_med3_f32 v39, v39, 0, v193
	v_pk_mul_f32 v[42:43], v[34:35], v[50:51] op_sel_hi:[1,0]
	v_med3_f32 v34, v40, 0, v193
	v_med3_f32 v35, v41, 0, v193
	v_pk_mul_f32 v[38:39], v[38:39], v[38:39]
	v_med3_f32 v36, v36, 0, v193
	v_med3_f32 v37, v37, 0, v193
	v_pk_mul_f32 v[34:35], v[34:35], v[34:35]
	v_pk_mul_f32 v[38:39], v[38:39], v[50:51] op_sel_hi:[1,0]
	v_pk_mul_f32 v[40:41], v[34:35], v[50:51] op_sel_hi:[1,0]
	v_pk_mul_f32 v[34:35], v[36:37], v[36:37]
	v_med3_f32 v26, v26, 0, v193
	v_pk_mul_f32 v[44:45], v[34:35], v[50:51] op_sel_hi:[1,0]
	v_cvt_pk_bf16_f32 v34, v38, v39
	ds_read2_b32 v[38:39], v148 offset0:160 offset1:176
	v_med3_f32 v27, v27, 0, v193
	v_cvt_pk_bf16_f32 v35, v40, v41
	v_cvt_pk_bf16_f32 v36, v42, v43
	v_cvt_pk_bf16_f32 v37, v44, v45
	v_subrev_u32_e32 v250, s82, v64
	v_add_u32_e32 v250, 0x840, v250
	ds_bpermute_b32 v242, v252, v34
	ds_bpermute_b32 v246, v253, v34
	ds_bpermute_b32 v243, v252, v35
	ds_bpermute_b32 v247, v253, v35
	ds_bpermute_b32 v244, v252, v36
	ds_bpermute_b32 v248, v253, v36
	ds_bpermute_b32 v245, v252, v37
	ds_bpermute_b32 v249, v253, v37
	ds_bpermute_b32 v251, v253, v250
	ds_bpermute_b32 v250, v252, v250
	s_waitcnt lgkmcnt(0)
	v_cndmask_b32_e64 v232, v232, v242, s[100:101]
	v_cndmask_b32_e64 v233, v233, v243, s[100:101]
	v_cndmask_b32_e64 v234, v234, v244, s[100:101]
	v_cndmask_b32_e64 v235, v235, v245, s[100:101]
	v_cndmask_b32_e64 v236, v236, v246, s[100:101]
	v_cndmask_b32_e64 v237, v237, v247, s[100:101]
	v_cndmask_b32_e64 v238, v238, v248, s[100:101]
	v_cndmask_b32_e64 v239, v239, v249, s[100:101]
	v_cndmask_b32_e64 v240, v240, v250, s[100:101]
	v_cndmask_b32_e64 v241, v241, v251, s[100:101]
	global_store_dwordx4 v240, v[232:235], s[82:83]
	global_store_dwordx4 v241, v[236:239], s[82:83]
	v_pk_mul_f32 v[26:27], v[26:27], v[26:27]
	v_med3_f32 v30, v30, 0, v193
	s_waitcnt lgkmcnt(0)
	v_mul_f32_e32 v34, v38, v38
	v_pk_mul_f32 v[36:37], v[26:27], v[34:35] op_sel_hi:[1,0]
	v_med3_f32 v26, v32, 0, v193
	v_med3_f32 v27, v33, 0, v193
	v_med3_f32 v31, v31, 0, v193
	v_med3_f32 v28, v28, 0, v193
	v_med3_f32 v29, v29, 0, v193
	v_pk_mul_f32 v[26:27], v[26:27], v[26:27]
	v_pk_mul_f32 v[30:31], v[30:31], v[30:31]
	v_pk_mul_f32 v[32:33], v[26:27], v[34:35] op_sel_hi:[1,0]
	v_pk_mul_f32 v[26:27], v[28:29], v[28:29]
	v_med3_f32 v18, v18, 0, v193
	v_med3_f32 v19, v19, 0, v193
	v_pk_mul_f32 v[30:31], v[30:31], v[34:35] op_sel_hi:[1,0]
	v_pk_mul_f32 v[40:41], v[26:27], v[34:35] op_sel_hi:[1,0]
	v_cvt_pk_bf16_f32 v26, v30, v31
	v_cvt_pk_bf16_f32 v27, v32, v33
	v_pk_mul_f32 v[18:19], v[18:19], v[18:19]
	v_cvt_pk_bf16_f32 v28, v36, v37
	v_cvt_pk_bf16_f32 v29, v40, v41
	v_subrev_u32_e32 v240, s82, v58
	ds_bpermute_b32 v232, v252, v26
	ds_bpermute_b32 v236, v253, v26
	ds_bpermute_b32 v233, v252, v27
	ds_bpermute_b32 v237, v253, v27
	ds_bpermute_b32 v234, v252, v28
	ds_bpermute_b32 v238, v253, v28
	ds_bpermute_b32 v235, v252, v29
	ds_bpermute_b32 v239, v253, v29
	ds_bpermute_b32 v241, v253, v240
	ds_bpermute_b32 v240, v252, v240
	v_med3_f32 v22, v22, 0, v193
	v_med3_f32 v23, v23, 0, v193
	v_pk_mul_f32 v[26:27], v[18:19], v[34:35] op_sel_hi:[1,0]
	v_med3_f32 v18, v24, 0, v193
	v_med3_f32 v19, v25, 0, v193
	v_med3_f32 v20, v20, 0, v193
	v_med3_f32 v21, v21, 0, v193
	v_pk_mul_f32 v[18:19], v[18:19], v[18:19]
	v_pk_mul_f32 v[22:23], v[22:23], v[22:23]
	v_pk_mul_f32 v[24:25], v[18:19], v[34:35] op_sel_hi:[1,0]
	v_pk_mul_f32 v[18:19], v[20:21], v[20:21]
	v_pk_mul_f32 v[22:23], v[22:23], v[34:35] op_sel_hi:[1,0]
	v_pk_mul_f32 v[28:29], v[18:19], v[34:35] op_sel_hi:[1,0]
	v_cvt_pk_bf16_f32 v18, v22, v23
	v_med3_f32 v10, v10, 0, v193
	v_med3_f32 v11, v11, 0, v193
	v_cvt_pk_bf16_f32 v19, v24, v25
	v_cvt_pk_bf16_f32 v20, v26, v27
	v_cvt_pk_bf16_f32 v21, v28, v29
	v_subrev_u32_e32 v250, s82, v58
	v_add_u32_e32 v250, 0x40, v250
	ds_bpermute_b32 v242, v252, v18
	ds_bpermute_b32 v246, v253, v18
	ds_bpermute_b32 v243, v252, v19
	ds_bpermute_b32 v247, v253, v19
	ds_bpermute_b32 v244, v252, v20
	ds_bpermute_b32 v248, v253, v20
	ds_bpermute_b32 v245, v252, v21
	ds_bpermute_b32 v249, v253, v21
	ds_bpermute_b32 v251, v253, v250
	ds_bpermute_b32 v250, v252, v250
	s_waitcnt lgkmcnt(0)
	v_cndmask_b32_e64 v232, v232, v242, s[100:101]
	v_cndmask_b32_e64 v233, v233, v243, s[100:101]
	v_cndmask_b32_e64 v234, v234, v244, s[100:101]
	v_cndmask_b32_e64 v235, v235, v245, s[100:101]
	v_cndmask_b32_e64 v236, v236, v246, s[100:101]
	v_cndmask_b32_e64 v237, v237, v247, s[100:101]
	v_cndmask_b32_e64 v238, v238, v248, s[100:101]
	v_cndmask_b32_e64 v239, v239, v249, s[100:101]
	v_cndmask_b32_e64 v240, v240, v250, s[100:101]
	v_cndmask_b32_e64 v241, v241, v251, s[100:101]
	global_store_dwordx4 v240, v[232:235], s[82:83]
	global_store_dwordx4 v241, v[236:239], s[82:83]
	v_pk_mul_f32 v[10:11], v[10:11], v[10:11]
	v_med3_f32 v14, v14, 0, v193
	v_mul_f32_e32 v18, v39, v39
	v_pk_mul_f32 v[20:21], v[10:11], v[18:19] op_sel_hi:[1,0]
	v_med3_f32 v10, v16, 0, v193
	v_med3_f32 v11, v17, 0, v193
	v_med3_f32 v15, v15, 0, v193
	v_med3_f32 v12, v12, 0, v193
	v_med3_f32 v13, v13, 0, v193
	v_pk_mul_f32 v[10:11], v[10:11], v[10:11]
	v_pk_mul_f32 v[14:15], v[14:15], v[14:15]
	v_pk_mul_f32 v[16:17], v[10:11], v[18:19] op_sel_hi:[1,0]
	v_pk_mul_f32 v[10:11], v[12:13], v[12:13]
	v_med3_f32 v2, v2, 0, v193
	v_med3_f32 v3, v3, 0, v193
	v_pk_mul_f32 v[14:15], v[14:15], v[18:19] op_sel_hi:[1,0]
	v_pk_mul_f32 v[22:23], v[10:11], v[18:19] op_sel_hi:[1,0]
	v_cvt_pk_bf16_f32 v10, v14, v15
	v_cvt_pk_bf16_f32 v11, v16, v17
	v_pk_mul_f32 v[2:3], v[2:3], v[2:3]
	v_cvt_pk_bf16_f32 v12, v20, v21
	v_cvt_pk_bf16_f32 v13, v22, v23
	v_subrev_u32_e32 v240, s82, v58
	v_add_u32_e32 v240, 0x800, v240
	ds_bpermute_b32 v232, v252, v10
	ds_bpermute_b32 v236, v253, v10
	ds_bpermute_b32 v233, v252, v11
	ds_bpermute_b32 v237, v253, v11
	ds_bpermute_b32 v234, v252, v12
	ds_bpermute_b32 v238, v253, v12
	ds_bpermute_b32 v235, v252, v13
	ds_bpermute_b32 v239, v253, v13
	ds_bpermute_b32 v241, v253, v240
	ds_bpermute_b32 v240, v252, v240
	v_med3_f32 v6, v6, 0, v193
	v_med3_f32 v7, v7, 0, v193
	v_pk_mul_f32 v[10:11], v[2:3], v[18:19] op_sel_hi:[1,0]
	v_med3_f32 v2, v8, 0, v193
	v_med3_f32 v3, v9, 0, v193
	v_med3_f32 v4, v4, 0, v193
	v_med3_f32 v5, v5, 0, v193
	v_pk_mul_f32 v[2:3], v[2:3], v[2:3]
	v_pk_mul_f32 v[6:7], v[6:7], v[6:7]
	v_pk_mul_f32 v[8:9], v[2:3], v[18:19] op_sel_hi:[1,0]
	v_pk_mul_f32 v[2:3], v[4:5], v[4:5]
	s_andn2_b64 vcc, exec, s[38:39]
	s_mov_b64 s[38:39], -1
	v_pk_mul_f32 v[6:7], v[6:7], v[18:19] op_sel_hi:[1,0]
	v_pk_mul_f32 v[12:13], v[2:3], v[18:19] op_sel_hi:[1,0]
	v_cvt_pk_bf16_f32 v2, v6, v7
	v_cvt_pk_bf16_f32 v3, v8, v9
	v_cvt_pk_bf16_f32 v4, v10, v11
	s_nop 0
	v_cvt_pk_bf16_f32 v5, v12, v13
	v_subrev_u32_e32 v250, s82, v58
	v_add_u32_e32 v250, 0x840, v250
	ds_bpermute_b32 v242, v252, v2
	ds_bpermute_b32 v246, v253, v2
	ds_bpermute_b32 v243, v252, v3
	ds_bpermute_b32 v247, v253, v3
	ds_bpermute_b32 v244, v252, v4
	ds_bpermute_b32 v248, v253, v4
	ds_bpermute_b32 v245, v252, v5
	ds_bpermute_b32 v249, v253, v5
	ds_bpermute_b32 v251, v253, v250
	ds_bpermute_b32 v250, v252, v250
	s_waitcnt lgkmcnt(0)
	v_cndmask_b32_e64 v232, v232, v242, s[100:101]
	v_cndmask_b32_e64 v233, v233, v243, s[100:101]
	v_cndmask_b32_e64 v234, v234, v244, s[100:101]
	v_cndmask_b32_e64 v235, v235, v245, s[100:101]
	v_cndmask_b32_e64 v236, v236, v246, s[100:101]
	v_cndmask_b32_e64 v237, v237, v247, s[100:101]
	v_cndmask_b32_e64 v238, v238, v248, s[100:101]
	v_cndmask_b32_e64 v239, v239, v249, s[100:101]
	v_cndmask_b32_e64 v240, v240, v250, s[100:101]
	v_cndmask_b32_e64 v241, v241, v251, s[100:101]
	global_store_dwordx4 v240, v[232:235], s[82:83]
	global_store_dwordx4 v241, v[236:239], s[82:83]
	s_cbranch_vccnz .LBB0_1222
	s_andn2_b64 vcc, exec, s[0:1]
	s_cbranch_vccnz .LBB0_1221
	s_barrier
	s_branch .LBB0_1221

.LBB0_1337:
	v_mbcnt_lo_u32_b32 v231, -1, 0
	v_mbcnt_hi_u32_b32 v231, -1, v231
	v_and_b32_e32 v253, 3, v231
	v_lshrrev_b32_e32 v252, 3, v231
	v_lshl_add_u32 v252, v253, 4, v252
	v_lshlrev_b32_e32 v252, 2, v252
	v_lshrrev_b32_e32 v231, 2, v231
	v_lshl_add_u32 v231, v253, 4, v231
	v_lshlrev_b32_e32 v231, 2, v231
	v_add_u32_e32 v253, 32, v252
	s_mov_b32 s100, 0xf0f0f0f0
	s_mov_b32 s101, 0xf0f0f0f0
	v_pk_mul_f32 v[148:149], v[118:119], v[118:119]
	v_pk_mul_f32 v[150:151], v[126:127], v[126:127]
	v_pk_fma_f32 v[148:149], v[116:117], v[116:117], v[148:149]
	v_pk_fma_f32 v[150:151], v[124:125], v[124:125], v[150:151]
	v_lshl_add_u32 v144, s46, 8, v1
	v_pk_add_f32 v[152:153], v[148:149], v[150:151]
	v_cvt_pk_bf16_f32 v149, v118, v119
	v_cvt_pk_bf16_f32 v150, v124, v125
	v_pk_mul_f32 v[118:119], v[122:123], v[122:123]
	v_pk_mul_f32 v[124:125], v[130:131], v[130:131]
	v_pk_fma_f32 v[118:119], v[120:121], v[120:121], v[118:119]
	v_pk_fma_f32 v[124:125], v[128:129], v[128:129], v[124:125]
	s_lshl_b32 s16, s46, 5
	v_pk_add_f32 v[118:119], v[118:119], v[124:125]
	s_lshl_b32 s46, s48, 2
	v_pk_add_f32 v[124:125], v[152:153], v[118:119]
	s_or_b32 s17, s46, s14
	v_add_f32_e32 v124, v124, v125
	ds_swizzle_b32 v125, v124 offset:swizzle(SWAP,16)
	s_add_i32 s16, s17, s16
	s_ashr_i32 s17, s16, 31
	s_lshl_b64 s[16:17], s[16:17], 15
	v_cvt_pk_bf16_f32 v148, v116, v117
	v_lshl_add_u64 v[116:117], v[138:139], 0, s[16:17]
	v_cvt_pk_bf16_f32 v118, v120, v121
	v_cvt_pk_bf16_f32 v119, v122, v123
	v_cvt_pk_bf16_f32 v120, v128, v129
	v_cvt_pk_bf16_f32 v121, v130, v131
	v_subrev_u32_e32 v240, s82, v116
	v_add_u32_e32 v240, 0x40, v240
	ds_bpermute_b32 v232, v252, v118
	ds_bpermute_b32 v236, v253, v118
	ds_bpermute_b32 v233, v252, v119
	ds_bpermute_b32 v237, v253, v119
	ds_bpermute_b32 v234, v252, v120
	ds_bpermute_b32 v238, v253, v120
	ds_bpermute_b32 v235, v252, v121
	ds_bpermute_b32 v239, v253, v121
	ds_bpermute_b32 v241, v253, v240
	ds_bpermute_b32 v240, v252, v240
	s_ashr_i32 s47, s46, 31
	v_cvt_pk_bf16_f32 v151, v126, v127
	v_subrev_u32_e32 v250, s82, v116
	ds_bpermute_b32 v242, v252, v148
	ds_bpermute_b32 v246, v253, v148
	ds_bpermute_b32 v243, v252, v149
	ds_bpermute_b32 v247, v253, v149
	ds_bpermute_b32 v244, v252, v150
	ds_bpermute_b32 v248, v253, v150
	ds_bpermute_b32 v245, v252, v151
	ds_bpermute_b32 v249, v253, v151
	ds_bpermute_b32 v251, v253, v250
	ds_bpermute_b32 v250, v252, v250
	s_waitcnt lgkmcnt(0)
	v_cndmask_b32_e64 v232, v232, v242, s[100:101]
	v_cndmask_b32_e64 v233, v233, v243, s[100:101]
	v_cndmask_b32_e64 v234, v234, v244, s[100:101]
	v_cndmask_b32_e64 v235, v235, v245, s[100:101]
	v_cndmask_b32_e64 v236, v236, v246, s[100:101]
	v_cndmask_b32_e64 v237, v237, v247, s[100:101]
	v_cndmask_b32_e64 v238, v238, v248, s[100:101]
	v_cndmask_b32_e64 v239, v239, v249, s[100:101]
	v_cndmask_b32_e64 v240, v240, v250, s[100:101]
	v_cndmask_b32_e64 v241, v241, v251, s[100:101]
	global_store_dwordx4 v240, v[232:235], s[82:83]
	global_store_dwordx4 v241, v[236:239], s[82:83]
	s_waitcnt lgkmcnt(0)
	v_add_f32_e32 v118, v124, v125
	v_mov_b32_e32 v119, v118
	s_nop 1
	v_permlane32_swap_b32_e32 v118, v119
	s_and_saveexec_b64 s[48:49], s[38:39]
	s_cbranch_execz .LBB0_1339
	v_ashrrev_i32_e32 v145, 31, v144
	v_add_f32_e32 v120, v118, v119
	v_lshlrev_b64 v[118:119], 7, v[144:145]
	v_lshl_add_u64 v[118:119], s[8:9], 0, v[118:119]
	v_lshl_add_u64 v[118:119], s[46:47], 2, v[118:119]
	s_lshl_b32 s24, s14, 2
	v_lshl_add_u64 v[118:119], v[118:119], 0, s[24:25]
	global_store_dword v[118:119], v120, off
.LBB0_1339:
	s_or_b64 exec, exec, s[48:49]
	v_pk_mul_f32 v[118:119], v[100:101], v[100:101]
	v_pk_mul_f32 v[120:121], v[104:105], v[104:105]
	v_pk_fma_f32 v[118:119], v[98:99], v[98:99], v[118:119]
	v_cvt_pk_bf16_f32 v98, v98, v99
	v_cvt_pk_bf16_f32 v99, v100, v101
	v_cvt_pk_bf16_f32 v100, v102, v103
	v_cvt_pk_bf16_f32 v101, v104, v105
	v_subrev_u32_e32 v240, s82, v116
	v_add_u32_e32 v240, 0x800, v240
	ds_bpermute_b32 v232, v252, v98
	ds_bpermute_b32 v236, v253, v98
	ds_bpermute_b32 v233, v252, v99
	ds_bpermute_b32 v237, v253, v99
	ds_bpermute_b32 v234, v252, v100
	ds_bpermute_b32 v238, v253, v100
	ds_bpermute_b32 v235, v252, v101
	ds_bpermute_b32 v239, v253, v101
	ds_bpermute_b32 v241, v253, v240
	ds_bpermute_b32 v240, v252, v240
	v_pk_fma_f32 v[120:121], v[102:103], v[102:103], v[120:121]
	s_nop 0
	v_pk_mul_f32 v[98:99], v[108:109], v[108:109]
	v_pk_mul_f32 v[100:101], v[112:113], v[112:113]
	v_pk_fma_f32 v[98:99], v[106:107], v[106:107], v[98:99]
	v_pk_fma_f32 v[100:101], v[110:111], v[110:111], v[100:101]
	v_pk_add_f32 v[118:119], v[118:119], v[120:121]
	v_pk_add_f32 v[98:99], v[98:99], v[100:101]
	s_nop 0
	v_pk_add_f32 v[100:101], v[118:119], v[98:99]
	v_cvt_pk_bf16_f32 v98, v106, v107
	v_cvt_pk_bf16_f32 v99, v108, v109
	s_nop 0
	v_add_f32_e32 v102, v100, v101
	ds_swizzle_b32 v103, v102 offset:swizzle(SWAP,16)
	v_cvt_pk_bf16_f32 v100, v110, v111
	v_cvt_pk_bf16_f32 v101, v112, v113
	v_subrev_u32_e32 v250, s82, v116
	v_add_u32_e32 v250, 0x840, v250
	ds_bpermute_b32 v242, v252, v98
	ds_bpermute_b32 v246, v253, v98
	ds_bpermute_b32 v243, v252, v99
	ds_bpermute_b32 v247, v253, v99
	ds_bpermute_b32 v244, v252, v100
	ds_bpermute_b32 v248, v253, v100
	ds_bpermute_b32 v245, v252, v101
	ds_bpermute_b32 v249, v253, v101
	ds_bpermute_b32 v251, v253, v250
	ds_bpermute_b32 v250, v252, v250
	s_waitcnt lgkmcnt(0)
	v_cndmask_b32_e64 v232, v232, v242, s[100:101]
	v_cndmask_b32_e64 v233, v233, v243, s[100:101]
	v_cndmask_b32_e64 v234, v234, v244, s[100:101]
	v_cndmask_b32_e64 v235, v235, v245, s[100:101]
	v_cndmask_b32_e64 v236, v236, v246, s[100:101]
	v_cndmask_b32_e64 v237, v237, v247, s[100:101]
	v_cndmask_b32_e64 v238, v238, v248, s[100:101]
	v_cndmask_b32_e64 v239, v239, v249, s[100:101]
	v_cndmask_b32_e64 v240, v240, v250, s[100:101]
	v_cndmask_b32_e64 v241, v241, v251, s[100:101]
	global_store_dwordx4 v240, v[232:235], s[82:83]
	global_store_dwordx4 v241, v[236:239], s[82:83]
	s_waitcnt lgkmcnt(0)
	s_nop 0
	v_add_f32_e32 v98, v102, v103
	v_mov_b32_e32 v99, v98
	s_nop 1
	v_permlane32_swap_b32_e32 v98, v99
	s_and_saveexec_b64 s[48:49], s[38:39]
	s_cbranch_execz .LBB0_1341
	v_or_b32_e32 v100, 16, v144
	v_ashrrev_i32_e32 v101, 31, v100
	v_add_f32_e32 v102, v98, v99
	v_lshlrev_b64 v[98:99], 7, v[100:101]
	v_lshl_add_u64 v[98:99], s[8:9], 0, v[98:99]
	v_lshl_add_u64 v[98:99], s[46:47], 2, v[98:99]
	s_lshl_b32 s24, s14, 2
	v_lshl_add_u64 v[98:99], v[98:99], 0, s[24:25]
	global_store_dword v[98:99], v102, off
.LBB0_1341:
	s_or_b64 exec, exec, s[48:49]
	v_pk_mul_f32 v[98:99], v[84:85], v[84:85]
	v_pk_mul_f32 v[100:101], v[92:93], v[92:93]
	v_pk_fma_f32 v[98:99], v[82:83], v[82:83], v[98:99]
	v_pk_fma_f32 v[100:101], v[90:91], v[90:91], v[100:101]
	s_nop 0
	v_pk_add_f32 v[102:103], v[98:99], v[100:101]
	v_cvt_pk_bf16_f32 v99, v84, v85
	v_cvt_pk_bf16_f32 v100, v90, v91
	v_pk_mul_f32 v[84:85], v[88:89], v[88:89]
	v_pk_mul_f32 v[90:91], v[96:97], v[96:97]
	v_pk_fma_f32 v[84:85], v[86:87], v[86:87], v[84:85]
	v_pk_fma_f32 v[90:91], v[94:95], v[94:95], v[90:91]
	v_cvt_pk_bf16_f32 v98, v82, v83
	v_add_co_u32_e32 v82, vcc, s73, v116
	v_pk_add_f32 v[84:85], v[84:85], v[90:91]
	s_nop 0
	v_addc_co_u32_e32 v83, vcc, 0, v117, vcc
	v_pk_add_f32 v[90:91], v[102:103], v[84:85]
	v_cvt_pk_bf16_f32 v84, v86, v87
	v_cvt_pk_bf16_f32 v85, v88, v89
	v_cvt_pk_bf16_f32 v86, v94, v95
	v_cvt_pk_bf16_f32 v87, v96, v97
	v_subrev_u32_e32 v240, s82, v82
	v_add_u32_e32 v240, 0x40, v240
	ds_bpermute_b32 v232, v252, v84
	ds_bpermute_b32 v236, v253, v84
	ds_bpermute_b32 v233, v252, v85
	ds_bpermute_b32 v237, v253, v85
	ds_bpermute_b32 v234, v252, v86
	ds_bpermute_b32 v238, v253, v86
	ds_bpermute_b32 v235, v252, v87
	ds_bpermute_b32 v239, v253, v87
	ds_bpermute_b32 v241, v253, v240
	ds_bpermute_b32 v240, v252, v240
	v_add_f32_e32 v90, v90, v91
	ds_swizzle_b32 v91, v90 offset:swizzle(SWAP,16)
	v_cvt_pk_bf16_f32 v101, v92, v93
	v_subrev_u32_e32 v250, s82, v82
	ds_bpermute_b32 v242, v252, v98
	ds_bpermute_b32 v246, v253, v98
	ds_bpermute_b32 v243, v252, v99
	ds_bpermute_b32 v247, v253, v99
	ds_bpermute_b32 v244, v252, v100
	ds_bpermute_b32 v248, v253, v100
	ds_bpermute_b32 v245, v252, v101
	ds_bpermute_b32 v249, v253, v101
	ds_bpermute_b32 v251, v253, v250
	ds_bpermute_b32 v250, v252, v250
	s_waitcnt lgkmcnt(0)
	v_cndmask_b32_e64 v232, v232, v242, s[100:101]
	v_cndmask_b32_e64 v233, v233, v243, s[100:101]
	v_cndmask_b32_e64 v234, v234, v244, s[100:101]
	v_cndmask_b32_e64 v235, v235, v245, s[100:101]
	v_cndmask_b32_e64 v236, v236, v246, s[100:101]
	v_cndmask_b32_e64 v237, v237, v247, s[100:101]
	v_cndmask_b32_e64 v238, v238, v248, s[100:101]
	v_cndmask_b32_e64 v239, v239, v249, s[100:101]
	v_cndmask_b32_e64 v240, v240, v250, s[100:101]
	v_cndmask_b32_e64 v241, v241, v251, s[100:101]
	global_store_dwordx4 v240, v[232:235], s[82:83]
	global_store_dwordx4 v241, v[236:239], s[82:83]
	s_waitcnt lgkmcnt(0)
	v_add_f32_e32 v84, v90, v91
	v_mov_b32_e32 v85, v84
	s_nop 1
	v_permlane32_swap_b32_e32 v84, v85
	s_and_saveexec_b64 s[48:49], s[38:39]
	s_cbranch_execz .LBB0_1343
	v_or_b32_e32 v86, 32, v144
	v_ashrrev_i32_e32 v87, 31, v86
	v_add_f32_e32 v88, v84, v85
	v_lshlrev_b64 v[84:85], 7, v[86:87]
	v_lshl_add_u64 v[84:85], s[8:9], 0, v[84:85]
	v_lshl_add_u64 v[84:85], s[46:47], 2, v[84:85]
	s_lshl_b32 s24, s14, 2
	v_lshl_add_u64 v[84:85], v[84:85], 0, s[24:25]
	global_store_dword v[84:85], v88, off
.LBB0_1343:
	s_or_b64 exec, exec, s[48:49]
	v_pk_mul_f32 v[84:85], v[60:61], v[60:61]
	v_pk_mul_f32 v[86:87], v[72:73], v[72:73]
	v_pk_fma_f32 v[84:85], v[58:59], v[58:59], v[84:85]
	v_cvt_pk_bf16_f32 v58, v58, v59
	v_cvt_pk_bf16_f32 v59, v60, v61
	v_cvt_pk_bf16_f32 v60, v70, v71
	v_cvt_pk_bf16_f32 v61, v72, v73
	v_subrev_u32_e32 v240, s82, v82
	v_add_u32_e32 v240, 0x800, v240
	ds_bpermute_b32 v232, v252, v58
	ds_bpermute_b32 v236, v253, v58
	ds_bpermute_b32 v233, v252, v59
	ds_bpermute_b32 v237, v253, v59
	ds_bpermute_b32 v234, v252, v60
	ds_bpermute_b32 v238, v253, v60
	ds_bpermute_b32 v235, v252, v61
	ds_bpermute_b32 v239, v253, v61
	ds_bpermute_b32 v241, v253, v240
	ds_bpermute_b32 v240, v252, v240
	v_pk_fma_f32 v[86:87], v[70:71], v[70:71], v[86:87]
	s_nop 0
	v_pk_mul_f32 v[58:59], v[76:77], v[76:77]
	v_pk_mul_f32 v[60:61], v[80:81], v[80:81]
	v_pk_fma_f32 v[58:59], v[74:75], v[74:75], v[58:59]
	v_pk_fma_f32 v[60:61], v[78:79], v[78:79], v[60:61]
	v_pk_add_f32 v[84:85], v[84:85], v[86:87]
	v_pk_add_f32 v[58:59], v[58:59], v[60:61]
	s_nop 0
	v_pk_add_f32 v[60:61], v[84:85], v[58:59]
	v_cvt_pk_bf16_f32 v58, v74, v75
	v_cvt_pk_bf16_f32 v59, v76, v77
	s_nop 0
	v_add_f32_e32 v70, v60, v61
	ds_swizzle_b32 v71, v70 offset:swizzle(SWAP,16)
	v_cvt_pk_bf16_f32 v60, v78, v79
	v_cvt_pk_bf16_f32 v61, v80, v81
	v_subrev_u32_e32 v250, s82, v82
	v_add_u32_e32 v250, 0x840, v250
	ds_bpermute_b32 v242, v252, v58
	ds_bpermute_b32 v246, v253, v58
	ds_bpermute_b32 v243, v252, v59
	ds_bpermute_b32 v247, v253, v59
	ds_bpermute_b32 v244, v252, v60
	ds_bpermute_b32 v248, v253, v60
	ds_bpermute_b32 v245, v252, v61
	ds_bpermute_b32 v249, v253, v61
	ds_bpermute_b32 v251, v253, v250
	ds_bpermute_b32 v250, v252, v250
	s_waitcnt lgkmcnt(0)
	v_cndmask_b32_e64 v232, v232, v242, s[100:101]
	v_cndmask_b32_e64 v233, v233, v243, s[100:101]
	v_cndmask_b32_e64 v234, v234, v244, s[100:101]
	v_cndmask_b32_e64 v235, v235, v245, s[100:101]
	v_cndmask_b32_e64 v236, v236, v246, s[100:101]
	v_cndmask_b32_e64 v237, v237, v247, s[100:101]
	v_cndmask_b32_e64 v238, v238, v248, s[100:101]
	v_cndmask_b32_e64 v239, v239, v249, s[100:101]
	v_cndmask_b32_e64 v240, v240, v250, s[100:101]
	v_cndmask_b32_e64 v241, v241, v251, s[100:101]
	global_store_dwordx4 v240, v[232:235], s[82:83]
	global_store_dwordx4 v241, v[236:239], s[82:83]
	s_waitcnt lgkmcnt(0)
	s_nop 0
	v_add_f32_e32 v58, v70, v71
	v_mov_b32_e32 v59, v58
	s_nop 1
	v_permlane32_swap_b32_e32 v58, v59
	s_and_saveexec_b64 s[48:49], s[38:39]
	s_cbranch_execz .LBB0_1345
	v_or_b32_e32 v60, 48, v144
	v_ashrrev_i32_e32 v61, 31, v60
	v_add_f32_e32 v70, v58, v59
	v_lshlrev_b64 v[58:59], 7, v[60:61]
	v_lshl_add_u64 v[58:59], s[8:9], 0, v[58:59]
	v_lshl_add_u64 v[58:59], s[46:47], 2, v[58:59]
	s_lshl_b32 s24, s14, 2
	v_lshl_add_u64 v[58:59], v[58:59], 0, s[24:25]
	global_store_dword v[58:59], v70, off
.LBB0_1345:
	s_or_b64 exec, exec, s[48:49]
	v_pk_mul_f32 v[58:59], v[52:53], v[52:53]
	v_pk_mul_f32 v[60:61], v[64:65], v[64:65]
	v_pk_fma_f32 v[58:59], v[50:51], v[50:51], v[58:59]
	v_pk_fma_f32 v[60:61], v[62:63], v[62:63], v[60:61]
	s_nop 0
	v_pk_add_f32 v[70:71], v[58:59], v[60:61]
	v_cvt_pk_bf16_f32 v58, v50, v51
	v_add_co_u32_e32 v50, vcc, s72, v116
	v_cvt_pk_bf16_f32 v59, v52, v53
	v_cvt_pk_bf16_f32 v60, v62, v63
	v_cvt_pk_bf16_f32 v61, v64, v65
	v_pk_mul_f32 v[52:53], v[56:57], v[56:57]
	s_nop 0
	v_addc_co_u32_e32 v51, vcc, 0, v117, vcc
	v_subrev_u32_e32 v240, s82, v50
	ds_bpermute_b32 v232, v252, v58
	ds_bpermute_b32 v236, v253, v58
	ds_bpermute_b32 v233, v252, v59
	ds_bpermute_b32 v237, v253, v59
	ds_bpermute_b32 v234, v252, v60
	ds_bpermute_b32 v238, v253, v60
	ds_bpermute_b32 v235, v252, v61
	ds_bpermute_b32 v239, v253, v61
	ds_bpermute_b32 v241, v253, v240
	ds_bpermute_b32 v240, v252, v240
	v_pk_fma_f32 v[52:53], v[54:55], v[54:55], v[52:53]
	s_nop 0
	v_pk_mul_f32 v[58:59], v[68:69], v[68:69]
	s_nop 0
	v_pk_fma_f32 v[58:59], v[66:67], v[66:67], v[58:59]
	s_nop 0
	v_pk_add_f32 v[52:53], v[52:53], v[58:59]
	s_nop 0
	v_pk_add_f32 v[58:59], v[70:71], v[52:53]
	v_cvt_pk_bf16_f32 v52, v54, v55
	v_cvt_pk_bf16_f32 v53, v56, v57
	v_cvt_pk_bf16_f32 v54, v66, v67
	v_cvt_pk_bf16_f32 v55, v68, v69
	v_subrev_u32_e32 v250, s82, v50
	v_add_u32_e32 v250, 0x40, v250
	ds_bpermute_b32 v242, v252, v52
	ds_bpermute_b32 v246, v253, v52
	ds_bpermute_b32 v243, v252, v53
	ds_bpermute_b32 v247, v253, v53
	ds_bpermute_b32 v244, v252, v54
	ds_bpermute_b32 v248, v253, v54
	ds_bpermute_b32 v245, v252, v55
	ds_bpermute_b32 v249, v253, v55
	ds_bpermute_b32 v251, v253, v250
	ds_bpermute_b32 v250, v252, v250
	s_waitcnt lgkmcnt(0)
	v_cndmask_b32_e64 v232, v232, v242, s[100:101]
	v_cndmask_b32_e64 v233, v233, v243, s[100:101]
	v_cndmask_b32_e64 v234, v234, v244, s[100:101]
	v_cndmask_b32_e64 v235, v235, v245, s[100:101]
	v_cndmask_b32_e64 v236, v236, v246, s[100:101]
	v_cndmask_b32_e64 v237, v237, v247, s[100:101]
	v_cndmask_b32_e64 v238, v238, v248, s[100:101]
	v_cndmask_b32_e64 v239, v239, v249, s[100:101]
	v_cndmask_b32_e64 v240, v240, v250, s[100:101]
	v_cndmask_b32_e64 v241, v241, v251, s[100:101]
	global_store_dwordx4 v240, v[232:235], s[82:83]
	global_store_dwordx4 v241, v[236:239], s[82:83]
	v_add_f32_e32 v58, v58, v59
	ds_swizzle_b32 v59, v58 offset:swizzle(SWAP,16)
	s_waitcnt lgkmcnt(0)
	v_add_f32_e32 v52, v58, v59
	v_mov_b32_e32 v53, v52
	s_nop 1
	v_permlane32_swap_b32_e32 v52, v53
	s_and_saveexec_b64 s[48:49], s[38:39]
	s_cbranch_execz .LBB0_1347
	v_ashrrev_i32_e32 v145, 31, v144
	v_add_f32_e32 v54, v52, v53
	v_lshlrev_b64 v[52:53], 7, v[144:145]
	v_lshl_add_u64 v[52:53], s[8:9], 0, v[52:53]
	v_lshl_add_u64 v[52:53], s[46:47], 2, v[52:53]
	s_lshl_b32 s24, s14, 2
	v_lshl_add_u64 v[52:53], v[52:53], 0, s[24:25]
	v_add_co_u32_e32 v52, vcc, 0x4000, v52
	s_nop 1
	v_addc_co_u32_e32 v53, vcc, 0, v53, vcc
	global_store_dword v[52:53], v54, off
.LBB0_1347:
	s_or_b64 exec, exec, s[48:49]
	v_pk_mul_f32 v[52:53], v[36:37], v[36:37]
	v_pk_mul_f32 v[54:55], v[40:41], v[40:41]
	v_pk_fma_f32 v[52:53], v[34:35], v[34:35], v[52:53]
	v_cvt_pk_bf16_f32 v34, v34, v35
	v_cvt_pk_bf16_f32 v35, v36, v37
	v_cvt_pk_bf16_f32 v36, v38, v39
	v_cvt_pk_bf16_f32 v37, v40, v41
	v_subrev_u32_e32 v240, s82, v50
	v_add_u32_e32 v240, 0x800, v240
	ds_bpermute_b32 v232, v252, v34
	ds_bpermute_b32 v236, v253, v34
	ds_bpermute_b32 v233, v252, v35
	ds_bpermute_b32 v237, v253, v35
	ds_bpermute_b32 v234, v252, v36
	ds_bpermute_b32 v238, v253, v36
	ds_bpermute_b32 v235, v252, v37
	ds_bpermute_b32 v239, v253, v37
	ds_bpermute_b32 v241, v253, v240
	ds_bpermute_b32 v240, v252, v240
	v_pk_fma_f32 v[54:55], v[38:39], v[38:39], v[54:55]
	s_nop 0
	v_pk_mul_f32 v[34:35], v[44:45], v[44:45]
	v_pk_mul_f32 v[36:37], v[48:49], v[48:49]
	v_pk_fma_f32 v[34:35], v[42:43], v[42:43], v[34:35]
	v_pk_fma_f32 v[36:37], v[46:47], v[46:47], v[36:37]
	v_pk_add_f32 v[52:53], v[52:53], v[54:55]
	v_pk_add_f32 v[34:35], v[34:35], v[36:37]
	s_nop 0
	v_pk_add_f32 v[36:37], v[52:53], v[34:35]
	v_cvt_pk_bf16_f32 v34, v42, v43
	v_cvt_pk_bf16_f32 v35, v44, v45
	s_nop 0
	v_add_f32_e32 v38, v36, v37
	ds_swizzle_b32 v39, v38 offset:swizzle(SWAP,16)
	v_cvt_pk_bf16_f32 v36, v46, v47
	v_cvt_pk_bf16_f32 v37, v48, v49
	v_subrev_u32_e32 v250, s82, v50
	v_add_u32_e32 v250, 0x840, v250
	ds_bpermute_b32 v242, v252, v34
	ds_bpermute_b32 v246, v253, v34
	ds_bpermute_b32 v243, v252, v35
	ds_bpermute_b32 v247, v253, v35
	ds_bpermute_b32 v244, v252, v36
	ds_bpermute_b32 v248, v253, v36
	ds_bpermute_b32 v245, v252, v37
	ds_bpermute_b32 v249, v253, v37
	ds_bpermute_b32 v251, v253, v250
	ds_bpermute_b32 v250, v252, v250
	s_waitcnt lgkmcnt(0)
	v_cndmask_b32_e64 v232, v232, v242, s[100:101]
	v_cndmask_b32_e64 v233, v233, v243, s[100:101]
	v_cndmask_b32_e64 v234, v234, v244, s[100:101]
	v_cndmask_b32_e64 v235, v235, v245, s[100:101]
	v_cndmask_b32_e64 v236, v236, v246, s[100:101]
	v_cndmask_b32_e64 v237, v237, v247, s[100:101]
	v_cndmask_b32_e64 v238, v238, v248, s[100:101]
	v_cndmask_b32_e64 v239, v239, v249, s[100:101]
	v_cndmask_b32_e64 v240, v240, v250, s[100:101]
	v_cndmask_b32_e64 v241, v241, v251, s[100:101]
	global_store_dwordx4 v240, v[232:235], s[82:83]
	global_store_dwordx4 v241, v[236:239], s[82:83]
	s_waitcnt lgkmcnt(0)
	s_nop 0
	v_add_f32_e32 v34, v38, v39
	v_mov_b32_e32 v35, v34
	s_nop 1
	v_permlane32_swap_b32_e32 v34, v35
	s_and_saveexec_b64 s[48:49], s[38:39]
	s_cbranch_execz .LBB0_1349
	v_ashrrev_i32_e32 v145, 31, v144
	v_add_f32_e32 v36, v34, v35
	v_lshlrev_b64 v[34:35], 7, v[144:145]
	v_lshl_add_u64 v[34:35], s[8:9], 0, v[34:35]
	v_lshl_add_u64 v[34:35], s[46:47], 2, v[34:35]
	s_lshl_b32 s24, s14, 2
	v_lshl_add_u64 v[34:35], v[34:35], 0, s[24:25]
	v_add_co_u32_e32 v34, vcc, 0x4000, v34
	s_nop 1
	v_addc_co_u32_e32 v35, vcc, 0, v35, vcc
	global_store_dword v[34:35], v36, off offset:2048
.LBB0_1349:
	s_or_b64 exec, exec, s[48:49]
	v_pk_mul_f32 v[34:35], v[20:21], v[20:21]
	v_pk_mul_f32 v[36:37], v[28:29], v[28:29]
	v_pk_fma_f32 v[34:35], v[18:19], v[18:19], v[34:35]
	v_pk_fma_f32 v[36:37], v[26:27], v[26:27], v[36:37]
	s_nop 0
	v_pk_add_f32 v[38:39], v[34:35], v[36:37]
	v_cvt_pk_bf16_f32 v35, v20, v21
	v_cvt_pk_bf16_f32 v36, v26, v27
	v_pk_mul_f32 v[20:21], v[24:25], v[24:25]
	v_pk_mul_f32 v[26:27], v[32:33], v[32:33]
	v_pk_fma_f32 v[20:21], v[22:23], v[22:23], v[20:21]
	v_pk_fma_f32 v[26:27], v[30:31], v[30:31], v[26:27]
	v_cvt_pk_bf16_f32 v34, v18, v19
	v_add_co_u32_e32 v18, vcc, s31, v116
	v_pk_add_f32 v[20:21], v[20:21], v[26:27]
	s_nop 0
	v_addc_co_u32_e32 v19, vcc, 0, v117, vcc
	v_pk_add_f32 v[26:27], v[38:39], v[20:21]
	v_cvt_pk_bf16_f32 v20, v22, v23
	v_cvt_pk_bf16_f32 v21, v24, v25
	v_cvt_pk_bf16_f32 v22, v30, v31
	v_cvt_pk_bf16_f32 v23, v32, v33
	v_subrev_u32_e32 v240, s82, v18
	v_add_u32_e32 v240, 0x40, v240
	ds_bpermute_b32 v232, v252, v20
	ds_bpermute_b32 v236, v253, v20
	ds_bpermute_b32 v233, v252, v21
	ds_bpermute_b32 v237, v253, v21
	ds_bpermute_b32 v234, v252, v22
	ds_bpermute_b32 v238, v253, v22
	ds_bpermute_b32 v235, v252, v23
	ds_bpermute_b32 v239, v253, v23
	ds_bpermute_b32 v241, v253, v240
	ds_bpermute_b32 v240, v252, v240
	v_add_f32_e32 v26, v26, v27
	ds_swizzle_b32 v27, v26 offset:swizzle(SWAP,16)
	v_cvt_pk_bf16_f32 v37, v28, v29
	v_subrev_u32_e32 v250, s82, v18
	ds_bpermute_b32 v242, v252, v34
	ds_bpermute_b32 v246, v253, v34
	ds_bpermute_b32 v243, v252, v35
	ds_bpermute_b32 v247, v253, v35
	ds_bpermute_b32 v244, v252, v36
	ds_bpermute_b32 v248, v253, v36
	ds_bpermute_b32 v245, v252, v37
	ds_bpermute_b32 v249, v253, v37
	ds_bpermute_b32 v251, v253, v250
	ds_bpermute_b32 v250, v252, v250
	s_waitcnt lgkmcnt(0)
	v_cndmask_b32_e64 v232, v232, v242, s[100:101]
	v_cndmask_b32_e64 v233, v233, v243, s[100:101]
	v_cndmask_b32_e64 v234, v234, v244, s[100:101]
	v_cndmask_b32_e64 v235, v235, v245, s[100:101]
	v_cndmask_b32_e64 v236, v236, v246, s[100:101]
	v_cndmask_b32_e64 v237, v237, v247, s[100:101]
	v_cndmask_b32_e64 v238, v238, v248, s[100:101]
	v_cndmask_b32_e64 v239, v239, v249, s[100:101]
	v_cndmask_b32_e64 v240, v240, v250, s[100:101]
	v_cndmask_b32_e64 v241, v241, v251, s[100:101]
	global_store_dwordx4 v240, v[232:235], s[82:83]
	global_store_dwordx4 v241, v[236:239], s[82:83]
	s_waitcnt lgkmcnt(0)
	v_add_f32_e32 v20, v26, v27
	v_mov_b32_e32 v21, v20
	s_nop 1
	v_permlane32_swap_b32_e32 v20, v21
	s_and_saveexec_b64 s[48:49], s[38:39]
	s_cbranch_execz .LBB0_1351
	v_ashrrev_i32_e32 v145, 31, v144
	v_add_f32_e32 v22, v20, v21
	v_lshlrev_b64 v[20:21], 7, v[144:145]
	v_lshl_add_u64 v[20:21], s[8:9], 0, v[20:21]
	v_lshl_add_u64 v[20:21], s[46:47], 2, v[20:21]
	s_lshl_b32 s24, s14, 2
	v_lshl_add_u64 v[20:21], v[20:21], 0, s[24:25]
	v_add_co_u32_e32 v20, vcc, 0x5000, v20
	s_nop 1
	v_addc_co_u32_e32 v21, vcc, 0, v21, vcc
	global_store_dword v[20:21], v22, off
.LBB0_1351:
	s_or_b64 exec, exec, s[48:49]
	v_pk_mul_f32 v[20:21], v[4:5], v[4:5]
	v_pk_mul_f32 v[22:23], v[8:9], v[8:9]
	v_pk_fma_f32 v[20:21], v[2:3], v[2:3], v[20:21]
	v_cvt_pk_bf16_f32 v2, v2, v3
	v_cvt_pk_bf16_f32 v3, v4, v5
	v_cvt_pk_bf16_f32 v4, v6, v7
	v_cvt_pk_bf16_f32 v5, v8, v9
	v_subrev_u32_e32 v240, s82, v18
	v_add_u32_e32 v240, 0x800, v240
	ds_bpermute_b32 v232, v252, v2
	ds_bpermute_b32 v236, v253, v2
	ds_bpermute_b32 v233, v252, v3
	ds_bpermute_b32 v237, v253, v3
	ds_bpermute_b32 v234, v252, v4
	ds_bpermute_b32 v238, v253, v4
	ds_bpermute_b32 v235, v252, v5
	ds_bpermute_b32 v239, v253, v5
	ds_bpermute_b32 v241, v253, v240
	ds_bpermute_b32 v240, v252, v240
	v_pk_fma_f32 v[22:23], v[6:7], v[6:7], v[22:23]
	s_nop 0
	v_pk_mul_f32 v[2:3], v[12:13], v[12:13]
	v_pk_mul_f32 v[4:5], v[16:17], v[16:17]
	v_pk_fma_f32 v[2:3], v[10:11], v[10:11], v[2:3]
	v_pk_fma_f32 v[4:5], v[14:15], v[14:15], v[4:5]
	v_pk_add_f32 v[20:21], v[20:21], v[22:23]
	v_pk_add_f32 v[2:3], v[2:3], v[4:5]
	s_nop 0
	v_pk_add_f32 v[4:5], v[20:21], v[2:3]
	v_cvt_pk_bf16_f32 v2, v10, v11
	v_cvt_pk_bf16_f32 v3, v12, v13
	s_nop 0
	v_add_f32_e32 v6, v4, v5
	ds_swizzle_b32 v7, v6 offset:swizzle(SWAP,16)
	v_cvt_pk_bf16_f32 v4, v14, v15
	v_cvt_pk_bf16_f32 v5, v16, v17
	v_subrev_u32_e32 v250, s82, v18
	v_add_u32_e32 v250, 0x840, v250
	ds_bpermute_b32 v242, v252, v2
	ds_bpermute_b32 v246, v253, v2
	ds_bpermute_b32 v243, v252, v3
	ds_bpermute_b32 v247, v253, v3
	ds_bpermute_b32 v244, v252, v4
	ds_bpermute_b32 v248, v253, v4
	ds_bpermute_b32 v245, v252, v5
	ds_bpermute_b32 v249, v253, v5
	ds_bpermute_b32 v251, v253, v250
	ds_bpermute_b32 v250, v252, v250
	s_waitcnt lgkmcnt(0)
	v_cndmask_b32_e64 v232, v232, v242, s[100:101]
	v_cndmask_b32_e64 v233, v233, v243, s[100:101]
	v_cndmask_b32_e64 v234, v234, v244, s[100:101]
	v_cndmask_b32_e64 v235, v235, v245, s[100:101]
	v_cndmask_b32_e64 v236, v236, v246, s[100:101]
	v_cndmask_b32_e64 v237, v237, v247, s[100:101]
	v_cndmask_b32_e64 v238, v238, v248, s[100:101]
	v_cndmask_b32_e64 v239, v239, v249, s[100:101]
	v_cndmask_b32_e64 v240, v240, v250, s[100:101]
	v_cndmask_b32_e64 v241, v241, v251, s[100:101]
	global_store_dwordx4 v240, v[232:235], s[82:83]
	global_store_dwordx4 v241, v[236:239], s[82:83]
	s_waitcnt lgkmcnt(0)
	s_nop 0
	v_add_f32_e32 v2, v6, v7
	v_mov_b32_e32 v3, v2
	s_nop 1
	v_permlane32_swap_b32_e32 v2, v3
	s_and_saveexec_b64 s[48:49], s[38:39]
	s_cbranch_execz .LBB0_1353
	v_ashrrev_i32_e32 v145, 31, v144
	v_add_f32_e32 v4, v2, v3
	v_lshlrev_b64 v[2:3], 7, v[144:145]
	v_lshl_add_u64 v[2:3], s[8:9], 0, v[2:3]
	v_lshl_add_u64 v[2:3], s[46:47], 2, v[2:3]
	s_lshl_b32 s24, s14, 2
	v_lshl_add_u64 v[2:3], v[2:3], 0, s[24:25]
	v_add_co_u32_e32 v2, vcc, 0x5000, v2
	s_nop 1
	v_addc_co_u32_e32 v3, vcc, 0, v3, vcc
	global_store_dword v[2:3], v4, off offset:2048
